# PEER gather: expert row loads with sc1
# speedup vs baseline: 1.1864x; 1.1864x over previous
.LBB0_1138:
	v_and_b32_e32 v4, 15, v148
	v_cmp_eq_u32_e32 vcc, 0, v4
	v_lshlrev_b32_e32 v5, 5, v40
	v_add_u32_e32 v10, 0x80, v148
	v_cndmask_b32_e32 v10, v10, v5, vcc
	v_cmp_gt_u32_e64 s[6:7], 8, v4
	v_lshl_add_u32 v32, v10, 2, v111
	v_and_b32_e32 v36, 12, v148
	v_cndmask_b32_e64 v10, 0, v252, s[6:7]
	v_cmp_lt_u32_e64 s[6:7], 3, v4
	v_lshl_or_b32 v4, v41, 3, v5
	v_add_u32_e32 v34, 0x400, v4
	v_lshlrev_b32_e32 v4, 4, v41
	v_lshl_or_b32 v35, v40, 6, v4
	ds_bpermute_b32 v4, v36, v130
	v_cmp_eq_u32_e32 vcc, 3, v41
	v_cmp_eq_u32_e64 s[2:3], 2, v41
	v_cmp_eq_u32_e64 s[4:5], 1, v41
	v_lshlrev_b32_e32 v129, 4, v148
	s_waitcnt lgkmcnt(0)
	v_mul_lo_u32 v4, v4, s43
	v_add_u32_e32 v5, v4, v35
	v_add_u32_e32 v4, v4, v34
	buffer_load_dwordx4 v[38:41], v5, s[44:47], 0 offen sc1
	buffer_load_dwordx2 v[42:43], v4, s[44:47], 0 offen sc1
	buffer_load_dwordx4 v[44:47], v5, s[44:47], s21 offen sc1
	buffer_load_dwordx2 v[48:49], v4, s[44:47], s33 offen sc1
	buffer_load_dwordx4 v[50:53], v5, s[44:47], s20 offen sc1
	buffer_load_dwordx2 v[54:55], v4, s[44:47], s21 offen sc1
	buffer_load_dwordx4 v[56:59], v5, s[44:47], s23 offen sc1
	buffer_load_dwordx2 v[60:61], v4, s[44:47], s94 offen sc1
	s_mov_b32 s0, 0
	v_cndmask_b32_e64 v33, 1.0, v10, s[6:7]
	ds_bpermute_b32 v4, v36, v130 offset:16
	s_waitcnt lgkmcnt(0)
	v_mul_lo_u32 v4, v4, s43
	v_add_u32_e32 v5, v4, v35
	v_add_u32_e32 v4, v4, v34
	buffer_load_dwordx4 v[62:65], v5, s[44:47], 0 offen sc1
	buffer_load_dwordx4 v[68:71], v5, s[44:47], s20 offen sc1
	buffer_load_dwordx4 v[74:77], v5, s[44:47], s21 offen sc1
	buffer_load_dwordx4 v[86:89], v5, s[44:47], s23 offen sc1
	buffer_load_dwordx2 v[66:67], v4, s[44:47], 0 offen sc1
	buffer_load_dwordx2 v[78:79], v4, s[44:47], s33 offen sc1
	buffer_load_dwordx2 v[72:73], v4, s[44:47], s21 offen sc1
	buffer_load_dwordx2 v[90:91], v4, s[44:47], s94 offen sc1
	ds_bpermute_b32 v4, v36, v130 offset:32
	s_waitcnt lgkmcnt(0)
	v_mul_lo_u32 v4, v4, s43
	v_add_u32_e32 v5, v4, v35
	v_add_u32_e32 v4, v4, v34
	buffer_load_dwordx4 v[92:95], v5, s[44:47], 0 offen sc1
	buffer_load_dwordx4 v[98:101], v5, s[44:47], s20 offen sc1
	buffer_load_dwordx4 v[150:153], v5, s[44:47], s21 offen sc1
	buffer_load_dwordx4 v[156:159], v5, s[44:47], s23 offen sc1
	buffer_load_dwordx2 v[96:97], v4, s[44:47], 0 offen sc1
	buffer_load_dwordx2 v[154:155], v4, s[44:47], s33 offen sc1
	buffer_load_dwordx2 v[102:103], v4, s[44:47], s21 offen sc1
	buffer_load_dwordx2 v[160:161], v4, s[44:47], s94 offen sc1
	ds_bpermute_b32 v4, v36, v130 offset:48
	s_waitcnt lgkmcnt(0)
	v_mul_lo_u32 v4, v4, s43
	v_add_u32_e32 v5, v4, v35
	v_add_u32_e32 v4, v4, v34
	buffer_load_dwordx4 v[162:165], v5, s[44:47], 0 offen sc1
	buffer_load_dwordx4 v[168:171], v5, s[44:47], s20 offen sc1
	buffer_load_dwordx4 v[174:177], v5, s[44:47], s21 offen sc1
	buffer_load_dwordx4 v[216:219], v5, s[44:47], s23 offen sc1
	buffer_load_dwordx2 v[166:167], v4, s[44:47], 0 offen sc1
	buffer_load_dwordx2 v[178:179], v4, s[44:47], s33 offen sc1
	buffer_load_dwordx2 v[172:173], v4, s[44:47], s21 offen sc1
	buffer_load_dwordx2 v[220:221], v4, s[44:47], s94 offen sc1
	v_mov_b32_e32 v22, v28
	v_mov_b32_e32 v23, v29
	v_mov_b32_e32 v16, v30
	v_mov_b32_e32 v17, v31
	s_waitcnt vmcnt(30)
	v_mfma_f32_16x16x128_f8f6f4 v[38:41], v[38:43], v[18:23], 0 cbsz:2 blgp:2
	v_mov_b32_e32 v10, v24
	v_mov_b32_e32 v11, v25
	v_mov_b32_e32 v4, v26
	s_waitcnt vmcnt(28)
	v_mfma_f32_16x16x128_f8f6f4 v[28:31], v[44:49], v[12:17], v[38:41] cbsz:2 blgp:2
	v_mov_b32_e32 v5, v27
	s_waitcnt vmcnt(26)
	v_mfma_f32_16x16x128_f8f6f4 v[28:31], v[50:55], v[6:11], v[28:31] cbsz:2 blgp:2
	s_waitcnt vmcnt(24)
	v_mfma_f32_16x16x128_f8f6f4 v[24:27], v[56:61], v[0:5], v[28:31] cbsz:2 blgp:2
	s_nop 7
	v_cndmask_b32_e64 v24, v24, v25, s[4:5]
	v_cndmask_b32_e64 v24, v24, v26, s[2:3]
	v_cndmask_b32_e32 v24, v24, v27, vcc
	v_mul_f32_e32 v25, v33, v24
	s_nop 1
	v_mov_b32_dpp v25, v25 quad_perm:[1,0,3,2] row_mask:0xf bank_mask:0xf bound_ctrl:1
	v_fmac_f32_e32 v25, v33, v24
	s_nop 1
	v_add_f32_dpp v24, v25, v25 quad_perm:[2,3,0,1] row_mask:0xf bank_mask:0xf bound_ctrl:1
	s_nop 1
	v_add_f32_dpp v24, v24, v24 row_half_mirror row_mask:0xf bank_mask:0xf bound_ctrl:1
	ds_write_b32 v32, v24 offset:49152
	ds_bpermute_b32 v24, v36, v130 offset:64
	s_waitcnt lgkmcnt(0)
	v_mul_lo_u32 v24, v24, s43
	v_add_u32_e32 v28, v24, v35
	v_add_u32_e32 v30, v24, v34
	buffer_load_dwordx4 v[24:27], v28, s[44:47], 0 offen sc1
	buffer_load_dwordx4 v[38:41], v28, s[44:47], s20 offen sc1
	buffer_load_dwordx4 v[44:47], v28, s[44:47], s21 offen sc1
	buffer_load_dwordx4 v[50:53], v28, s[44:47], s23 offen sc1
	s_nop 0
	buffer_load_dwordx2 v[28:29], v30, s[44:47], 0 offen sc1
	buffer_load_dwordx2 v[48:49], v30, s[44:47], s33 offen sc1
	buffer_load_dwordx2 v[42:43], v30, s[44:47], s21 offen sc1
	buffer_load_dwordx2 v[54:55], v30, s[44:47], s94 offen sc1
	s_waitcnt vmcnt(27)
	v_mfma_f32_16x16x128_f8f6f4 v[56:59], v[62:67], v[18:23], 0 cbsz:2 blgp:2
	s_waitcnt vmcnt(26)
	v_mfma_f32_16x16x128_f8f6f4 v[56:59], v[74:79], v[12:17], v[56:59] cbsz:2 blgp:2
	s_waitcnt vmcnt(25)
	v_mfma_f32_16x16x128_f8f6f4 v[56:59], v[68:73], v[6:11], v[56:59] cbsz:2 blgp:2
	s_waitcnt vmcnt(24)
	v_mfma_f32_16x16x128_f8f6f4 v[56:59], v[86:91], v[0:5], v[56:59] cbsz:2 blgp:2
	s_nop 7
	v_cndmask_b32_e64 v30, v56, v57, s[4:5]
	v_cndmask_b32_e64 v30, v30, v58, s[2:3]
	v_cndmask_b32_e32 v30, v30, v59, vcc
	v_mul_f32_e32 v31, v33, v30
	s_nop 1
	v_mov_b32_dpp v31, v31 quad_perm:[1,0,3,2] row_mask:0xf bank_mask:0xf bound_ctrl:1
	v_fmac_f32_e32 v31, v33, v30
	s_nop 1
	v_add_f32_dpp v30, v31, v31 quad_perm:[2,3,0,1] row_mask:0xf bank_mask:0xf bound_ctrl:1
	s_nop 1
	v_add_f32_dpp v30, v30, v30 row_half_mirror row_mask:0xf bank_mask:0xf bound_ctrl:1
	ds_write_b32 v32, v30 offset:49156
	ds_bpermute_b32 v30, v36, v130 offset:80
	s_waitcnt lgkmcnt(0)
	v_mul_lo_u32 v30, v30, s43
	v_add_u32_e32 v31, v30, v35
	v_add_u32_e32 v30, v30, v34
	buffer_load_dwordx4 v[56:59], v31, s[44:47], 0 offen sc1
	buffer_load_dwordx4 v[62:65], v31, s[44:47], s20 offen sc1
	buffer_load_dwordx4 v[68:71], v31, s[44:47], s21 offen sc1
	buffer_load_dwordx4 v[74:77], v31, s[44:47], s23 offen sc1
	buffer_load_dwordx2 v[60:61], v30, s[44:47], 0 offen sc1
	buffer_load_dwordx2 v[72:73], v30, s[44:47], s33 offen sc1
	buffer_load_dwordx2 v[66:67], v30, s[44:47], s21 offen sc1
	buffer_load_dwordx2 v[78:79], v30, s[44:47], s94 offen sc1
	s_waitcnt vmcnt(27)
	v_mfma_f32_16x16x128_f8f6f4 v[86:89], v[92:97], v[18:23], 0 cbsz:2 blgp:2
	s_waitcnt vmcnt(26)
	v_mfma_f32_16x16x128_f8f6f4 v[86:89], v[150:155], v[12:17], v[86:89] cbsz:2 blgp:2
	s_waitcnt vmcnt(25)
	v_mfma_f32_16x16x128_f8f6f4 v[86:89], v[98:103], v[6:11], v[86:89] cbsz:2 blgp:2
	s_waitcnt vmcnt(24)
	v_mfma_f32_16x16x128_f8f6f4 v[86:89], v[156:161], v[0:5], v[86:89] cbsz:2 blgp:2
	s_nop 7
	v_cndmask_b32_e64 v30, v86, v87, s[4:5]
	v_cndmask_b32_e64 v30, v30, v88, s[2:3]
	v_cndmask_b32_e32 v30, v30, v89, vcc
	v_mul_f32_e32 v31, v33, v30
	s_nop 1
	v_mov_b32_dpp v31, v31 quad_perm:[1,0,3,2] row_mask:0xf bank_mask:0xf bound_ctrl:1
	v_fmac_f32_e32 v31, v33, v30
	s_nop 1
	v_add_f32_dpp v30, v31, v31 quad_perm:[2,3,0,1] row_mask:0xf bank_mask:0xf bound_ctrl:1
	s_nop 1
	v_add_f32_dpp v30, v30, v30 row_half_mirror row_mask:0xf bank_mask:0xf bound_ctrl:1
	ds_write_b32 v32, v30 offset:49160
	ds_bpermute_b32 v30, v36, v130 offset:96
	s_waitcnt lgkmcnt(0)
	v_mul_lo_u32 v30, v30, s43
	v_add_u32_e32 v31, v30, v35
	v_add_u32_e32 v30, v30, v34
	buffer_load_dwordx4 v[86:89], v31, s[44:47], 0 offen sc1
	buffer_load_dwordx4 v[92:95], v31, s[44:47], s20 offen sc1
	buffer_load_dwordx4 v[98:101], v31, s[44:47], s21 offen sc1
	buffer_load_dwordx4 v[150:153], v31, s[44:47], s23 offen sc1
	buffer_load_dwordx2 v[90:91], v30, s[44:47], 0 offen sc1
	buffer_load_dwordx2 v[102:103], v30, s[44:47], s33 offen sc1
	buffer_load_dwordx2 v[96:97], v30, s[44:47], s21 offen sc1
	buffer_load_dwordx2 v[154:155], v30, s[44:47], s94 offen sc1
	s_waitcnt vmcnt(27)
	v_mfma_f32_16x16x128_f8f6f4 v[156:159], v[162:167], v[18:23], 0 cbsz:2 blgp:2
	s_waitcnt vmcnt(26)
	v_mfma_f32_16x16x128_f8f6f4 v[156:159], v[174:179], v[12:17], v[156:159] cbsz:2 blgp:2
	s_waitcnt vmcnt(25)
	v_mfma_f32_16x16x128_f8f6f4 v[156:159], v[168:173], v[6:11], v[156:159] cbsz:2 blgp:2
	s_waitcnt vmcnt(24)
	v_mfma_f32_16x16x128_f8f6f4 v[156:159], v[216:221], v[0:5], v[156:159] cbsz:2 blgp:2
	s_nop 7
	v_cndmask_b32_e64 v30, v156, v157, s[4:5]
	v_cndmask_b32_e64 v30, v30, v158, s[2:3]
	v_cndmask_b32_e32 v30, v30, v159, vcc
	v_mul_f32_e32 v31, v33, v30
	s_nop 1
	v_mov_b32_dpp v31, v31 quad_perm:[1,0,3,2] row_mask:0xf bank_mask:0xf bound_ctrl:1
	v_fmac_f32_e32 v31, v33, v30
	s_nop 1
	v_add_f32_dpp v30, v31, v31 quad_perm:[2,3,0,1] row_mask:0xf bank_mask:0xf bound_ctrl:1
	s_nop 1
	v_add_f32_dpp v30, v30, v30 row_half_mirror row_mask:0xf bank_mask:0xf bound_ctrl:1
	ds_write_b32 v32, v30 offset:49164
	ds_bpermute_b32 v30, v36, v130 offset:112
	s_waitcnt lgkmcnt(0)
	v_mul_lo_u32 v30, v30, s43
	v_add_u32_e32 v31, v30, v35
	v_add_u32_e32 v30, v30, v34
	buffer_load_dwordx4 v[156:159], v31, s[44:47], 0 offen sc1
	buffer_load_dwordx4 v[162:165], v31, s[44:47], s20 offen sc1
	buffer_load_dwordx4 v[168:171], v31, s[44:47], s21 offen sc1
	buffer_load_dwordx4 v[174:177], v31, s[44:47], s23 offen sc1
	buffer_load_dwordx2 v[160:161], v30, s[44:47], 0 offen sc1
	buffer_load_dwordx2 v[172:173], v30, s[44:47], s33 offen sc1
	buffer_load_dwordx2 v[166:167], v30, s[44:47], s21 offen sc1
	buffer_load_dwordx2 v[178:179], v30, s[44:47], s94 offen sc1
	s_waitcnt vmcnt(27)
	v_mfma_f32_16x16x128_f8f6f4 v[24:27], v[24:29], v[18:23], 0 cbsz:2 blgp:2
	s_waitcnt vmcnt(26)
	v_mfma_f32_16x16x128_f8f6f4 v[24:27], v[44:49], v[12:17], v[24:27] cbsz:2 blgp:2
	s_waitcnt vmcnt(25)
	v_mfma_f32_16x16x128_f8f6f4 v[24:27], v[38:43], v[6:11], v[24:27] cbsz:2 blgp:2
	s_waitcnt vmcnt(24)
	v_mfma_f32_16x16x128_f8f6f4 v[24:27], v[50:55], v[0:5], v[24:27] cbsz:2 blgp:2
	s_nop 7
	v_cndmask_b32_e64 v24, v24, v25, s[4:5]
	v_cndmask_b32_e64 v24, v24, v26, s[2:3]
	v_cndmask_b32_e32 v24, v24, v27, vcc
	v_mul_f32_e32 v25, v33, v24
	s_nop 1
	v_mov_b32_dpp v25, v25 quad_perm:[1,0,3,2] row_mask:0xf bank_mask:0xf bound_ctrl:1
	v_fmac_f32_e32 v25, v33, v24
	s_nop 1
	v_add_f32_dpp v24, v25, v25 quad_perm:[2,3,0,1] row_mask:0xf bank_mask:0xf bound_ctrl:1
	s_nop 1
	v_add_f32_dpp v24, v24, v24 row_half_mirror row_mask:0xf bank_mask:0xf bound_ctrl:1
	ds_write_b32 v32, v24 offset:49168
	ds_bpermute_b32 v24, v36, v130 offset:128
	s_waitcnt lgkmcnt(0)
	v_mul_lo_u32 v24, v24, s43
	v_add_u32_e32 v28, v24, v35
	v_add_u32_e32 v30, v24, v34
	buffer_load_dwordx4 v[24:27], v28, s[44:47], 0 offen sc1
	buffer_load_dwordx4 v[38:41], v28, s[44:47], s20 offen sc1
	buffer_load_dwordx4 v[44:47], v28, s[44:47], s21 offen sc1
	buffer_load_dwordx4 v[50:53], v28, s[44:47], s23 offen sc1
	s_nop 0
	buffer_load_dwordx2 v[28:29], v30, s[44:47], 0 offen sc1
	buffer_load_dwordx2 v[48:49], v30, s[44:47], s33 offen sc1
	buffer_load_dwordx2 v[42:43], v30, s[44:47], s21 offen sc1
	buffer_load_dwordx2 v[54:55], v30, s[44:47], s94 offen sc1
	s_waitcnt vmcnt(27)
	v_mfma_f32_16x16x128_f8f6f4 v[56:59], v[56:61], v[18:23], 0 cbsz:2 blgp:2
	s_waitcnt vmcnt(26)
	v_mfma_f32_16x16x128_f8f6f4 v[56:59], v[68:73], v[12:17], v[56:59] cbsz:2 blgp:2
	s_waitcnt vmcnt(25)
	v_mfma_f32_16x16x128_f8f6f4 v[56:59], v[62:67], v[6:11], v[56:59] cbsz:2 blgp:2
	s_waitcnt vmcnt(24)
	v_mfma_f32_16x16x128_f8f6f4 v[56:59], v[74:79], v[0:5], v[56:59] cbsz:2 blgp:2
	s_nop 7
	v_cndmask_b32_e64 v30, v56, v57, s[4:5]
	v_cndmask_b32_e64 v30, v30, v58, s[2:3]
	v_cndmask_b32_e32 v30, v30, v59, vcc
	v_mul_f32_e32 v31, v33, v30
	s_nop 1
	v_mov_b32_dpp v31, v31 quad_perm:[1,0,3,2] row_mask:0xf bank_mask:0xf bound_ctrl:1
	v_fmac_f32_e32 v31, v33, v30
	s_nop 1
	v_add_f32_dpp v30, v31, v31 quad_perm:[2,3,0,1] row_mask:0xf bank_mask:0xf bound_ctrl:1
	s_nop 1
	v_add_f32_dpp v30, v30, v30 row_half_mirror row_mask:0xf bank_mask:0xf bound_ctrl:1
	ds_write_b32 v32, v30 offset:49172
	ds_bpermute_b32 v30, v36, v130 offset:144
	s_waitcnt lgkmcnt(0)
	v_mul_lo_u32 v30, v30, s43
	v_add_u32_e32 v31, v30, v35
	v_add_u32_e32 v30, v30, v34
	buffer_load_dwordx4 v[56:59], v31, s[44:47], 0 offen sc1
	buffer_load_dwordx4 v[62:65], v31, s[44:47], s20 offen sc1
	buffer_load_dwordx4 v[68:71], v31, s[44:47], s21 offen sc1
	buffer_load_dwordx4 v[74:77], v31, s[44:47], s23 offen sc1
	buffer_load_dwordx2 v[60:61], v30, s[44:47], 0 offen sc1
	buffer_load_dwordx2 v[72:73], v30, s[44:47], s33 offen sc1
	buffer_load_dwordx2 v[66:67], v30, s[44:47], s21 offen sc1
	buffer_load_dwordx2 v[78:79], v30, s[44:47], s94 offen sc1
	s_waitcnt vmcnt(27)
	v_mfma_f32_16x16x128_f8f6f4 v[86:89], v[86:91], v[18:23], 0 cbsz:2 blgp:2
	s_waitcnt vmcnt(26)
	v_mfma_f32_16x16x128_f8f6f4 v[86:89], v[98:103], v[12:17], v[86:89] cbsz:2 blgp:2
	s_waitcnt vmcnt(25)
	v_mfma_f32_16x16x128_f8f6f4 v[86:89], v[92:97], v[6:11], v[86:89] cbsz:2 blgp:2
	s_waitcnt vmcnt(24)
	v_mfma_f32_16x16x128_f8f6f4 v[86:89], v[150:155], v[0:5], v[86:89] cbsz:2 blgp:2
	s_nop 7
	v_cndmask_b32_e64 v30, v86, v87, s[4:5]
	v_cndmask_b32_e64 v30, v30, v88, s[2:3]
	v_cndmask_b32_e32 v30, v30, v89, vcc
	v_mul_f32_e32 v31, v33, v30
	s_nop 1
	v_mov_b32_dpp v31, v31 quad_perm:[1,0,3,2] row_mask:0xf bank_mask:0xf bound_ctrl:1
	v_fmac_f32_e32 v31, v33, v30
	s_nop 1
	v_add_f32_dpp v30, v31, v31 quad_perm:[2,3,0,1] row_mask:0xf bank_mask:0xf bound_ctrl:1
	s_nop 1
	v_add_f32_dpp v30, v30, v30 row_half_mirror row_mask:0xf bank_mask:0xf bound_ctrl:1
	ds_write_b32 v32, v30 offset:49176
	ds_bpermute_b32 v30, v36, v130 offset:160
	s_waitcnt lgkmcnt(0)
	v_mul_lo_u32 v30, v30, s43
	v_add_u32_e32 v31, v30, v35
	v_add_u32_e32 v30, v30, v34
	buffer_load_dwordx4 v[86:89], v31, s[44:47], 0 offen sc1
	buffer_load_dwordx4 v[92:95], v31, s[44:47], s20 offen sc1
	buffer_load_dwordx4 v[98:101], v31, s[44:47], s21 offen sc1
	buffer_load_dwordx4 v[150:153], v31, s[44:47], s23 offen sc1
	buffer_load_dwordx2 v[90:91], v30, s[44:47], 0 offen sc1
	buffer_load_dwordx2 v[102:103], v30, s[44:47], s33 offen sc1
	buffer_load_dwordx2 v[96:97], v30, s[44:47], s21 offen sc1
	buffer_load_dwordx2 v[154:155], v30, s[44:47], s94 offen sc1
	s_waitcnt vmcnt(27)
	v_mfma_f32_16x16x128_f8f6f4 v[156:159], v[156:161], v[18:23], 0 cbsz:2 blgp:2
	s_waitcnt vmcnt(26)
	v_mfma_f32_16x16x128_f8f6f4 v[156:159], v[168:173], v[12:17], v[156:159] cbsz:2 blgp:2
	s_waitcnt vmcnt(25)
	v_mfma_f32_16x16x128_f8f6f4 v[156:159], v[162:167], v[6:11], v[156:159] cbsz:2 blgp:2
	s_waitcnt vmcnt(24)
	v_mfma_f32_16x16x128_f8f6f4 v[156:159], v[174:179], v[0:5], v[156:159] cbsz:2 blgp:2
	s_nop 7
	v_cndmask_b32_e64 v30, v156, v157, s[4:5]
	v_cndmask_b32_e64 v30, v30, v158, s[2:3]
	v_cndmask_b32_e32 v30, v30, v159, vcc
	v_mul_f32_e32 v31, v33, v30
	s_nop 1
	v_mov_b32_dpp v31, v31 quad_perm:[1,0,3,2] row_mask:0xf bank_mask:0xf bound_ctrl:1
	v_fmac_f32_e32 v31, v33, v30
	s_nop 1
	v_add_f32_dpp v30, v31, v31 quad_perm:[2,3,0,1] row_mask:0xf bank_mask:0xf bound_ctrl:1
	s_nop 1
	v_add_f32_dpp v30, v30, v30 row_half_mirror row_mask:0xf bank_mask:0xf bound_ctrl:1
	ds_write_b32 v32, v30 offset:49180
	ds_bpermute_b32 v30, v36, v130 offset:176
	s_waitcnt lgkmcnt(0)
	v_mul_lo_u32 v30, v30, s43
	v_add_u32_e32 v31, v30, v35
	v_add_u32_e32 v30, v30, v34
	buffer_load_dwordx4 v[156:159], v31, s[44:47], 0 offen sc1
	buffer_load_dwordx4 v[162:165], v31, s[44:47], s20 offen sc1
	buffer_load_dwordx4 v[168:171], v31, s[44:47], s21 offen sc1
	buffer_load_dwordx4 v[174:177], v31, s[44:47], s23 offen sc1
	buffer_load_dwordx2 v[160:161], v30, s[44:47], 0 offen sc1
	buffer_load_dwordx2 v[172:173], v30, s[44:47], s33 offen sc1
	buffer_load_dwordx2 v[166:167], v30, s[44:47], s21 offen sc1
	buffer_load_dwordx2 v[178:179], v30, s[44:47], s94 offen sc1
	s_waitcnt vmcnt(27)
	v_mfma_f32_16x16x128_f8f6f4 v[24:27], v[24:29], v[18:23], 0 cbsz:2 blgp:2
	s_waitcnt vmcnt(26)
	v_mfma_f32_16x16x128_f8f6f4 v[24:27], v[44:49], v[12:17], v[24:27] cbsz:2 blgp:2
	s_waitcnt vmcnt(25)
	v_mfma_f32_16x16x128_f8f6f4 v[24:27], v[38:43], v[6:11], v[24:27] cbsz:2 blgp:2
	s_waitcnt vmcnt(24)
	v_mfma_f32_16x16x128_f8f6f4 v[24:27], v[50:55], v[0:5], v[24:27] cbsz:2 blgp:2
	s_nop 7
	v_cndmask_b32_e64 v24, v24, v25, s[4:5]
	v_cndmask_b32_e64 v24, v24, v26, s[2:3]
	v_cndmask_b32_e32 v24, v24, v27, vcc
	v_mul_f32_e32 v25, v33, v24
	s_nop 1
	v_mov_b32_dpp v25, v25 quad_perm:[1,0,3,2] row_mask:0xf bank_mask:0xf bound_ctrl:1
	v_fmac_f32_e32 v25, v33, v24
	s_nop 1
	v_add_f32_dpp v24, v25, v25 quad_perm:[2,3,0,1] row_mask:0xf bank_mask:0xf bound_ctrl:1
	s_nop 1
	v_add_f32_dpp v24, v24, v24 row_half_mirror row_mask:0xf bank_mask:0xf bound_ctrl:1
	ds_write_b32 v32, v24 offset:49184
	ds_bpermute_b32 v24, v36, v130 offset:192
	s_waitcnt lgkmcnt(0)
	v_mul_lo_u32 v24, v24, s43
	v_add_u32_e32 v28, v24, v35
	v_add_u32_e32 v30, v24, v34
	buffer_load_dwordx4 v[24:27], v28, s[44:47], 0 offen sc1
	buffer_load_dwordx4 v[38:41], v28, s[44:47], s20 offen sc1
	buffer_load_dwordx4 v[44:47], v28, s[44:47], s21 offen sc1
	buffer_load_dwordx4 v[50:53], v28, s[44:47], s23 offen sc1
	s_nop 0
	buffer_load_dwordx2 v[28:29], v30, s[44:47], 0 offen sc1
	buffer_load_dwordx2 v[48:49], v30, s[44:47], s33 offen sc1
	buffer_load_dwordx2 v[42:43], v30, s[44:47], s21 offen sc1
	buffer_load_dwordx2 v[54:55], v30, s[44:47], s94 offen sc1
	s_waitcnt vmcnt(27)
	v_mfma_f32_16x16x128_f8f6f4 v[56:59], v[56:61], v[18:23], 0 cbsz:2 blgp:2
	s_waitcnt vmcnt(26)
	v_mfma_f32_16x16x128_f8f6f4 v[56:59], v[68:73], v[12:17], v[56:59] cbsz:2 blgp:2
	s_waitcnt vmcnt(25)
	v_mfma_f32_16x16x128_f8f6f4 v[56:59], v[62:67], v[6:11], v[56:59] cbsz:2 blgp:2
	s_waitcnt vmcnt(24)
	v_mfma_f32_16x16x128_f8f6f4 v[56:59], v[74:79], v[0:5], v[56:59] cbsz:2 blgp:2
	s_nop 7
	v_cndmask_b32_e64 v30, v56, v57, s[4:5]
	v_cndmask_b32_e64 v30, v30, v58, s[2:3]
	v_cndmask_b32_e32 v30, v30, v59, vcc
	v_mul_f32_e32 v31, v33, v30
	s_nop 1
	v_mov_b32_dpp v31, v31 quad_perm:[1,0,3,2] row_mask:0xf bank_mask:0xf bound_ctrl:1
	v_fmac_f32_e32 v31, v33, v30
	s_nop 1
	v_add_f32_dpp v30, v31, v31 quad_perm:[2,3,0,1] row_mask:0xf bank_mask:0xf bound_ctrl:1
	s_nop 1
	v_add_f32_dpp v30, v30, v30 row_half_mirror row_mask:0xf bank_mask:0xf bound_ctrl:1
	ds_write_b32 v32, v30 offset:49188
	ds_bpermute_b32 v30, v36, v130 offset:208
	s_waitcnt lgkmcnt(0)
	v_mul_lo_u32 v30, v30, s43
	v_add_u32_e32 v31, v30, v35
	v_add_u32_e32 v30, v30, v34
	buffer_load_dwordx4 v[56:59], v31, s[44:47], 0 offen sc1
	buffer_load_dwordx4 v[62:65], v31, s[44:47], s20 offen sc1
	buffer_load_dwordx4 v[68:71], v31, s[44:47], s21 offen sc1
	buffer_load_dwordx4 v[74:77], v31, s[44:47], s23 offen sc1
	buffer_load_dwordx2 v[60:61], v30, s[44:47], 0 offen sc1
	buffer_load_dwordx2 v[72:73], v30, s[44:47], s33 offen sc1
	buffer_load_dwordx2 v[66:67], v30, s[44:47], s21 offen sc1
	buffer_load_dwordx2 v[78:79], v30, s[44:47], s94 offen sc1
	s_waitcnt vmcnt(27)
	v_mfma_f32_16x16x128_f8f6f4 v[86:89], v[86:91], v[18:23], 0 cbsz:2 blgp:2
	s_waitcnt vmcnt(26)
	v_mfma_f32_16x16x128_f8f6f4 v[86:89], v[98:103], v[12:17], v[86:89] cbsz:2 blgp:2
	s_waitcnt vmcnt(25)
	v_mfma_f32_16x16x128_f8f6f4 v[86:89], v[92:97], v[6:11], v[86:89] cbsz:2 blgp:2
	s_waitcnt vmcnt(24)
	v_mfma_f32_16x16x128_f8f6f4 v[86:89], v[150:155], v[0:5], v[86:89] cbsz:2 blgp:2
	s_nop 7
	v_cndmask_b32_e64 v30, v86, v87, s[4:5]
	v_cndmask_b32_e64 v30, v30, v88, s[2:3]
	v_cndmask_b32_e32 v30, v30, v89, vcc
	v_mul_f32_e32 v31, v33, v30
	s_nop 1
	v_mov_b32_dpp v31, v31 quad_perm:[1,0,3,2] row_mask:0xf bank_mask:0xf bound_ctrl:1
	v_fmac_f32_e32 v31, v33, v30
	s_nop 1
	v_add_f32_dpp v30, v31, v31 quad_perm:[2,3,0,1] row_mask:0xf bank_mask:0xf bound_ctrl:1
	s_nop 1
	v_add_f32_dpp v30, v30, v30 row_half_mirror row_mask:0xf bank_mask:0xf bound_ctrl:1
	ds_write_b32 v32, v30 offset:49192
	ds_bpermute_b32 v30, v36, v130 offset:224
	s_waitcnt lgkmcnt(0)
	v_mul_lo_u32 v30, v30, s43
	v_add_u32_e32 v31, v30, v35
	v_add_u32_e32 v30, v30, v34
	buffer_load_dwordx4 v[86:89], v31, s[44:47], 0 offen sc1
	buffer_load_dwordx4 v[92:95], v31, s[44:47], s20 offen sc1
	buffer_load_dwordx4 v[98:101], v31, s[44:47], s21 offen sc1
	buffer_load_dwordx4 v[150:153], v31, s[44:47], s23 offen sc1
	buffer_load_dwordx2 v[90:91], v30, s[44:47], 0 offen sc1
	buffer_load_dwordx2 v[102:103], v30, s[44:47], s33 offen sc1
	buffer_load_dwordx2 v[96:97], v30, s[44:47], s21 offen sc1
	buffer_load_dwordx2 v[154:155], v30, s[44:47], s94 offen sc1
	s_waitcnt vmcnt(27)
	v_mfma_f32_16x16x128_f8f6f4 v[156:159], v[156:161], v[18:23], 0 cbsz:2 blgp:2
	s_waitcnt vmcnt(26)
	v_mfma_f32_16x16x128_f8f6f4 v[156:159], v[168:173], v[12:17], v[156:159] cbsz:2 blgp:2
	s_waitcnt vmcnt(25)
	v_mfma_f32_16x16x128_f8f6f4 v[156:159], v[162:167], v[6:11], v[156:159] cbsz:2 blgp:2
	s_waitcnt vmcnt(24)
	v_mfma_f32_16x16x128_f8f6f4 v[156:159], v[174:179], v[0:5], v[156:159] cbsz:2 blgp:2
	s_nop 7
	v_cndmask_b32_e64 v30, v156, v157, s[4:5]
	v_cndmask_b32_e64 v30, v30, v158, s[2:3]
	v_cndmask_b32_e32 v30, v30, v159, vcc
	v_mul_f32_e32 v31, v33, v30
	s_nop 1
	v_mov_b32_dpp v31, v31 quad_perm:[1,0,3,2] row_mask:0xf bank_mask:0xf bound_ctrl:1
	v_fmac_f32_e32 v31, v33, v30
	s_nop 1
	v_add_f32_dpp v30, v31, v31 quad_perm:[2,3,0,1] row_mask:0xf bank_mask:0xf bound_ctrl:1
	s_nop 1
	v_add_f32_dpp v30, v30, v30 row_half_mirror row_mask:0xf bank_mask:0xf bound_ctrl:1
	ds_write_b32 v32, v30 offset:49196
	ds_bpermute_b32 v30, v36, v130 offset:240
	s_waitcnt lgkmcnt(0)
	v_mul_lo_u32 v30, v30, s43
	v_add_u32_e32 v31, v30, v35
	v_add_u32_e32 v30, v30, v34
	buffer_load_dwordx4 v[156:159], v31, s[44:47], 0 offen sc1
	buffer_load_dwordx4 v[162:165], v31, s[44:47], s20 offen sc1
	buffer_load_dwordx4 v[168:171], v31, s[44:47], s21 offen sc1
	buffer_load_dwordx4 v[174:177], v31, s[44:47], s23 offen sc1
	buffer_load_dwordx2 v[160:161], v30, s[44:47], 0 offen sc1
	buffer_load_dwordx2 v[172:173], v30, s[44:47], s33 offen sc1
	buffer_load_dwordx2 v[166:167], v30, s[44:47], s21 offen sc1
	buffer_load_dwordx2 v[178:179], v30, s[44:47], s94 offen sc1
	s_waitcnt vmcnt(27)
	v_mfma_f32_16x16x128_f8f6f4 v[24:27], v[24:29], v[18:23], 0 cbsz:2 blgp:2
	s_waitcnt vmcnt(26)
	v_mfma_f32_16x16x128_f8f6f4 v[24:27], v[44:49], v[12:17], v[24:27] cbsz:2 blgp:2
	s_waitcnt vmcnt(25)
	v_mfma_f32_16x16x128_f8f6f4 v[24:27], v[38:43], v[6:11], v[24:27] cbsz:2 blgp:2
	s_waitcnt vmcnt(24)
	v_mfma_f32_16x16x128_f8f6f4 v[24:27], v[50:55], v[0:5], v[24:27] cbsz:2 blgp:2
	s_nop 7
	v_cndmask_b32_e64 v24, v24, v25, s[4:5]
	v_cndmask_b32_e64 v24, v24, v26, s[2:3]
	v_cndmask_b32_e32 v24, v24, v27, vcc
	v_mul_f32_e32 v25, v33, v24
	s_nop 1
	v_mov_b32_dpp v25, v25 quad_perm:[1,0,3,2] row_mask:0xf bank_mask:0xf bound_ctrl:1
	v_fmac_f32_e32 v25, v33, v24
	s_nop 1
	v_add_f32_dpp v24, v25, v25 quad_perm:[2,3,0,1] row_mask:0xf bank_mask:0xf bound_ctrl:1
	s_nop 1
	v_add_f32_dpp v24, v24, v24 row_half_mirror row_mask:0xf bank_mask:0xf bound_ctrl:1
	ds_write_b32 v32, v24 offset:49200
	ds_bpermute_b32 v24, v36, v128
	s_waitcnt lgkmcnt(0)
	v_mul_lo_u32 v24, v24, s43
	v_add_u32_e32 v28, v24, v35
	v_add_u32_e32 v30, v24, v34
	buffer_load_dwordx4 v[24:27], v28, s[44:47], 0 offen sc1
	buffer_load_dwordx4 v[38:41], v28, s[44:47], s20 offen sc1
	buffer_load_dwordx4 v[44:47], v28, s[44:47], s21 offen sc1
	buffer_load_dwordx4 v[50:53], v28, s[44:47], s23 offen sc1
	s_nop 0
	buffer_load_dwordx2 v[28:29], v30, s[44:47], 0 offen sc1
	buffer_load_dwordx2 v[48:49], v30, s[44:47], s33 offen sc1
	buffer_load_dwordx2 v[42:43], v30, s[44:47], s21 offen sc1
	buffer_load_dwordx2 v[54:55], v30, s[44:47], s94 offen sc1
	s_waitcnt vmcnt(27)
	v_mfma_f32_16x16x128_f8f6f4 v[56:59], v[56:61], v[18:23], 0 cbsz:2 blgp:2
	s_waitcnt vmcnt(26)
	v_mfma_f32_16x16x128_f8f6f4 v[56:59], v[68:73], v[12:17], v[56:59] cbsz:2 blgp:2
	s_waitcnt vmcnt(25)
	v_mfma_f32_16x16x128_f8f6f4 v[56:59], v[62:67], v[6:11], v[56:59] cbsz:2 blgp:2
	s_waitcnt vmcnt(24)
	v_mfma_f32_16x16x128_f8f6f4 v[56:59], v[74:79], v[0:5], v[56:59] cbsz:2 blgp:2
	s_nop 7
	v_cndmask_b32_e64 v30, v56, v57, s[4:5]
	v_cndmask_b32_e64 v30, v30, v58, s[2:3]
	v_cndmask_b32_e32 v30, v30, v59, vcc
	v_mul_f32_e32 v31, v33, v30
	s_nop 1
	v_mov_b32_dpp v31, v31 quad_perm:[1,0,3,2] row_mask:0xf bank_mask:0xf bound_ctrl:1
	v_fmac_f32_e32 v31, v33, v30
	s_nop 1
	v_add_f32_dpp v30, v31, v31 quad_perm:[2,3,0,1] row_mask:0xf bank_mask:0xf bound_ctrl:1
	s_nop 1
	v_add_f32_dpp v30, v30, v30 row_half_mirror row_mask:0xf bank_mask:0xf bound_ctrl:1
	ds_write_b32 v32, v30 offset:49204
	ds_bpermute_b32 v30, v36, v128 offset:16
	s_waitcnt lgkmcnt(0)
	v_mul_lo_u32 v30, v30, s43
	v_add_u32_e32 v31, v30, v35
	v_add_u32_e32 v30, v30, v34
	buffer_load_dwordx4 v[56:59], v31, s[44:47], 0 offen sc1
	buffer_load_dwordx4 v[62:65], v31, s[44:47], s20 offen sc1
	buffer_load_dwordx4 v[68:71], v31, s[44:47], s21 offen sc1
	buffer_load_dwordx4 v[74:77], v31, s[44:47], s23 offen sc1
	buffer_load_dwordx2 v[60:61], v30, s[44:47], 0 offen sc1
	buffer_load_dwordx2 v[72:73], v30, s[44:47], s33 offen sc1
	buffer_load_dwordx2 v[66:67], v30, s[44:47], s21 offen sc1
	buffer_load_dwordx2 v[78:79], v30, s[44:47], s94 offen sc1
	s_waitcnt vmcnt(27)
	v_mfma_f32_16x16x128_f8f6f4 v[86:89], v[86:91], v[18:23], 0 cbsz:2 blgp:2
	s_waitcnt vmcnt(26)
	v_mfma_f32_16x16x128_f8f6f4 v[86:89], v[98:103], v[12:17], v[86:89] cbsz:2 blgp:2
	s_waitcnt vmcnt(25)
	v_mfma_f32_16x16x128_f8f6f4 v[86:89], v[92:97], v[6:11], v[86:89] cbsz:2 blgp:2
	s_waitcnt vmcnt(24)
	v_mfma_f32_16x16x128_f8f6f4 v[86:89], v[150:155], v[0:5], v[86:89] cbsz:2 blgp:2
	s_nop 7
	v_cndmask_b32_e64 v30, v86, v87, s[4:5]
	v_cndmask_b32_e64 v30, v30, v88, s[2:3]
	v_cndmask_b32_e32 v30, v30, v89, vcc
	v_mul_f32_e32 v31, v33, v30
	s_nop 1
	v_mov_b32_dpp v31, v31 quad_perm:[1,0,3,2] row_mask:0xf bank_mask:0xf bound_ctrl:1
	v_fmac_f32_e32 v31, v33, v30
	s_nop 1
	v_add_f32_dpp v30, v31, v31 quad_perm:[2,3,0,1] row_mask:0xf bank_mask:0xf bound_ctrl:1
	s_nop 1
	v_add_f32_dpp v30, v30, v30 row_half_mirror row_mask:0xf bank_mask:0xf bound_ctrl:1
	ds_write_b32 v32, v30 offset:49208
	ds_bpermute_b32 v30, v36, v128 offset:32
	s_waitcnt lgkmcnt(0)
	v_mul_lo_u32 v30, v30, s43
	v_add_u32_e32 v31, v30, v35
	v_add_u32_e32 v30, v30, v34
	buffer_load_dwordx4 v[86:89], v31, s[44:47], 0 offen sc1
	buffer_load_dwordx4 v[92:95], v31, s[44:47], s20 offen sc1
	buffer_load_dwordx4 v[98:101], v31, s[44:47], s21 offen sc1
	buffer_load_dwordx4 v[150:153], v31, s[44:47], s23 offen sc1
	buffer_load_dwordx2 v[90:91], v30, s[44:47], 0 offen sc1
	buffer_load_dwordx2 v[102:103], v30, s[44:47], s33 offen sc1
	buffer_load_dwordx2 v[96:97], v30, s[44:47], s21 offen sc1
	buffer_load_dwordx2 v[154:155], v30, s[44:47], s94 offen sc1
	s_waitcnt vmcnt(27)
	v_mfma_f32_16x16x128_f8f6f4 v[156:159], v[156:161], v[18:23], 0 cbsz:2 blgp:2
	s_waitcnt vmcnt(26)
	v_mfma_f32_16x16x128_f8f6f4 v[156:159], v[168:173], v[12:17], v[156:159] cbsz:2 blgp:2
	s_waitcnt vmcnt(25)
	v_mfma_f32_16x16x128_f8f6f4 v[156:159], v[162:167], v[6:11], v[156:159] cbsz:2 blgp:2
	s_waitcnt vmcnt(24)
	v_mfma_f32_16x16x128_f8f6f4 v[156:159], v[174:179], v[0:5], v[156:159] cbsz:2 blgp:2
	s_nop 7
	v_cndmask_b32_e64 v30, v156, v157, s[4:5]
	v_cndmask_b32_e64 v30, v30, v158, s[2:3]
	v_cndmask_b32_e32 v30, v30, v159, vcc
	v_mul_f32_e32 v31, v33, v30
	s_nop 1
	v_mov_b32_dpp v31, v31 quad_perm:[1,0,3,2] row_mask:0xf bank_mask:0xf bound_ctrl:1
	v_fmac_f32_e32 v31, v33, v30
	s_nop 1
	v_add_f32_dpp v30, v31, v31 quad_perm:[2,3,0,1] row_mask:0xf bank_mask:0xf bound_ctrl:1
	s_nop 1
	v_add_f32_dpp v30, v30, v30 row_half_mirror row_mask:0xf bank_mask:0xf bound_ctrl:1
	ds_write_b32 v32, v30 offset:49212
	ds_bpermute_b32 v30, v36, v128 offset:48
	s_waitcnt lgkmcnt(0)
	v_mul_lo_u32 v30, v30, s43
	v_add_u32_e32 v31, v30, v35
	v_add_u32_e32 v30, v30, v34
	buffer_load_dwordx4 v[156:159], v31, s[44:47], 0 offen sc1
	buffer_load_dwordx4 v[162:165], v31, s[44:47], s20 offen sc1
	buffer_load_dwordx4 v[168:171], v31, s[44:47], s21 offen sc1
	buffer_load_dwordx4 v[174:177], v31, s[44:47], s23 offen sc1
	buffer_load_dwordx2 v[160:161], v30, s[44:47], 0 offen sc1
	buffer_load_dwordx2 v[172:173], v30, s[44:47], s33 offen sc1
	buffer_load_dwordx2 v[166:167], v30, s[44:47], s21 offen sc1
	buffer_load_dwordx2 v[178:179], v30, s[44:47], s94 offen sc1
	s_waitcnt vmcnt(27)
	v_mfma_f32_16x16x128_f8f6f4 v[24:27], v[24:29], v[18:23], 0 cbsz:2 blgp:2
	s_waitcnt vmcnt(26)
	v_mfma_f32_16x16x128_f8f6f4 v[24:27], v[44:49], v[12:17], v[24:27] cbsz:2 blgp:2
	s_waitcnt vmcnt(25)
	v_mfma_f32_16x16x128_f8f6f4 v[24:27], v[38:43], v[6:11], v[24:27] cbsz:2 blgp:2
	s_waitcnt vmcnt(24)
	v_mfma_f32_16x16x128_f8f6f4 v[24:27], v[50:55], v[0:5], v[24:27] cbsz:2 blgp:2
	s_nop 7
	v_cndmask_b32_e64 v24, v24, v25, s[4:5]
	v_cndmask_b32_e64 v24, v24, v26, s[2:3]
	v_cndmask_b32_e32 v24, v24, v27, vcc
	v_mul_f32_e32 v25, v33, v24
	s_nop 1
	v_mov_b32_dpp v25, v25 quad_perm:[1,0,3,2] row_mask:0xf bank_mask:0xf bound_ctrl:1
	v_fmac_f32_e32 v25, v33, v24
	s_nop 1
	v_add_f32_dpp v24, v25, v25 quad_perm:[2,3,0,1] row_mask:0xf bank_mask:0xf bound_ctrl:1
	s_nop 1
	v_add_f32_dpp v24, v24, v24 row_half_mirror row_mask:0xf bank_mask:0xf bound_ctrl:1
	ds_write_b32 v32, v24 offset:49216
	ds_bpermute_b32 v24, v36, v128 offset:64
	s_waitcnt lgkmcnt(0)
	v_mul_lo_u32 v24, v24, s43
	v_add_u32_e32 v28, v24, v35
	v_add_u32_e32 v30, v24, v34
	buffer_load_dwordx4 v[24:27], v28, s[44:47], 0 offen sc1
	buffer_load_dwordx4 v[38:41], v28, s[44:47], s20 offen sc1
	buffer_load_dwordx4 v[44:47], v28, s[44:47], s21 offen sc1
	buffer_load_dwordx4 v[50:53], v28, s[44:47], s23 offen sc1
	s_nop 0
	buffer_load_dwordx2 v[28:29], v30, s[44:47], 0 offen sc1
	buffer_load_dwordx2 v[48:49], v30, s[44:47], s33 offen sc1
	buffer_load_dwordx2 v[42:43], v30, s[44:47], s21 offen sc1
	buffer_load_dwordx2 v[54:55], v30, s[44:47], s94 offen sc1
	s_waitcnt vmcnt(27)
	v_mfma_f32_16x16x128_f8f6f4 v[56:59], v[56:61], v[18:23], 0 cbsz:2 blgp:2
	s_waitcnt vmcnt(26)
	v_mfma_f32_16x16x128_f8f6f4 v[56:59], v[68:73], v[12:17], v[56:59] cbsz:2 blgp:2
	s_waitcnt vmcnt(25)
	v_mfma_f32_16x16x128_f8f6f4 v[56:59], v[62:67], v[6:11], v[56:59] cbsz:2 blgp:2
	s_waitcnt vmcnt(24)
	v_mfma_f32_16x16x128_f8f6f4 v[56:59], v[74:79], v[0:5], v[56:59] cbsz:2 blgp:2
	s_nop 7
	v_cndmask_b32_e64 v30, v56, v57, s[4:5]
	v_cndmask_b32_e64 v30, v30, v58, s[2:3]
	v_cndmask_b32_e32 v30, v30, v59, vcc
	v_mul_f32_e32 v31, v33, v30
	s_nop 1
	v_mov_b32_dpp v31, v31 quad_perm:[1,0,3,2] row_mask:0xf bank_mask:0xf bound_ctrl:1
	v_fmac_f32_e32 v31, v33, v30
	s_nop 1
	v_add_f32_dpp v30, v31, v31 quad_perm:[2,3,0,1] row_mask:0xf bank_mask:0xf bound_ctrl:1
	s_nop 1
	v_add_f32_dpp v30, v30, v30 row_half_mirror row_mask:0xf bank_mask:0xf bound_ctrl:1
	ds_write_b32 v32, v30 offset:49220
	ds_bpermute_b32 v30, v36, v128 offset:80
	s_waitcnt lgkmcnt(0)
	v_mul_lo_u32 v30, v30, s43
	v_add_u32_e32 v31, v30, v35
	v_add_u32_e32 v30, v30, v34
	buffer_load_dwordx4 v[56:59], v31, s[44:47], 0 offen sc1
	buffer_load_dwordx4 v[62:65], v31, s[44:47], s20 offen sc1
	buffer_load_dwordx4 v[68:71], v31, s[44:47], s21 offen sc1
	buffer_load_dwordx4 v[74:77], v31, s[44:47], s23 offen sc1
	buffer_load_dwordx2 v[60:61], v30, s[44:47], 0 offen sc1
	buffer_load_dwordx2 v[72:73], v30, s[44:47], s33 offen sc1
	buffer_load_dwordx2 v[66:67], v30, s[44:47], s21 offen sc1
	buffer_load_dwordx2 v[78:79], v30, s[44:47], s94 offen sc1
	s_waitcnt vmcnt(27)
	v_mfma_f32_16x16x128_f8f6f4 v[86:89], v[86:91], v[18:23], 0 cbsz:2 blgp:2
	s_waitcnt vmcnt(26)
	v_mfma_f32_16x16x128_f8f6f4 v[86:89], v[98:103], v[12:17], v[86:89] cbsz:2 blgp:2
	s_waitcnt vmcnt(25)
	v_mfma_f32_16x16x128_f8f6f4 v[86:89], v[92:97], v[6:11], v[86:89] cbsz:2 blgp:2
	s_waitcnt vmcnt(24)
	v_mfma_f32_16x16x128_f8f6f4 v[86:89], v[150:155], v[0:5], v[86:89] cbsz:2 blgp:2
	s_nop 7
	v_cndmask_b32_e64 v30, v86, v87, s[4:5]
	v_cndmask_b32_e64 v30, v30, v88, s[2:3]
	v_cndmask_b32_e32 v30, v30, v89, vcc
	v_mul_f32_e32 v31, v33, v30
	s_nop 1
	v_mov_b32_dpp v31, v31 quad_perm:[1,0,3,2] row_mask:0xf bank_mask:0xf bound_ctrl:1
	v_fmac_f32_e32 v31, v33, v30
	s_nop 1
	v_add_f32_dpp v30, v31, v31 quad_perm:[2,3,0,1] row_mask:0xf bank_mask:0xf bound_ctrl:1
	s_nop 1
	v_add_f32_dpp v30, v30, v30 row_half_mirror row_mask:0xf bank_mask:0xf bound_ctrl:1
	ds_write_b32 v32, v30 offset:49224
	ds_bpermute_b32 v30, v36, v128 offset:96
	s_waitcnt lgkmcnt(0)
	v_mul_lo_u32 v30, v30, s43
	v_add_u32_e32 v31, v30, v35
	v_add_u32_e32 v30, v30, v34
	buffer_load_dwordx4 v[86:89], v31, s[44:47], 0 offen sc1
	buffer_load_dwordx4 v[92:95], v31, s[44:47], s20 offen sc1
	buffer_load_dwordx4 v[98:101], v31, s[44:47], s21 offen sc1
	buffer_load_dwordx4 v[150:153], v31, s[44:47], s23 offen sc1
	buffer_load_dwordx2 v[90:91], v30, s[44:47], 0 offen sc1
	buffer_load_dwordx2 v[102:103], v30, s[44:47], s33 offen sc1
	buffer_load_dwordx2 v[96:97], v30, s[44:47], s21 offen sc1
	buffer_load_dwordx2 v[154:155], v30, s[44:47], s94 offen sc1
	s_waitcnt vmcnt(27)
	v_mfma_f32_16x16x128_f8f6f4 v[156:159], v[156:161], v[18:23], 0 cbsz:2 blgp:2
	s_waitcnt vmcnt(26)
	v_mfma_f32_16x16x128_f8f6f4 v[156:159], v[168:173], v[12:17], v[156:159] cbsz:2 blgp:2
	s_waitcnt vmcnt(25)
	v_mfma_f32_16x16x128_f8f6f4 v[156:159], v[162:167], v[6:11], v[156:159] cbsz:2 blgp:2
	s_waitcnt vmcnt(24)
	v_mfma_f32_16x16x128_f8f6f4 v[156:159], v[174:179], v[0:5], v[156:159] cbsz:2 blgp:2
	s_nop 7
	v_cndmask_b32_e64 v30, v156, v157, s[4:5]
	v_cndmask_b32_e64 v30, v30, v158, s[2:3]
	v_cndmask_b32_e32 v30, v30, v159, vcc
	v_mul_f32_e32 v31, v33, v30
	s_nop 1
	v_mov_b32_dpp v31, v31 quad_perm:[1,0,3,2] row_mask:0xf bank_mask:0xf bound_ctrl:1
	v_fmac_f32_e32 v31, v33, v30
	s_nop 1
	v_add_f32_dpp v30, v31, v31 quad_perm:[2,3,0,1] row_mask:0xf bank_mask:0xf bound_ctrl:1
	s_nop 1
	v_add_f32_dpp v30, v30, v30 row_half_mirror row_mask:0xf bank_mask:0xf bound_ctrl:1
	ds_write_b32 v32, v30 offset:49228
	ds_bpermute_b32 v30, v36, v128 offset:112
	s_waitcnt lgkmcnt(0)
	v_mul_lo_u32 v30, v30, s43
	v_add_u32_e32 v31, v30, v35
	v_add_u32_e32 v30, v30, v34
	buffer_load_dwordx4 v[156:159], v31, s[44:47], 0 offen sc1
	buffer_load_dwordx4 v[162:165], v31, s[44:47], s20 offen sc1
	buffer_load_dwordx4 v[168:171], v31, s[44:47], s21 offen sc1
	buffer_load_dwordx4 v[174:177], v31, s[44:47], s23 offen sc1
	buffer_load_dwordx2 v[160:161], v30, s[44:47], 0 offen sc1
	buffer_load_dwordx2 v[172:173], v30, s[44:47], s33 offen sc1
	buffer_load_dwordx2 v[166:167], v30, s[44:47], s21 offen sc1
	buffer_load_dwordx2 v[178:179], v30, s[44:47], s94 offen sc1
	s_waitcnt vmcnt(27)
	v_mfma_f32_16x16x128_f8f6f4 v[24:27], v[24:29], v[18:23], 0 cbsz:2 blgp:2
	s_waitcnt vmcnt(26)
	v_mfma_f32_16x16x128_f8f6f4 v[24:27], v[44:49], v[12:17], v[24:27] cbsz:2 blgp:2
	s_waitcnt vmcnt(25)
	v_mfma_f32_16x16x128_f8f6f4 v[24:27], v[38:43], v[6:11], v[24:27] cbsz:2 blgp:2
	s_waitcnt vmcnt(24)
	v_mfma_f32_16x16x128_f8f6f4 v[24:27], v[50:55], v[0:5], v[24:27] cbsz:2 blgp:2
	s_nop 7
	v_cndmask_b32_e64 v24, v24, v25, s[4:5]
	v_cndmask_b32_e64 v24, v24, v26, s[2:3]
	v_cndmask_b32_e32 v24, v24, v27, vcc
	v_mul_f32_e32 v25, v33, v24
	s_nop 1
	v_mov_b32_dpp v25, v25 quad_perm:[1,0,3,2] row_mask:0xf bank_mask:0xf bound_ctrl:1
	v_fmac_f32_e32 v25, v33, v24
	s_nop 1
	v_add_f32_dpp v24, v25, v25 quad_perm:[2,3,0,1] row_mask:0xf bank_mask:0xf bound_ctrl:1
	s_nop 1
	v_add_f32_dpp v24, v24, v24 row_half_mirror row_mask:0xf bank_mask:0xf bound_ctrl:1
	ds_write_b32 v32, v24 offset:49232
	ds_bpermute_b32 v24, v36, v128 offset:128
	s_waitcnt lgkmcnt(0)
	v_mul_lo_u32 v24, v24, s43
	v_add_u32_e32 v28, v24, v35
	v_add_u32_e32 v30, v24, v34
	buffer_load_dwordx4 v[24:27], v28, s[44:47], 0 offen sc1
	buffer_load_dwordx4 v[38:41], v28, s[44:47], s20 offen sc1
	buffer_load_dwordx4 v[44:47], v28, s[44:47], s21 offen sc1
	buffer_load_dwordx4 v[50:53], v28, s[44:47], s23 offen sc1
	s_nop 0
	buffer_load_dwordx2 v[28:29], v30, s[44:47], 0 offen sc1
	buffer_load_dwordx2 v[48:49], v30, s[44:47], s33 offen sc1
	buffer_load_dwordx2 v[42:43], v30, s[44:47], s21 offen sc1
	buffer_load_dwordx2 v[54:55], v30, s[44:47], s94 offen sc1
	s_waitcnt vmcnt(27)
	v_mfma_f32_16x16x128_f8f6f4 v[56:59], v[56:61], v[18:23], 0 cbsz:2 blgp:2
	s_waitcnt vmcnt(26)
	v_mfma_f32_16x16x128_f8f6f4 v[56:59], v[68:73], v[12:17], v[56:59] cbsz:2 blgp:2
	s_waitcnt vmcnt(25)
	v_mfma_f32_16x16x128_f8f6f4 v[56:59], v[62:67], v[6:11], v[56:59] cbsz:2 blgp:2
	s_waitcnt vmcnt(24)
	v_mfma_f32_16x16x128_f8f6f4 v[56:59], v[74:79], v[0:5], v[56:59] cbsz:2 blgp:2
	s_nop 7
	v_cndmask_b32_e64 v30, v56, v57, s[4:5]
	v_cndmask_b32_e64 v30, v30, v58, s[2:3]
	v_cndmask_b32_e32 v30, v30, v59, vcc
	v_mul_f32_e32 v31, v33, v30
	s_nop 1
	v_mov_b32_dpp v31, v31 quad_perm:[1,0,3,2] row_mask:0xf bank_mask:0xf bound_ctrl:1
	v_fmac_f32_e32 v31, v33, v30
	s_nop 1
	v_add_f32_dpp v30, v31, v31 quad_perm:[2,3,0,1] row_mask:0xf bank_mask:0xf bound_ctrl:1
	s_nop 1
	v_add_f32_dpp v30, v30, v30 row_half_mirror row_mask:0xf bank_mask:0xf bound_ctrl:1
	ds_write_b32 v32, v30 offset:49236
	ds_bpermute_b32 v30, v36, v128 offset:144
	s_waitcnt lgkmcnt(0)
	v_mul_lo_u32 v30, v30, s43
	v_add_u32_e32 v31, v30, v35
	v_add_u32_e32 v30, v30, v34
	buffer_load_dwordx4 v[56:59], v31, s[44:47], 0 offen sc1
	buffer_load_dwordx4 v[62:65], v31, s[44:47], s20 offen sc1
	buffer_load_dwordx4 v[68:71], v31, s[44:47], s21 offen sc1
	buffer_load_dwordx4 v[74:77], v31, s[44:47], s23 offen sc1
	buffer_load_dwordx2 v[60:61], v30, s[44:47], 0 offen sc1
	buffer_load_dwordx2 v[72:73], v30, s[44:47], s33 offen sc1
	buffer_load_dwordx2 v[66:67], v30, s[44:47], s21 offen sc1
	buffer_load_dwordx2 v[78:79], v30, s[44:47], s94 offen sc1
	s_waitcnt vmcnt(27)
	v_mfma_f32_16x16x128_f8f6f4 v[86:89], v[86:91], v[18:23], 0 cbsz:2 blgp:2
	s_waitcnt vmcnt(26)
	v_mfma_f32_16x16x128_f8f6f4 v[86:89], v[98:103], v[12:17], v[86:89] cbsz:2 blgp:2
	s_waitcnt vmcnt(25)
	v_mfma_f32_16x16x128_f8f6f4 v[86:89], v[92:97], v[6:11], v[86:89] cbsz:2 blgp:2
	s_waitcnt vmcnt(24)
	v_mfma_f32_16x16x128_f8f6f4 v[86:89], v[150:155], v[0:5], v[86:89] cbsz:2 blgp:2
	s_nop 7
	v_cndmask_b32_e64 v30, v86, v87, s[4:5]
	v_cndmask_b32_e64 v30, v30, v88, s[2:3]
	v_cndmask_b32_e32 v30, v30, v89, vcc
	v_mul_f32_e32 v31, v33, v30
	s_nop 1
	v_mov_b32_dpp v31, v31 quad_perm:[1,0,3,2] row_mask:0xf bank_mask:0xf bound_ctrl:1
	v_fmac_f32_e32 v31, v33, v30
	s_nop 1
	v_add_f32_dpp v30, v31, v31 quad_perm:[2,3,0,1] row_mask:0xf bank_mask:0xf bound_ctrl:1
	s_nop 1
	v_add_f32_dpp v30, v30, v30 row_half_mirror row_mask:0xf bank_mask:0xf bound_ctrl:1
	ds_write_b32 v32, v30 offset:49240
	ds_bpermute_b32 v30, v36, v128 offset:160
	s_waitcnt lgkmcnt(0)
	v_mul_lo_u32 v30, v30, s43
	v_add_u32_e32 v31, v30, v35
	v_add_u32_e32 v30, v30, v34
	buffer_load_dwordx4 v[86:89], v31, s[44:47], 0 offen sc1
	buffer_load_dwordx4 v[92:95], v31, s[44:47], s20 offen sc1
	buffer_load_dwordx4 v[98:101], v31, s[44:47], s21 offen sc1
	buffer_load_dwordx4 v[150:153], v31, s[44:47], s23 offen sc1
	buffer_load_dwordx2 v[90:91], v30, s[44:47], 0 offen sc1
	buffer_load_dwordx2 v[102:103], v30, s[44:47], s33 offen sc1
	buffer_load_dwordx2 v[96:97], v30, s[44:47], s21 offen sc1
	buffer_load_dwordx2 v[154:155], v30, s[44:47], s94 offen sc1
	s_waitcnt vmcnt(27)
	v_mfma_f32_16x16x128_f8f6f4 v[156:159], v[156:161], v[18:23], 0 cbsz:2 blgp:2
	s_waitcnt vmcnt(26)
	v_mfma_f32_16x16x128_f8f6f4 v[156:159], v[168:173], v[12:17], v[156:159] cbsz:2 blgp:2
	s_waitcnt vmcnt(25)
	v_mfma_f32_16x16x128_f8f6f4 v[156:159], v[162:167], v[6:11], v[156:159] cbsz:2 blgp:2
	s_waitcnt vmcnt(24)
	v_mfma_f32_16x16x128_f8f6f4 v[156:159], v[174:179], v[0:5], v[156:159] cbsz:2 blgp:2
	s_nop 7
	v_cndmask_b32_e64 v30, v156, v157, s[4:5]
	v_cndmask_b32_e64 v30, v30, v158, s[2:3]
	v_cndmask_b32_e32 v30, v30, v159, vcc
	v_mul_f32_e32 v31, v33, v30
	s_nop 1
	v_mov_b32_dpp v31, v31 quad_perm:[1,0,3,2] row_mask:0xf bank_mask:0xf bound_ctrl:1
	v_fmac_f32_e32 v31, v33, v30
	s_nop 1
	v_add_f32_dpp v30, v31, v31 quad_perm:[2,3,0,1] row_mask:0xf bank_mask:0xf bound_ctrl:1
	s_nop 1
	v_add_f32_dpp v30, v30, v30 row_half_mirror row_mask:0xf bank_mask:0xf bound_ctrl:1
	ds_write_b32 v32, v30 offset:49244
	ds_bpermute_b32 v30, v36, v128 offset:176
	s_waitcnt lgkmcnt(0)
	v_mul_lo_u32 v30, v30, s43
	v_add_u32_e32 v31, v30, v35
	v_add_u32_e32 v30, v30, v34
	buffer_load_dwordx4 v[156:159], v31, s[44:47], 0 offen sc1
	buffer_load_dwordx4 v[162:165], v31, s[44:47], s20 offen sc1
	buffer_load_dwordx4 v[168:171], v31, s[44:47], s21 offen sc1
	buffer_load_dwordx4 v[174:177], v31, s[44:47], s23 offen sc1
	buffer_load_dwordx2 v[160:161], v30, s[44:47], 0 offen sc1
	buffer_load_dwordx2 v[172:173], v30, s[44:47], s33 offen sc1
	buffer_load_dwordx2 v[166:167], v30, s[44:47], s21 offen sc1
	buffer_load_dwordx2 v[178:179], v30, s[44:47], s94 offen sc1
	s_waitcnt vmcnt(27)
	v_mfma_f32_16x16x128_f8f6f4 v[24:27], v[24:29], v[18:23], 0 cbsz:2 blgp:2
	s_waitcnt vmcnt(26)
	v_mfma_f32_16x16x128_f8f6f4 v[24:27], v[44:49], v[12:17], v[24:27] cbsz:2 blgp:2
	s_waitcnt vmcnt(25)
	v_mfma_f32_16x16x128_f8f6f4 v[24:27], v[38:43], v[6:11], v[24:27] cbsz:2 blgp:2
	s_waitcnt vmcnt(24)
	v_mfma_f32_16x16x128_f8f6f4 v[24:27], v[50:55], v[0:5], v[24:27] cbsz:2 blgp:2
	s_nop 7
	v_cndmask_b32_e64 v24, v24, v25, s[4:5]
	v_cndmask_b32_e64 v24, v24, v26, s[2:3]
	v_cndmask_b32_e32 v24, v24, v27, vcc
	v_mul_f32_e32 v25, v33, v24
	s_nop 1
	v_mov_b32_dpp v25, v25 quad_perm:[1,0,3,2] row_mask:0xf bank_mask:0xf bound_ctrl:1
	v_fmac_f32_e32 v25, v33, v24
	s_nop 1
	v_add_f32_dpp v24, v25, v25 quad_perm:[2,3,0,1] row_mask:0xf bank_mask:0xf bound_ctrl:1
	s_nop 1
	v_add_f32_dpp v24, v24, v24 row_half_mirror row_mask:0xf bank_mask:0xf bound_ctrl:1
	ds_write_b32 v32, v24 offset:49248
	ds_bpermute_b32 v24, v36, v128 offset:192
	s_waitcnt lgkmcnt(0)
	v_mul_lo_u32 v24, v24, s43
	v_add_u32_e32 v28, v24, v35
	v_add_u32_e32 v30, v24, v34
	buffer_load_dwordx4 v[24:27], v28, s[44:47], 0 offen sc1
	buffer_load_dwordx4 v[38:41], v28, s[44:47], s20 offen sc1
	buffer_load_dwordx4 v[44:47], v28, s[44:47], s21 offen sc1
	buffer_load_dwordx4 v[50:53], v28, s[44:47], s23 offen sc1
	s_nop 0
	buffer_load_dwordx2 v[28:29], v30, s[44:47], 0 offen sc1
	buffer_load_dwordx2 v[48:49], v30, s[44:47], s33 offen sc1
	buffer_load_dwordx2 v[42:43], v30, s[44:47], s21 offen sc1
	buffer_load_dwordx2 v[54:55], v30, s[44:47], s94 offen sc1
	s_waitcnt vmcnt(27)
	v_mfma_f32_16x16x128_f8f6f4 v[56:59], v[56:61], v[18:23], 0 cbsz:2 blgp:2
	s_waitcnt vmcnt(26)
	v_mfma_f32_16x16x128_f8f6f4 v[56:59], v[68:73], v[12:17], v[56:59] cbsz:2 blgp:2
	s_waitcnt vmcnt(25)
	v_mfma_f32_16x16x128_f8f6f4 v[56:59], v[62:67], v[6:11], v[56:59] cbsz:2 blgp:2
	s_waitcnt vmcnt(24)
	v_mfma_f32_16x16x128_f8f6f4 v[56:59], v[74:79], v[0:5], v[56:59] cbsz:2 blgp:2
	s_nop 7
	v_cndmask_b32_e64 v30, v56, v57, s[4:5]
	v_cndmask_b32_e64 v30, v30, v58, s[2:3]
	v_cndmask_b32_e32 v30, v30, v59, vcc
	v_mul_f32_e32 v31, v33, v30
	s_nop 1
	v_mov_b32_dpp v31, v31 quad_perm:[1,0,3,2] row_mask:0xf bank_mask:0xf bound_ctrl:1
	v_fmac_f32_e32 v31, v33, v30
	s_nop 1
	v_add_f32_dpp v30, v31, v31 quad_perm:[2,3,0,1] row_mask:0xf bank_mask:0xf bound_ctrl:1
	s_nop 1
	v_add_f32_dpp v30, v30, v30 row_half_mirror row_mask:0xf bank_mask:0xf bound_ctrl:1
	ds_write_b32 v32, v30 offset:49252
	ds_bpermute_b32 v30, v36, v128 offset:208
	s_waitcnt lgkmcnt(0)
	v_mul_lo_u32 v30, v30, s43
	v_add_u32_e32 v31, v30, v35
	v_add_u32_e32 v30, v30, v34
	buffer_load_dwordx4 v[56:59], v31, s[44:47], 0 offen sc1
	buffer_load_dwordx4 v[62:65], v31, s[44:47], s20 offen sc1
	buffer_load_dwordx4 v[68:71], v31, s[44:47], s21 offen sc1
	buffer_load_dwordx4 v[74:77], v31, s[44:47], s23 offen sc1
	buffer_load_dwordx2 v[60:61], v30, s[44:47], 0 offen sc1
	buffer_load_dwordx2 v[72:73], v30, s[44:47], s33 offen sc1
	buffer_load_dwordx2 v[66:67], v30, s[44:47], s21 offen sc1
	buffer_load_dwordx2 v[78:79], v30, s[44:47], s94 offen sc1
	s_waitcnt vmcnt(27)
	v_mfma_f32_16x16x128_f8f6f4 v[86:89], v[86:91], v[18:23], 0 cbsz:2 blgp:2
	s_waitcnt vmcnt(26)
	v_mfma_f32_16x16x128_f8f6f4 v[86:89], v[98:103], v[12:17], v[86:89] cbsz:2 blgp:2
	s_waitcnt vmcnt(25)
	v_mfma_f32_16x16x128_f8f6f4 v[86:89], v[92:97], v[6:11], v[86:89] cbsz:2 blgp:2
	s_waitcnt vmcnt(24)
	v_mfma_f32_16x16x128_f8f6f4 v[86:89], v[150:155], v[0:5], v[86:89] cbsz:2 blgp:2
	s_nop 7
	v_cndmask_b32_e64 v30, v86, v87, s[4:5]
	v_cndmask_b32_e64 v30, v30, v88, s[2:3]
	v_cndmask_b32_e32 v30, v30, v89, vcc
	v_mul_f32_e32 v31, v33, v30
	s_nop 1
	v_mov_b32_dpp v31, v31 quad_perm:[1,0,3,2] row_mask:0xf bank_mask:0xf bound_ctrl:1
	v_fmac_f32_e32 v31, v33, v30
	s_nop 1
	v_add_f32_dpp v30, v31, v31 quad_perm:[2,3,0,1] row_mask:0xf bank_mask:0xf bound_ctrl:1
	s_nop 1
	v_add_f32_dpp v30, v30, v30 row_half_mirror row_mask:0xf bank_mask:0xf bound_ctrl:1
	ds_write_b32 v32, v30 offset:49256
	ds_bpermute_b32 v30, v36, v128 offset:224
	s_waitcnt lgkmcnt(0)
	v_mul_lo_u32 v30, v30, s43
	v_add_u32_e32 v31, v30, v35
	v_add_u32_e32 v30, v30, v34
	buffer_load_dwordx4 v[86:89], v31, s[44:47], 0 offen sc1
	buffer_load_dwordx4 v[92:95], v31, s[44:47], s20 offen sc1
	buffer_load_dwordx4 v[98:101], v31, s[44:47], s21 offen sc1
	buffer_load_dwordx4 v[150:153], v31, s[44:47], s23 offen sc1
	buffer_load_dwordx2 v[90:91], v30, s[44:47], 0 offen sc1
	buffer_load_dwordx2 v[102:103], v30, s[44:47], s33 offen sc1
	buffer_load_dwordx2 v[96:97], v30, s[44:47], s21 offen sc1
	buffer_load_dwordx2 v[154:155], v30, s[44:47], s94 offen sc1
	s_waitcnt vmcnt(27)
	v_mfma_f32_16x16x128_f8f6f4 v[156:159], v[156:161], v[18:23], 0 cbsz:2 blgp:2
	s_waitcnt vmcnt(26)
	v_mfma_f32_16x16x128_f8f6f4 v[156:159], v[168:173], v[12:17], v[156:159] cbsz:2 blgp:2
	s_waitcnt vmcnt(25)
	v_mfma_f32_16x16x128_f8f6f4 v[156:159], v[162:167], v[6:11], v[156:159] cbsz:2 blgp:2
	s_waitcnt vmcnt(24)
	v_mfma_f32_16x16x128_f8f6f4 v[156:159], v[174:179], v[0:5], v[156:159] cbsz:2 blgp:2
	s_nop 7
	v_cndmask_b32_e64 v30, v156, v157, s[4:5]
	v_cndmask_b32_e64 v30, v30, v158, s[2:3]
	v_cndmask_b32_e32 v30, v30, v159, vcc
	v_mul_f32_e32 v31, v33, v30
	s_nop 1
	v_mov_b32_dpp v31, v31 quad_perm:[1,0,3,2] row_mask:0xf bank_mask:0xf bound_ctrl:1
	v_fmac_f32_e32 v31, v33, v30
	s_nop 1
	v_add_f32_dpp v30, v31, v31 quad_perm:[2,3,0,1] row_mask:0xf bank_mask:0xf bound_ctrl:1
	s_nop 1
	v_add_f32_dpp v30, v30, v30 row_half_mirror row_mask:0xf bank_mask:0xf bound_ctrl:1
	ds_write_b32 v32, v30 offset:49260
	ds_bpermute_b32 v30, v36, v128 offset:240
	s_waitcnt lgkmcnt(0)
	v_mul_lo_u32 v30, v30, s43
	v_add_u32_e32 v31, v30, v35
	v_add_u32_e32 v30, v30, v34
	buffer_load_dwordx4 v[156:159], v31, s[44:47], 0 offen sc1
	buffer_load_dwordx4 v[162:165], v31, s[44:47], s20 offen sc1
	buffer_load_dwordx4 v[168:171], v31, s[44:47], s21 offen sc1
	buffer_load_dwordx4 v[174:177], v31, s[44:47], s23 offen sc1
	buffer_load_dwordx2 v[160:161], v30, s[44:47], 0 offen sc1
	buffer_load_dwordx2 v[172:173], v30, s[44:47], s33 offen sc1
	buffer_load_dwordx2 v[166:167], v30, s[44:47], s21 offen sc1
	buffer_load_dwordx2 v[178:179], v30, s[44:47], s94 offen sc1
	s_waitcnt vmcnt(27)
	v_mfma_f32_16x16x128_f8f6f4 v[24:27], v[24:29], v[18:23], 0 cbsz:2 blgp:2
	s_waitcnt vmcnt(26)
	v_mfma_f32_16x16x128_f8f6f4 v[24:27], v[44:49], v[12:17], v[24:27] cbsz:2 blgp:2
	s_waitcnt vmcnt(25)
	v_mfma_f32_16x16x128_f8f6f4 v[24:27], v[38:43], v[6:11], v[24:27] cbsz:2 blgp:2
	s_waitcnt vmcnt(24)
	v_mfma_f32_16x16x128_f8f6f4 v[24:27], v[50:55], v[0:5], v[24:27] cbsz:2 blgp:2
	s_nop 7
	v_cndmask_b32_e64 v24, v24, v25, s[4:5]
	v_cndmask_b32_e64 v24, v24, v26, s[2:3]
	v_cndmask_b32_e32 v24, v24, v27, vcc
	v_mul_f32_e32 v25, v33, v24
	s_nop 1
	v_mov_b32_dpp v25, v25 quad_perm:[1,0,3,2] row_mask:0xf bank_mask:0xf bound_ctrl:1
	v_fmac_f32_e32 v25, v33, v24
	s_nop 1
	v_add_f32_dpp v24, v25, v25 quad_perm:[2,3,0,1] row_mask:0xf bank_mask:0xf bound_ctrl:1
	s_nop 1
	v_add_f32_dpp v24, v24, v24 row_half_mirror row_mask:0xf bank_mask:0xf bound_ctrl:1
	ds_write_b32 v32, v24 offset:49264
	s_waitcnt vmcnt(19)
	v_mfma_f32_16x16x128_f8f6f4 v[24:27], v[56:61], v[18:23], 0 cbsz:2 blgp:2
	s_waitcnt vmcnt(18)
	v_mfma_f32_16x16x128_f8f6f4 v[24:27], v[68:73], v[12:17], v[24:27] cbsz:2 blgp:2
	s_waitcnt vmcnt(17)
	v_mfma_f32_16x16x128_f8f6f4 v[24:27], v[62:67], v[6:11], v[24:27] cbsz:2 blgp:2
	s_waitcnt vmcnt(16)
	v_mfma_f32_16x16x128_f8f6f4 v[24:27], v[74:79], v[0:5], v[24:27] cbsz:2 blgp:2
	s_nop 7
	v_cndmask_b32_e64 v24, v24, v25, s[4:5]
	v_cndmask_b32_e64 v24, v24, v26, s[2:3]
	v_cndmask_b32_e32 v24, v24, v27, vcc
	v_mul_f32_e32 v25, v33, v24
	s_nop 1
	v_mov_b32_dpp v25, v25 quad_perm:[1,0,3,2] row_mask:0xf bank_mask:0xf bound_ctrl:1
	v_fmac_f32_e32 v25, v33, v24
	s_nop 1
	v_add_f32_dpp v24, v25, v25 quad_perm:[2,3,0,1] row_mask:0xf bank_mask:0xf bound_ctrl:1
	s_nop 1
	v_add_f32_dpp v24, v24, v24 row_half_mirror row_mask:0xf bank_mask:0xf bound_ctrl:1
	ds_write_b32 v32, v24 offset:49268
	s_waitcnt vmcnt(11)
	v_mfma_f32_16x16x128_f8f6f4 v[24:27], v[86:91], v[18:23], 0 cbsz:2 blgp:2
	s_waitcnt vmcnt(10)
	v_mfma_f32_16x16x128_f8f6f4 v[24:27], v[98:103], v[12:17], v[24:27] cbsz:2 blgp:2
	s_waitcnt vmcnt(9)
	v_mfma_f32_16x16x128_f8f6f4 v[24:27], v[92:97], v[6:11], v[24:27] cbsz:2 blgp:2
	s_waitcnt vmcnt(8)
	v_mfma_f32_16x16x128_f8f6f4 v[24:27], v[150:155], v[0:5], v[24:27] cbsz:2 blgp:2
	s_nop 7
	v_cndmask_b32_e64 v24, v24, v25, s[4:5]
	v_cndmask_b32_e64 v24, v24, v26, s[2:3]
	v_cndmask_b32_e32 v24, v24, v27, vcc
	v_mul_f32_e32 v25, v33, v24
	s_nop 1
	v_mov_b32_dpp v25, v25 quad_perm:[1,0,3,2] row_mask:0xf bank_mask:0xf bound_ctrl:1
	v_fmac_f32_e32 v25, v33, v24
	s_nop 1
	v_add_f32_dpp v24, v25, v25 quad_perm:[2,3,0,1] row_mask:0xf bank_mask:0xf bound_ctrl:1
	s_nop 1
	v_add_f32_dpp v24, v24, v24 row_half_mirror row_mask:0xf bank_mask:0xf bound_ctrl:1
	ds_write_b32 v32, v24 offset:49272
	s_waitcnt vmcnt(3)
	v_mfma_f32_16x16x128_f8f6f4 v[18:21], v[156:161], v[18:23], 0 cbsz:2 blgp:2
	s_waitcnt vmcnt(2)
	v_mfma_f32_16x16x128_f8f6f4 v[12:15], v[168:173], v[12:17], v[18:21] cbsz:2 blgp:2
	s_waitcnt vmcnt(1)
	v_mfma_f32_16x16x128_f8f6f4 v[6:9], v[162:167], v[6:11], v[12:15] cbsz:2 blgp:2
	s_waitcnt vmcnt(0)
	v_mfma_f32_16x16x128_f8f6f4 v[0:3], v[174:179], v[0:5], v[6:9] cbsz:2 blgp:2
	s_nop 7
	v_cndmask_b32_e64 v0, v0, v1, s[4:5]
	v_cndmask_b32_e64 v0, v0, v2, s[2:3]
	v_cndmask_b32_e32 v0, v0, v3, vcc
	v_mul_f32_e32 v1, v33, v0
	s_nop 1
	v_mov_b32_dpp v1, v1 quad_perm:[1,0,3,2] row_mask:0xf bank_mask:0xf bound_ctrl:1
	v_fmac_f32_e32 v1, v33, v0
	s_nop 1
	v_add_f32_dpp v0, v1, v1 quad_perm:[2,3,0,1] row_mask:0xf bank_mask:0xf bound_ctrl:1
	s_nop 1
	v_add_f32_dpp v0, v0, v0 row_half_mirror row_mask:0xf bank_mask:0xf bound_ctrl:1
	ds_write_b32 v32, v0 offset:49276
	v_mul_u32_u24_e32 v240, 0x600, v130
	v_mul_u32_u24_e32 v241, 0x600, v128
	v_add_u32_e32 v240, 0x8000000, v240
	v_add_u32_e32 v241, 0x8000000, v241
	v_lshrrev_b32_e32 v0, 1, v129
	v_readlane_b32 s100, v240, 0
	v_readlane_b32 s101, v240, 1
	v_readlane_b32 s2, v240, 2
	v_readlane_b32 s3, v240, 3
	s_nop 1
	buffer_load_dwordx4 v[74:77], v129, s[44:47], s100 offen sc1
	buffer_load_dwordx2 v[78:79], v0, s[44:47], s100 offen offset:1024 sc1
	buffer_load_dwordx4 v[68:71], v129, s[44:47], s101 offen sc1
	buffer_load_dwordx2 v[72:73], v0, s[44:47], s101 offen offset:1024 sc1
	buffer_load_dwordx4 v[56:59], v129, s[44:47], s2 offen sc1
	buffer_load_dwordx2 v[60:61], v0, s[44:47], s2 offen offset:1024 sc1
	buffer_load_dwordx4 v[44:47], v129, s[44:47], s3 offen sc1
	buffer_load_dwordx2 v[48:49], v0, s[44:47], s3 offen offset:1024 sc1
	v_add_u32_e32 v210, 0x400, v0
	v_readlane_b32 s100, v240, 4
	v_readlane_b32 s101, v240, 5
	v_readlane_b32 s2, v240, 6
	v_readlane_b32 s3, v240, 7
	s_nop 1
	buffer_load_dwordx4 v[62:65], v129, s[44:47], s100 offen sc1
	buffer_load_dwordx2 v[66:67], v0, s[44:47], s100 offen offset:1024 sc1
	buffer_load_dwordx4 v[50:53], v129, s[44:47], s101 offen sc1
	buffer_load_dwordx2 v[54:55], v0, s[44:47], s101 offen offset:1024 sc1
	buffer_load_dwordx4 v[38:41], v129, s[44:47], s2 offen sc1
	buffer_load_dwordx2 v[42:43], v0, s[44:47], s2 offen offset:1024 sc1
	buffer_load_dwordx4 v[32:35], v129, s[44:47], s3 offen sc1
	buffer_load_dwordx2 v[36:37], v0, s[44:47], s3 offen offset:1024 sc1
	v_div_scale_f32 v2, s[2:3], v80, v80, 1.0
	v_rcp_f32_e32 v3, v2
	v_div_scale_f32 v4, vcc, 1.0, v80, 1.0
	v_and_b32_e32 v1, -4, v148
	v_fma_f32 v0, -v2, v3, 1.0
	v_fmac_f32_e32 v3, v0, v3
	v_mul_f32_e32 v5, v4, v3
	v_fma_f32 v0, -v2, v5, v4
	v_fmac_f32_e32 v5, v0, v3
	v_lshlrev_b32_e32 v0, 7, v148
	v_and_b32_e32 v0, 0x180, v0
	v_add3_u32 v0, v111, v0, v1
	v_add_u32_e32 v0, 0xc000, v0
	ds_read2_b32 v[0:1], v0 offset1:16
	v_fma_f32 v2, -v2, v5, v4
	v_div_fmas_f32 v2, v2, v3, v5
	v_div_fixup_f32 v2, v2, v80, 1.0
	s_mov_b32 s1, 0x3e6d3388
	s_waitcnt lgkmcnt(0)
	v_mul_f32_e32 v0, v2, v0
	v_mul_f32_e32 v0, v83, v0
	v_fma_f32 v3, |v0|, s1, 1.0
	v_rcp_f32_e32 v3, v3
	v_mul_f32_e32 v5, v0, v0
	v_mul_f32_e32 v5, 0xbf38aa3b, v5
	v_exp_f32_e32 v5, v5
	v_fmamk_f32 v4, v3, 0x3f07dc22, v184
	v_fmaak_f32 v4, v3, v4, 0x3f35f0e3
	v_fmaak_f32 v4, v3, v4, 0xbe11a98e
	v_mul_f32_e32 v1, v2, v1
	v_fmaak_f32 v4, v3, v4, 0x3e027906
	v_mul_f32_e32 v3, v3, v4
	v_mul_f32_e32 v1, v82, v1
	v_mul_f32_e32 v3, v5, v3
	v_fma_f32 v5, |v1|, s1, 1.0
	v_rcp_f32_e32 v5, v5
	v_mul_f32_e32 v4, v0, v3
	v_fma_f32 v3, -v0, v3, v0
	v_cmp_gt_f32_e32 vcc, 0, v0
	v_mul_f32_e32 v2, v206, v84
	v_mov_b32_e32 v180, 0
	v_cndmask_b32_e32 v0, v3, v4, vcc
	v_mul_f32_e32 v211, v2, v0
	v_mul_f32_e32 v2, v1, v1
	v_fmamk_f32 v0, v5, 0x3f07dc22, v184
	v_mul_f32_e32 v2, 0xbf38aa3b, v2
	v_fmaak_f32 v0, v5, v0, 0x3f35f0e3
	v_exp_f32_e32 v2, v2
	v_fmaak_f32 v0, v5, v0, 0xbe11a98e
	v_fmaak_f32 v0, v5, v0, 0x3e027906
	v_mul_f32_e32 v0, v5, v0
	v_mul_f32_e32 v0, v2, v0
	v_mul_f32_e32 v2, v1, v0
	v_fma_f32 v0, -v1, v0, v1
	v_cmp_gt_f32_e32 vcc, 0, v1
	v_mul_f32_e32 v1, v205, v81
	v_mov_b32_e32 v181, v180
	v_cndmask_b32_e32 v0, v0, v2, vcc
	v_mul_f32_e32 v131, v1, v0
	v_mov_b32_e32 v178, v180
	v_mov_b32_e32 v179, v180
	v_mov_b32_e32 v176, v180
	v_mov_b32_e32 v177, v180
	v_mov_b32_e32 v174, v180
	v_mov_b32_e32 v175, v180
	v_mov_b32_e32 v172, v180
	v_mov_b32_e32 v173, v180
	v_mov_b32_e32 v170, v180
	v_mov_b32_e32 v171, v180
	v_mov_b32_e32 v168, v180
	v_mov_b32_e32 v169, v180
	v_mov_b32_e32 v166, v180
	v_mov_b32_e32 v167, v180
	v_mov_b32_e32 v164, v180
	v_mov_b32_e32 v165, v180
	v_mov_b32_e32 v162, v180
	v_mov_b32_e32 v163, v180
	v_mov_b32_e32 v160, v180
	v_mov_b32_e32 v161, v180
	v_mov_b32_e32 v158, v180
	v_mov_b32_e32 v159, v180
	v_mov_b32_e32 v156, v180
	v_mov_b32_e32 v157, v180
	v_mov_b32_e32 v154, v180
	v_mov_b32_e32 v155, v180
	v_mov_b32_e32 v152, v180
	v_mov_b32_e32 v153, v180
	v_mov_b32_e32 v150, v180
	v_mov_b32_e32 v151, v180
	v_readlane_b32 s2, v240, 8
	v_readlane_b32 s3, v240, 9
	v_readlane_b32 s100, v240, 10
	v_readlane_b32 s101, v240, 11
	s_nop 1
	buffer_load_dwordx4 v[98:101], v129, s[44:47], s2 offen sc1
	buffer_load_dwordx2 v[102:103], v210, s[44:47], s2 offen sc1
	buffer_load_dwordx4 v[92:95], v129, s[44:47], s3 offen sc1
	buffer_load_dwordx2 v[96:97], v210, s[44:47], s3 offen sc1
	buffer_load_dwordx4 v[86:89], v129, s[44:47], s100 offen sc1
	buffer_load_dwordx2 v[90:91], v210, s[44:47], s100 offen sc1
	buffer_load_dwordx4 v[80:83], v129, s[44:47], s101 offen sc1
	buffer_load_dwordx2 v[84:85], v210, s[44:47], s101 offen sc1
	v_readlane_b32 s2, v211, 0
	s_waitcnt vmcnt(22)
	v_cvt_scalef32_pk32_f32_fp6 v[0:31], v[74:79], 1.0
	v_pk_fma_f32 v[74:75], v[0:1], s[2:3], v[180:181] op_sel_hi:[1,0,1]
	v_pk_fma_f32 v[76:77], v[2:3], s[2:3], v[178:179] op_sel_hi:[1,0,1]
	v_pk_fma_f32 v[78:79], v[4:5], s[2:3], v[176:177] op_sel_hi:[1,0,1]
	v_pk_fma_f32 v[174:175], v[6:7], s[2:3], v[174:175] op_sel_hi:[1,0,1]
	v_pk_fma_f32 v[172:173], v[8:9], s[2:3], v[172:173] op_sel_hi:[1,0,1]
	v_pk_fma_f32 v[170:171], v[10:11], s[2:3], v[170:171] op_sel_hi:[1,0,1]
	v_pk_fma_f32 v[168:169], v[12:13], s[2:3], v[168:169] op_sel_hi:[1,0,1]
	v_pk_fma_f32 v[166:167], v[14:15], s[2:3], v[166:167] op_sel_hi:[1,0,1]
	v_pk_fma_f32 v[164:165], v[16:17], s[2:3], v[164:165] op_sel_hi:[1,0,1]
	v_pk_fma_f32 v[162:163], v[18:19], s[2:3], v[162:163] op_sel_hi:[1,0,1]
	v_pk_fma_f32 v[160:161], v[20:21], s[2:3], v[160:161] op_sel_hi:[1,0,1]
	v_pk_fma_f32 v[158:159], v[22:23], s[2:3], v[158:159] op_sel_hi:[1,0,1]
	v_pk_fma_f32 v[156:157], v[24:25], s[2:3], v[156:157] op_sel_hi:[1,0,1]
	v_pk_fma_f32 v[154:155], v[26:27], s[2:3], v[154:155] op_sel_hi:[1,0,1]
	v_pk_fma_f32 v[152:153], v[28:29], s[2:3], v[152:153] op_sel_hi:[1,0,1]
	v_pk_fma_f32 v[150:151], v[30:31], s[2:3], v[150:151] op_sel_hi:[1,0,1]
	v_readlane_b32 s2, v211, 1
	s_waitcnt vmcnt(20)
	v_cvt_scalef32_pk32_f32_fp6 v[0:31], v[68:73], 1.0
	v_pk_fma_f32 v[68:69], v[0:1], s[2:3], v[74:75] op_sel_hi:[1,0,1]
	v_pk_fma_f32 v[70:71], v[2:3], s[2:3], v[76:77] op_sel_hi:[1,0,1]
	v_pk_fma_f32 v[72:73], v[4:5], s[2:3], v[78:79] op_sel_hi:[1,0,1]
	v_pk_fma_f32 v[74:75], v[6:7], s[2:3], v[174:175] op_sel_hi:[1,0,1]
	v_pk_fma_f32 v[76:77], v[8:9], s[2:3], v[172:173] op_sel_hi:[1,0,1]
	v_pk_fma_f32 v[78:79], v[10:11], s[2:3], v[170:171] op_sel_hi:[1,0,1]
	v_pk_fma_f32 v[168:169], v[12:13], s[2:3], v[168:169] op_sel_hi:[1,0,1]
	v_pk_fma_f32 v[166:167], v[14:15], s[2:3], v[166:167] op_sel_hi:[1,0,1]
	v_pk_fma_f32 v[164:165], v[16:17], s[2:3], v[164:165] op_sel_hi:[1,0,1]
	v_pk_fma_f32 v[162:163], v[18:19], s[2:3], v[162:163] op_sel_hi:[1,0,1]
	v_pk_fma_f32 v[160:161], v[20:21], s[2:3], v[160:161] op_sel_hi:[1,0,1]
	v_pk_fma_f32 v[158:159], v[22:23], s[2:3], v[158:159] op_sel_hi:[1,0,1]
	v_pk_fma_f32 v[156:157], v[24:25], s[2:3], v[156:157] op_sel_hi:[1,0,1]
	v_pk_fma_f32 v[154:155], v[26:27], s[2:3], v[154:155] op_sel_hi:[1,0,1]
	v_pk_fma_f32 v[152:153], v[28:29], s[2:3], v[152:153] op_sel_hi:[1,0,1]
	v_pk_fma_f32 v[150:151], v[30:31], s[2:3], v[150:151] op_sel_hi:[1,0,1]
	v_readlane_b32 s2, v211, 2
	s_waitcnt vmcnt(18)
	v_cvt_scalef32_pk32_f32_fp6 v[0:31], v[56:61], 1.0
	v_pk_fma_f32 v[56:57], v[0:1], s[2:3], v[68:69] op_sel_hi:[1,0,1]
	v_pk_fma_f32 v[58:59], v[2:3], s[2:3], v[70:71] op_sel_hi:[1,0,1]
	v_pk_fma_f32 v[60:61], v[4:5], s[2:3], v[72:73] op_sel_hi:[1,0,1]
	v_pk_fma_f32 v[68:69], v[6:7], s[2:3], v[74:75] op_sel_hi:[1,0,1]
	v_pk_fma_f32 v[70:71], v[8:9], s[2:3], v[76:77] op_sel_hi:[1,0,1]
	v_pk_fma_f32 v[72:73], v[10:11], s[2:3], v[78:79] op_sel_hi:[1,0,1]
	v_pk_fma_f32 v[74:75], v[12:13], s[2:3], v[168:169] op_sel_hi:[1,0,1]
	v_pk_fma_f32 v[76:77], v[14:15], s[2:3], v[166:167] op_sel_hi:[1,0,1]
	v_pk_fma_f32 v[78:79], v[16:17], s[2:3], v[164:165] op_sel_hi:[1,0,1]
	v_pk_fma_f32 v[162:163], v[18:19], s[2:3], v[162:163] op_sel_hi:[1,0,1]
	v_pk_fma_f32 v[160:161], v[20:21], s[2:3], v[160:161] op_sel_hi:[1,0,1]
	v_pk_fma_f32 v[158:159], v[22:23], s[2:3], v[158:159] op_sel_hi:[1,0,1]
	v_pk_fma_f32 v[156:157], v[24:25], s[2:3], v[156:157] op_sel_hi:[1,0,1]
	v_pk_fma_f32 v[154:155], v[26:27], s[2:3], v[154:155] op_sel_hi:[1,0,1]
	v_pk_fma_f32 v[152:153], v[28:29], s[2:3], v[152:153] op_sel_hi:[1,0,1]
	v_pk_fma_f32 v[150:151], v[30:31], s[2:3], v[150:151] op_sel_hi:[1,0,1]
	v_readlane_b32 s2, v211, 3
	s_waitcnt vmcnt(16)
	v_cvt_scalef32_pk32_f32_fp6 v[0:31], v[44:49], 1.0
	v_pk_fma_f32 v[164:165], v[0:1], s[2:3], v[56:57] op_sel_hi:[1,0,1]
	v_pk_fma_f32 v[166:167], v[2:3], s[2:3], v[58:59] op_sel_hi:[1,0,1]
	v_pk_fma_f32 v[168:169], v[4:5], s[2:3], v[60:61] op_sel_hi:[1,0,1]
	v_pk_fma_f32 v[170:171], v[6:7], s[2:3], v[68:69] op_sel_hi:[1,0,1]
	v_pk_fma_f32 v[172:173], v[8:9], s[2:3], v[70:71] op_sel_hi:[1,0,1]
	v_pk_fma_f32 v[174:175], v[10:11], s[2:3], v[72:73] op_sel_hi:[1,0,1]
	v_pk_fma_f32 v[176:177], v[12:13], s[2:3], v[74:75] op_sel_hi:[1,0,1]
	v_pk_fma_f32 v[178:179], v[14:15], s[2:3], v[76:77] op_sel_hi:[1,0,1]
	v_pk_fma_f32 v[180:181], v[16:17], s[2:3], v[78:79] op_sel_hi:[1,0,1]
	v_pk_fma_f32 v[162:163], v[18:19], s[2:3], v[162:163] op_sel_hi:[1,0,1]
	v_pk_fma_f32 v[160:161], v[20:21], s[2:3], v[160:161] op_sel_hi:[1,0,1]
	v_pk_fma_f32 v[158:159], v[22:23], s[2:3], v[158:159] op_sel_hi:[1,0,1]
	v_pk_fma_f32 v[156:157], v[24:25], s[2:3], v[156:157] op_sel_hi:[1,0,1]
	v_pk_fma_f32 v[154:155], v[26:27], s[2:3], v[154:155] op_sel_hi:[1,0,1]
	v_pk_fma_f32 v[152:153], v[28:29], s[2:3], v[152:153] op_sel_hi:[1,0,1]
	v_pk_fma_f32 v[150:151], v[30:31], s[2:3], v[150:151] op_sel_hi:[1,0,1]
	v_readlane_b32 s2, v240, 12
	v_readlane_b32 s3, v240, 13
	v_readlane_b32 s100, v240, 14
	v_readlane_b32 s101, v240, 15
	s_nop 1
	buffer_load_dwordx4 v[74:77], v129, s[44:47], s2 offen sc1
	buffer_load_dwordx2 v[78:79], v210, s[44:47], s2 offen sc1
	buffer_load_dwordx4 v[68:71], v129, s[44:47], s3 offen sc1
	buffer_load_dwordx2 v[72:73], v210, s[44:47], s3 offen sc1
	buffer_load_dwordx4 v[56:59], v129, s[44:47], s100 offen sc1
	buffer_load_dwordx2 v[60:61], v210, s[44:47], s100 offen sc1
	buffer_load_dwordx4 v[44:47], v129, s[44:47], s101 offen sc1
	buffer_load_dwordx2 v[48:49], v210, s[44:47], s101 offen sc1
	v_readlane_b32 s2, v211, 4
	s_waitcnt vmcnt(22)
	v_cvt_scalef32_pk32_f32_fp6 v[0:31], v[62:67], 1.0
	v_pk_fma_f32 v[62:63], v[0:1], s[2:3], v[164:165] op_sel_hi:[1,0,1]
	v_pk_fma_f32 v[64:65], v[2:3], s[2:3], v[166:167] op_sel_hi:[1,0,1]
	v_pk_fma_f32 v[66:67], v[4:5], s[2:3], v[168:169] op_sel_hi:[1,0,1]
	v_pk_fma_f32 v[164:165], v[6:7], s[2:3], v[170:171] op_sel_hi:[1,0,1]
	v_pk_fma_f32 v[166:167], v[8:9], s[2:3], v[172:173] op_sel_hi:[1,0,1]
	v_pk_fma_f32 v[168:169], v[10:11], s[2:3], v[174:175] op_sel_hi:[1,0,1]
	v_pk_fma_f32 v[170:171], v[12:13], s[2:3], v[176:177] op_sel_hi:[1,0,1]
	v_pk_fma_f32 v[172:173], v[14:15], s[2:3], v[178:179] op_sel_hi:[1,0,1]
	v_pk_fma_f32 v[174:175], v[16:17], s[2:3], v[180:181] op_sel_hi:[1,0,1]
	v_pk_fma_f32 v[162:163], v[18:19], s[2:3], v[162:163] op_sel_hi:[1,0,1]
	v_pk_fma_f32 v[160:161], v[20:21], s[2:3], v[160:161] op_sel_hi:[1,0,1]
	v_pk_fma_f32 v[158:159], v[22:23], s[2:3], v[158:159] op_sel_hi:[1,0,1]
	v_pk_fma_f32 v[156:157], v[24:25], s[2:3], v[156:157] op_sel_hi:[1,0,1]
	v_pk_fma_f32 v[154:155], v[26:27], s[2:3], v[154:155] op_sel_hi:[1,0,1]
	v_pk_fma_f32 v[152:153], v[28:29], s[2:3], v[152:153] op_sel_hi:[1,0,1]
	v_pk_fma_f32 v[150:151], v[30:31], s[2:3], v[150:151] op_sel_hi:[1,0,1]
	v_readlane_b32 s2, v211, 5
	s_waitcnt vmcnt(20)
	v_cvt_scalef32_pk32_f32_fp6 v[0:31], v[50:55], 1.0
	v_pk_fma_f32 v[50:51], v[0:1], s[2:3], v[62:63] op_sel_hi:[1,0,1]
	v_pk_fma_f32 v[52:53], v[2:3], s[2:3], v[64:65] op_sel_hi:[1,0,1]
	v_pk_fma_f32 v[54:55], v[4:5], s[2:3], v[66:67] op_sel_hi:[1,0,1]
	v_pk_fma_f32 v[62:63], v[6:7], s[2:3], v[164:165] op_sel_hi:[1,0,1]
	v_pk_fma_f32 v[64:65], v[8:9], s[2:3], v[166:167] op_sel_hi:[1,0,1]
	v_pk_fma_f32 v[66:67], v[10:11], s[2:3], v[168:169] op_sel_hi:[1,0,1]
	v_pk_fma_f32 v[164:165], v[12:13], s[2:3], v[170:171] op_sel_hi:[1,0,1]
	v_pk_fma_f32 v[166:167], v[14:15], s[2:3], v[172:173] op_sel_hi:[1,0,1]
	v_pk_fma_f32 v[168:169], v[16:17], s[2:3], v[174:175] op_sel_hi:[1,0,1]
	v_pk_fma_f32 v[162:163], v[18:19], s[2:3], v[162:163] op_sel_hi:[1,0,1]
	v_pk_fma_f32 v[160:161], v[20:21], s[2:3], v[160:161] op_sel_hi:[1,0,1]
	v_pk_fma_f32 v[158:159], v[22:23], s[2:3], v[158:159] op_sel_hi:[1,0,1]
	v_pk_fma_f32 v[156:157], v[24:25], s[2:3], v[156:157] op_sel_hi:[1,0,1]
	v_pk_fma_f32 v[154:155], v[26:27], s[2:3], v[154:155] op_sel_hi:[1,0,1]
	v_pk_fma_f32 v[152:153], v[28:29], s[2:3], v[152:153] op_sel_hi:[1,0,1]
	v_pk_fma_f32 v[150:151], v[30:31], s[2:3], v[150:151] op_sel_hi:[1,0,1]
	v_readlane_b32 s2, v211, 6
	s_waitcnt vmcnt(18)
	v_cvt_scalef32_pk32_f32_fp6 v[0:31], v[38:43], 1.0
	v_pk_fma_f32 v[38:39], v[0:1], s[2:3], v[50:51] op_sel_hi:[1,0,1]
	v_pk_fma_f32 v[40:41], v[2:3], s[2:3], v[52:53] op_sel_hi:[1,0,1]
	v_pk_fma_f32 v[42:43], v[4:5], s[2:3], v[54:55] op_sel_hi:[1,0,1]
	v_pk_fma_f32 v[50:51], v[6:7], s[2:3], v[62:63] op_sel_hi:[1,0,1]
	v_pk_fma_f32 v[52:53], v[8:9], s[2:3], v[64:65] op_sel_hi:[1,0,1]
	v_pk_fma_f32 v[54:55], v[10:11], s[2:3], v[66:67] op_sel_hi:[1,0,1]
	v_pk_fma_f32 v[62:63], v[12:13], s[2:3], v[164:165] op_sel_hi:[1,0,1]
	v_pk_fma_f32 v[64:65], v[14:15], s[2:3], v[166:167] op_sel_hi:[1,0,1]
	v_pk_fma_f32 v[66:67], v[16:17], s[2:3], v[168:169] op_sel_hi:[1,0,1]
	v_pk_fma_f32 v[162:163], v[18:19], s[2:3], v[162:163] op_sel_hi:[1,0,1]
	v_pk_fma_f32 v[160:161], v[20:21], s[2:3], v[160:161] op_sel_hi:[1,0,1]
	v_pk_fma_f32 v[158:159], v[22:23], s[2:3], v[158:159] op_sel_hi:[1,0,1]
	v_pk_fma_f32 v[156:157], v[24:25], s[2:3], v[156:157] op_sel_hi:[1,0,1]
	v_pk_fma_f32 v[154:155], v[26:27], s[2:3], v[154:155] op_sel_hi:[1,0,1]
	v_pk_fma_f32 v[152:153], v[28:29], s[2:3], v[152:153] op_sel_hi:[1,0,1]
	v_pk_fma_f32 v[150:151], v[30:31], s[2:3], v[150:151] op_sel_hi:[1,0,1]
	v_readlane_b32 s2, v211, 7
	s_waitcnt vmcnt(16)
	v_cvt_scalef32_pk32_f32_fp6 v[0:31], v[32:37], 1.0
	v_pk_fma_f32 v[164:165], v[0:1], s[2:3], v[38:39] op_sel_hi:[1,0,1]
	v_pk_fma_f32 v[166:167], v[2:3], s[2:3], v[40:41] op_sel_hi:[1,0,1]
	v_pk_fma_f32 v[168:169], v[4:5], s[2:3], v[42:43] op_sel_hi:[1,0,1]
	v_pk_fma_f32 v[170:171], v[6:7], s[2:3], v[50:51] op_sel_hi:[1,0,1]
	v_pk_fma_f32 v[172:173], v[8:9], s[2:3], v[52:53] op_sel_hi:[1,0,1]
	v_pk_fma_f32 v[174:175], v[10:11], s[2:3], v[54:55] op_sel_hi:[1,0,1]
	v_pk_fma_f32 v[176:177], v[12:13], s[2:3], v[62:63] op_sel_hi:[1,0,1]
	v_pk_fma_f32 v[178:179], v[14:15], s[2:3], v[64:65] op_sel_hi:[1,0,1]
	v_pk_fma_f32 v[180:181], v[16:17], s[2:3], v[66:67] op_sel_hi:[1,0,1]
	v_pk_fma_f32 v[162:163], v[18:19], s[2:3], v[162:163] op_sel_hi:[1,0,1]
	v_pk_fma_f32 v[160:161], v[20:21], s[2:3], v[160:161] op_sel_hi:[1,0,1]
	v_pk_fma_f32 v[158:159], v[22:23], s[2:3], v[158:159] op_sel_hi:[1,0,1]
	v_pk_fma_f32 v[156:157], v[24:25], s[2:3], v[156:157] op_sel_hi:[1,0,1]
	v_pk_fma_f32 v[154:155], v[26:27], s[2:3], v[154:155] op_sel_hi:[1,0,1]
	v_pk_fma_f32 v[152:153], v[28:29], s[2:3], v[152:153] op_sel_hi:[1,0,1]
	v_pk_fma_f32 v[150:151], v[30:31], s[2:3], v[150:151] op_sel_hi:[1,0,1]
	v_readlane_b32 s2, v240, 16
	v_readlane_b32 s3, v240, 17
	v_readlane_b32 s100, v240, 18
	v_readlane_b32 s101, v240, 19
	s_nop 1
	buffer_load_dwordx4 v[62:65], v129, s[44:47], s2 offen sc1
	buffer_load_dwordx2 v[66:67], v210, s[44:47], s2 offen sc1
	buffer_load_dwordx4 v[50:53], v129, s[44:47], s3 offen sc1
	buffer_load_dwordx2 v[54:55], v210, s[44:47], s3 offen sc1
	buffer_load_dwordx4 v[38:41], v129, s[44:47], s100 offen sc1
	buffer_load_dwordx2 v[42:43], v210, s[44:47], s100 offen sc1
	buffer_load_dwordx4 v[32:35], v129, s[44:47], s101 offen sc1
	buffer_load_dwordx2 v[36:37], v210, s[44:47], s101 offen sc1
	v_readlane_b32 s2, v211, 8
	s_waitcnt vmcnt(22)
	v_cvt_scalef32_pk32_f32_fp6 v[0:31], v[98:103], 1.0
	v_pk_fma_f32 v[98:99], v[0:1], s[2:3], v[164:165] op_sel_hi:[1,0,1]
	v_pk_fma_f32 v[100:101], v[2:3], s[2:3], v[166:167] op_sel_hi:[1,0,1]
	v_pk_fma_f32 v[102:103], v[4:5], s[2:3], v[168:169] op_sel_hi:[1,0,1]
	v_pk_fma_f32 v[164:165], v[6:7], s[2:3], v[170:171] op_sel_hi:[1,0,1]
	v_pk_fma_f32 v[166:167], v[8:9], s[2:3], v[172:173] op_sel_hi:[1,0,1]
	v_pk_fma_f32 v[168:169], v[10:11], s[2:3], v[174:175] op_sel_hi:[1,0,1]
	v_pk_fma_f32 v[170:171], v[12:13], s[2:3], v[176:177] op_sel_hi:[1,0,1]
	v_pk_fma_f32 v[172:173], v[14:15], s[2:3], v[178:179] op_sel_hi:[1,0,1]
	v_pk_fma_f32 v[174:175], v[16:17], s[2:3], v[180:181] op_sel_hi:[1,0,1]
	v_pk_fma_f32 v[162:163], v[18:19], s[2:3], v[162:163] op_sel_hi:[1,0,1]
	v_pk_fma_f32 v[160:161], v[20:21], s[2:3], v[160:161] op_sel_hi:[1,0,1]
	v_pk_fma_f32 v[158:159], v[22:23], s[2:3], v[158:159] op_sel_hi:[1,0,1]
	v_pk_fma_f32 v[156:157], v[24:25], s[2:3], v[156:157] op_sel_hi:[1,0,1]
	v_pk_fma_f32 v[154:155], v[26:27], s[2:3], v[154:155] op_sel_hi:[1,0,1]
	v_pk_fma_f32 v[152:153], v[28:29], s[2:3], v[152:153] op_sel_hi:[1,0,1]
	v_pk_fma_f32 v[150:151], v[30:31], s[2:3], v[150:151] op_sel_hi:[1,0,1]
	v_readlane_b32 s2, v211, 9
	s_waitcnt vmcnt(20)
	v_cvt_scalef32_pk32_f32_fp6 v[0:31], v[92:97], 1.0
	v_pk_fma_f32 v[92:93], v[0:1], s[2:3], v[98:99] op_sel_hi:[1,0,1]
	v_pk_fma_f32 v[94:95], v[2:3], s[2:3], v[100:101] op_sel_hi:[1,0,1]
	v_pk_fma_f32 v[96:97], v[4:5], s[2:3], v[102:103] op_sel_hi:[1,0,1]
	v_pk_fma_f32 v[98:99], v[6:7], s[2:3], v[164:165] op_sel_hi:[1,0,1]
	v_pk_fma_f32 v[100:101], v[8:9], s[2:3], v[166:167] op_sel_hi:[1,0,1]
	v_pk_fma_f32 v[102:103], v[10:11], s[2:3], v[168:169] op_sel_hi:[1,0,1]
	v_pk_fma_f32 v[164:165], v[12:13], s[2:3], v[170:171] op_sel_hi:[1,0,1]
	v_pk_fma_f32 v[166:167], v[14:15], s[2:3], v[172:173] op_sel_hi:[1,0,1]
	v_pk_fma_f32 v[168:169], v[16:17], s[2:3], v[174:175] op_sel_hi:[1,0,1]
	v_pk_fma_f32 v[162:163], v[18:19], s[2:3], v[162:163] op_sel_hi:[1,0,1]
	v_pk_fma_f32 v[160:161], v[20:21], s[2:3], v[160:161] op_sel_hi:[1,0,1]
	v_pk_fma_f32 v[158:159], v[22:23], s[2:3], v[158:159] op_sel_hi:[1,0,1]
	v_pk_fma_f32 v[156:157], v[24:25], s[2:3], v[156:157] op_sel_hi:[1,0,1]
	v_pk_fma_f32 v[154:155], v[26:27], s[2:3], v[154:155] op_sel_hi:[1,0,1]
	v_pk_fma_f32 v[152:153], v[28:29], s[2:3], v[152:153] op_sel_hi:[1,0,1]
	v_pk_fma_f32 v[150:151], v[30:31], s[2:3], v[150:151] op_sel_hi:[1,0,1]
	v_readlane_b32 s2, v211, 10
	s_waitcnt vmcnt(18)
	v_cvt_scalef32_pk32_f32_fp6 v[0:31], v[86:91], 1.0
	v_pk_fma_f32 v[86:87], v[0:1], s[2:3], v[92:93] op_sel_hi:[1,0,1]
	v_pk_fma_f32 v[88:89], v[2:3], s[2:3], v[94:95] op_sel_hi:[1,0,1]
	v_pk_fma_f32 v[90:91], v[4:5], s[2:3], v[96:97] op_sel_hi:[1,0,1]
	v_pk_fma_f32 v[92:93], v[6:7], s[2:3], v[98:99] op_sel_hi:[1,0,1]
	v_pk_fma_f32 v[94:95], v[8:9], s[2:3], v[100:101] op_sel_hi:[1,0,1]
	v_pk_fma_f32 v[96:97], v[10:11], s[2:3], v[102:103] op_sel_hi:[1,0,1]
	v_pk_fma_f32 v[98:99], v[12:13], s[2:3], v[164:165] op_sel_hi:[1,0,1]
	v_pk_fma_f32 v[100:101], v[14:15], s[2:3], v[166:167] op_sel_hi:[1,0,1]
	v_pk_fma_f32 v[102:103], v[16:17], s[2:3], v[168:169] op_sel_hi:[1,0,1]
	v_pk_fma_f32 v[162:163], v[18:19], s[2:3], v[162:163] op_sel_hi:[1,0,1]
	v_pk_fma_f32 v[160:161], v[20:21], s[2:3], v[160:161] op_sel_hi:[1,0,1]
	v_pk_fma_f32 v[158:159], v[22:23], s[2:3], v[158:159] op_sel_hi:[1,0,1]
	v_pk_fma_f32 v[156:157], v[24:25], s[2:3], v[156:157] op_sel_hi:[1,0,1]
	v_pk_fma_f32 v[154:155], v[26:27], s[2:3], v[154:155] op_sel_hi:[1,0,1]
	v_pk_fma_f32 v[152:153], v[28:29], s[2:3], v[152:153] op_sel_hi:[1,0,1]
	v_pk_fma_f32 v[150:151], v[30:31], s[2:3], v[150:151] op_sel_hi:[1,0,1]
	v_readlane_b32 s2, v211, 11
	s_waitcnt vmcnt(16)
	v_cvt_scalef32_pk32_f32_fp6 v[0:31], v[80:85], 1.0
	v_pk_fma_f32 v[180:181], v[0:1], s[2:3], v[86:87] op_sel_hi:[1,0,1]
	v_pk_fma_f32 v[178:179], v[2:3], s[2:3], v[88:89] op_sel_hi:[1,0,1]
	v_pk_fma_f32 v[176:177], v[4:5], s[2:3], v[90:91] op_sel_hi:[1,0,1]
	v_pk_fma_f32 v[174:175], v[6:7], s[2:3], v[92:93] op_sel_hi:[1,0,1]
	v_pk_fma_f32 v[172:173], v[8:9], s[2:3], v[94:95] op_sel_hi:[1,0,1]
	v_pk_fma_f32 v[170:171], v[10:11], s[2:3], v[96:97] op_sel_hi:[1,0,1]
	v_pk_fma_f32 v[168:169], v[12:13], s[2:3], v[98:99] op_sel_hi:[1,0,1]
	v_pk_fma_f32 v[166:167], v[14:15], s[2:3], v[100:101] op_sel_hi:[1,0,1]
	v_pk_fma_f32 v[164:165], v[16:17], s[2:3], v[102:103] op_sel_hi:[1,0,1]
	v_pk_fma_f32 v[162:163], v[18:19], s[2:3], v[162:163] op_sel_hi:[1,0,1]
	v_pk_fma_f32 v[160:161], v[20:21], s[2:3], v[160:161] op_sel_hi:[1,0,1]
	v_pk_fma_f32 v[158:159], v[22:23], s[2:3], v[158:159] op_sel_hi:[1,0,1]
	v_pk_fma_f32 v[156:157], v[24:25], s[2:3], v[156:157] op_sel_hi:[1,0,1]
	v_pk_fma_f32 v[154:155], v[26:27], s[2:3], v[154:155] op_sel_hi:[1,0,1]
	v_pk_fma_f32 v[152:153], v[28:29], s[2:3], v[152:153] op_sel_hi:[1,0,1]
	v_pk_fma_f32 v[150:151], v[30:31], s[2:3], v[150:151] op_sel_hi:[1,0,1]
	v_readlane_b32 s2, v240, 20
	v_readlane_b32 s3, v240, 21
	v_readlane_b32 s100, v240, 22
	v_readlane_b32 s101, v240, 23
	s_nop 1
	buffer_load_dwordx4 v[98:101], v129, s[44:47], s2 offen sc1
	buffer_load_dwordx2 v[102:103], v210, s[44:47], s2 offen sc1
	buffer_load_dwordx4 v[92:95], v129, s[44:47], s3 offen sc1
	buffer_load_dwordx2 v[96:97], v210, s[44:47], s3 offen sc1
	buffer_load_dwordx4 v[86:89], v129, s[44:47], s100 offen sc1
	buffer_load_dwordx2 v[90:91], v210, s[44:47], s100 offen sc1
	buffer_load_dwordx4 v[80:83], v129, s[44:47], s101 offen sc1
	buffer_load_dwordx2 v[84:85], v210, s[44:47], s101 offen sc1
	v_readlane_b32 s2, v211, 12
	s_waitcnt vmcnt(22)
	v_cvt_scalef32_pk32_f32_fp6 v[0:31], v[74:79], 1.0
	v_pk_fma_f32 v[74:75], v[0:1], s[2:3], v[180:181] op_sel_hi:[1,0,1]
	v_pk_fma_f32 v[76:77], v[2:3], s[2:3], v[178:179] op_sel_hi:[1,0,1]
	v_pk_fma_f32 v[78:79], v[4:5], s[2:3], v[176:177] op_sel_hi:[1,0,1]
	v_pk_fma_f32 v[174:175], v[6:7], s[2:3], v[174:175] op_sel_hi:[1,0,1]
	v_pk_fma_f32 v[172:173], v[8:9], s[2:3], v[172:173] op_sel_hi:[1,0,1]
	v_pk_fma_f32 v[170:171], v[10:11], s[2:3], v[170:171] op_sel_hi:[1,0,1]
	v_pk_fma_f32 v[168:169], v[12:13], s[2:3], v[168:169] op_sel_hi:[1,0,1]
	v_pk_fma_f32 v[166:167], v[14:15], s[2:3], v[166:167] op_sel_hi:[1,0,1]
	v_pk_fma_f32 v[164:165], v[16:17], s[2:3], v[164:165] op_sel_hi:[1,0,1]
	v_pk_fma_f32 v[162:163], v[18:19], s[2:3], v[162:163] op_sel_hi:[1,0,1]
	v_pk_fma_f32 v[160:161], v[20:21], s[2:3], v[160:161] op_sel_hi:[1,0,1]
	v_pk_fma_f32 v[158:159], v[22:23], s[2:3], v[158:159] op_sel_hi:[1,0,1]
	v_pk_fma_f32 v[156:157], v[24:25], s[2:3], v[156:157] op_sel_hi:[1,0,1]
	v_pk_fma_f32 v[154:155], v[26:27], s[2:3], v[154:155] op_sel_hi:[1,0,1]
	v_pk_fma_f32 v[152:153], v[28:29], s[2:3], v[152:153] op_sel_hi:[1,0,1]
	v_pk_fma_f32 v[150:151], v[30:31], s[2:3], v[150:151] op_sel_hi:[1,0,1]
	v_readlane_b32 s2, v211, 13
	s_waitcnt vmcnt(20)
	v_cvt_scalef32_pk32_f32_fp6 v[0:31], v[68:73], 1.0
	v_pk_fma_f32 v[68:69], v[0:1], s[2:3], v[74:75] op_sel_hi:[1,0,1]
	v_pk_fma_f32 v[70:71], v[2:3], s[2:3], v[76:77] op_sel_hi:[1,0,1]
	v_pk_fma_f32 v[72:73], v[4:5], s[2:3], v[78:79] op_sel_hi:[1,0,1]
	v_pk_fma_f32 v[74:75], v[6:7], s[2:3], v[174:175] op_sel_hi:[1,0,1]
	v_pk_fma_f32 v[76:77], v[8:9], s[2:3], v[172:173] op_sel_hi:[1,0,1]
	v_pk_fma_f32 v[78:79], v[10:11], s[2:3], v[170:171] op_sel_hi:[1,0,1]
	v_pk_fma_f32 v[168:169], v[12:13], s[2:3], v[168:169] op_sel_hi:[1,0,1]
	v_pk_fma_f32 v[166:167], v[14:15], s[2:3], v[166:167] op_sel_hi:[1,0,1]
	v_pk_fma_f32 v[164:165], v[16:17], s[2:3], v[164:165] op_sel_hi:[1,0,1]
	v_pk_fma_f32 v[162:163], v[18:19], s[2:3], v[162:163] op_sel_hi:[1,0,1]
	v_pk_fma_f32 v[160:161], v[20:21], s[2:3], v[160:161] op_sel_hi:[1,0,1]
	v_pk_fma_f32 v[158:159], v[22:23], s[2:3], v[158:159] op_sel_hi:[1,0,1]
	v_pk_fma_f32 v[156:157], v[24:25], s[2:3], v[156:157] op_sel_hi:[1,0,1]
	v_pk_fma_f32 v[154:155], v[26:27], s[2:3], v[154:155] op_sel_hi:[1,0,1]
	v_pk_fma_f32 v[152:153], v[28:29], s[2:3], v[152:153] op_sel_hi:[1,0,1]
	v_pk_fma_f32 v[150:151], v[30:31], s[2:3], v[150:151] op_sel_hi:[1,0,1]
	v_readlane_b32 s2, v211, 14
	s_waitcnt vmcnt(18)
	v_cvt_scalef32_pk32_f32_fp6 v[0:31], v[56:61], 1.0
	v_pk_fma_f32 v[56:57], v[0:1], s[2:3], v[68:69] op_sel_hi:[1,0,1]
	v_pk_fma_f32 v[58:59], v[2:3], s[2:3], v[70:71] op_sel_hi:[1,0,1]
	v_pk_fma_f32 v[60:61], v[4:5], s[2:3], v[72:73] op_sel_hi:[1,0,1]
	v_pk_fma_f32 v[68:69], v[6:7], s[2:3], v[74:75] op_sel_hi:[1,0,1]
	v_pk_fma_f32 v[70:71], v[8:9], s[2:3], v[76:77] op_sel_hi:[1,0,1]
	v_pk_fma_f32 v[72:73], v[10:11], s[2:3], v[78:79] op_sel_hi:[1,0,1]
	v_pk_fma_f32 v[74:75], v[12:13], s[2:3], v[168:169] op_sel_hi:[1,0,1]
	v_pk_fma_f32 v[76:77], v[14:15], s[2:3], v[166:167] op_sel_hi:[1,0,1]
	v_pk_fma_f32 v[78:79], v[16:17], s[2:3], v[164:165] op_sel_hi:[1,0,1]
	v_pk_fma_f32 v[162:163], v[18:19], s[2:3], v[162:163] op_sel_hi:[1,0,1]
	v_pk_fma_f32 v[160:161], v[20:21], s[2:3], v[160:161] op_sel_hi:[1,0,1]
	v_pk_fma_f32 v[158:159], v[22:23], s[2:3], v[158:159] op_sel_hi:[1,0,1]
	v_pk_fma_f32 v[156:157], v[24:25], s[2:3], v[156:157] op_sel_hi:[1,0,1]
	v_pk_fma_f32 v[154:155], v[26:27], s[2:3], v[154:155] op_sel_hi:[1,0,1]
	v_pk_fma_f32 v[152:153], v[28:29], s[2:3], v[152:153] op_sel_hi:[1,0,1]
	v_pk_fma_f32 v[150:151], v[30:31], s[2:3], v[150:151] op_sel_hi:[1,0,1]
	v_readlane_b32 s2, v211, 15
	s_waitcnt vmcnt(16)
	v_cvt_scalef32_pk32_f32_fp6 v[0:31], v[44:49], 1.0
	v_pk_fma_f32 v[164:165], v[0:1], s[2:3], v[56:57] op_sel_hi:[1,0,1]
	v_pk_fma_f32 v[166:167], v[2:3], s[2:3], v[58:59] op_sel_hi:[1,0,1]
	v_pk_fma_f32 v[168:169], v[4:5], s[2:3], v[60:61] op_sel_hi:[1,0,1]
	v_pk_fma_f32 v[170:171], v[6:7], s[2:3], v[68:69] op_sel_hi:[1,0,1]
	v_pk_fma_f32 v[172:173], v[8:9], s[2:3], v[70:71] op_sel_hi:[1,0,1]
	v_pk_fma_f32 v[174:175], v[10:11], s[2:3], v[72:73] op_sel_hi:[1,0,1]
	v_pk_fma_f32 v[176:177], v[12:13], s[2:3], v[74:75] op_sel_hi:[1,0,1]
	v_pk_fma_f32 v[178:179], v[14:15], s[2:3], v[76:77] op_sel_hi:[1,0,1]
	v_pk_fma_f32 v[180:181], v[16:17], s[2:3], v[78:79] op_sel_hi:[1,0,1]
	v_pk_fma_f32 v[162:163], v[18:19], s[2:3], v[162:163] op_sel_hi:[1,0,1]
	v_pk_fma_f32 v[160:161], v[20:21], s[2:3], v[160:161] op_sel_hi:[1,0,1]
	v_pk_fma_f32 v[158:159], v[22:23], s[2:3], v[158:159] op_sel_hi:[1,0,1]
	v_pk_fma_f32 v[156:157], v[24:25], s[2:3], v[156:157] op_sel_hi:[1,0,1]
	v_pk_fma_f32 v[154:155], v[26:27], s[2:3], v[154:155] op_sel_hi:[1,0,1]
	v_pk_fma_f32 v[152:153], v[28:29], s[2:3], v[152:153] op_sel_hi:[1,0,1]
	v_pk_fma_f32 v[150:151], v[30:31], s[2:3], v[150:151] op_sel_hi:[1,0,1]
	v_readlane_b32 s2, v240, 24
	v_readlane_b32 s3, v240, 25
	v_readlane_b32 s100, v240, 26
	v_readlane_b32 s101, v240, 27
	s_nop 1
	buffer_load_dwordx4 v[74:77], v129, s[44:47], s2 offen sc1
	buffer_load_dwordx2 v[78:79], v210, s[44:47], s2 offen sc1
	buffer_load_dwordx4 v[68:71], v129, s[44:47], s3 offen sc1
	buffer_load_dwordx2 v[72:73], v210, s[44:47], s3 offen sc1
	buffer_load_dwordx4 v[56:59], v129, s[44:47], s100 offen sc1
	buffer_load_dwordx2 v[60:61], v210, s[44:47], s100 offen sc1
	buffer_load_dwordx4 v[44:47], v129, s[44:47], s101 offen sc1
	buffer_load_dwordx2 v[48:49], v210, s[44:47], s101 offen sc1
	v_readlane_b32 s2, v211, 16
	s_waitcnt vmcnt(22)
	v_cvt_scalef32_pk32_f32_fp6 v[0:31], v[62:67], 1.0
	v_pk_fma_f32 v[62:63], v[0:1], s[2:3], v[164:165] op_sel_hi:[1,0,1]
	v_pk_fma_f32 v[64:65], v[2:3], s[2:3], v[166:167] op_sel_hi:[1,0,1]
	v_pk_fma_f32 v[66:67], v[4:5], s[2:3], v[168:169] op_sel_hi:[1,0,1]
	v_pk_fma_f32 v[164:165], v[6:7], s[2:3], v[170:171] op_sel_hi:[1,0,1]
	v_pk_fma_f32 v[166:167], v[8:9], s[2:3], v[172:173] op_sel_hi:[1,0,1]
	v_pk_fma_f32 v[168:169], v[10:11], s[2:3], v[174:175] op_sel_hi:[1,0,1]
	v_pk_fma_f32 v[170:171], v[12:13], s[2:3], v[176:177] op_sel_hi:[1,0,1]
	v_pk_fma_f32 v[172:173], v[14:15], s[2:3], v[178:179] op_sel_hi:[1,0,1]
	v_pk_fma_f32 v[174:175], v[16:17], s[2:3], v[180:181] op_sel_hi:[1,0,1]
	v_pk_fma_f32 v[162:163], v[18:19], s[2:3], v[162:163] op_sel_hi:[1,0,1]
	v_pk_fma_f32 v[160:161], v[20:21], s[2:3], v[160:161] op_sel_hi:[1,0,1]
	v_pk_fma_f32 v[158:159], v[22:23], s[2:3], v[158:159] op_sel_hi:[1,0,1]
	v_pk_fma_f32 v[156:157], v[24:25], s[2:3], v[156:157] op_sel_hi:[1,0,1]
	v_pk_fma_f32 v[154:155], v[26:27], s[2:3], v[154:155] op_sel_hi:[1,0,1]
	v_pk_fma_f32 v[152:153], v[28:29], s[2:3], v[152:153] op_sel_hi:[1,0,1]
	v_pk_fma_f32 v[150:151], v[30:31], s[2:3], v[150:151] op_sel_hi:[1,0,1]
	v_readlane_b32 s2, v211, 17
	s_waitcnt vmcnt(20)
	v_cvt_scalef32_pk32_f32_fp6 v[0:31], v[50:55], 1.0
	v_pk_fma_f32 v[50:51], v[0:1], s[2:3], v[62:63] op_sel_hi:[1,0,1]
	v_pk_fma_f32 v[52:53], v[2:3], s[2:3], v[64:65] op_sel_hi:[1,0,1]
	v_pk_fma_f32 v[54:55], v[4:5], s[2:3], v[66:67] op_sel_hi:[1,0,1]
	v_pk_fma_f32 v[62:63], v[6:7], s[2:3], v[164:165] op_sel_hi:[1,0,1]
	v_pk_fma_f32 v[64:65], v[8:9], s[2:3], v[166:167] op_sel_hi:[1,0,1]
	v_pk_fma_f32 v[66:67], v[10:11], s[2:3], v[168:169] op_sel_hi:[1,0,1]
	v_pk_fma_f32 v[164:165], v[12:13], s[2:3], v[170:171] op_sel_hi:[1,0,1]
	v_pk_fma_f32 v[166:167], v[14:15], s[2:3], v[172:173] op_sel_hi:[1,0,1]
	v_pk_fma_f32 v[168:169], v[16:17], s[2:3], v[174:175] op_sel_hi:[1,0,1]
	v_pk_fma_f32 v[162:163], v[18:19], s[2:3], v[162:163] op_sel_hi:[1,0,1]
	v_pk_fma_f32 v[160:161], v[20:21], s[2:3], v[160:161] op_sel_hi:[1,0,1]
	v_pk_fma_f32 v[158:159], v[22:23], s[2:3], v[158:159] op_sel_hi:[1,0,1]
	v_pk_fma_f32 v[156:157], v[24:25], s[2:3], v[156:157] op_sel_hi:[1,0,1]
	v_pk_fma_f32 v[154:155], v[26:27], s[2:3], v[154:155] op_sel_hi:[1,0,1]
	v_pk_fma_f32 v[152:153], v[28:29], s[2:3], v[152:153] op_sel_hi:[1,0,1]
	v_pk_fma_f32 v[150:151], v[30:31], s[2:3], v[150:151] op_sel_hi:[1,0,1]
	v_readlane_b32 s2, v211, 18
	s_waitcnt vmcnt(18)
	v_cvt_scalef32_pk32_f32_fp6 v[0:31], v[38:43], 1.0
	v_pk_fma_f32 v[38:39], v[0:1], s[2:3], v[50:51] op_sel_hi:[1,0,1]
	v_pk_fma_f32 v[40:41], v[2:3], s[2:3], v[52:53] op_sel_hi:[1,0,1]
	v_pk_fma_f32 v[42:43], v[4:5], s[2:3], v[54:55] op_sel_hi:[1,0,1]
	v_pk_fma_f32 v[50:51], v[6:7], s[2:3], v[62:63] op_sel_hi:[1,0,1]
	v_pk_fma_f32 v[52:53], v[8:9], s[2:3], v[64:65] op_sel_hi:[1,0,1]
	v_pk_fma_f32 v[54:55], v[10:11], s[2:3], v[66:67] op_sel_hi:[1,0,1]
	v_pk_fma_f32 v[62:63], v[12:13], s[2:3], v[164:165] op_sel_hi:[1,0,1]
	v_pk_fma_f32 v[64:65], v[14:15], s[2:3], v[166:167] op_sel_hi:[1,0,1]
	v_pk_fma_f32 v[66:67], v[16:17], s[2:3], v[168:169] op_sel_hi:[1,0,1]
	v_pk_fma_f32 v[162:163], v[18:19], s[2:3], v[162:163] op_sel_hi:[1,0,1]
	v_pk_fma_f32 v[160:161], v[20:21], s[2:3], v[160:161] op_sel_hi:[1,0,1]
	v_pk_fma_f32 v[158:159], v[22:23], s[2:3], v[158:159] op_sel_hi:[1,0,1]
	v_pk_fma_f32 v[156:157], v[24:25], s[2:3], v[156:157] op_sel_hi:[1,0,1]
	v_pk_fma_f32 v[154:155], v[26:27], s[2:3], v[154:155] op_sel_hi:[1,0,1]
	v_pk_fma_f32 v[152:153], v[28:29], s[2:3], v[152:153] op_sel_hi:[1,0,1]
	v_pk_fma_f32 v[150:151], v[30:31], s[2:3], v[150:151] op_sel_hi:[1,0,1]
	v_readlane_b32 s2, v211, 19
	s_waitcnt vmcnt(16)
	v_cvt_scalef32_pk32_f32_fp6 v[0:31], v[32:37], 1.0
	v_pk_fma_f32 v[164:165], v[0:1], s[2:3], v[38:39] op_sel_hi:[1,0,1]
	v_pk_fma_f32 v[166:167], v[2:3], s[2:3], v[40:41] op_sel_hi:[1,0,1]
	v_pk_fma_f32 v[168:169], v[4:5], s[2:3], v[42:43] op_sel_hi:[1,0,1]
	v_pk_fma_f32 v[170:171], v[6:7], s[2:3], v[50:51] op_sel_hi:[1,0,1]
	v_pk_fma_f32 v[172:173], v[8:9], s[2:3], v[52:53] op_sel_hi:[1,0,1]
	v_pk_fma_f32 v[174:175], v[10:11], s[2:3], v[54:55] op_sel_hi:[1,0,1]
	v_pk_fma_f32 v[176:177], v[12:13], s[2:3], v[62:63] op_sel_hi:[1,0,1]
	v_pk_fma_f32 v[178:179], v[14:15], s[2:3], v[64:65] op_sel_hi:[1,0,1]
	v_pk_fma_f32 v[180:181], v[16:17], s[2:3], v[66:67] op_sel_hi:[1,0,1]
	v_pk_fma_f32 v[162:163], v[18:19], s[2:3], v[162:163] op_sel_hi:[1,0,1]
	v_pk_fma_f32 v[160:161], v[20:21], s[2:3], v[160:161] op_sel_hi:[1,0,1]
	v_pk_fma_f32 v[158:159], v[22:23], s[2:3], v[158:159] op_sel_hi:[1,0,1]
	v_pk_fma_f32 v[156:157], v[24:25], s[2:3], v[156:157] op_sel_hi:[1,0,1]
	v_pk_fma_f32 v[154:155], v[26:27], s[2:3], v[154:155] op_sel_hi:[1,0,1]
	v_pk_fma_f32 v[152:153], v[28:29], s[2:3], v[152:153] op_sel_hi:[1,0,1]
	v_pk_fma_f32 v[150:151], v[30:31], s[2:3], v[150:151] op_sel_hi:[1,0,1]
	v_readlane_b32 s2, v240, 28
	v_readlane_b32 s3, v240, 29
	v_readlane_b32 s100, v240, 30
	v_readlane_b32 s101, v240, 31
	s_nop 1
	buffer_load_dwordx4 v[62:65], v129, s[44:47], s2 offen sc1
	buffer_load_dwordx2 v[66:67], v210, s[44:47], s2 offen sc1
	buffer_load_dwordx4 v[50:53], v129, s[44:47], s3 offen sc1
	buffer_load_dwordx2 v[54:55], v210, s[44:47], s3 offen sc1
	buffer_load_dwordx4 v[38:41], v129, s[44:47], s100 offen sc1
	buffer_load_dwordx2 v[42:43], v210, s[44:47], s100 offen sc1
	buffer_load_dwordx4 v[32:35], v129, s[44:47], s101 offen sc1
	buffer_load_dwordx2 v[36:37], v210, s[44:47], s101 offen sc1
	v_readlane_b32 s2, v211, 20
	s_waitcnt vmcnt(22)
	v_cvt_scalef32_pk32_f32_fp6 v[0:31], v[98:103], 1.0
	v_pk_fma_f32 v[98:99], v[0:1], s[2:3], v[164:165] op_sel_hi:[1,0,1]
	v_pk_fma_f32 v[100:101], v[2:3], s[2:3], v[166:167] op_sel_hi:[1,0,1]
	v_pk_fma_f32 v[102:103], v[4:5], s[2:3], v[168:169] op_sel_hi:[1,0,1]
	v_pk_fma_f32 v[164:165], v[6:7], s[2:3], v[170:171] op_sel_hi:[1,0,1]
	v_pk_fma_f32 v[166:167], v[8:9], s[2:3], v[172:173] op_sel_hi:[1,0,1]
	v_pk_fma_f32 v[168:169], v[10:11], s[2:3], v[174:175] op_sel_hi:[1,0,1]
	v_pk_fma_f32 v[170:171], v[12:13], s[2:3], v[176:177] op_sel_hi:[1,0,1]
	v_pk_fma_f32 v[172:173], v[14:15], s[2:3], v[178:179] op_sel_hi:[1,0,1]
	v_pk_fma_f32 v[174:175], v[16:17], s[2:3], v[180:181] op_sel_hi:[1,0,1]
	v_pk_fma_f32 v[162:163], v[18:19], s[2:3], v[162:163] op_sel_hi:[1,0,1]
	v_pk_fma_f32 v[160:161], v[20:21], s[2:3], v[160:161] op_sel_hi:[1,0,1]
	v_pk_fma_f32 v[158:159], v[22:23], s[2:3], v[158:159] op_sel_hi:[1,0,1]
	v_pk_fma_f32 v[156:157], v[24:25], s[2:3], v[156:157] op_sel_hi:[1,0,1]
	v_pk_fma_f32 v[154:155], v[26:27], s[2:3], v[154:155] op_sel_hi:[1,0,1]
	v_pk_fma_f32 v[152:153], v[28:29], s[2:3], v[152:153] op_sel_hi:[1,0,1]
	v_pk_fma_f32 v[150:151], v[30:31], s[2:3], v[150:151] op_sel_hi:[1,0,1]
	v_readlane_b32 s2, v211, 21
	s_waitcnt vmcnt(20)
	v_cvt_scalef32_pk32_f32_fp6 v[0:31], v[92:97], 1.0
	v_pk_fma_f32 v[92:93], v[0:1], s[2:3], v[98:99] op_sel_hi:[1,0,1]
	v_pk_fma_f32 v[94:95], v[2:3], s[2:3], v[100:101] op_sel_hi:[1,0,1]
	v_pk_fma_f32 v[96:97], v[4:5], s[2:3], v[102:103] op_sel_hi:[1,0,1]
	v_pk_fma_f32 v[98:99], v[6:7], s[2:3], v[164:165] op_sel_hi:[1,0,1]
	v_pk_fma_f32 v[100:101], v[8:9], s[2:3], v[166:167] op_sel_hi:[1,0,1]
	v_pk_fma_f32 v[102:103], v[10:11], s[2:3], v[168:169] op_sel_hi:[1,0,1]
	v_pk_fma_f32 v[164:165], v[12:13], s[2:3], v[170:171] op_sel_hi:[1,0,1]
	v_pk_fma_f32 v[166:167], v[14:15], s[2:3], v[172:173] op_sel_hi:[1,0,1]
	v_pk_fma_f32 v[168:169], v[16:17], s[2:3], v[174:175] op_sel_hi:[1,0,1]
	v_pk_fma_f32 v[162:163], v[18:19], s[2:3], v[162:163] op_sel_hi:[1,0,1]
	v_pk_fma_f32 v[160:161], v[20:21], s[2:3], v[160:161] op_sel_hi:[1,0,1]
	v_pk_fma_f32 v[158:159], v[22:23], s[2:3], v[158:159] op_sel_hi:[1,0,1]
	v_pk_fma_f32 v[156:157], v[24:25], s[2:3], v[156:157] op_sel_hi:[1,0,1]
	v_pk_fma_f32 v[154:155], v[26:27], s[2:3], v[154:155] op_sel_hi:[1,0,1]
	v_pk_fma_f32 v[152:153], v[28:29], s[2:3], v[152:153] op_sel_hi:[1,0,1]
	v_pk_fma_f32 v[150:151], v[30:31], s[2:3], v[150:151] op_sel_hi:[1,0,1]
	v_readlane_b32 s2, v211, 22
	s_waitcnt vmcnt(18)
	v_cvt_scalef32_pk32_f32_fp6 v[0:31], v[86:91], 1.0
	v_pk_fma_f32 v[86:87], v[0:1], s[2:3], v[92:93] op_sel_hi:[1,0,1]
	v_pk_fma_f32 v[88:89], v[2:3], s[2:3], v[94:95] op_sel_hi:[1,0,1]
	v_pk_fma_f32 v[90:91], v[4:5], s[2:3], v[96:97] op_sel_hi:[1,0,1]
	v_pk_fma_f32 v[92:93], v[6:7], s[2:3], v[98:99] op_sel_hi:[1,0,1]
	v_pk_fma_f32 v[94:95], v[8:9], s[2:3], v[100:101] op_sel_hi:[1,0,1]
	v_pk_fma_f32 v[96:97], v[10:11], s[2:3], v[102:103] op_sel_hi:[1,0,1]
	v_pk_fma_f32 v[98:99], v[12:13], s[2:3], v[164:165] op_sel_hi:[1,0,1]
	v_pk_fma_f32 v[100:101], v[14:15], s[2:3], v[166:167] op_sel_hi:[1,0,1]
	v_pk_fma_f32 v[102:103], v[16:17], s[2:3], v[168:169] op_sel_hi:[1,0,1]
	v_pk_fma_f32 v[162:163], v[18:19], s[2:3], v[162:163] op_sel_hi:[1,0,1]
	v_pk_fma_f32 v[160:161], v[20:21], s[2:3], v[160:161] op_sel_hi:[1,0,1]
	v_pk_fma_f32 v[158:159], v[22:23], s[2:3], v[158:159] op_sel_hi:[1,0,1]
	v_pk_fma_f32 v[156:157], v[24:25], s[2:3], v[156:157] op_sel_hi:[1,0,1]
	v_pk_fma_f32 v[154:155], v[26:27], s[2:3], v[154:155] op_sel_hi:[1,0,1]
	v_pk_fma_f32 v[152:153], v[28:29], s[2:3], v[152:153] op_sel_hi:[1,0,1]
	v_pk_fma_f32 v[150:151], v[30:31], s[2:3], v[150:151] op_sel_hi:[1,0,1]
	v_readlane_b32 s2, v211, 23
	s_waitcnt vmcnt(16)
	v_cvt_scalef32_pk32_f32_fp6 v[0:31], v[80:85], 1.0
	v_pk_fma_f32 v[180:181], v[0:1], s[2:3], v[86:87] op_sel_hi:[1,0,1]
	v_pk_fma_f32 v[178:179], v[2:3], s[2:3], v[88:89] op_sel_hi:[1,0,1]
	v_pk_fma_f32 v[176:177], v[4:5], s[2:3], v[90:91] op_sel_hi:[1,0,1]
	v_pk_fma_f32 v[174:175], v[6:7], s[2:3], v[92:93] op_sel_hi:[1,0,1]
	v_pk_fma_f32 v[172:173], v[8:9], s[2:3], v[94:95] op_sel_hi:[1,0,1]
	v_pk_fma_f32 v[170:171], v[10:11], s[2:3], v[96:97] op_sel_hi:[1,0,1]
	v_pk_fma_f32 v[168:169], v[12:13], s[2:3], v[98:99] op_sel_hi:[1,0,1]
	v_pk_fma_f32 v[166:167], v[14:15], s[2:3], v[100:101] op_sel_hi:[1,0,1]
	v_pk_fma_f32 v[164:165], v[16:17], s[2:3], v[102:103] op_sel_hi:[1,0,1]
	v_pk_fma_f32 v[162:163], v[18:19], s[2:3], v[162:163] op_sel_hi:[1,0,1]
	v_pk_fma_f32 v[160:161], v[20:21], s[2:3], v[160:161] op_sel_hi:[1,0,1]
	v_pk_fma_f32 v[158:159], v[22:23], s[2:3], v[158:159] op_sel_hi:[1,0,1]
	v_pk_fma_f32 v[156:157], v[24:25], s[2:3], v[156:157] op_sel_hi:[1,0,1]
	v_pk_fma_f32 v[154:155], v[26:27], s[2:3], v[154:155] op_sel_hi:[1,0,1]
	v_pk_fma_f32 v[152:153], v[28:29], s[2:3], v[152:153] op_sel_hi:[1,0,1]
	v_pk_fma_f32 v[150:151], v[30:31], s[2:3], v[150:151] op_sel_hi:[1,0,1]
	v_readlane_b32 s2, v240, 32
	v_readlane_b32 s3, v240, 33
	v_readlane_b32 s100, v240, 34
	v_readlane_b32 s101, v240, 35
	s_nop 1
	buffer_load_dwordx4 v[98:101], v129, s[44:47], s2 offen sc1
	buffer_load_dwordx2 v[102:103], v210, s[44:47], s2 offen sc1
	buffer_load_dwordx4 v[92:95], v129, s[44:47], s3 offen sc1
	buffer_load_dwordx2 v[96:97], v210, s[44:47], s3 offen sc1
	buffer_load_dwordx4 v[86:89], v129, s[44:47], s100 offen sc1
	buffer_load_dwordx2 v[90:91], v210, s[44:47], s100 offen sc1
	buffer_load_dwordx4 v[80:83], v129, s[44:47], s101 offen sc1
	buffer_load_dwordx2 v[84:85], v210, s[44:47], s101 offen sc1
	v_readlane_b32 s2, v211, 24
	s_waitcnt vmcnt(22)
	v_cvt_scalef32_pk32_f32_fp6 v[0:31], v[74:79], 1.0
	v_pk_fma_f32 v[74:75], v[0:1], s[2:3], v[180:181] op_sel_hi:[1,0,1]
	v_pk_fma_f32 v[76:77], v[2:3], s[2:3], v[178:179] op_sel_hi:[1,0,1]
	v_pk_fma_f32 v[78:79], v[4:5], s[2:3], v[176:177] op_sel_hi:[1,0,1]
	v_pk_fma_f32 v[174:175], v[6:7], s[2:3], v[174:175] op_sel_hi:[1,0,1]
	v_pk_fma_f32 v[172:173], v[8:9], s[2:3], v[172:173] op_sel_hi:[1,0,1]
	v_pk_fma_f32 v[170:171], v[10:11], s[2:3], v[170:171] op_sel_hi:[1,0,1]
	v_pk_fma_f32 v[168:169], v[12:13], s[2:3], v[168:169] op_sel_hi:[1,0,1]
	v_pk_fma_f32 v[166:167], v[14:15], s[2:3], v[166:167] op_sel_hi:[1,0,1]
	v_pk_fma_f32 v[164:165], v[16:17], s[2:3], v[164:165] op_sel_hi:[1,0,1]
	v_pk_fma_f32 v[162:163], v[18:19], s[2:3], v[162:163] op_sel_hi:[1,0,1]
	v_pk_fma_f32 v[160:161], v[20:21], s[2:3], v[160:161] op_sel_hi:[1,0,1]
	v_pk_fma_f32 v[158:159], v[22:23], s[2:3], v[158:159] op_sel_hi:[1,0,1]
	v_pk_fma_f32 v[156:157], v[24:25], s[2:3], v[156:157] op_sel_hi:[1,0,1]
	v_pk_fma_f32 v[154:155], v[26:27], s[2:3], v[154:155] op_sel_hi:[1,0,1]
	v_pk_fma_f32 v[152:153], v[28:29], s[2:3], v[152:153] op_sel_hi:[1,0,1]
	v_pk_fma_f32 v[150:151], v[30:31], s[2:3], v[150:151] op_sel_hi:[1,0,1]
	v_readlane_b32 s2, v211, 25
	s_waitcnt vmcnt(20)
	v_cvt_scalef32_pk32_f32_fp6 v[0:31], v[68:73], 1.0
	v_pk_fma_f32 v[68:69], v[0:1], s[2:3], v[74:75] op_sel_hi:[1,0,1]
	v_pk_fma_f32 v[70:71], v[2:3], s[2:3], v[76:77] op_sel_hi:[1,0,1]
	v_pk_fma_f32 v[72:73], v[4:5], s[2:3], v[78:79] op_sel_hi:[1,0,1]
	v_pk_fma_f32 v[74:75], v[6:7], s[2:3], v[174:175] op_sel_hi:[1,0,1]
	v_pk_fma_f32 v[76:77], v[8:9], s[2:3], v[172:173] op_sel_hi:[1,0,1]
	v_pk_fma_f32 v[78:79], v[10:11], s[2:3], v[170:171] op_sel_hi:[1,0,1]
	v_pk_fma_f32 v[168:169], v[12:13], s[2:3], v[168:169] op_sel_hi:[1,0,1]
	v_pk_fma_f32 v[166:167], v[14:15], s[2:3], v[166:167] op_sel_hi:[1,0,1]
	v_pk_fma_f32 v[164:165], v[16:17], s[2:3], v[164:165] op_sel_hi:[1,0,1]
	v_pk_fma_f32 v[162:163], v[18:19], s[2:3], v[162:163] op_sel_hi:[1,0,1]
	v_pk_fma_f32 v[160:161], v[20:21], s[2:3], v[160:161] op_sel_hi:[1,0,1]
	v_pk_fma_f32 v[158:159], v[22:23], s[2:3], v[158:159] op_sel_hi:[1,0,1]
	v_pk_fma_f32 v[156:157], v[24:25], s[2:3], v[156:157] op_sel_hi:[1,0,1]
	v_pk_fma_f32 v[154:155], v[26:27], s[2:3], v[154:155] op_sel_hi:[1,0,1]
	v_pk_fma_f32 v[152:153], v[28:29], s[2:3], v[152:153] op_sel_hi:[1,0,1]
	v_pk_fma_f32 v[150:151], v[30:31], s[2:3], v[150:151] op_sel_hi:[1,0,1]
	v_readlane_b32 s2, v211, 26
	s_waitcnt vmcnt(18)
	v_cvt_scalef32_pk32_f32_fp6 v[0:31], v[56:61], 1.0
	v_pk_fma_f32 v[56:57], v[0:1], s[2:3], v[68:69] op_sel_hi:[1,0,1]
	v_pk_fma_f32 v[58:59], v[2:3], s[2:3], v[70:71] op_sel_hi:[1,0,1]
	v_pk_fma_f32 v[60:61], v[4:5], s[2:3], v[72:73] op_sel_hi:[1,0,1]
	v_pk_fma_f32 v[68:69], v[6:7], s[2:3], v[74:75] op_sel_hi:[1,0,1]
	v_pk_fma_f32 v[70:71], v[8:9], s[2:3], v[76:77] op_sel_hi:[1,0,1]
	v_pk_fma_f32 v[72:73], v[10:11], s[2:3], v[78:79] op_sel_hi:[1,0,1]
	v_pk_fma_f32 v[74:75], v[12:13], s[2:3], v[168:169] op_sel_hi:[1,0,1]
	v_pk_fma_f32 v[76:77], v[14:15], s[2:3], v[166:167] op_sel_hi:[1,0,1]
	v_pk_fma_f32 v[78:79], v[16:17], s[2:3], v[164:165] op_sel_hi:[1,0,1]
	v_pk_fma_f32 v[162:163], v[18:19], s[2:3], v[162:163] op_sel_hi:[1,0,1]
	v_pk_fma_f32 v[160:161], v[20:21], s[2:3], v[160:161] op_sel_hi:[1,0,1]
	v_pk_fma_f32 v[158:159], v[22:23], s[2:3], v[158:159] op_sel_hi:[1,0,1]
	v_pk_fma_f32 v[156:157], v[24:25], s[2:3], v[156:157] op_sel_hi:[1,0,1]
	v_pk_fma_f32 v[154:155], v[26:27], s[2:3], v[154:155] op_sel_hi:[1,0,1]
	v_pk_fma_f32 v[152:153], v[28:29], s[2:3], v[152:153] op_sel_hi:[1,0,1]
	v_pk_fma_f32 v[150:151], v[30:31], s[2:3], v[150:151] op_sel_hi:[1,0,1]
	v_readlane_b32 s2, v211, 27
	s_waitcnt vmcnt(16)
	v_cvt_scalef32_pk32_f32_fp6 v[0:31], v[44:49], 1.0
	v_pk_fma_f32 v[164:165], v[0:1], s[2:3], v[56:57] op_sel_hi:[1,0,1]
	v_pk_fma_f32 v[166:167], v[2:3], s[2:3], v[58:59] op_sel_hi:[1,0,1]
	v_pk_fma_f32 v[168:169], v[4:5], s[2:3], v[60:61] op_sel_hi:[1,0,1]
	v_pk_fma_f32 v[170:171], v[6:7], s[2:3], v[68:69] op_sel_hi:[1,0,1]
	v_pk_fma_f32 v[172:173], v[8:9], s[2:3], v[70:71] op_sel_hi:[1,0,1]
	v_pk_fma_f32 v[174:175], v[10:11], s[2:3], v[72:73] op_sel_hi:[1,0,1]
	v_pk_fma_f32 v[176:177], v[12:13], s[2:3], v[74:75] op_sel_hi:[1,0,1]
	v_pk_fma_f32 v[178:179], v[14:15], s[2:3], v[76:77] op_sel_hi:[1,0,1]
	v_pk_fma_f32 v[180:181], v[16:17], s[2:3], v[78:79] op_sel_hi:[1,0,1]
	v_pk_fma_f32 v[162:163], v[18:19], s[2:3], v[162:163] op_sel_hi:[1,0,1]
	v_pk_fma_f32 v[160:161], v[20:21], s[2:3], v[160:161] op_sel_hi:[1,0,1]
	v_pk_fma_f32 v[158:159], v[22:23], s[2:3], v[158:159] op_sel_hi:[1,0,1]
	v_pk_fma_f32 v[156:157], v[24:25], s[2:3], v[156:157] op_sel_hi:[1,0,1]
	v_pk_fma_f32 v[154:155], v[26:27], s[2:3], v[154:155] op_sel_hi:[1,0,1]
	v_pk_fma_f32 v[152:153], v[28:29], s[2:3], v[152:153] op_sel_hi:[1,0,1]
	v_pk_fma_f32 v[150:151], v[30:31], s[2:3], v[150:151] op_sel_hi:[1,0,1]
	v_readlane_b32 s2, v240, 36
	v_readlane_b32 s3, v240, 37
	v_readlane_b32 s100, v240, 38
	v_readlane_b32 s101, v240, 39
	s_nop 1
	buffer_load_dwordx4 v[74:77], v129, s[44:47], s2 offen sc1
	buffer_load_dwordx2 v[78:79], v210, s[44:47], s2 offen sc1
	buffer_load_dwordx4 v[68:71], v129, s[44:47], s3 offen sc1
	buffer_load_dwordx2 v[72:73], v210, s[44:47], s3 offen sc1
	buffer_load_dwordx4 v[56:59], v129, s[44:47], s100 offen sc1
	buffer_load_dwordx2 v[60:61], v210, s[44:47], s100 offen sc1
	buffer_load_dwordx4 v[44:47], v129, s[44:47], s101 offen sc1
	buffer_load_dwordx2 v[48:49], v210, s[44:47], s101 offen sc1
	v_readlane_b32 s2, v211, 28
	s_waitcnt vmcnt(22)
	v_cvt_scalef32_pk32_f32_fp6 v[0:31], v[62:67], 1.0
	v_pk_fma_f32 v[62:63], v[0:1], s[2:3], v[164:165] op_sel_hi:[1,0,1]
	v_pk_fma_f32 v[64:65], v[2:3], s[2:3], v[166:167] op_sel_hi:[1,0,1]
	v_pk_fma_f32 v[66:67], v[4:5], s[2:3], v[168:169] op_sel_hi:[1,0,1]
	v_pk_fma_f32 v[164:165], v[6:7], s[2:3], v[170:171] op_sel_hi:[1,0,1]
	v_pk_fma_f32 v[166:167], v[8:9], s[2:3], v[172:173] op_sel_hi:[1,0,1]
	v_pk_fma_f32 v[168:169], v[10:11], s[2:3], v[174:175] op_sel_hi:[1,0,1]
	v_pk_fma_f32 v[170:171], v[12:13], s[2:3], v[176:177] op_sel_hi:[1,0,1]
	v_pk_fma_f32 v[172:173], v[14:15], s[2:3], v[178:179] op_sel_hi:[1,0,1]
	v_pk_fma_f32 v[174:175], v[16:17], s[2:3], v[180:181] op_sel_hi:[1,0,1]
	v_pk_fma_f32 v[162:163], v[18:19], s[2:3], v[162:163] op_sel_hi:[1,0,1]
	v_pk_fma_f32 v[160:161], v[20:21], s[2:3], v[160:161] op_sel_hi:[1,0,1]
	v_pk_fma_f32 v[158:159], v[22:23], s[2:3], v[158:159] op_sel_hi:[1,0,1]
	v_pk_fma_f32 v[156:157], v[24:25], s[2:3], v[156:157] op_sel_hi:[1,0,1]
	v_pk_fma_f32 v[154:155], v[26:27], s[2:3], v[154:155] op_sel_hi:[1,0,1]
	v_pk_fma_f32 v[152:153], v[28:29], s[2:3], v[152:153] op_sel_hi:[1,0,1]
	v_pk_fma_f32 v[150:151], v[30:31], s[2:3], v[150:151] op_sel_hi:[1,0,1]
	v_readlane_b32 s2, v211, 29
	s_waitcnt vmcnt(20)
	v_cvt_scalef32_pk32_f32_fp6 v[0:31], v[50:55], 1.0
	v_pk_fma_f32 v[50:51], v[0:1], s[2:3], v[62:63] op_sel_hi:[1,0,1]
	v_pk_fma_f32 v[52:53], v[2:3], s[2:3], v[64:65] op_sel_hi:[1,0,1]
	v_pk_fma_f32 v[54:55], v[4:5], s[2:3], v[66:67] op_sel_hi:[1,0,1]
	v_pk_fma_f32 v[62:63], v[6:7], s[2:3], v[164:165] op_sel_hi:[1,0,1]
	v_pk_fma_f32 v[64:65], v[8:9], s[2:3], v[166:167] op_sel_hi:[1,0,1]
	v_pk_fma_f32 v[66:67], v[10:11], s[2:3], v[168:169] op_sel_hi:[1,0,1]
	v_pk_fma_f32 v[164:165], v[12:13], s[2:3], v[170:171] op_sel_hi:[1,0,1]
	v_pk_fma_f32 v[166:167], v[14:15], s[2:3], v[172:173] op_sel_hi:[1,0,1]
	v_pk_fma_f32 v[168:169], v[16:17], s[2:3], v[174:175] op_sel_hi:[1,0,1]
	v_pk_fma_f32 v[162:163], v[18:19], s[2:3], v[162:163] op_sel_hi:[1,0,1]
	v_pk_fma_f32 v[160:161], v[20:21], s[2:3], v[160:161] op_sel_hi:[1,0,1]
	v_pk_fma_f32 v[158:159], v[22:23], s[2:3], v[158:159] op_sel_hi:[1,0,1]
	v_pk_fma_f32 v[156:157], v[24:25], s[2:3], v[156:157] op_sel_hi:[1,0,1]
	v_pk_fma_f32 v[154:155], v[26:27], s[2:3], v[154:155] op_sel_hi:[1,0,1]
	v_pk_fma_f32 v[152:153], v[28:29], s[2:3], v[152:153] op_sel_hi:[1,0,1]
	v_pk_fma_f32 v[150:151], v[30:31], s[2:3], v[150:151] op_sel_hi:[1,0,1]
	v_readlane_b32 s2, v211, 30
	s_waitcnt vmcnt(18)
	v_cvt_scalef32_pk32_f32_fp6 v[0:31], v[38:43], 1.0
	v_pk_fma_f32 v[38:39], v[0:1], s[2:3], v[50:51] op_sel_hi:[1,0,1]
	v_pk_fma_f32 v[40:41], v[2:3], s[2:3], v[52:53] op_sel_hi:[1,0,1]
	v_pk_fma_f32 v[42:43], v[4:5], s[2:3], v[54:55] op_sel_hi:[1,0,1]
	v_pk_fma_f32 v[50:51], v[6:7], s[2:3], v[62:63] op_sel_hi:[1,0,1]
	v_pk_fma_f32 v[52:53], v[8:9], s[2:3], v[64:65] op_sel_hi:[1,0,1]
	v_pk_fma_f32 v[54:55], v[10:11], s[2:3], v[66:67] op_sel_hi:[1,0,1]
	v_pk_fma_f32 v[62:63], v[12:13], s[2:3], v[164:165] op_sel_hi:[1,0,1]
	v_pk_fma_f32 v[64:65], v[14:15], s[2:3], v[166:167] op_sel_hi:[1,0,1]
	v_pk_fma_f32 v[66:67], v[16:17], s[2:3], v[168:169] op_sel_hi:[1,0,1]
	v_pk_fma_f32 v[162:163], v[18:19], s[2:3], v[162:163] op_sel_hi:[1,0,1]
	v_pk_fma_f32 v[160:161], v[20:21], s[2:3], v[160:161] op_sel_hi:[1,0,1]
	v_pk_fma_f32 v[158:159], v[22:23], s[2:3], v[158:159] op_sel_hi:[1,0,1]
	v_pk_fma_f32 v[156:157], v[24:25], s[2:3], v[156:157] op_sel_hi:[1,0,1]
	v_pk_fma_f32 v[154:155], v[26:27], s[2:3], v[154:155] op_sel_hi:[1,0,1]
	v_pk_fma_f32 v[152:153], v[28:29], s[2:3], v[152:153] op_sel_hi:[1,0,1]
	v_pk_fma_f32 v[150:151], v[30:31], s[2:3], v[150:151] op_sel_hi:[1,0,1]
	v_readlane_b32 s2, v211, 31
	s_waitcnt vmcnt(16)
	v_cvt_scalef32_pk32_f32_fp6 v[0:31], v[32:37], 1.0
	v_pk_fma_f32 v[164:165], v[0:1], s[2:3], v[38:39] op_sel_hi:[1,0,1]
	v_pk_fma_f32 v[166:167], v[2:3], s[2:3], v[40:41] op_sel_hi:[1,0,1]
	v_pk_fma_f32 v[168:169], v[4:5], s[2:3], v[42:43] op_sel_hi:[1,0,1]
	v_pk_fma_f32 v[170:171], v[6:7], s[2:3], v[50:51] op_sel_hi:[1,0,1]
	v_pk_fma_f32 v[172:173], v[8:9], s[2:3], v[52:53] op_sel_hi:[1,0,1]
	v_pk_fma_f32 v[174:175], v[10:11], s[2:3], v[54:55] op_sel_hi:[1,0,1]
	v_pk_fma_f32 v[176:177], v[12:13], s[2:3], v[62:63] op_sel_hi:[1,0,1]
	v_pk_fma_f32 v[178:179], v[14:15], s[2:3], v[64:65] op_sel_hi:[1,0,1]
	v_pk_fma_f32 v[180:181], v[16:17], s[2:3], v[66:67] op_sel_hi:[1,0,1]
	v_pk_fma_f32 v[162:163], v[18:19], s[2:3], v[162:163] op_sel_hi:[1,0,1]
	v_pk_fma_f32 v[160:161], v[20:21], s[2:3], v[160:161] op_sel_hi:[1,0,1]
	v_pk_fma_f32 v[158:159], v[22:23], s[2:3], v[158:159] op_sel_hi:[1,0,1]
	v_pk_fma_f32 v[156:157], v[24:25], s[2:3], v[156:157] op_sel_hi:[1,0,1]
	v_pk_fma_f32 v[154:155], v[26:27], s[2:3], v[154:155] op_sel_hi:[1,0,1]
	v_pk_fma_f32 v[152:153], v[28:29], s[2:3], v[152:153] op_sel_hi:[1,0,1]
	v_pk_fma_f32 v[150:151], v[30:31], s[2:3], v[150:151] op_sel_hi:[1,0,1]
	v_readlane_b32 s2, v240, 40
	v_readlane_b32 s3, v240, 41
	v_readlane_b32 s100, v240, 42
	v_readlane_b32 s101, v240, 43
	s_nop 1
	buffer_load_dwordx4 v[62:65], v129, s[44:47], s2 offen sc1
	buffer_load_dwordx2 v[66:67], v210, s[44:47], s2 offen sc1
	buffer_load_dwordx4 v[50:53], v129, s[44:47], s3 offen sc1
	buffer_load_dwordx2 v[54:55], v210, s[44:47], s3 offen sc1
	buffer_load_dwordx4 v[38:41], v129, s[44:47], s100 offen sc1
	buffer_load_dwordx2 v[42:43], v210, s[44:47], s100 offen sc1
	buffer_load_dwordx4 v[32:35], v129, s[44:47], s101 offen sc1
	buffer_load_dwordx2 v[36:37], v210, s[44:47], s101 offen sc1
	v_readlane_b32 s2, v211, 32
	s_waitcnt vmcnt(22)
	v_cvt_scalef32_pk32_f32_fp6 v[0:31], v[98:103], 1.0
	v_pk_fma_f32 v[98:99], v[0:1], s[2:3], v[164:165] op_sel_hi:[1,0,1]
	v_pk_fma_f32 v[100:101], v[2:3], s[2:3], v[166:167] op_sel_hi:[1,0,1]
	v_pk_fma_f32 v[102:103], v[4:5], s[2:3], v[168:169] op_sel_hi:[1,0,1]
	v_pk_fma_f32 v[164:165], v[6:7], s[2:3], v[170:171] op_sel_hi:[1,0,1]
	v_pk_fma_f32 v[166:167], v[8:9], s[2:3], v[172:173] op_sel_hi:[1,0,1]
	v_pk_fma_f32 v[168:169], v[10:11], s[2:3], v[174:175] op_sel_hi:[1,0,1]
	v_pk_fma_f32 v[170:171], v[12:13], s[2:3], v[176:177] op_sel_hi:[1,0,1]
	v_pk_fma_f32 v[172:173], v[14:15], s[2:3], v[178:179] op_sel_hi:[1,0,1]
	v_pk_fma_f32 v[174:175], v[16:17], s[2:3], v[180:181] op_sel_hi:[1,0,1]
	v_pk_fma_f32 v[162:163], v[18:19], s[2:3], v[162:163] op_sel_hi:[1,0,1]
	v_pk_fma_f32 v[160:161], v[20:21], s[2:3], v[160:161] op_sel_hi:[1,0,1]
	v_pk_fma_f32 v[158:159], v[22:23], s[2:3], v[158:159] op_sel_hi:[1,0,1]
	v_pk_fma_f32 v[156:157], v[24:25], s[2:3], v[156:157] op_sel_hi:[1,0,1]
	v_pk_fma_f32 v[154:155], v[26:27], s[2:3], v[154:155] op_sel_hi:[1,0,1]
	v_pk_fma_f32 v[152:153], v[28:29], s[2:3], v[152:153] op_sel_hi:[1,0,1]
	v_pk_fma_f32 v[150:151], v[30:31], s[2:3], v[150:151] op_sel_hi:[1,0,1]
	v_readlane_b32 s2, v211, 33
	s_waitcnt vmcnt(20)
	v_cvt_scalef32_pk32_f32_fp6 v[0:31], v[92:97], 1.0
	v_pk_fma_f32 v[92:93], v[0:1], s[2:3], v[98:99] op_sel_hi:[1,0,1]
	v_pk_fma_f32 v[94:95], v[2:3], s[2:3], v[100:101] op_sel_hi:[1,0,1]
	v_pk_fma_f32 v[96:97], v[4:5], s[2:3], v[102:103] op_sel_hi:[1,0,1]
	v_pk_fma_f32 v[98:99], v[6:7], s[2:3], v[164:165] op_sel_hi:[1,0,1]
	v_pk_fma_f32 v[100:101], v[8:9], s[2:3], v[166:167] op_sel_hi:[1,0,1]
	v_pk_fma_f32 v[102:103], v[10:11], s[2:3], v[168:169] op_sel_hi:[1,0,1]
	v_pk_fma_f32 v[164:165], v[12:13], s[2:3], v[170:171] op_sel_hi:[1,0,1]
	v_pk_fma_f32 v[166:167], v[14:15], s[2:3], v[172:173] op_sel_hi:[1,0,1]
	v_pk_fma_f32 v[168:169], v[16:17], s[2:3], v[174:175] op_sel_hi:[1,0,1]
	v_pk_fma_f32 v[162:163], v[18:19], s[2:3], v[162:163] op_sel_hi:[1,0,1]
	v_pk_fma_f32 v[160:161], v[20:21], s[2:3], v[160:161] op_sel_hi:[1,0,1]
	v_pk_fma_f32 v[158:159], v[22:23], s[2:3], v[158:159] op_sel_hi:[1,0,1]
	v_pk_fma_f32 v[156:157], v[24:25], s[2:3], v[156:157] op_sel_hi:[1,0,1]
	v_pk_fma_f32 v[154:155], v[26:27], s[2:3], v[154:155] op_sel_hi:[1,0,1]
	v_pk_fma_f32 v[152:153], v[28:29], s[2:3], v[152:153] op_sel_hi:[1,0,1]
	v_pk_fma_f32 v[150:151], v[30:31], s[2:3], v[150:151] op_sel_hi:[1,0,1]
	v_readlane_b32 s2, v211, 34
	s_waitcnt vmcnt(18)
	v_cvt_scalef32_pk32_f32_fp6 v[0:31], v[86:91], 1.0
	v_pk_fma_f32 v[86:87], v[0:1], s[2:3], v[92:93] op_sel_hi:[1,0,1]
	v_pk_fma_f32 v[88:89], v[2:3], s[2:3], v[94:95] op_sel_hi:[1,0,1]
	v_pk_fma_f32 v[90:91], v[4:5], s[2:3], v[96:97] op_sel_hi:[1,0,1]
	v_pk_fma_f32 v[92:93], v[6:7], s[2:3], v[98:99] op_sel_hi:[1,0,1]
	v_pk_fma_f32 v[94:95], v[8:9], s[2:3], v[100:101] op_sel_hi:[1,0,1]
	v_pk_fma_f32 v[96:97], v[10:11], s[2:3], v[102:103] op_sel_hi:[1,0,1]
	v_pk_fma_f32 v[98:99], v[12:13], s[2:3], v[164:165] op_sel_hi:[1,0,1]
	v_pk_fma_f32 v[100:101], v[14:15], s[2:3], v[166:167] op_sel_hi:[1,0,1]
	v_pk_fma_f32 v[102:103], v[16:17], s[2:3], v[168:169] op_sel_hi:[1,0,1]
	v_pk_fma_f32 v[162:163], v[18:19], s[2:3], v[162:163] op_sel_hi:[1,0,1]
	v_pk_fma_f32 v[160:161], v[20:21], s[2:3], v[160:161] op_sel_hi:[1,0,1]
	v_pk_fma_f32 v[158:159], v[22:23], s[2:3], v[158:159] op_sel_hi:[1,0,1]
	v_pk_fma_f32 v[156:157], v[24:25], s[2:3], v[156:157] op_sel_hi:[1,0,1]
	v_pk_fma_f32 v[154:155], v[26:27], s[2:3], v[154:155] op_sel_hi:[1,0,1]
	v_pk_fma_f32 v[152:153], v[28:29], s[2:3], v[152:153] op_sel_hi:[1,0,1]
	v_pk_fma_f32 v[150:151], v[30:31], s[2:3], v[150:151] op_sel_hi:[1,0,1]
	v_readlane_b32 s2, v211, 35
	s_waitcnt vmcnt(16)
	v_cvt_scalef32_pk32_f32_fp6 v[0:31], v[80:85], 1.0
	v_pk_fma_f32 v[180:181], v[0:1], s[2:3], v[86:87] op_sel_hi:[1,0,1]
	v_pk_fma_f32 v[178:179], v[2:3], s[2:3], v[88:89] op_sel_hi:[1,0,1]
	v_pk_fma_f32 v[176:177], v[4:5], s[2:3], v[90:91] op_sel_hi:[1,0,1]
	v_pk_fma_f32 v[174:175], v[6:7], s[2:3], v[92:93] op_sel_hi:[1,0,1]
	v_pk_fma_f32 v[172:173], v[8:9], s[2:3], v[94:95] op_sel_hi:[1,0,1]
	v_pk_fma_f32 v[170:171], v[10:11], s[2:3], v[96:97] op_sel_hi:[1,0,1]
	v_pk_fma_f32 v[168:169], v[12:13], s[2:3], v[98:99] op_sel_hi:[1,0,1]
	v_pk_fma_f32 v[166:167], v[14:15], s[2:3], v[100:101] op_sel_hi:[1,0,1]
	v_pk_fma_f32 v[164:165], v[16:17], s[2:3], v[102:103] op_sel_hi:[1,0,1]
	v_pk_fma_f32 v[162:163], v[18:19], s[2:3], v[162:163] op_sel_hi:[1,0,1]
	v_pk_fma_f32 v[160:161], v[20:21], s[2:3], v[160:161] op_sel_hi:[1,0,1]
	v_pk_fma_f32 v[158:159], v[22:23], s[2:3], v[158:159] op_sel_hi:[1,0,1]
	v_pk_fma_f32 v[156:157], v[24:25], s[2:3], v[156:157] op_sel_hi:[1,0,1]
	v_pk_fma_f32 v[154:155], v[26:27], s[2:3], v[154:155] op_sel_hi:[1,0,1]
	v_pk_fma_f32 v[152:153], v[28:29], s[2:3], v[152:153] op_sel_hi:[1,0,1]
	v_pk_fma_f32 v[150:151], v[30:31], s[2:3], v[150:151] op_sel_hi:[1,0,1]
	v_readlane_b32 s2, v240, 44
	v_readlane_b32 s3, v240, 45
	v_readlane_b32 s100, v240, 46
	v_readlane_b32 s101, v240, 47
	s_nop 1
	buffer_load_dwordx4 v[98:101], v129, s[44:47], s2 offen sc1
	buffer_load_dwordx2 v[102:103], v210, s[44:47], s2 offen sc1
	buffer_load_dwordx4 v[92:95], v129, s[44:47], s3 offen sc1
	buffer_load_dwordx2 v[96:97], v210, s[44:47], s3 offen sc1
	buffer_load_dwordx4 v[86:89], v129, s[44:47], s100 offen sc1
	buffer_load_dwordx2 v[90:91], v210, s[44:47], s100 offen sc1
	buffer_load_dwordx4 v[80:83], v129, s[44:47], s101 offen sc1
	buffer_load_dwordx2 v[84:85], v210, s[44:47], s101 offen sc1
	v_readlane_b32 s2, v211, 36
	s_waitcnt vmcnt(22)
	v_cvt_scalef32_pk32_f32_fp6 v[0:31], v[74:79], 1.0
	v_pk_fma_f32 v[74:75], v[0:1], s[2:3], v[180:181] op_sel_hi:[1,0,1]
	v_pk_fma_f32 v[76:77], v[2:3], s[2:3], v[178:179] op_sel_hi:[1,0,1]
	v_pk_fma_f32 v[78:79], v[4:5], s[2:3], v[176:177] op_sel_hi:[1,0,1]
	v_pk_fma_f32 v[174:175], v[6:7], s[2:3], v[174:175] op_sel_hi:[1,0,1]
	v_pk_fma_f32 v[172:173], v[8:9], s[2:3], v[172:173] op_sel_hi:[1,0,1]
	v_pk_fma_f32 v[170:171], v[10:11], s[2:3], v[170:171] op_sel_hi:[1,0,1]
	v_pk_fma_f32 v[168:169], v[12:13], s[2:3], v[168:169] op_sel_hi:[1,0,1]
	v_pk_fma_f32 v[166:167], v[14:15], s[2:3], v[166:167] op_sel_hi:[1,0,1]
	v_pk_fma_f32 v[164:165], v[16:17], s[2:3], v[164:165] op_sel_hi:[1,0,1]
	v_pk_fma_f32 v[162:163], v[18:19], s[2:3], v[162:163] op_sel_hi:[1,0,1]
	v_pk_fma_f32 v[160:161], v[20:21], s[2:3], v[160:161] op_sel_hi:[1,0,1]
	v_pk_fma_f32 v[158:159], v[22:23], s[2:3], v[158:159] op_sel_hi:[1,0,1]
	v_pk_fma_f32 v[156:157], v[24:25], s[2:3], v[156:157] op_sel_hi:[1,0,1]
	v_pk_fma_f32 v[154:155], v[26:27], s[2:3], v[154:155] op_sel_hi:[1,0,1]
	v_pk_fma_f32 v[152:153], v[28:29], s[2:3], v[152:153] op_sel_hi:[1,0,1]
	v_pk_fma_f32 v[150:151], v[30:31], s[2:3], v[150:151] op_sel_hi:[1,0,1]
	v_readlane_b32 s2, v211, 37
	s_waitcnt vmcnt(20)
	v_cvt_scalef32_pk32_f32_fp6 v[0:31], v[68:73], 1.0
	v_pk_fma_f32 v[68:69], v[0:1], s[2:3], v[74:75] op_sel_hi:[1,0,1]
	v_pk_fma_f32 v[70:71], v[2:3], s[2:3], v[76:77] op_sel_hi:[1,0,1]
	v_pk_fma_f32 v[72:73], v[4:5], s[2:3], v[78:79] op_sel_hi:[1,0,1]
	v_pk_fma_f32 v[74:75], v[6:7], s[2:3], v[174:175] op_sel_hi:[1,0,1]
	v_pk_fma_f32 v[76:77], v[8:9], s[2:3], v[172:173] op_sel_hi:[1,0,1]
	v_pk_fma_f32 v[78:79], v[10:11], s[2:3], v[170:171] op_sel_hi:[1,0,1]
	v_pk_fma_f32 v[168:169], v[12:13], s[2:3], v[168:169] op_sel_hi:[1,0,1]
	v_pk_fma_f32 v[166:167], v[14:15], s[2:3], v[166:167] op_sel_hi:[1,0,1]
	v_pk_fma_f32 v[164:165], v[16:17], s[2:3], v[164:165] op_sel_hi:[1,0,1]
	v_pk_fma_f32 v[162:163], v[18:19], s[2:3], v[162:163] op_sel_hi:[1,0,1]
	v_pk_fma_f32 v[160:161], v[20:21], s[2:3], v[160:161] op_sel_hi:[1,0,1]
	v_pk_fma_f32 v[158:159], v[22:23], s[2:3], v[158:159] op_sel_hi:[1,0,1]
	v_pk_fma_f32 v[156:157], v[24:25], s[2:3], v[156:157] op_sel_hi:[1,0,1]
	v_pk_fma_f32 v[154:155], v[26:27], s[2:3], v[154:155] op_sel_hi:[1,0,1]
	v_pk_fma_f32 v[152:153], v[28:29], s[2:3], v[152:153] op_sel_hi:[1,0,1]
	v_pk_fma_f32 v[150:151], v[30:31], s[2:3], v[150:151] op_sel_hi:[1,0,1]
	v_readlane_b32 s2, v211, 38
	s_waitcnt vmcnt(18)
	v_cvt_scalef32_pk32_f32_fp6 v[0:31], v[56:61], 1.0
	v_pk_fma_f32 v[56:57], v[0:1], s[2:3], v[68:69] op_sel_hi:[1,0,1]
	v_pk_fma_f32 v[58:59], v[2:3], s[2:3], v[70:71] op_sel_hi:[1,0,1]
	v_pk_fma_f32 v[60:61], v[4:5], s[2:3], v[72:73] op_sel_hi:[1,0,1]
	v_pk_fma_f32 v[68:69], v[6:7], s[2:3], v[74:75] op_sel_hi:[1,0,1]
	v_pk_fma_f32 v[70:71], v[8:9], s[2:3], v[76:77] op_sel_hi:[1,0,1]
	v_pk_fma_f32 v[72:73], v[10:11], s[2:3], v[78:79] op_sel_hi:[1,0,1]
	v_pk_fma_f32 v[74:75], v[12:13], s[2:3], v[168:169] op_sel_hi:[1,0,1]
	v_pk_fma_f32 v[76:77], v[14:15], s[2:3], v[166:167] op_sel_hi:[1,0,1]
	v_pk_fma_f32 v[78:79], v[16:17], s[2:3], v[164:165] op_sel_hi:[1,0,1]
	v_pk_fma_f32 v[162:163], v[18:19], s[2:3], v[162:163] op_sel_hi:[1,0,1]
	v_pk_fma_f32 v[160:161], v[20:21], s[2:3], v[160:161] op_sel_hi:[1,0,1]
	v_pk_fma_f32 v[158:159], v[22:23], s[2:3], v[158:159] op_sel_hi:[1,0,1]
	v_pk_fma_f32 v[156:157], v[24:25], s[2:3], v[156:157] op_sel_hi:[1,0,1]
	v_pk_fma_f32 v[154:155], v[26:27], s[2:3], v[154:155] op_sel_hi:[1,0,1]
	v_pk_fma_f32 v[152:153], v[28:29], s[2:3], v[152:153] op_sel_hi:[1,0,1]
	v_pk_fma_f32 v[150:151], v[30:31], s[2:3], v[150:151] op_sel_hi:[1,0,1]
	v_readlane_b32 s2, v211, 39
	s_waitcnt vmcnt(16)
	v_cvt_scalef32_pk32_f32_fp6 v[0:31], v[44:49], 1.0
	v_pk_fma_f32 v[164:165], v[0:1], s[2:3], v[56:57] op_sel_hi:[1,0,1]
	v_pk_fma_f32 v[166:167], v[2:3], s[2:3], v[58:59] op_sel_hi:[1,0,1]
	v_pk_fma_f32 v[168:169], v[4:5], s[2:3], v[60:61] op_sel_hi:[1,0,1]
	v_pk_fma_f32 v[170:171], v[6:7], s[2:3], v[68:69] op_sel_hi:[1,0,1]
	v_pk_fma_f32 v[172:173], v[8:9], s[2:3], v[70:71] op_sel_hi:[1,0,1]
	v_pk_fma_f32 v[174:175], v[10:11], s[2:3], v[72:73] op_sel_hi:[1,0,1]
	v_pk_fma_f32 v[176:177], v[12:13], s[2:3], v[74:75] op_sel_hi:[1,0,1]
	v_pk_fma_f32 v[178:179], v[14:15], s[2:3], v[76:77] op_sel_hi:[1,0,1]
	v_pk_fma_f32 v[180:181], v[16:17], s[2:3], v[78:79] op_sel_hi:[1,0,1]
	v_pk_fma_f32 v[162:163], v[18:19], s[2:3], v[162:163] op_sel_hi:[1,0,1]
	v_pk_fma_f32 v[160:161], v[20:21], s[2:3], v[160:161] op_sel_hi:[1,0,1]
	v_pk_fma_f32 v[158:159], v[22:23], s[2:3], v[158:159] op_sel_hi:[1,0,1]
	v_pk_fma_f32 v[156:157], v[24:25], s[2:3], v[156:157] op_sel_hi:[1,0,1]
	v_pk_fma_f32 v[154:155], v[26:27], s[2:3], v[154:155] op_sel_hi:[1,0,1]
	v_pk_fma_f32 v[152:153], v[28:29], s[2:3], v[152:153] op_sel_hi:[1,0,1]
	v_pk_fma_f32 v[150:151], v[30:31], s[2:3], v[150:151] op_sel_hi:[1,0,1]
	v_readlane_b32 s2, v240, 48
	v_readlane_b32 s3, v240, 49
	v_readlane_b32 s100, v240, 50
	v_readlane_b32 s101, v240, 51
	s_nop 1
	buffer_load_dwordx4 v[74:77], v129, s[44:47], s2 offen sc1
	buffer_load_dwordx2 v[78:79], v210, s[44:47], s2 offen sc1
	buffer_load_dwordx4 v[68:71], v129, s[44:47], s3 offen sc1
	buffer_load_dwordx2 v[72:73], v210, s[44:47], s3 offen sc1
	buffer_load_dwordx4 v[56:59], v129, s[44:47], s100 offen sc1
	buffer_load_dwordx2 v[60:61], v210, s[44:47], s100 offen sc1
	buffer_load_dwordx4 v[44:47], v129, s[44:47], s101 offen sc1
	buffer_load_dwordx2 v[48:49], v210, s[44:47], s101 offen sc1
	v_readlane_b32 s2, v211, 40
	s_waitcnt vmcnt(22)
	v_cvt_scalef32_pk32_f32_fp6 v[0:31], v[62:67], 1.0
	v_pk_fma_f32 v[62:63], v[0:1], s[2:3], v[164:165] op_sel_hi:[1,0,1]
	v_pk_fma_f32 v[64:65], v[2:3], s[2:3], v[166:167] op_sel_hi:[1,0,1]
	v_pk_fma_f32 v[66:67], v[4:5], s[2:3], v[168:169] op_sel_hi:[1,0,1]
	v_pk_fma_f32 v[164:165], v[6:7], s[2:3], v[170:171] op_sel_hi:[1,0,1]
	v_pk_fma_f32 v[166:167], v[8:9], s[2:3], v[172:173] op_sel_hi:[1,0,1]
	v_pk_fma_f32 v[168:169], v[10:11], s[2:3], v[174:175] op_sel_hi:[1,0,1]
	v_pk_fma_f32 v[170:171], v[12:13], s[2:3], v[176:177] op_sel_hi:[1,0,1]
	v_pk_fma_f32 v[172:173], v[14:15], s[2:3], v[178:179] op_sel_hi:[1,0,1]
	v_pk_fma_f32 v[174:175], v[16:17], s[2:3], v[180:181] op_sel_hi:[1,0,1]
	v_pk_fma_f32 v[162:163], v[18:19], s[2:3], v[162:163] op_sel_hi:[1,0,1]
	v_pk_fma_f32 v[160:161], v[20:21], s[2:3], v[160:161] op_sel_hi:[1,0,1]
	v_pk_fma_f32 v[158:159], v[22:23], s[2:3], v[158:159] op_sel_hi:[1,0,1]
	v_pk_fma_f32 v[156:157], v[24:25], s[2:3], v[156:157] op_sel_hi:[1,0,1]
	v_pk_fma_f32 v[154:155], v[26:27], s[2:3], v[154:155] op_sel_hi:[1,0,1]
	v_pk_fma_f32 v[152:153], v[28:29], s[2:3], v[152:153] op_sel_hi:[1,0,1]
	v_pk_fma_f32 v[150:151], v[30:31], s[2:3], v[150:151] op_sel_hi:[1,0,1]
	v_readlane_b32 s2, v211, 41
	s_waitcnt vmcnt(20)
	v_cvt_scalef32_pk32_f32_fp6 v[0:31], v[50:55], 1.0
	v_pk_fma_f32 v[50:51], v[0:1], s[2:3], v[62:63] op_sel_hi:[1,0,1]
	v_pk_fma_f32 v[52:53], v[2:3], s[2:3], v[64:65] op_sel_hi:[1,0,1]
	v_pk_fma_f32 v[54:55], v[4:5], s[2:3], v[66:67] op_sel_hi:[1,0,1]
	v_pk_fma_f32 v[62:63], v[6:7], s[2:3], v[164:165] op_sel_hi:[1,0,1]
	v_pk_fma_f32 v[64:65], v[8:9], s[2:3], v[166:167] op_sel_hi:[1,0,1]
	v_pk_fma_f32 v[66:67], v[10:11], s[2:3], v[168:169] op_sel_hi:[1,0,1]
	v_pk_fma_f32 v[164:165], v[12:13], s[2:3], v[170:171] op_sel_hi:[1,0,1]
	v_pk_fma_f32 v[166:167], v[14:15], s[2:3], v[172:173] op_sel_hi:[1,0,1]
	v_pk_fma_f32 v[168:169], v[16:17], s[2:3], v[174:175] op_sel_hi:[1,0,1]
	v_pk_fma_f32 v[162:163], v[18:19], s[2:3], v[162:163] op_sel_hi:[1,0,1]
	v_pk_fma_f32 v[160:161], v[20:21], s[2:3], v[160:161] op_sel_hi:[1,0,1]
	v_pk_fma_f32 v[158:159], v[22:23], s[2:3], v[158:159] op_sel_hi:[1,0,1]
	v_pk_fma_f32 v[156:157], v[24:25], s[2:3], v[156:157] op_sel_hi:[1,0,1]
	v_pk_fma_f32 v[154:155], v[26:27], s[2:3], v[154:155] op_sel_hi:[1,0,1]
	v_pk_fma_f32 v[152:153], v[28:29], s[2:3], v[152:153] op_sel_hi:[1,0,1]
	v_pk_fma_f32 v[150:151], v[30:31], s[2:3], v[150:151] op_sel_hi:[1,0,1]
	v_readlane_b32 s2, v211, 42
	s_waitcnt vmcnt(18)
	v_cvt_scalef32_pk32_f32_fp6 v[0:31], v[38:43], 1.0
	v_pk_fma_f32 v[38:39], v[0:1], s[2:3], v[50:51] op_sel_hi:[1,0,1]
	v_pk_fma_f32 v[40:41], v[2:3], s[2:3], v[52:53] op_sel_hi:[1,0,1]
	v_pk_fma_f32 v[42:43], v[4:5], s[2:3], v[54:55] op_sel_hi:[1,0,1]
	v_pk_fma_f32 v[50:51], v[6:7], s[2:3], v[62:63] op_sel_hi:[1,0,1]
	v_pk_fma_f32 v[52:53], v[8:9], s[2:3], v[64:65] op_sel_hi:[1,0,1]
	v_pk_fma_f32 v[54:55], v[10:11], s[2:3], v[66:67] op_sel_hi:[1,0,1]
	v_pk_fma_f32 v[62:63], v[12:13], s[2:3], v[164:165] op_sel_hi:[1,0,1]
	v_pk_fma_f32 v[64:65], v[14:15], s[2:3], v[166:167] op_sel_hi:[1,0,1]
	v_pk_fma_f32 v[66:67], v[16:17], s[2:3], v[168:169] op_sel_hi:[1,0,1]
	v_pk_fma_f32 v[162:163], v[18:19], s[2:3], v[162:163] op_sel_hi:[1,0,1]
	v_pk_fma_f32 v[160:161], v[20:21], s[2:3], v[160:161] op_sel_hi:[1,0,1]
	v_pk_fma_f32 v[158:159], v[22:23], s[2:3], v[158:159] op_sel_hi:[1,0,1]
	v_pk_fma_f32 v[156:157], v[24:25], s[2:3], v[156:157] op_sel_hi:[1,0,1]
	v_pk_fma_f32 v[154:155], v[26:27], s[2:3], v[154:155] op_sel_hi:[1,0,1]
	v_pk_fma_f32 v[152:153], v[28:29], s[2:3], v[152:153] op_sel_hi:[1,0,1]
	v_pk_fma_f32 v[150:151], v[30:31], s[2:3], v[150:151] op_sel_hi:[1,0,1]
	v_readlane_b32 s2, v211, 43
	s_waitcnt vmcnt(16)
	v_cvt_scalef32_pk32_f32_fp6 v[0:31], v[32:37], 1.0
	v_pk_fma_f32 v[164:165], v[0:1], s[2:3], v[38:39] op_sel_hi:[1,0,1]
	v_pk_fma_f32 v[166:167], v[2:3], s[2:3], v[40:41] op_sel_hi:[1,0,1]
	v_pk_fma_f32 v[168:169], v[4:5], s[2:3], v[42:43] op_sel_hi:[1,0,1]
	v_pk_fma_f32 v[170:171], v[6:7], s[2:3], v[50:51] op_sel_hi:[1,0,1]
	v_pk_fma_f32 v[172:173], v[8:9], s[2:3], v[52:53] op_sel_hi:[1,0,1]
	v_pk_fma_f32 v[174:175], v[10:11], s[2:3], v[54:55] op_sel_hi:[1,0,1]
	v_pk_fma_f32 v[176:177], v[12:13], s[2:3], v[62:63] op_sel_hi:[1,0,1]
	v_pk_fma_f32 v[178:179], v[14:15], s[2:3], v[64:65] op_sel_hi:[1,0,1]
	v_pk_fma_f32 v[180:181], v[16:17], s[2:3], v[66:67] op_sel_hi:[1,0,1]
	v_pk_fma_f32 v[162:163], v[18:19], s[2:3], v[162:163] op_sel_hi:[1,0,1]
	v_pk_fma_f32 v[160:161], v[20:21], s[2:3], v[160:161] op_sel_hi:[1,0,1]
	v_pk_fma_f32 v[158:159], v[22:23], s[2:3], v[158:159] op_sel_hi:[1,0,1]
	v_pk_fma_f32 v[156:157], v[24:25], s[2:3], v[156:157] op_sel_hi:[1,0,1]
	v_pk_fma_f32 v[154:155], v[26:27], s[2:3], v[154:155] op_sel_hi:[1,0,1]
	v_pk_fma_f32 v[152:153], v[28:29], s[2:3], v[152:153] op_sel_hi:[1,0,1]
	v_pk_fma_f32 v[150:151], v[30:31], s[2:3], v[150:151] op_sel_hi:[1,0,1]
	v_readlane_b32 s2, v240, 52
	v_readlane_b32 s3, v240, 53
	v_readlane_b32 s100, v240, 54
	v_readlane_b32 s101, v240, 55
	s_nop 1
	buffer_load_dwordx4 v[62:65], v129, s[44:47], s2 offen sc1
	buffer_load_dwordx2 v[66:67], v210, s[44:47], s2 offen sc1
	buffer_load_dwordx4 v[50:53], v129, s[44:47], s3 offen sc1
	buffer_load_dwordx2 v[54:55], v210, s[44:47], s3 offen sc1
	buffer_load_dwordx4 v[38:41], v129, s[44:47], s100 offen sc1
	buffer_load_dwordx2 v[42:43], v210, s[44:47], s100 offen sc1
	buffer_load_dwordx4 v[32:35], v129, s[44:47], s101 offen sc1
	buffer_load_dwordx2 v[36:37], v210, s[44:47], s101 offen sc1
	v_readlane_b32 s2, v211, 44
	s_waitcnt vmcnt(22)
	v_cvt_scalef32_pk32_f32_fp6 v[0:31], v[98:103], 1.0
	v_pk_fma_f32 v[98:99], v[0:1], s[2:3], v[164:165] op_sel_hi:[1,0,1]
	v_pk_fma_f32 v[100:101], v[2:3], s[2:3], v[166:167] op_sel_hi:[1,0,1]
	v_pk_fma_f32 v[102:103], v[4:5], s[2:3], v[168:169] op_sel_hi:[1,0,1]
	v_pk_fma_f32 v[164:165], v[6:7], s[2:3], v[170:171] op_sel_hi:[1,0,1]
	v_pk_fma_f32 v[166:167], v[8:9], s[2:3], v[172:173] op_sel_hi:[1,0,1]
	v_pk_fma_f32 v[168:169], v[10:11], s[2:3], v[174:175] op_sel_hi:[1,0,1]
	v_pk_fma_f32 v[170:171], v[12:13], s[2:3], v[176:177] op_sel_hi:[1,0,1]
	v_pk_fma_f32 v[172:173], v[14:15], s[2:3], v[178:179] op_sel_hi:[1,0,1]
	v_pk_fma_f32 v[174:175], v[16:17], s[2:3], v[180:181] op_sel_hi:[1,0,1]
	v_pk_fma_f32 v[162:163], v[18:19], s[2:3], v[162:163] op_sel_hi:[1,0,1]
	v_pk_fma_f32 v[160:161], v[20:21], s[2:3], v[160:161] op_sel_hi:[1,0,1]
	v_pk_fma_f32 v[158:159], v[22:23], s[2:3], v[158:159] op_sel_hi:[1,0,1]
	v_pk_fma_f32 v[156:157], v[24:25], s[2:3], v[156:157] op_sel_hi:[1,0,1]
	v_pk_fma_f32 v[154:155], v[26:27], s[2:3], v[154:155] op_sel_hi:[1,0,1]
	v_pk_fma_f32 v[152:153], v[28:29], s[2:3], v[152:153] op_sel_hi:[1,0,1]
	v_pk_fma_f32 v[150:151], v[30:31], s[2:3], v[150:151] op_sel_hi:[1,0,1]
	v_readlane_b32 s2, v211, 45
	s_waitcnt vmcnt(20)
	v_cvt_scalef32_pk32_f32_fp6 v[0:31], v[92:97], 1.0
	v_pk_fma_f32 v[92:93], v[0:1], s[2:3], v[98:99] op_sel_hi:[1,0,1]
	v_pk_fma_f32 v[94:95], v[2:3], s[2:3], v[100:101] op_sel_hi:[1,0,1]
	v_pk_fma_f32 v[96:97], v[4:5], s[2:3], v[102:103] op_sel_hi:[1,0,1]
	v_pk_fma_f32 v[98:99], v[6:7], s[2:3], v[164:165] op_sel_hi:[1,0,1]
	v_pk_fma_f32 v[100:101], v[8:9], s[2:3], v[166:167] op_sel_hi:[1,0,1]
	v_pk_fma_f32 v[102:103], v[10:11], s[2:3], v[168:169] op_sel_hi:[1,0,1]
	v_pk_fma_f32 v[164:165], v[12:13], s[2:3], v[170:171] op_sel_hi:[1,0,1]
	v_pk_fma_f32 v[166:167], v[14:15], s[2:3], v[172:173] op_sel_hi:[1,0,1]
	v_pk_fma_f32 v[168:169], v[16:17], s[2:3], v[174:175] op_sel_hi:[1,0,1]
	v_pk_fma_f32 v[162:163], v[18:19], s[2:3], v[162:163] op_sel_hi:[1,0,1]
	v_pk_fma_f32 v[160:161], v[20:21], s[2:3], v[160:161] op_sel_hi:[1,0,1]
	v_pk_fma_f32 v[158:159], v[22:23], s[2:3], v[158:159] op_sel_hi:[1,0,1]
	v_pk_fma_f32 v[156:157], v[24:25], s[2:3], v[156:157] op_sel_hi:[1,0,1]
	v_pk_fma_f32 v[154:155], v[26:27], s[2:3], v[154:155] op_sel_hi:[1,0,1]
	v_pk_fma_f32 v[152:153], v[28:29], s[2:3], v[152:153] op_sel_hi:[1,0,1]
	v_pk_fma_f32 v[150:151], v[30:31], s[2:3], v[150:151] op_sel_hi:[1,0,1]
	v_readlane_b32 s2, v211, 46
	s_waitcnt vmcnt(18)
	v_cvt_scalef32_pk32_f32_fp6 v[0:31], v[86:91], 1.0
	v_pk_fma_f32 v[86:87], v[0:1], s[2:3], v[92:93] op_sel_hi:[1,0,1]
	v_pk_fma_f32 v[88:89], v[2:3], s[2:3], v[94:95] op_sel_hi:[1,0,1]
	v_pk_fma_f32 v[90:91], v[4:5], s[2:3], v[96:97] op_sel_hi:[1,0,1]
	v_pk_fma_f32 v[92:93], v[6:7], s[2:3], v[98:99] op_sel_hi:[1,0,1]
	v_pk_fma_f32 v[94:95], v[8:9], s[2:3], v[100:101] op_sel_hi:[1,0,1]
	v_pk_fma_f32 v[96:97], v[10:11], s[2:3], v[102:103] op_sel_hi:[1,0,1]
	v_pk_fma_f32 v[98:99], v[12:13], s[2:3], v[164:165] op_sel_hi:[1,0,1]
	v_pk_fma_f32 v[100:101], v[14:15], s[2:3], v[166:167] op_sel_hi:[1,0,1]
	v_pk_fma_f32 v[102:103], v[16:17], s[2:3], v[168:169] op_sel_hi:[1,0,1]
	v_pk_fma_f32 v[162:163], v[18:19], s[2:3], v[162:163] op_sel_hi:[1,0,1]
	v_pk_fma_f32 v[160:161], v[20:21], s[2:3], v[160:161] op_sel_hi:[1,0,1]
	v_pk_fma_f32 v[158:159], v[22:23], s[2:3], v[158:159] op_sel_hi:[1,0,1]
	v_pk_fma_f32 v[156:157], v[24:25], s[2:3], v[156:157] op_sel_hi:[1,0,1]
	v_pk_fma_f32 v[154:155], v[26:27], s[2:3], v[154:155] op_sel_hi:[1,0,1]
	v_pk_fma_f32 v[152:153], v[28:29], s[2:3], v[152:153] op_sel_hi:[1,0,1]
	v_pk_fma_f32 v[150:151], v[30:31], s[2:3], v[150:151] op_sel_hi:[1,0,1]
	v_readlane_b32 s2, v211, 47
	s_waitcnt vmcnt(16)
	v_cvt_scalef32_pk32_f32_fp6 v[0:31], v[80:85], 1.0
	v_pk_fma_f32 v[180:181], v[0:1], s[2:3], v[86:87] op_sel_hi:[1,0,1]
	v_pk_fma_f32 v[178:179], v[2:3], s[2:3], v[88:89] op_sel_hi:[1,0,1]
	v_pk_fma_f32 v[176:177], v[4:5], s[2:3], v[90:91] op_sel_hi:[1,0,1]
	v_pk_fma_f32 v[174:175], v[6:7], s[2:3], v[92:93] op_sel_hi:[1,0,1]
	v_pk_fma_f32 v[172:173], v[8:9], s[2:3], v[94:95] op_sel_hi:[1,0,1]
	v_pk_fma_f32 v[170:171], v[10:11], s[2:3], v[96:97] op_sel_hi:[1,0,1]
	v_pk_fma_f32 v[168:169], v[12:13], s[2:3], v[98:99] op_sel_hi:[1,0,1]
	v_pk_fma_f32 v[166:167], v[14:15], s[2:3], v[100:101] op_sel_hi:[1,0,1]
	v_pk_fma_f32 v[164:165], v[16:17], s[2:3], v[102:103] op_sel_hi:[1,0,1]
	v_pk_fma_f32 v[162:163], v[18:19], s[2:3], v[162:163] op_sel_hi:[1,0,1]
	v_pk_fma_f32 v[160:161], v[20:21], s[2:3], v[160:161] op_sel_hi:[1,0,1]
	v_pk_fma_f32 v[158:159], v[22:23], s[2:3], v[158:159] op_sel_hi:[1,0,1]
	v_pk_fma_f32 v[156:157], v[24:25], s[2:3], v[156:157] op_sel_hi:[1,0,1]
	v_pk_fma_f32 v[154:155], v[26:27], s[2:3], v[154:155] op_sel_hi:[1,0,1]
	v_pk_fma_f32 v[152:153], v[28:29], s[2:3], v[152:153] op_sel_hi:[1,0,1]
	v_pk_fma_f32 v[150:151], v[30:31], s[2:3], v[150:151] op_sel_hi:[1,0,1]
	v_readlane_b32 s2, v240, 56
	v_readlane_b32 s3, v240, 57
	v_readlane_b32 s100, v240, 58
	v_readlane_b32 s101, v240, 59
	s_nop 1
	buffer_load_dwordx4 v[98:101], v129, s[44:47], s2 offen sc1
	buffer_load_dwordx2 v[102:103], v210, s[44:47], s2 offen sc1
	buffer_load_dwordx4 v[92:95], v129, s[44:47], s3 offen sc1
	buffer_load_dwordx2 v[96:97], v210, s[44:47], s3 offen sc1
	buffer_load_dwordx4 v[86:89], v129, s[44:47], s100 offen sc1
	buffer_load_dwordx2 v[90:91], v210, s[44:47], s100 offen sc1
	buffer_load_dwordx4 v[80:83], v129, s[44:47], s101 offen sc1
	buffer_load_dwordx2 v[84:85], v210, s[44:47], s101 offen sc1
	v_readlane_b32 s2, v211, 48
	s_waitcnt vmcnt(22)
	v_cvt_scalef32_pk32_f32_fp6 v[0:31], v[74:79], 1.0
	v_pk_fma_f32 v[74:75], v[0:1], s[2:3], v[180:181] op_sel_hi:[1,0,1]
	v_pk_fma_f32 v[76:77], v[2:3], s[2:3], v[178:179] op_sel_hi:[1,0,1]
	v_pk_fma_f32 v[78:79], v[4:5], s[2:3], v[176:177] op_sel_hi:[1,0,1]
	v_pk_fma_f32 v[174:175], v[6:7], s[2:3], v[174:175] op_sel_hi:[1,0,1]
	v_pk_fma_f32 v[172:173], v[8:9], s[2:3], v[172:173] op_sel_hi:[1,0,1]
	v_pk_fma_f32 v[170:171], v[10:11], s[2:3], v[170:171] op_sel_hi:[1,0,1]
	v_pk_fma_f32 v[168:169], v[12:13], s[2:3], v[168:169] op_sel_hi:[1,0,1]
	v_pk_fma_f32 v[166:167], v[14:15], s[2:3], v[166:167] op_sel_hi:[1,0,1]
	v_pk_fma_f32 v[164:165], v[16:17], s[2:3], v[164:165] op_sel_hi:[1,0,1]
	v_pk_fma_f32 v[162:163], v[18:19], s[2:3], v[162:163] op_sel_hi:[1,0,1]
	v_pk_fma_f32 v[160:161], v[20:21], s[2:3], v[160:161] op_sel_hi:[1,0,1]
	v_pk_fma_f32 v[158:159], v[22:23], s[2:3], v[158:159] op_sel_hi:[1,0,1]
	v_pk_fma_f32 v[156:157], v[24:25], s[2:3], v[156:157] op_sel_hi:[1,0,1]
	v_pk_fma_f32 v[154:155], v[26:27], s[2:3], v[154:155] op_sel_hi:[1,0,1]
	v_pk_fma_f32 v[152:153], v[28:29], s[2:3], v[152:153] op_sel_hi:[1,0,1]
	v_pk_fma_f32 v[150:151], v[30:31], s[2:3], v[150:151] op_sel_hi:[1,0,1]
	v_readlane_b32 s2, v211, 49
	s_waitcnt vmcnt(20)
	v_cvt_scalef32_pk32_f32_fp6 v[0:31], v[68:73], 1.0
	v_pk_fma_f32 v[68:69], v[0:1], s[2:3], v[74:75] op_sel_hi:[1,0,1]
	v_pk_fma_f32 v[70:71], v[2:3], s[2:3], v[76:77] op_sel_hi:[1,0,1]
	v_pk_fma_f32 v[72:73], v[4:5], s[2:3], v[78:79] op_sel_hi:[1,0,1]
	v_pk_fma_f32 v[74:75], v[6:7], s[2:3], v[174:175] op_sel_hi:[1,0,1]
	v_pk_fma_f32 v[76:77], v[8:9], s[2:3], v[172:173] op_sel_hi:[1,0,1]
	v_pk_fma_f32 v[78:79], v[10:11], s[2:3], v[170:171] op_sel_hi:[1,0,1]
	v_pk_fma_f32 v[168:169], v[12:13], s[2:3], v[168:169] op_sel_hi:[1,0,1]
	v_pk_fma_f32 v[166:167], v[14:15], s[2:3], v[166:167] op_sel_hi:[1,0,1]
	v_pk_fma_f32 v[164:165], v[16:17], s[2:3], v[164:165] op_sel_hi:[1,0,1]
	v_pk_fma_f32 v[162:163], v[18:19], s[2:3], v[162:163] op_sel_hi:[1,0,1]
	v_pk_fma_f32 v[160:161], v[20:21], s[2:3], v[160:161] op_sel_hi:[1,0,1]
	v_pk_fma_f32 v[158:159], v[22:23], s[2:3], v[158:159] op_sel_hi:[1,0,1]
	v_pk_fma_f32 v[156:157], v[24:25], s[2:3], v[156:157] op_sel_hi:[1,0,1]
	v_pk_fma_f32 v[154:155], v[26:27], s[2:3], v[154:155] op_sel_hi:[1,0,1]
	v_pk_fma_f32 v[152:153], v[28:29], s[2:3], v[152:153] op_sel_hi:[1,0,1]
	v_pk_fma_f32 v[150:151], v[30:31], s[2:3], v[150:151] op_sel_hi:[1,0,1]
	v_readlane_b32 s2, v211, 50
	s_waitcnt vmcnt(18)
	v_cvt_scalef32_pk32_f32_fp6 v[0:31], v[56:61], 1.0
	v_pk_fma_f32 v[56:57], v[0:1], s[2:3], v[68:69] op_sel_hi:[1,0,1]
	v_pk_fma_f32 v[58:59], v[2:3], s[2:3], v[70:71] op_sel_hi:[1,0,1]
	v_pk_fma_f32 v[60:61], v[4:5], s[2:3], v[72:73] op_sel_hi:[1,0,1]
	v_pk_fma_f32 v[68:69], v[6:7], s[2:3], v[74:75] op_sel_hi:[1,0,1]
	v_pk_fma_f32 v[70:71], v[8:9], s[2:3], v[76:77] op_sel_hi:[1,0,1]
	v_pk_fma_f32 v[72:73], v[10:11], s[2:3], v[78:79] op_sel_hi:[1,0,1]
	v_pk_fma_f32 v[74:75], v[12:13], s[2:3], v[168:169] op_sel_hi:[1,0,1]
	v_pk_fma_f32 v[76:77], v[14:15], s[2:3], v[166:167] op_sel_hi:[1,0,1]
	v_pk_fma_f32 v[78:79], v[16:17], s[2:3], v[164:165] op_sel_hi:[1,0,1]
	v_pk_fma_f32 v[162:163], v[18:19], s[2:3], v[162:163] op_sel_hi:[1,0,1]
	v_pk_fma_f32 v[160:161], v[20:21], s[2:3], v[160:161] op_sel_hi:[1,0,1]
	v_pk_fma_f32 v[158:159], v[22:23], s[2:3], v[158:159] op_sel_hi:[1,0,1]
	v_pk_fma_f32 v[156:157], v[24:25], s[2:3], v[156:157] op_sel_hi:[1,0,1]
	v_pk_fma_f32 v[154:155], v[26:27], s[2:3], v[154:155] op_sel_hi:[1,0,1]
	v_pk_fma_f32 v[152:153], v[28:29], s[2:3], v[152:153] op_sel_hi:[1,0,1]
	v_pk_fma_f32 v[150:151], v[30:31], s[2:3], v[150:151] op_sel_hi:[1,0,1]
	v_readlane_b32 s2, v211, 51
	s_waitcnt vmcnt(16)
	v_cvt_scalef32_pk32_f32_fp6 v[0:31], v[44:49], 1.0
	v_pk_fma_f32 v[164:165], v[0:1], s[2:3], v[56:57] op_sel_hi:[1,0,1]
	v_pk_fma_f32 v[166:167], v[2:3], s[2:3], v[58:59] op_sel_hi:[1,0,1]
	v_pk_fma_f32 v[168:169], v[4:5], s[2:3], v[60:61] op_sel_hi:[1,0,1]
	v_pk_fma_f32 v[170:171], v[6:7], s[2:3], v[68:69] op_sel_hi:[1,0,1]
	v_pk_fma_f32 v[172:173], v[8:9], s[2:3], v[70:71] op_sel_hi:[1,0,1]
	v_pk_fma_f32 v[174:175], v[10:11], s[2:3], v[72:73] op_sel_hi:[1,0,1]
	v_pk_fma_f32 v[176:177], v[12:13], s[2:3], v[74:75] op_sel_hi:[1,0,1]
	v_pk_fma_f32 v[178:179], v[14:15], s[2:3], v[76:77] op_sel_hi:[1,0,1]
	v_pk_fma_f32 v[180:181], v[16:17], s[2:3], v[78:79] op_sel_hi:[1,0,1]
	v_pk_fma_f32 v[162:163], v[18:19], s[2:3], v[162:163] op_sel_hi:[1,0,1]
	v_pk_fma_f32 v[160:161], v[20:21], s[2:3], v[160:161] op_sel_hi:[1,0,1]
	v_pk_fma_f32 v[158:159], v[22:23], s[2:3], v[158:159] op_sel_hi:[1,0,1]
	v_pk_fma_f32 v[156:157], v[24:25], s[2:3], v[156:157] op_sel_hi:[1,0,1]
	v_pk_fma_f32 v[154:155], v[26:27], s[2:3], v[154:155] op_sel_hi:[1,0,1]
	v_pk_fma_f32 v[152:153], v[28:29], s[2:3], v[152:153] op_sel_hi:[1,0,1]
	v_pk_fma_f32 v[150:151], v[30:31], s[2:3], v[150:151] op_sel_hi:[1,0,1]
	v_readlane_b32 s2, v240, 60
	v_readlane_b32 s3, v240, 61
	v_readlane_b32 s100, v240, 62
	v_readlane_b32 s101, v240, 63
	s_nop 1
	buffer_load_dwordx4 v[74:77], v129, s[44:47], s2 offen sc1
	buffer_load_dwordx2 v[78:79], v210, s[44:47], s2 offen sc1
	buffer_load_dwordx4 v[68:71], v129, s[44:47], s3 offen sc1
	buffer_load_dwordx2 v[72:73], v210, s[44:47], s3 offen sc1
	buffer_load_dwordx4 v[56:59], v129, s[44:47], s100 offen sc1
	buffer_load_dwordx2 v[60:61], v210, s[44:47], s100 offen sc1
	buffer_load_dwordx4 v[44:47], v129, s[44:47], s101 offen sc1
	buffer_load_dwordx2 v[48:49], v210, s[44:47], s101 offen sc1
	v_readlane_b32 s2, v211, 52
	s_waitcnt vmcnt(22)
	v_cvt_scalef32_pk32_f32_fp6 v[0:31], v[62:67], 1.0
	v_pk_fma_f32 v[62:63], v[0:1], s[2:3], v[164:165] op_sel_hi:[1,0,1]
	v_pk_fma_f32 v[64:65], v[2:3], s[2:3], v[166:167] op_sel_hi:[1,0,1]
	v_pk_fma_f32 v[66:67], v[4:5], s[2:3], v[168:169] op_sel_hi:[1,0,1]
	v_pk_fma_f32 v[164:165], v[6:7], s[2:3], v[170:171] op_sel_hi:[1,0,1]
	v_pk_fma_f32 v[166:167], v[8:9], s[2:3], v[172:173] op_sel_hi:[1,0,1]
	v_pk_fma_f32 v[168:169], v[10:11], s[2:3], v[174:175] op_sel_hi:[1,0,1]
	v_pk_fma_f32 v[170:171], v[12:13], s[2:3], v[176:177] op_sel_hi:[1,0,1]
	v_pk_fma_f32 v[172:173], v[14:15], s[2:3], v[178:179] op_sel_hi:[1,0,1]
	v_pk_fma_f32 v[174:175], v[16:17], s[2:3], v[180:181] op_sel_hi:[1,0,1]
	v_pk_fma_f32 v[162:163], v[18:19], s[2:3], v[162:163] op_sel_hi:[1,0,1]
	v_pk_fma_f32 v[160:161], v[20:21], s[2:3], v[160:161] op_sel_hi:[1,0,1]
	v_pk_fma_f32 v[158:159], v[22:23], s[2:3], v[158:159] op_sel_hi:[1,0,1]
	v_pk_fma_f32 v[156:157], v[24:25], s[2:3], v[156:157] op_sel_hi:[1,0,1]
	v_pk_fma_f32 v[154:155], v[26:27], s[2:3], v[154:155] op_sel_hi:[1,0,1]
	v_pk_fma_f32 v[152:153], v[28:29], s[2:3], v[152:153] op_sel_hi:[1,0,1]
	v_pk_fma_f32 v[150:151], v[30:31], s[2:3], v[150:151] op_sel_hi:[1,0,1]
	v_readlane_b32 s2, v211, 53
	s_waitcnt vmcnt(20)
	v_cvt_scalef32_pk32_f32_fp6 v[0:31], v[50:55], 1.0
	v_pk_fma_f32 v[50:51], v[0:1], s[2:3], v[62:63] op_sel_hi:[1,0,1]
	v_pk_fma_f32 v[52:53], v[2:3], s[2:3], v[64:65] op_sel_hi:[1,0,1]
	v_pk_fma_f32 v[54:55], v[4:5], s[2:3], v[66:67] op_sel_hi:[1,0,1]
	v_pk_fma_f32 v[62:63], v[6:7], s[2:3], v[164:165] op_sel_hi:[1,0,1]
	v_pk_fma_f32 v[64:65], v[8:9], s[2:3], v[166:167] op_sel_hi:[1,0,1]
	v_pk_fma_f32 v[66:67], v[10:11], s[2:3], v[168:169] op_sel_hi:[1,0,1]
	v_pk_fma_f32 v[164:165], v[12:13], s[2:3], v[170:171] op_sel_hi:[1,0,1]
	v_pk_fma_f32 v[166:167], v[14:15], s[2:3], v[172:173] op_sel_hi:[1,0,1]
	v_pk_fma_f32 v[168:169], v[16:17], s[2:3], v[174:175] op_sel_hi:[1,0,1]
	v_pk_fma_f32 v[162:163], v[18:19], s[2:3], v[162:163] op_sel_hi:[1,0,1]
	v_pk_fma_f32 v[160:161], v[20:21], s[2:3], v[160:161] op_sel_hi:[1,0,1]
	v_pk_fma_f32 v[158:159], v[22:23], s[2:3], v[158:159] op_sel_hi:[1,0,1]
	v_pk_fma_f32 v[156:157], v[24:25], s[2:3], v[156:157] op_sel_hi:[1,0,1]
	v_pk_fma_f32 v[154:155], v[26:27], s[2:3], v[154:155] op_sel_hi:[1,0,1]
	v_pk_fma_f32 v[152:153], v[28:29], s[2:3], v[152:153] op_sel_hi:[1,0,1]
	v_pk_fma_f32 v[150:151], v[30:31], s[2:3], v[150:151] op_sel_hi:[1,0,1]
	v_readlane_b32 s2, v211, 54
	s_waitcnt vmcnt(18)
	v_cvt_scalef32_pk32_f32_fp6 v[0:31], v[38:43], 1.0
	v_pk_fma_f32 v[38:39], v[0:1], s[2:3], v[50:51] op_sel_hi:[1,0,1]
	v_pk_fma_f32 v[40:41], v[2:3], s[2:3], v[52:53] op_sel_hi:[1,0,1]
	v_pk_fma_f32 v[42:43], v[4:5], s[2:3], v[54:55] op_sel_hi:[1,0,1]
	v_pk_fma_f32 v[50:51], v[6:7], s[2:3], v[62:63] op_sel_hi:[1,0,1]
	v_pk_fma_f32 v[52:53], v[8:9], s[2:3], v[64:65] op_sel_hi:[1,0,1]
	v_pk_fma_f32 v[54:55], v[10:11], s[2:3], v[66:67] op_sel_hi:[1,0,1]
	v_pk_fma_f32 v[62:63], v[12:13], s[2:3], v[164:165] op_sel_hi:[1,0,1]
	v_pk_fma_f32 v[64:65], v[14:15], s[2:3], v[166:167] op_sel_hi:[1,0,1]
	v_pk_fma_f32 v[66:67], v[16:17], s[2:3], v[168:169] op_sel_hi:[1,0,1]
	v_pk_fma_f32 v[162:163], v[18:19], s[2:3], v[162:163] op_sel_hi:[1,0,1]
	v_pk_fma_f32 v[160:161], v[20:21], s[2:3], v[160:161] op_sel_hi:[1,0,1]
	v_pk_fma_f32 v[158:159], v[22:23], s[2:3], v[158:159] op_sel_hi:[1,0,1]
	v_pk_fma_f32 v[156:157], v[24:25], s[2:3], v[156:157] op_sel_hi:[1,0,1]
	v_pk_fma_f32 v[154:155], v[26:27], s[2:3], v[154:155] op_sel_hi:[1,0,1]
	v_pk_fma_f32 v[152:153], v[28:29], s[2:3], v[152:153] op_sel_hi:[1,0,1]
	v_pk_fma_f32 v[150:151], v[30:31], s[2:3], v[150:151] op_sel_hi:[1,0,1]
	v_readlane_b32 s2, v211, 55
	s_waitcnt vmcnt(16)
	v_cvt_scalef32_pk32_f32_fp6 v[0:31], v[32:37], 1.0
	v_pk_fma_f32 v[164:165], v[0:1], s[2:3], v[38:39] op_sel_hi:[1,0,1]
	v_pk_fma_f32 v[166:167], v[2:3], s[2:3], v[40:41] op_sel_hi:[1,0,1]
	v_pk_fma_f32 v[168:169], v[4:5], s[2:3], v[42:43] op_sel_hi:[1,0,1]
	v_pk_fma_f32 v[170:171], v[6:7], s[2:3], v[50:51] op_sel_hi:[1,0,1]
	v_pk_fma_f32 v[172:173], v[8:9], s[2:3], v[52:53] op_sel_hi:[1,0,1]
	v_pk_fma_f32 v[174:175], v[10:11], s[2:3], v[54:55] op_sel_hi:[1,0,1]
	v_pk_fma_f32 v[176:177], v[12:13], s[2:3], v[62:63] op_sel_hi:[1,0,1]
	v_pk_fma_f32 v[178:179], v[14:15], s[2:3], v[64:65] op_sel_hi:[1,0,1]
	v_pk_fma_f32 v[180:181], v[16:17], s[2:3], v[66:67] op_sel_hi:[1,0,1]
	v_pk_fma_f32 v[162:163], v[18:19], s[2:3], v[162:163] op_sel_hi:[1,0,1]
	v_pk_fma_f32 v[160:161], v[20:21], s[2:3], v[160:161] op_sel_hi:[1,0,1]
	v_pk_fma_f32 v[158:159], v[22:23], s[2:3], v[158:159] op_sel_hi:[1,0,1]
	v_pk_fma_f32 v[156:157], v[24:25], s[2:3], v[156:157] op_sel_hi:[1,0,1]
	v_pk_fma_f32 v[154:155], v[26:27], s[2:3], v[154:155] op_sel_hi:[1,0,1]
	v_pk_fma_f32 v[152:153], v[28:29], s[2:3], v[152:153] op_sel_hi:[1,0,1]
	v_pk_fma_f32 v[150:151], v[30:31], s[2:3], v[150:151] op_sel_hi:[1,0,1]
	v_readlane_b32 s2, v241, 0
	v_readlane_b32 s3, v241, 1
	v_readlane_b32 s100, v241, 2
	v_readlane_b32 s101, v241, 3
	s_nop 1
	buffer_load_dwordx4 v[62:65], v129, s[44:47], s2 offen sc1
	buffer_load_dwordx2 v[66:67], v210, s[44:47], s2 offen sc1
	buffer_load_dwordx4 v[50:53], v129, s[44:47], s3 offen sc1
	buffer_load_dwordx2 v[54:55], v210, s[44:47], s3 offen sc1
	buffer_load_dwordx4 v[38:41], v129, s[44:47], s100 offen sc1
	buffer_load_dwordx2 v[42:43], v210, s[44:47], s100 offen sc1
	buffer_load_dwordx4 v[32:35], v129, s[44:47], s101 offen sc1
	buffer_load_dwordx2 v[36:37], v210, s[44:47], s101 offen sc1
	v_readlane_b32 s2, v211, 56
	s_waitcnt vmcnt(22)
	v_cvt_scalef32_pk32_f32_fp6 v[0:31], v[98:103], 1.0
	v_pk_fma_f32 v[98:99], v[0:1], s[2:3], v[164:165] op_sel_hi:[1,0,1]
	v_pk_fma_f32 v[100:101], v[2:3], s[2:3], v[166:167] op_sel_hi:[1,0,1]
	v_pk_fma_f32 v[102:103], v[4:5], s[2:3], v[168:169] op_sel_hi:[1,0,1]
	v_pk_fma_f32 v[164:165], v[6:7], s[2:3], v[170:171] op_sel_hi:[1,0,1]
	v_pk_fma_f32 v[166:167], v[8:9], s[2:3], v[172:173] op_sel_hi:[1,0,1]
	v_pk_fma_f32 v[168:169], v[10:11], s[2:3], v[174:175] op_sel_hi:[1,0,1]
	v_pk_fma_f32 v[170:171], v[12:13], s[2:3], v[176:177] op_sel_hi:[1,0,1]
	v_pk_fma_f32 v[172:173], v[14:15], s[2:3], v[178:179] op_sel_hi:[1,0,1]
	v_pk_fma_f32 v[174:175], v[16:17], s[2:3], v[180:181] op_sel_hi:[1,0,1]
	v_pk_fma_f32 v[162:163], v[18:19], s[2:3], v[162:163] op_sel_hi:[1,0,1]
	v_pk_fma_f32 v[160:161], v[20:21], s[2:3], v[160:161] op_sel_hi:[1,0,1]
	v_pk_fma_f32 v[158:159], v[22:23], s[2:3], v[158:159] op_sel_hi:[1,0,1]
	v_pk_fma_f32 v[156:157], v[24:25], s[2:3], v[156:157] op_sel_hi:[1,0,1]
	v_pk_fma_f32 v[154:155], v[26:27], s[2:3], v[154:155] op_sel_hi:[1,0,1]
	v_pk_fma_f32 v[152:153], v[28:29], s[2:3], v[152:153] op_sel_hi:[1,0,1]
	v_pk_fma_f32 v[150:151], v[30:31], s[2:3], v[150:151] op_sel_hi:[1,0,1]
	v_readlane_b32 s2, v211, 57
	s_waitcnt vmcnt(20)
	v_cvt_scalef32_pk32_f32_fp6 v[0:31], v[92:97], 1.0
	v_pk_fma_f32 v[92:93], v[0:1], s[2:3], v[98:99] op_sel_hi:[1,0,1]
	v_pk_fma_f32 v[94:95], v[2:3], s[2:3], v[100:101] op_sel_hi:[1,0,1]
	v_pk_fma_f32 v[96:97], v[4:5], s[2:3], v[102:103] op_sel_hi:[1,0,1]
	v_pk_fma_f32 v[98:99], v[6:7], s[2:3], v[164:165] op_sel_hi:[1,0,1]
	v_pk_fma_f32 v[100:101], v[8:9], s[2:3], v[166:167] op_sel_hi:[1,0,1]
	v_pk_fma_f32 v[102:103], v[10:11], s[2:3], v[168:169] op_sel_hi:[1,0,1]
	v_pk_fma_f32 v[164:165], v[12:13], s[2:3], v[170:171] op_sel_hi:[1,0,1]
	v_pk_fma_f32 v[166:167], v[14:15], s[2:3], v[172:173] op_sel_hi:[1,0,1]
	v_pk_fma_f32 v[168:169], v[16:17], s[2:3], v[174:175] op_sel_hi:[1,0,1]
	v_pk_fma_f32 v[162:163], v[18:19], s[2:3], v[162:163] op_sel_hi:[1,0,1]
	v_pk_fma_f32 v[160:161], v[20:21], s[2:3], v[160:161] op_sel_hi:[1,0,1]
	v_pk_fma_f32 v[158:159], v[22:23], s[2:3], v[158:159] op_sel_hi:[1,0,1]
	v_pk_fma_f32 v[156:157], v[24:25], s[2:3], v[156:157] op_sel_hi:[1,0,1]
	v_pk_fma_f32 v[154:155], v[26:27], s[2:3], v[154:155] op_sel_hi:[1,0,1]
	v_pk_fma_f32 v[152:153], v[28:29], s[2:3], v[152:153] op_sel_hi:[1,0,1]
	v_pk_fma_f32 v[150:151], v[30:31], s[2:3], v[150:151] op_sel_hi:[1,0,1]
	v_readlane_b32 s2, v211, 58
	s_waitcnt vmcnt(18)
	v_cvt_scalef32_pk32_f32_fp6 v[0:31], v[86:91], 1.0
	v_pk_fma_f32 v[86:87], v[0:1], s[2:3], v[92:93] op_sel_hi:[1,0,1]
	v_pk_fma_f32 v[88:89], v[2:3], s[2:3], v[94:95] op_sel_hi:[1,0,1]
	v_pk_fma_f32 v[90:91], v[4:5], s[2:3], v[96:97] op_sel_hi:[1,0,1]
	v_pk_fma_f32 v[92:93], v[6:7], s[2:3], v[98:99] op_sel_hi:[1,0,1]
	v_pk_fma_f32 v[94:95], v[8:9], s[2:3], v[100:101] op_sel_hi:[1,0,1]
	v_pk_fma_f32 v[96:97], v[10:11], s[2:3], v[102:103] op_sel_hi:[1,0,1]
	v_pk_fma_f32 v[98:99], v[12:13], s[2:3], v[164:165] op_sel_hi:[1,0,1]
	v_pk_fma_f32 v[100:101], v[14:15], s[2:3], v[166:167] op_sel_hi:[1,0,1]
	v_pk_fma_f32 v[102:103], v[16:17], s[2:3], v[168:169] op_sel_hi:[1,0,1]
	v_pk_fma_f32 v[162:163], v[18:19], s[2:3], v[162:163] op_sel_hi:[1,0,1]
	v_pk_fma_f32 v[160:161], v[20:21], s[2:3], v[160:161] op_sel_hi:[1,0,1]
	v_pk_fma_f32 v[158:159], v[22:23], s[2:3], v[158:159] op_sel_hi:[1,0,1]
	v_pk_fma_f32 v[156:157], v[24:25], s[2:3], v[156:157] op_sel_hi:[1,0,1]
	v_pk_fma_f32 v[154:155], v[26:27], s[2:3], v[154:155] op_sel_hi:[1,0,1]
	v_pk_fma_f32 v[152:153], v[28:29], s[2:3], v[152:153] op_sel_hi:[1,0,1]
	v_pk_fma_f32 v[150:151], v[30:31], s[2:3], v[150:151] op_sel_hi:[1,0,1]
	v_readlane_b32 s2, v211, 59
	s_waitcnt vmcnt(16)
	v_cvt_scalef32_pk32_f32_fp6 v[0:31], v[80:85], 1.0
	v_pk_fma_f32 v[180:181], v[0:1], s[2:3], v[86:87] op_sel_hi:[1,0,1]
	v_pk_fma_f32 v[178:179], v[2:3], s[2:3], v[88:89] op_sel_hi:[1,0,1]
	v_pk_fma_f32 v[176:177], v[4:5], s[2:3], v[90:91] op_sel_hi:[1,0,1]
	v_pk_fma_f32 v[174:175], v[6:7], s[2:3], v[92:93] op_sel_hi:[1,0,1]
	v_pk_fma_f32 v[172:173], v[8:9], s[2:3], v[94:95] op_sel_hi:[1,0,1]
	v_pk_fma_f32 v[170:171], v[10:11], s[2:3], v[96:97] op_sel_hi:[1,0,1]
	v_pk_fma_f32 v[168:169], v[12:13], s[2:3], v[98:99] op_sel_hi:[1,0,1]
	v_pk_fma_f32 v[166:167], v[14:15], s[2:3], v[100:101] op_sel_hi:[1,0,1]
	v_pk_fma_f32 v[164:165], v[16:17], s[2:3], v[102:103] op_sel_hi:[1,0,1]
	v_pk_fma_f32 v[162:163], v[18:19], s[2:3], v[162:163] op_sel_hi:[1,0,1]
	v_pk_fma_f32 v[160:161], v[20:21], s[2:3], v[160:161] op_sel_hi:[1,0,1]
	v_pk_fma_f32 v[158:159], v[22:23], s[2:3], v[158:159] op_sel_hi:[1,0,1]
	v_pk_fma_f32 v[156:157], v[24:25], s[2:3], v[156:157] op_sel_hi:[1,0,1]
	v_pk_fma_f32 v[154:155], v[26:27], s[2:3], v[154:155] op_sel_hi:[1,0,1]
	v_pk_fma_f32 v[152:153], v[28:29], s[2:3], v[152:153] op_sel_hi:[1,0,1]
	v_pk_fma_f32 v[150:151], v[30:31], s[2:3], v[150:151] op_sel_hi:[1,0,1]
	v_readlane_b32 s2, v241, 4
	v_readlane_b32 s3, v241, 5
	v_readlane_b32 s100, v241, 6
	v_readlane_b32 s101, v241, 7
	s_nop 1
	buffer_load_dwordx4 v[98:101], v129, s[44:47], s2 offen sc1
	buffer_load_dwordx2 v[102:103], v210, s[44:47], s2 offen sc1
	buffer_load_dwordx4 v[92:95], v129, s[44:47], s3 offen sc1
	buffer_load_dwordx2 v[96:97], v210, s[44:47], s3 offen sc1
	buffer_load_dwordx4 v[86:89], v129, s[44:47], s100 offen sc1
	buffer_load_dwordx2 v[90:91], v210, s[44:47], s100 offen sc1
	buffer_load_dwordx4 v[80:83], v129, s[44:47], s101 offen sc1
	buffer_load_dwordx2 v[84:85], v210, s[44:47], s101 offen sc1
	v_readlane_b32 s2, v211, 60
	s_waitcnt vmcnt(22)
	v_cvt_scalef32_pk32_f32_fp6 v[0:31], v[74:79], 1.0
	v_pk_fma_f32 v[74:75], v[0:1], s[2:3], v[180:181] op_sel_hi:[1,0,1]
	v_pk_fma_f32 v[76:77], v[2:3], s[2:3], v[178:179] op_sel_hi:[1,0,1]
	v_pk_fma_f32 v[78:79], v[4:5], s[2:3], v[176:177] op_sel_hi:[1,0,1]
	v_pk_fma_f32 v[174:175], v[6:7], s[2:3], v[174:175] op_sel_hi:[1,0,1]
	v_pk_fma_f32 v[172:173], v[8:9], s[2:3], v[172:173] op_sel_hi:[1,0,1]
	v_pk_fma_f32 v[170:171], v[10:11], s[2:3], v[170:171] op_sel_hi:[1,0,1]
	v_pk_fma_f32 v[168:169], v[12:13], s[2:3], v[168:169] op_sel_hi:[1,0,1]
	v_pk_fma_f32 v[166:167], v[14:15], s[2:3], v[166:167] op_sel_hi:[1,0,1]
	v_pk_fma_f32 v[164:165], v[16:17], s[2:3], v[164:165] op_sel_hi:[1,0,1]
	v_pk_fma_f32 v[162:163], v[18:19], s[2:3], v[162:163] op_sel_hi:[1,0,1]
	v_pk_fma_f32 v[160:161], v[20:21], s[2:3], v[160:161] op_sel_hi:[1,0,1]
	v_pk_fma_f32 v[158:159], v[22:23], s[2:3], v[158:159] op_sel_hi:[1,0,1]
	v_pk_fma_f32 v[156:157], v[24:25], s[2:3], v[156:157] op_sel_hi:[1,0,1]
	v_pk_fma_f32 v[154:155], v[26:27], s[2:3], v[154:155] op_sel_hi:[1,0,1]
	v_pk_fma_f32 v[152:153], v[28:29], s[2:3], v[152:153] op_sel_hi:[1,0,1]
	v_pk_fma_f32 v[150:151], v[30:31], s[2:3], v[150:151] op_sel_hi:[1,0,1]
	v_readlane_b32 s2, v211, 61
	s_waitcnt vmcnt(20)
	v_cvt_scalef32_pk32_f32_fp6 v[0:31], v[68:73], 1.0
	v_pk_fma_f32 v[68:69], v[0:1], s[2:3], v[74:75] op_sel_hi:[1,0,1]
	v_pk_fma_f32 v[70:71], v[2:3], s[2:3], v[76:77] op_sel_hi:[1,0,1]
	v_pk_fma_f32 v[72:73], v[4:5], s[2:3], v[78:79] op_sel_hi:[1,0,1]
	v_pk_fma_f32 v[74:75], v[6:7], s[2:3], v[174:175] op_sel_hi:[1,0,1]
	v_pk_fma_f32 v[76:77], v[8:9], s[2:3], v[172:173] op_sel_hi:[1,0,1]
	v_pk_fma_f32 v[78:79], v[10:11], s[2:3], v[170:171] op_sel_hi:[1,0,1]
	v_pk_fma_f32 v[168:169], v[12:13], s[2:3], v[168:169] op_sel_hi:[1,0,1]
	v_pk_fma_f32 v[166:167], v[14:15], s[2:3], v[166:167] op_sel_hi:[1,0,1]
	v_pk_fma_f32 v[164:165], v[16:17], s[2:3], v[164:165] op_sel_hi:[1,0,1]
	v_pk_fma_f32 v[162:163], v[18:19], s[2:3], v[162:163] op_sel_hi:[1,0,1]
	v_pk_fma_f32 v[160:161], v[20:21], s[2:3], v[160:161] op_sel_hi:[1,0,1]
	v_pk_fma_f32 v[158:159], v[22:23], s[2:3], v[158:159] op_sel_hi:[1,0,1]
	v_pk_fma_f32 v[156:157], v[24:25], s[2:3], v[156:157] op_sel_hi:[1,0,1]
	v_pk_fma_f32 v[154:155], v[26:27], s[2:3], v[154:155] op_sel_hi:[1,0,1]
	v_pk_fma_f32 v[152:153], v[28:29], s[2:3], v[152:153] op_sel_hi:[1,0,1]
	v_pk_fma_f32 v[150:151], v[30:31], s[2:3], v[150:151] op_sel_hi:[1,0,1]
	v_readlane_b32 s2, v211, 62
	s_waitcnt vmcnt(18)
	v_cvt_scalef32_pk32_f32_fp6 v[0:31], v[56:61], 1.0
	v_pk_fma_f32 v[56:57], v[0:1], s[2:3], v[68:69] op_sel_hi:[1,0,1]
	v_pk_fma_f32 v[58:59], v[2:3], s[2:3], v[70:71] op_sel_hi:[1,0,1]
	v_pk_fma_f32 v[60:61], v[4:5], s[2:3], v[72:73] op_sel_hi:[1,0,1]
	v_pk_fma_f32 v[68:69], v[6:7], s[2:3], v[74:75] op_sel_hi:[1,0,1]
	v_pk_fma_f32 v[70:71], v[8:9], s[2:3], v[76:77] op_sel_hi:[1,0,1]
	v_pk_fma_f32 v[72:73], v[10:11], s[2:3], v[78:79] op_sel_hi:[1,0,1]
	v_pk_fma_f32 v[74:75], v[12:13], s[2:3], v[168:169] op_sel_hi:[1,0,1]
	v_pk_fma_f32 v[76:77], v[14:15], s[2:3], v[166:167] op_sel_hi:[1,0,1]
	v_pk_fma_f32 v[78:79], v[16:17], s[2:3], v[164:165] op_sel_hi:[1,0,1]
	v_pk_fma_f32 v[162:163], v[18:19], s[2:3], v[162:163] op_sel_hi:[1,0,1]
	v_pk_fma_f32 v[160:161], v[20:21], s[2:3], v[160:161] op_sel_hi:[1,0,1]
	v_pk_fma_f32 v[158:159], v[22:23], s[2:3], v[158:159] op_sel_hi:[1,0,1]
	v_pk_fma_f32 v[156:157], v[24:25], s[2:3], v[156:157] op_sel_hi:[1,0,1]
	v_pk_fma_f32 v[154:155], v[26:27], s[2:3], v[154:155] op_sel_hi:[1,0,1]
	v_pk_fma_f32 v[152:153], v[28:29], s[2:3], v[152:153] op_sel_hi:[1,0,1]
	v_pk_fma_f32 v[150:151], v[30:31], s[2:3], v[150:151] op_sel_hi:[1,0,1]
	v_readlane_b32 s2, v211, 63
	s_waitcnt vmcnt(16)
	v_cvt_scalef32_pk32_f32_fp6 v[0:31], v[44:49], 1.0
	v_pk_fma_f32 v[164:165], v[0:1], s[2:3], v[56:57] op_sel_hi:[1,0,1]
	v_pk_fma_f32 v[166:167], v[2:3], s[2:3], v[58:59] op_sel_hi:[1,0,1]
	v_pk_fma_f32 v[168:169], v[4:5], s[2:3], v[60:61] op_sel_hi:[1,0,1]
	v_pk_fma_f32 v[170:171], v[6:7], s[2:3], v[68:69] op_sel_hi:[1,0,1]
	v_pk_fma_f32 v[172:173], v[8:9], s[2:3], v[70:71] op_sel_hi:[1,0,1]
	v_pk_fma_f32 v[174:175], v[10:11], s[2:3], v[72:73] op_sel_hi:[1,0,1]
	v_pk_fma_f32 v[176:177], v[12:13], s[2:3], v[74:75] op_sel_hi:[1,0,1]
	v_pk_fma_f32 v[178:179], v[14:15], s[2:3], v[76:77] op_sel_hi:[1,0,1]
	v_pk_fma_f32 v[180:181], v[16:17], s[2:3], v[78:79] op_sel_hi:[1,0,1]
	v_pk_fma_f32 v[162:163], v[18:19], s[2:3], v[162:163] op_sel_hi:[1,0,1]
	v_pk_fma_f32 v[160:161], v[20:21], s[2:3], v[160:161] op_sel_hi:[1,0,1]
	v_pk_fma_f32 v[158:159], v[22:23], s[2:3], v[158:159] op_sel_hi:[1,0,1]
	v_pk_fma_f32 v[156:157], v[24:25], s[2:3], v[156:157] op_sel_hi:[1,0,1]
	v_pk_fma_f32 v[154:155], v[26:27], s[2:3], v[154:155] op_sel_hi:[1,0,1]
	v_pk_fma_f32 v[152:153], v[28:29], s[2:3], v[152:153] op_sel_hi:[1,0,1]
	v_pk_fma_f32 v[150:151], v[30:31], s[2:3], v[150:151] op_sel_hi:[1,0,1]
	v_readlane_b32 s2, v241, 8
	v_readlane_b32 s3, v241, 9
	v_readlane_b32 s100, v241, 10
	v_readlane_b32 s101, v241, 11
	s_nop 1
	buffer_load_dwordx4 v[74:77], v129, s[44:47], s2 offen sc1
	buffer_load_dwordx2 v[78:79], v210, s[44:47], s2 offen sc1
	buffer_load_dwordx4 v[68:71], v129, s[44:47], s3 offen sc1
	buffer_load_dwordx2 v[72:73], v210, s[44:47], s3 offen sc1
	buffer_load_dwordx4 v[56:59], v129, s[44:47], s100 offen sc1
	buffer_load_dwordx2 v[60:61], v210, s[44:47], s100 offen sc1
	buffer_load_dwordx4 v[44:47], v129, s[44:47], s101 offen sc1
	buffer_load_dwordx2 v[48:49], v210, s[44:47], s101 offen sc1
	v_readlane_b32 s2, v131, 0
	s_waitcnt vmcnt(22)
	v_cvt_scalef32_pk32_f32_fp6 v[0:31], v[62:67], 1.0
	v_pk_fma_f32 v[62:63], v[0:1], s[2:3], v[164:165] op_sel_hi:[1,0,1]
	v_pk_fma_f32 v[64:65], v[2:3], s[2:3], v[166:167] op_sel_hi:[1,0,1]
	v_pk_fma_f32 v[66:67], v[4:5], s[2:3], v[168:169] op_sel_hi:[1,0,1]
	v_pk_fma_f32 v[164:165], v[6:7], s[2:3], v[170:171] op_sel_hi:[1,0,1]
	v_pk_fma_f32 v[166:167], v[8:9], s[2:3], v[172:173] op_sel_hi:[1,0,1]
	v_pk_fma_f32 v[168:169], v[10:11], s[2:3], v[174:175] op_sel_hi:[1,0,1]
	v_pk_fma_f32 v[170:171], v[12:13], s[2:3], v[176:177] op_sel_hi:[1,0,1]
	v_pk_fma_f32 v[172:173], v[14:15], s[2:3], v[178:179] op_sel_hi:[1,0,1]
	v_pk_fma_f32 v[174:175], v[16:17], s[2:3], v[180:181] op_sel_hi:[1,0,1]
	v_pk_fma_f32 v[162:163], v[18:19], s[2:3], v[162:163] op_sel_hi:[1,0,1]
	v_pk_fma_f32 v[160:161], v[20:21], s[2:3], v[160:161] op_sel_hi:[1,0,1]
	v_pk_fma_f32 v[158:159], v[22:23], s[2:3], v[158:159] op_sel_hi:[1,0,1]
	v_pk_fma_f32 v[156:157], v[24:25], s[2:3], v[156:157] op_sel_hi:[1,0,1]
	v_pk_fma_f32 v[154:155], v[26:27], s[2:3], v[154:155] op_sel_hi:[1,0,1]
	v_pk_fma_f32 v[152:153], v[28:29], s[2:3], v[152:153] op_sel_hi:[1,0,1]
	v_pk_fma_f32 v[150:151], v[30:31], s[2:3], v[150:151] op_sel_hi:[1,0,1]
	v_readlane_b32 s2, v131, 1
	s_waitcnt vmcnt(20)
	v_cvt_scalef32_pk32_f32_fp6 v[0:31], v[50:55], 1.0
	v_pk_fma_f32 v[50:51], v[0:1], s[2:3], v[62:63] op_sel_hi:[1,0,1]
	v_pk_fma_f32 v[52:53], v[2:3], s[2:3], v[64:65] op_sel_hi:[1,0,1]
	v_pk_fma_f32 v[54:55], v[4:5], s[2:3], v[66:67] op_sel_hi:[1,0,1]
	v_pk_fma_f32 v[62:63], v[6:7], s[2:3], v[164:165] op_sel_hi:[1,0,1]
	v_pk_fma_f32 v[64:65], v[8:9], s[2:3], v[166:167] op_sel_hi:[1,0,1]
	v_pk_fma_f32 v[66:67], v[10:11], s[2:3], v[168:169] op_sel_hi:[1,0,1]
	v_pk_fma_f32 v[164:165], v[12:13], s[2:3], v[170:171] op_sel_hi:[1,0,1]
	v_pk_fma_f32 v[166:167], v[14:15], s[2:3], v[172:173] op_sel_hi:[1,0,1]
	v_pk_fma_f32 v[168:169], v[16:17], s[2:3], v[174:175] op_sel_hi:[1,0,1]
	v_pk_fma_f32 v[162:163], v[18:19], s[2:3], v[162:163] op_sel_hi:[1,0,1]
	v_pk_fma_f32 v[160:161], v[20:21], s[2:3], v[160:161] op_sel_hi:[1,0,1]
	v_pk_fma_f32 v[158:159], v[22:23], s[2:3], v[158:159] op_sel_hi:[1,0,1]
	v_pk_fma_f32 v[156:157], v[24:25], s[2:3], v[156:157] op_sel_hi:[1,0,1]
	v_pk_fma_f32 v[154:155], v[26:27], s[2:3], v[154:155] op_sel_hi:[1,0,1]
	v_pk_fma_f32 v[152:153], v[28:29], s[2:3], v[152:153] op_sel_hi:[1,0,1]
	v_pk_fma_f32 v[150:151], v[30:31], s[2:3], v[150:151] op_sel_hi:[1,0,1]
	v_readlane_b32 s2, v131, 2
	s_waitcnt vmcnt(18)
	v_cvt_scalef32_pk32_f32_fp6 v[0:31], v[38:43], 1.0
	v_pk_fma_f32 v[38:39], v[0:1], s[2:3], v[50:51] op_sel_hi:[1,0,1]
	v_pk_fma_f32 v[40:41], v[2:3], s[2:3], v[52:53] op_sel_hi:[1,0,1]
	v_pk_fma_f32 v[42:43], v[4:5], s[2:3], v[54:55] op_sel_hi:[1,0,1]
	v_pk_fma_f32 v[50:51], v[6:7], s[2:3], v[62:63] op_sel_hi:[1,0,1]
	v_pk_fma_f32 v[52:53], v[8:9], s[2:3], v[64:65] op_sel_hi:[1,0,1]
	v_pk_fma_f32 v[54:55], v[10:11], s[2:3], v[66:67] op_sel_hi:[1,0,1]
	v_pk_fma_f32 v[62:63], v[12:13], s[2:3], v[164:165] op_sel_hi:[1,0,1]
	v_pk_fma_f32 v[64:65], v[14:15], s[2:3], v[166:167] op_sel_hi:[1,0,1]
	v_pk_fma_f32 v[66:67], v[16:17], s[2:3], v[168:169] op_sel_hi:[1,0,1]
	v_pk_fma_f32 v[162:163], v[18:19], s[2:3], v[162:163] op_sel_hi:[1,0,1]
	v_pk_fma_f32 v[160:161], v[20:21], s[2:3], v[160:161] op_sel_hi:[1,0,1]
	v_pk_fma_f32 v[158:159], v[22:23], s[2:3], v[158:159] op_sel_hi:[1,0,1]
	v_pk_fma_f32 v[156:157], v[24:25], s[2:3], v[156:157] op_sel_hi:[1,0,1]
	v_pk_fma_f32 v[154:155], v[26:27], s[2:3], v[154:155] op_sel_hi:[1,0,1]
	v_pk_fma_f32 v[152:153], v[28:29], s[2:3], v[152:153] op_sel_hi:[1,0,1]
	v_pk_fma_f32 v[150:151], v[30:31], s[2:3], v[150:151] op_sel_hi:[1,0,1]
	v_readlane_b32 s2, v131, 3
	s_waitcnt vmcnt(16)
	v_cvt_scalef32_pk32_f32_fp6 v[0:31], v[32:37], 1.0
	v_pk_fma_f32 v[164:165], v[0:1], s[2:3], v[38:39] op_sel_hi:[1,0,1]
	v_pk_fma_f32 v[166:167], v[2:3], s[2:3], v[40:41] op_sel_hi:[1,0,1]
	v_pk_fma_f32 v[168:169], v[4:5], s[2:3], v[42:43] op_sel_hi:[1,0,1]
	v_pk_fma_f32 v[170:171], v[6:7], s[2:3], v[50:51] op_sel_hi:[1,0,1]
	v_pk_fma_f32 v[172:173], v[8:9], s[2:3], v[52:53] op_sel_hi:[1,0,1]
	v_pk_fma_f32 v[174:175], v[10:11], s[2:3], v[54:55] op_sel_hi:[1,0,1]
	v_pk_fma_f32 v[176:177], v[12:13], s[2:3], v[62:63] op_sel_hi:[1,0,1]
	v_pk_fma_f32 v[178:179], v[14:15], s[2:3], v[64:65] op_sel_hi:[1,0,1]
	v_pk_fma_f32 v[180:181], v[16:17], s[2:3], v[66:67] op_sel_hi:[1,0,1]
	v_pk_fma_f32 v[162:163], v[18:19], s[2:3], v[162:163] op_sel_hi:[1,0,1]
	v_pk_fma_f32 v[160:161], v[20:21], s[2:3], v[160:161] op_sel_hi:[1,0,1]
	v_pk_fma_f32 v[158:159], v[22:23], s[2:3], v[158:159] op_sel_hi:[1,0,1]
	v_pk_fma_f32 v[156:157], v[24:25], s[2:3], v[156:157] op_sel_hi:[1,0,1]
	v_pk_fma_f32 v[154:155], v[26:27], s[2:3], v[154:155] op_sel_hi:[1,0,1]
	v_pk_fma_f32 v[152:153], v[28:29], s[2:3], v[152:153] op_sel_hi:[1,0,1]
	v_pk_fma_f32 v[150:151], v[30:31], s[2:3], v[150:151] op_sel_hi:[1,0,1]
	v_readlane_b32 s2, v241, 12
	v_readlane_b32 s3, v241, 13
	v_readlane_b32 s100, v241, 14
	v_readlane_b32 s101, v241, 15
	s_nop 1
	buffer_load_dwordx4 v[62:65], v129, s[44:47], s2 offen sc1
	buffer_load_dwordx2 v[66:67], v210, s[44:47], s2 offen sc1
	buffer_load_dwordx4 v[50:53], v129, s[44:47], s3 offen sc1
	buffer_load_dwordx2 v[54:55], v210, s[44:47], s3 offen sc1
	buffer_load_dwordx4 v[38:41], v129, s[44:47], s100 offen sc1
	buffer_load_dwordx2 v[42:43], v210, s[44:47], s100 offen sc1
	buffer_load_dwordx4 v[32:35], v129, s[44:47], s101 offen sc1
	buffer_load_dwordx2 v[36:37], v210, s[44:47], s101 offen sc1
	v_readlane_b32 s2, v131, 4
	s_waitcnt vmcnt(22)
	v_cvt_scalef32_pk32_f32_fp6 v[0:31], v[98:103], 1.0
	v_pk_fma_f32 v[98:99], v[0:1], s[2:3], v[164:165] op_sel_hi:[1,0,1]
	v_pk_fma_f32 v[100:101], v[2:3], s[2:3], v[166:167] op_sel_hi:[1,0,1]
	v_pk_fma_f32 v[102:103], v[4:5], s[2:3], v[168:169] op_sel_hi:[1,0,1]
	v_pk_fma_f32 v[164:165], v[6:7], s[2:3], v[170:171] op_sel_hi:[1,0,1]
	v_pk_fma_f32 v[166:167], v[8:9], s[2:3], v[172:173] op_sel_hi:[1,0,1]
	v_pk_fma_f32 v[168:169], v[10:11], s[2:3], v[174:175] op_sel_hi:[1,0,1]
	v_pk_fma_f32 v[170:171], v[12:13], s[2:3], v[176:177] op_sel_hi:[1,0,1]
	v_pk_fma_f32 v[172:173], v[14:15], s[2:3], v[178:179] op_sel_hi:[1,0,1]
	v_pk_fma_f32 v[174:175], v[16:17], s[2:3], v[180:181] op_sel_hi:[1,0,1]
	v_pk_fma_f32 v[162:163], v[18:19], s[2:3], v[162:163] op_sel_hi:[1,0,1]
	v_pk_fma_f32 v[160:161], v[20:21], s[2:3], v[160:161] op_sel_hi:[1,0,1]
	v_pk_fma_f32 v[158:159], v[22:23], s[2:3], v[158:159] op_sel_hi:[1,0,1]
	v_pk_fma_f32 v[156:157], v[24:25], s[2:3], v[156:157] op_sel_hi:[1,0,1]
	v_pk_fma_f32 v[154:155], v[26:27], s[2:3], v[154:155] op_sel_hi:[1,0,1]
	v_pk_fma_f32 v[152:153], v[28:29], s[2:3], v[152:153] op_sel_hi:[1,0,1]
	v_pk_fma_f32 v[150:151], v[30:31], s[2:3], v[150:151] op_sel_hi:[1,0,1]
	v_readlane_b32 s2, v131, 5
	s_waitcnt vmcnt(20)
	v_cvt_scalef32_pk32_f32_fp6 v[0:31], v[92:97], 1.0
	v_pk_fma_f32 v[92:93], v[0:1], s[2:3], v[98:99] op_sel_hi:[1,0,1]
	v_pk_fma_f32 v[94:95], v[2:3], s[2:3], v[100:101] op_sel_hi:[1,0,1]
	v_pk_fma_f32 v[96:97], v[4:5], s[2:3], v[102:103] op_sel_hi:[1,0,1]
	v_pk_fma_f32 v[98:99], v[6:7], s[2:3], v[164:165] op_sel_hi:[1,0,1]
	v_pk_fma_f32 v[100:101], v[8:9], s[2:3], v[166:167] op_sel_hi:[1,0,1]
	v_pk_fma_f32 v[102:103], v[10:11], s[2:3], v[168:169] op_sel_hi:[1,0,1]
	v_pk_fma_f32 v[164:165], v[12:13], s[2:3], v[170:171] op_sel_hi:[1,0,1]
	v_pk_fma_f32 v[166:167], v[14:15], s[2:3], v[172:173] op_sel_hi:[1,0,1]
	v_pk_fma_f32 v[168:169], v[16:17], s[2:3], v[174:175] op_sel_hi:[1,0,1]
	v_pk_fma_f32 v[162:163], v[18:19], s[2:3], v[162:163] op_sel_hi:[1,0,1]
	v_pk_fma_f32 v[160:161], v[20:21], s[2:3], v[160:161] op_sel_hi:[1,0,1]
	v_pk_fma_f32 v[158:159], v[22:23], s[2:3], v[158:159] op_sel_hi:[1,0,1]
	v_pk_fma_f32 v[156:157], v[24:25], s[2:3], v[156:157] op_sel_hi:[1,0,1]
	v_pk_fma_f32 v[154:155], v[26:27], s[2:3], v[154:155] op_sel_hi:[1,0,1]
	v_pk_fma_f32 v[152:153], v[28:29], s[2:3], v[152:153] op_sel_hi:[1,0,1]
	v_pk_fma_f32 v[150:151], v[30:31], s[2:3], v[150:151] op_sel_hi:[1,0,1]
	v_readlane_b32 s2, v131, 6
	s_waitcnt vmcnt(18)
	v_cvt_scalef32_pk32_f32_fp6 v[0:31], v[86:91], 1.0
	v_pk_fma_f32 v[86:87], v[0:1], s[2:3], v[92:93] op_sel_hi:[1,0,1]
	v_pk_fma_f32 v[88:89], v[2:3], s[2:3], v[94:95] op_sel_hi:[1,0,1]
	v_pk_fma_f32 v[90:91], v[4:5], s[2:3], v[96:97] op_sel_hi:[1,0,1]
	v_pk_fma_f32 v[92:93], v[6:7], s[2:3], v[98:99] op_sel_hi:[1,0,1]
	v_pk_fma_f32 v[94:95], v[8:9], s[2:3], v[100:101] op_sel_hi:[1,0,1]
	v_pk_fma_f32 v[96:97], v[10:11], s[2:3], v[102:103] op_sel_hi:[1,0,1]
	v_pk_fma_f32 v[98:99], v[12:13], s[2:3], v[164:165] op_sel_hi:[1,0,1]
	v_pk_fma_f32 v[100:101], v[14:15], s[2:3], v[166:167] op_sel_hi:[1,0,1]
	v_pk_fma_f32 v[102:103], v[16:17], s[2:3], v[168:169] op_sel_hi:[1,0,1]
	v_pk_fma_f32 v[162:163], v[18:19], s[2:3], v[162:163] op_sel_hi:[1,0,1]
	v_pk_fma_f32 v[160:161], v[20:21], s[2:3], v[160:161] op_sel_hi:[1,0,1]
	v_pk_fma_f32 v[158:159], v[22:23], s[2:3], v[158:159] op_sel_hi:[1,0,1]
	v_pk_fma_f32 v[156:157], v[24:25], s[2:3], v[156:157] op_sel_hi:[1,0,1]
	v_pk_fma_f32 v[154:155], v[26:27], s[2:3], v[154:155] op_sel_hi:[1,0,1]
	v_pk_fma_f32 v[152:153], v[28:29], s[2:3], v[152:153] op_sel_hi:[1,0,1]
	v_pk_fma_f32 v[150:151], v[30:31], s[2:3], v[150:151] op_sel_hi:[1,0,1]
	v_readlane_b32 s2, v131, 7
	s_waitcnt vmcnt(16)
	v_cvt_scalef32_pk32_f32_fp6 v[0:31], v[80:85], 1.0
	v_pk_fma_f32 v[180:181], v[0:1], s[2:3], v[86:87] op_sel_hi:[1,0,1]
	v_pk_fma_f32 v[178:179], v[2:3], s[2:3], v[88:89] op_sel_hi:[1,0,1]
	v_pk_fma_f32 v[176:177], v[4:5], s[2:3], v[90:91] op_sel_hi:[1,0,1]
	v_pk_fma_f32 v[174:175], v[6:7], s[2:3], v[92:93] op_sel_hi:[1,0,1]
	v_pk_fma_f32 v[172:173], v[8:9], s[2:3], v[94:95] op_sel_hi:[1,0,1]
	v_pk_fma_f32 v[170:171], v[10:11], s[2:3], v[96:97] op_sel_hi:[1,0,1]
	v_pk_fma_f32 v[168:169], v[12:13], s[2:3], v[98:99] op_sel_hi:[1,0,1]
	v_pk_fma_f32 v[166:167], v[14:15], s[2:3], v[100:101] op_sel_hi:[1,0,1]
	v_pk_fma_f32 v[164:165], v[16:17], s[2:3], v[102:103] op_sel_hi:[1,0,1]
	v_pk_fma_f32 v[162:163], v[18:19], s[2:3], v[162:163] op_sel_hi:[1,0,1]
	v_pk_fma_f32 v[160:161], v[20:21], s[2:3], v[160:161] op_sel_hi:[1,0,1]
	v_pk_fma_f32 v[158:159], v[22:23], s[2:3], v[158:159] op_sel_hi:[1,0,1]
	v_pk_fma_f32 v[156:157], v[24:25], s[2:3], v[156:157] op_sel_hi:[1,0,1]
	v_pk_fma_f32 v[154:155], v[26:27], s[2:3], v[154:155] op_sel_hi:[1,0,1]
	v_pk_fma_f32 v[152:153], v[28:29], s[2:3], v[152:153] op_sel_hi:[1,0,1]
	v_pk_fma_f32 v[150:151], v[30:31], s[2:3], v[150:151] op_sel_hi:[1,0,1]
	v_readlane_b32 s2, v241, 16
	v_readlane_b32 s3, v241, 17
	v_readlane_b32 s100, v241, 18
	v_readlane_b32 s101, v241, 19
	s_nop 1
	buffer_load_dwordx4 v[98:101], v129, s[44:47], s2 offen sc1
	buffer_load_dwordx2 v[102:103], v210, s[44:47], s2 offen sc1
	buffer_load_dwordx4 v[92:95], v129, s[44:47], s3 offen sc1
	buffer_load_dwordx2 v[96:97], v210, s[44:47], s3 offen sc1
	buffer_load_dwordx4 v[86:89], v129, s[44:47], s100 offen sc1
	buffer_load_dwordx2 v[90:91], v210, s[44:47], s100 offen sc1
	buffer_load_dwordx4 v[80:83], v129, s[44:47], s101 offen sc1
	buffer_load_dwordx2 v[84:85], v210, s[44:47], s101 offen sc1
	v_readlane_b32 s2, v131, 8
	s_waitcnt vmcnt(22)
	v_cvt_scalef32_pk32_f32_fp6 v[0:31], v[74:79], 1.0
	v_pk_fma_f32 v[74:75], v[0:1], s[2:3], v[180:181] op_sel_hi:[1,0,1]
	v_pk_fma_f32 v[76:77], v[2:3], s[2:3], v[178:179] op_sel_hi:[1,0,1]
	v_pk_fma_f32 v[78:79], v[4:5], s[2:3], v[176:177] op_sel_hi:[1,0,1]
	v_pk_fma_f32 v[174:175], v[6:7], s[2:3], v[174:175] op_sel_hi:[1,0,1]
	v_pk_fma_f32 v[172:173], v[8:9], s[2:3], v[172:173] op_sel_hi:[1,0,1]
	v_pk_fma_f32 v[170:171], v[10:11], s[2:3], v[170:171] op_sel_hi:[1,0,1]
	v_pk_fma_f32 v[168:169], v[12:13], s[2:3], v[168:169] op_sel_hi:[1,0,1]
	v_pk_fma_f32 v[166:167], v[14:15], s[2:3], v[166:167] op_sel_hi:[1,0,1]
	v_pk_fma_f32 v[164:165], v[16:17], s[2:3], v[164:165] op_sel_hi:[1,0,1]
	v_pk_fma_f32 v[162:163], v[18:19], s[2:3], v[162:163] op_sel_hi:[1,0,1]
	v_pk_fma_f32 v[160:161], v[20:21], s[2:3], v[160:161] op_sel_hi:[1,0,1]
	v_pk_fma_f32 v[158:159], v[22:23], s[2:3], v[158:159] op_sel_hi:[1,0,1]
	v_pk_fma_f32 v[156:157], v[24:25], s[2:3], v[156:157] op_sel_hi:[1,0,1]
	v_pk_fma_f32 v[154:155], v[26:27], s[2:3], v[154:155] op_sel_hi:[1,0,1]
	v_pk_fma_f32 v[152:153], v[28:29], s[2:3], v[152:153] op_sel_hi:[1,0,1]
	v_pk_fma_f32 v[150:151], v[30:31], s[2:3], v[150:151] op_sel_hi:[1,0,1]
	v_readlane_b32 s2, v131, 9
	s_waitcnt vmcnt(20)
	v_cvt_scalef32_pk32_f32_fp6 v[0:31], v[68:73], 1.0
	v_pk_fma_f32 v[68:69], v[0:1], s[2:3], v[74:75] op_sel_hi:[1,0,1]
	v_pk_fma_f32 v[70:71], v[2:3], s[2:3], v[76:77] op_sel_hi:[1,0,1]
	v_pk_fma_f32 v[72:73], v[4:5], s[2:3], v[78:79] op_sel_hi:[1,0,1]
	v_pk_fma_f32 v[74:75], v[6:7], s[2:3], v[174:175] op_sel_hi:[1,0,1]
	v_pk_fma_f32 v[76:77], v[8:9], s[2:3], v[172:173] op_sel_hi:[1,0,1]
	v_pk_fma_f32 v[78:79], v[10:11], s[2:3], v[170:171] op_sel_hi:[1,0,1]
	v_pk_fma_f32 v[168:169], v[12:13], s[2:3], v[168:169] op_sel_hi:[1,0,1]
	v_pk_fma_f32 v[166:167], v[14:15], s[2:3], v[166:167] op_sel_hi:[1,0,1]
	v_pk_fma_f32 v[164:165], v[16:17], s[2:3], v[164:165] op_sel_hi:[1,0,1]
	v_pk_fma_f32 v[162:163], v[18:19], s[2:3], v[162:163] op_sel_hi:[1,0,1]
	v_pk_fma_f32 v[160:161], v[20:21], s[2:3], v[160:161] op_sel_hi:[1,0,1]
	v_pk_fma_f32 v[158:159], v[22:23], s[2:3], v[158:159] op_sel_hi:[1,0,1]
	v_pk_fma_f32 v[156:157], v[24:25], s[2:3], v[156:157] op_sel_hi:[1,0,1]
	v_pk_fma_f32 v[154:155], v[26:27], s[2:3], v[154:155] op_sel_hi:[1,0,1]
	v_pk_fma_f32 v[152:153], v[28:29], s[2:3], v[152:153] op_sel_hi:[1,0,1]
	v_pk_fma_f32 v[150:151], v[30:31], s[2:3], v[150:151] op_sel_hi:[1,0,1]
	v_readlane_b32 s2, v131, 10
	s_waitcnt vmcnt(18)
	v_cvt_scalef32_pk32_f32_fp6 v[0:31], v[56:61], 1.0
	v_pk_fma_f32 v[56:57], v[0:1], s[2:3], v[68:69] op_sel_hi:[1,0,1]
	v_pk_fma_f32 v[58:59], v[2:3], s[2:3], v[70:71] op_sel_hi:[1,0,1]
	v_pk_fma_f32 v[60:61], v[4:5], s[2:3], v[72:73] op_sel_hi:[1,0,1]
	v_pk_fma_f32 v[68:69], v[6:7], s[2:3], v[74:75] op_sel_hi:[1,0,1]
	v_pk_fma_f32 v[70:71], v[8:9], s[2:3], v[76:77] op_sel_hi:[1,0,1]
	v_pk_fma_f32 v[72:73], v[10:11], s[2:3], v[78:79] op_sel_hi:[1,0,1]
	v_pk_fma_f32 v[74:75], v[12:13], s[2:3], v[168:169] op_sel_hi:[1,0,1]
	v_pk_fma_f32 v[76:77], v[14:15], s[2:3], v[166:167] op_sel_hi:[1,0,1]
	v_pk_fma_f32 v[78:79], v[16:17], s[2:3], v[164:165] op_sel_hi:[1,0,1]
	v_pk_fma_f32 v[162:163], v[18:19], s[2:3], v[162:163] op_sel_hi:[1,0,1]
	v_pk_fma_f32 v[160:161], v[20:21], s[2:3], v[160:161] op_sel_hi:[1,0,1]
	v_pk_fma_f32 v[158:159], v[22:23], s[2:3], v[158:159] op_sel_hi:[1,0,1]
	v_pk_fma_f32 v[156:157], v[24:25], s[2:3], v[156:157] op_sel_hi:[1,0,1]
	v_pk_fma_f32 v[154:155], v[26:27], s[2:3], v[154:155] op_sel_hi:[1,0,1]
	v_pk_fma_f32 v[152:153], v[28:29], s[2:3], v[152:153] op_sel_hi:[1,0,1]
	v_pk_fma_f32 v[150:151], v[30:31], s[2:3], v[150:151] op_sel_hi:[1,0,1]
	v_readlane_b32 s2, v131, 11
	s_waitcnt vmcnt(16)
	v_cvt_scalef32_pk32_f32_fp6 v[0:31], v[44:49], 1.0
	v_pk_fma_f32 v[164:165], v[0:1], s[2:3], v[56:57] op_sel_hi:[1,0,1]
	v_pk_fma_f32 v[166:167], v[2:3], s[2:3], v[58:59] op_sel_hi:[1,0,1]
	v_pk_fma_f32 v[168:169], v[4:5], s[2:3], v[60:61] op_sel_hi:[1,0,1]
	v_pk_fma_f32 v[170:171], v[6:7], s[2:3], v[68:69] op_sel_hi:[1,0,1]
	v_pk_fma_f32 v[172:173], v[8:9], s[2:3], v[70:71] op_sel_hi:[1,0,1]
	v_pk_fma_f32 v[174:175], v[10:11], s[2:3], v[72:73] op_sel_hi:[1,0,1]
	v_pk_fma_f32 v[176:177], v[12:13], s[2:3], v[74:75] op_sel_hi:[1,0,1]
	v_pk_fma_f32 v[178:179], v[14:15], s[2:3], v[76:77] op_sel_hi:[1,0,1]
	v_pk_fma_f32 v[180:181], v[16:17], s[2:3], v[78:79] op_sel_hi:[1,0,1]
	v_pk_fma_f32 v[162:163], v[18:19], s[2:3], v[162:163] op_sel_hi:[1,0,1]
	v_pk_fma_f32 v[160:161], v[20:21], s[2:3], v[160:161] op_sel_hi:[1,0,1]
	v_pk_fma_f32 v[158:159], v[22:23], s[2:3], v[158:159] op_sel_hi:[1,0,1]
	v_pk_fma_f32 v[156:157], v[24:25], s[2:3], v[156:157] op_sel_hi:[1,0,1]
	v_pk_fma_f32 v[154:155], v[26:27], s[2:3], v[154:155] op_sel_hi:[1,0,1]
	v_pk_fma_f32 v[152:153], v[28:29], s[2:3], v[152:153] op_sel_hi:[1,0,1]
	v_pk_fma_f32 v[150:151], v[30:31], s[2:3], v[150:151] op_sel_hi:[1,0,1]
	v_readlane_b32 s2, v241, 20
	v_readlane_b32 s3, v241, 21
	v_readlane_b32 s100, v241, 22
	v_readlane_b32 s101, v241, 23
	s_nop 1
	buffer_load_dwordx4 v[74:77], v129, s[44:47], s2 offen sc1
	buffer_load_dwordx2 v[78:79], v210, s[44:47], s2 offen sc1
	buffer_load_dwordx4 v[68:71], v129, s[44:47], s3 offen sc1
	buffer_load_dwordx2 v[72:73], v210, s[44:47], s3 offen sc1
	buffer_load_dwordx4 v[56:59], v129, s[44:47], s100 offen sc1
	buffer_load_dwordx2 v[60:61], v210, s[44:47], s100 offen sc1
	buffer_load_dwordx4 v[44:47], v129, s[44:47], s101 offen sc1
	buffer_load_dwordx2 v[48:49], v210, s[44:47], s101 offen sc1
	v_readlane_b32 s2, v131, 12
	s_waitcnt vmcnt(22)
	v_cvt_scalef32_pk32_f32_fp6 v[0:31], v[62:67], 1.0
	v_pk_fma_f32 v[62:63], v[0:1], s[2:3], v[164:165] op_sel_hi:[1,0,1]
	v_pk_fma_f32 v[64:65], v[2:3], s[2:3], v[166:167] op_sel_hi:[1,0,1]
	v_pk_fma_f32 v[66:67], v[4:5], s[2:3], v[168:169] op_sel_hi:[1,0,1]
	v_pk_fma_f32 v[164:165], v[6:7], s[2:3], v[170:171] op_sel_hi:[1,0,1]
	v_pk_fma_f32 v[166:167], v[8:9], s[2:3], v[172:173] op_sel_hi:[1,0,1]
	v_pk_fma_f32 v[168:169], v[10:11], s[2:3], v[174:175] op_sel_hi:[1,0,1]
	v_pk_fma_f32 v[170:171], v[12:13], s[2:3], v[176:177] op_sel_hi:[1,0,1]
	v_pk_fma_f32 v[172:173], v[14:15], s[2:3], v[178:179] op_sel_hi:[1,0,1]
	v_pk_fma_f32 v[174:175], v[16:17], s[2:3], v[180:181] op_sel_hi:[1,0,1]
	v_pk_fma_f32 v[162:163], v[18:19], s[2:3], v[162:163] op_sel_hi:[1,0,1]
	v_pk_fma_f32 v[160:161], v[20:21], s[2:3], v[160:161] op_sel_hi:[1,0,1]
	v_pk_fma_f32 v[158:159], v[22:23], s[2:3], v[158:159] op_sel_hi:[1,0,1]
	v_pk_fma_f32 v[156:157], v[24:25], s[2:3], v[156:157] op_sel_hi:[1,0,1]
	v_pk_fma_f32 v[154:155], v[26:27], s[2:3], v[154:155] op_sel_hi:[1,0,1]
	v_pk_fma_f32 v[152:153], v[28:29], s[2:3], v[152:153] op_sel_hi:[1,0,1]
	v_pk_fma_f32 v[150:151], v[30:31], s[2:3], v[150:151] op_sel_hi:[1,0,1]
	v_readlane_b32 s2, v131, 13
	s_waitcnt vmcnt(20)
	v_cvt_scalef32_pk32_f32_fp6 v[0:31], v[50:55], 1.0
	v_pk_fma_f32 v[50:51], v[0:1], s[2:3], v[62:63] op_sel_hi:[1,0,1]
	v_pk_fma_f32 v[52:53], v[2:3], s[2:3], v[64:65] op_sel_hi:[1,0,1]
	v_pk_fma_f32 v[54:55], v[4:5], s[2:3], v[66:67] op_sel_hi:[1,0,1]
	v_pk_fma_f32 v[62:63], v[6:7], s[2:3], v[164:165] op_sel_hi:[1,0,1]
	v_pk_fma_f32 v[64:65], v[8:9], s[2:3], v[166:167] op_sel_hi:[1,0,1]
	v_pk_fma_f32 v[66:67], v[10:11], s[2:3], v[168:169] op_sel_hi:[1,0,1]
	v_pk_fma_f32 v[164:165], v[12:13], s[2:3], v[170:171] op_sel_hi:[1,0,1]
	v_pk_fma_f32 v[166:167], v[14:15], s[2:3], v[172:173] op_sel_hi:[1,0,1]
	v_pk_fma_f32 v[168:169], v[16:17], s[2:3], v[174:175] op_sel_hi:[1,0,1]
	v_pk_fma_f32 v[162:163], v[18:19], s[2:3], v[162:163] op_sel_hi:[1,0,1]
	v_pk_fma_f32 v[160:161], v[20:21], s[2:3], v[160:161] op_sel_hi:[1,0,1]
	v_pk_fma_f32 v[158:159], v[22:23], s[2:3], v[158:159] op_sel_hi:[1,0,1]
	v_pk_fma_f32 v[156:157], v[24:25], s[2:3], v[156:157] op_sel_hi:[1,0,1]
	v_pk_fma_f32 v[154:155], v[26:27], s[2:3], v[154:155] op_sel_hi:[1,0,1]
	v_pk_fma_f32 v[152:153], v[28:29], s[2:3], v[152:153] op_sel_hi:[1,0,1]
	v_pk_fma_f32 v[150:151], v[30:31], s[2:3], v[150:151] op_sel_hi:[1,0,1]
	v_readlane_b32 s2, v131, 14
	s_waitcnt vmcnt(18)
	v_cvt_scalef32_pk32_f32_fp6 v[0:31], v[38:43], 1.0
	v_pk_fma_f32 v[38:39], v[0:1], s[2:3], v[50:51] op_sel_hi:[1,0,1]
	v_pk_fma_f32 v[40:41], v[2:3], s[2:3], v[52:53] op_sel_hi:[1,0,1]
	v_pk_fma_f32 v[42:43], v[4:5], s[2:3], v[54:55] op_sel_hi:[1,0,1]
	v_pk_fma_f32 v[50:51], v[6:7], s[2:3], v[62:63] op_sel_hi:[1,0,1]
	v_pk_fma_f32 v[52:53], v[8:9], s[2:3], v[64:65] op_sel_hi:[1,0,1]
	v_pk_fma_f32 v[54:55], v[10:11], s[2:3], v[66:67] op_sel_hi:[1,0,1]
	v_pk_fma_f32 v[62:63], v[12:13], s[2:3], v[164:165] op_sel_hi:[1,0,1]
	v_pk_fma_f32 v[64:65], v[14:15], s[2:3], v[166:167] op_sel_hi:[1,0,1]
	v_pk_fma_f32 v[66:67], v[16:17], s[2:3], v[168:169] op_sel_hi:[1,0,1]
	v_pk_fma_f32 v[162:163], v[18:19], s[2:3], v[162:163] op_sel_hi:[1,0,1]
	v_pk_fma_f32 v[160:161], v[20:21], s[2:3], v[160:161] op_sel_hi:[1,0,1]
	v_pk_fma_f32 v[158:159], v[22:23], s[2:3], v[158:159] op_sel_hi:[1,0,1]
	v_pk_fma_f32 v[156:157], v[24:25], s[2:3], v[156:157] op_sel_hi:[1,0,1]
	v_pk_fma_f32 v[154:155], v[26:27], s[2:3], v[154:155] op_sel_hi:[1,0,1]
	v_pk_fma_f32 v[152:153], v[28:29], s[2:3], v[152:153] op_sel_hi:[1,0,1]
	v_pk_fma_f32 v[150:151], v[30:31], s[2:3], v[150:151] op_sel_hi:[1,0,1]
	v_readlane_b32 s2, v131, 15
	s_waitcnt vmcnt(16)
	v_cvt_scalef32_pk32_f32_fp6 v[0:31], v[32:37], 1.0
	v_pk_fma_f32 v[164:165], v[0:1], s[2:3], v[38:39] op_sel_hi:[1,0,1]
	v_pk_fma_f32 v[166:167], v[2:3], s[2:3], v[40:41] op_sel_hi:[1,0,1]
	v_pk_fma_f32 v[168:169], v[4:5], s[2:3], v[42:43] op_sel_hi:[1,0,1]
	v_pk_fma_f32 v[170:171], v[6:7], s[2:3], v[50:51] op_sel_hi:[1,0,1]
	v_pk_fma_f32 v[172:173], v[8:9], s[2:3], v[52:53] op_sel_hi:[1,0,1]
	v_pk_fma_f32 v[174:175], v[10:11], s[2:3], v[54:55] op_sel_hi:[1,0,1]
	v_pk_fma_f32 v[176:177], v[12:13], s[2:3], v[62:63] op_sel_hi:[1,0,1]
	v_pk_fma_f32 v[178:179], v[14:15], s[2:3], v[64:65] op_sel_hi:[1,0,1]
	v_pk_fma_f32 v[180:181], v[16:17], s[2:3], v[66:67] op_sel_hi:[1,0,1]
	v_pk_fma_f32 v[162:163], v[18:19], s[2:3], v[162:163] op_sel_hi:[1,0,1]
	v_pk_fma_f32 v[160:161], v[20:21], s[2:3], v[160:161] op_sel_hi:[1,0,1]
	v_pk_fma_f32 v[158:159], v[22:23], s[2:3], v[158:159] op_sel_hi:[1,0,1]
	v_pk_fma_f32 v[156:157], v[24:25], s[2:3], v[156:157] op_sel_hi:[1,0,1]
	v_pk_fma_f32 v[154:155], v[26:27], s[2:3], v[154:155] op_sel_hi:[1,0,1]
	v_pk_fma_f32 v[152:153], v[28:29], s[2:3], v[152:153] op_sel_hi:[1,0,1]
	v_pk_fma_f32 v[150:151], v[30:31], s[2:3], v[150:151] op_sel_hi:[1,0,1]
	v_readlane_b32 s2, v241, 24
	v_readlane_b32 s3, v241, 25
	v_readlane_b32 s100, v241, 26
	v_readlane_b32 s101, v241, 27
	s_nop 1
	buffer_load_dwordx4 v[62:65], v129, s[44:47], s2 offen sc1
	buffer_load_dwordx2 v[66:67], v210, s[44:47], s2 offen sc1
	buffer_load_dwordx4 v[50:53], v129, s[44:47], s3 offen sc1
	buffer_load_dwordx2 v[54:55], v210, s[44:47], s3 offen sc1
	buffer_load_dwordx4 v[38:41], v129, s[44:47], s100 offen sc1
	buffer_load_dwordx2 v[42:43], v210, s[44:47], s100 offen sc1
	buffer_load_dwordx4 v[32:35], v129, s[44:47], s101 offen sc1
	buffer_load_dwordx2 v[36:37], v210, s[44:47], s101 offen sc1
	v_readlane_b32 s2, v131, 16
	s_waitcnt vmcnt(22)
	v_cvt_scalef32_pk32_f32_fp6 v[0:31], v[98:103], 1.0
	v_pk_fma_f32 v[98:99], v[0:1], s[2:3], v[164:165] op_sel_hi:[1,0,1]
	v_pk_fma_f32 v[100:101], v[2:3], s[2:3], v[166:167] op_sel_hi:[1,0,1]
	v_pk_fma_f32 v[102:103], v[4:5], s[2:3], v[168:169] op_sel_hi:[1,0,1]
	v_pk_fma_f32 v[164:165], v[6:7], s[2:3], v[170:171] op_sel_hi:[1,0,1]
	v_pk_fma_f32 v[166:167], v[8:9], s[2:3], v[172:173] op_sel_hi:[1,0,1]
	v_pk_fma_f32 v[168:169], v[10:11], s[2:3], v[174:175] op_sel_hi:[1,0,1]
	v_pk_fma_f32 v[170:171], v[12:13], s[2:3], v[176:177] op_sel_hi:[1,0,1]
	v_pk_fma_f32 v[172:173], v[14:15], s[2:3], v[178:179] op_sel_hi:[1,0,1]
	v_pk_fma_f32 v[174:175], v[16:17], s[2:3], v[180:181] op_sel_hi:[1,0,1]
	v_pk_fma_f32 v[162:163], v[18:19], s[2:3], v[162:163] op_sel_hi:[1,0,1]
	v_pk_fma_f32 v[160:161], v[20:21], s[2:3], v[160:161] op_sel_hi:[1,0,1]
	v_pk_fma_f32 v[158:159], v[22:23], s[2:3], v[158:159] op_sel_hi:[1,0,1]
	v_pk_fma_f32 v[156:157], v[24:25], s[2:3], v[156:157] op_sel_hi:[1,0,1]
	v_pk_fma_f32 v[154:155], v[26:27], s[2:3], v[154:155] op_sel_hi:[1,0,1]
	v_pk_fma_f32 v[152:153], v[28:29], s[2:3], v[152:153] op_sel_hi:[1,0,1]
	v_pk_fma_f32 v[150:151], v[30:31], s[2:3], v[150:151] op_sel_hi:[1,0,1]
	v_readlane_b32 s2, v131, 17
	s_waitcnt vmcnt(20)
	v_cvt_scalef32_pk32_f32_fp6 v[0:31], v[92:97], 1.0
	v_pk_fma_f32 v[92:93], v[0:1], s[2:3], v[98:99] op_sel_hi:[1,0,1]
	v_pk_fma_f32 v[94:95], v[2:3], s[2:3], v[100:101] op_sel_hi:[1,0,1]
	v_pk_fma_f32 v[96:97], v[4:5], s[2:3], v[102:103] op_sel_hi:[1,0,1]
	v_pk_fma_f32 v[98:99], v[6:7], s[2:3], v[164:165] op_sel_hi:[1,0,1]
	v_pk_fma_f32 v[100:101], v[8:9], s[2:3], v[166:167] op_sel_hi:[1,0,1]
	v_pk_fma_f32 v[102:103], v[10:11], s[2:3], v[168:169] op_sel_hi:[1,0,1]
	v_pk_fma_f32 v[164:165], v[12:13], s[2:3], v[170:171] op_sel_hi:[1,0,1]
	v_pk_fma_f32 v[166:167], v[14:15], s[2:3], v[172:173] op_sel_hi:[1,0,1]
	v_pk_fma_f32 v[168:169], v[16:17], s[2:3], v[174:175] op_sel_hi:[1,0,1]
	v_pk_fma_f32 v[162:163], v[18:19], s[2:3], v[162:163] op_sel_hi:[1,0,1]
	v_pk_fma_f32 v[160:161], v[20:21], s[2:3], v[160:161] op_sel_hi:[1,0,1]
	v_pk_fma_f32 v[158:159], v[22:23], s[2:3], v[158:159] op_sel_hi:[1,0,1]
	v_pk_fma_f32 v[156:157], v[24:25], s[2:3], v[156:157] op_sel_hi:[1,0,1]
	v_pk_fma_f32 v[154:155], v[26:27], s[2:3], v[154:155] op_sel_hi:[1,0,1]
	v_pk_fma_f32 v[152:153], v[28:29], s[2:3], v[152:153] op_sel_hi:[1,0,1]
	v_pk_fma_f32 v[150:151], v[30:31], s[2:3], v[150:151] op_sel_hi:[1,0,1]
	v_readlane_b32 s2, v131, 18
	s_waitcnt vmcnt(18)
	v_cvt_scalef32_pk32_f32_fp6 v[0:31], v[86:91], 1.0
	v_pk_fma_f32 v[86:87], v[0:1], s[2:3], v[92:93] op_sel_hi:[1,0,1]
	v_pk_fma_f32 v[88:89], v[2:3], s[2:3], v[94:95] op_sel_hi:[1,0,1]
	v_pk_fma_f32 v[90:91], v[4:5], s[2:3], v[96:97] op_sel_hi:[1,0,1]
	v_pk_fma_f32 v[92:93], v[6:7], s[2:3], v[98:99] op_sel_hi:[1,0,1]
	v_pk_fma_f32 v[94:95], v[8:9], s[2:3], v[100:101] op_sel_hi:[1,0,1]
	v_pk_fma_f32 v[96:97], v[10:11], s[2:3], v[102:103] op_sel_hi:[1,0,1]
	v_pk_fma_f32 v[98:99], v[12:13], s[2:3], v[164:165] op_sel_hi:[1,0,1]
	v_pk_fma_f32 v[100:101], v[14:15], s[2:3], v[166:167] op_sel_hi:[1,0,1]
	v_pk_fma_f32 v[102:103], v[16:17], s[2:3], v[168:169] op_sel_hi:[1,0,1]
	v_pk_fma_f32 v[162:163], v[18:19], s[2:3], v[162:163] op_sel_hi:[1,0,1]
	v_pk_fma_f32 v[160:161], v[20:21], s[2:3], v[160:161] op_sel_hi:[1,0,1]
	v_pk_fma_f32 v[158:159], v[22:23], s[2:3], v[158:159] op_sel_hi:[1,0,1]
	v_pk_fma_f32 v[156:157], v[24:25], s[2:3], v[156:157] op_sel_hi:[1,0,1]
	v_pk_fma_f32 v[154:155], v[26:27], s[2:3], v[154:155] op_sel_hi:[1,0,1]
	v_pk_fma_f32 v[152:153], v[28:29], s[2:3], v[152:153] op_sel_hi:[1,0,1]
	v_pk_fma_f32 v[150:151], v[30:31], s[2:3], v[150:151] op_sel_hi:[1,0,1]
	v_readlane_b32 s2, v131, 19
	s_waitcnt vmcnt(16)
	v_cvt_scalef32_pk32_f32_fp6 v[0:31], v[80:85], 1.0
	v_pk_fma_f32 v[180:181], v[0:1], s[2:3], v[86:87] op_sel_hi:[1,0,1]
	v_pk_fma_f32 v[178:179], v[2:3], s[2:3], v[88:89] op_sel_hi:[1,0,1]
	v_pk_fma_f32 v[176:177], v[4:5], s[2:3], v[90:91] op_sel_hi:[1,0,1]
	v_pk_fma_f32 v[174:175], v[6:7], s[2:3], v[92:93] op_sel_hi:[1,0,1]
	v_pk_fma_f32 v[172:173], v[8:9], s[2:3], v[94:95] op_sel_hi:[1,0,1]
	v_pk_fma_f32 v[170:171], v[10:11], s[2:3], v[96:97] op_sel_hi:[1,0,1]
	v_pk_fma_f32 v[168:169], v[12:13], s[2:3], v[98:99] op_sel_hi:[1,0,1]
	v_pk_fma_f32 v[166:167], v[14:15], s[2:3], v[100:101] op_sel_hi:[1,0,1]
	v_pk_fma_f32 v[164:165], v[16:17], s[2:3], v[102:103] op_sel_hi:[1,0,1]
	v_pk_fma_f32 v[162:163], v[18:19], s[2:3], v[162:163] op_sel_hi:[1,0,1]
	v_pk_fma_f32 v[160:161], v[20:21], s[2:3], v[160:161] op_sel_hi:[1,0,1]
	v_pk_fma_f32 v[158:159], v[22:23], s[2:3], v[158:159] op_sel_hi:[1,0,1]
	v_pk_fma_f32 v[156:157], v[24:25], s[2:3], v[156:157] op_sel_hi:[1,0,1]
	v_pk_fma_f32 v[154:155], v[26:27], s[2:3], v[154:155] op_sel_hi:[1,0,1]
	v_pk_fma_f32 v[152:153], v[28:29], s[2:3], v[152:153] op_sel_hi:[1,0,1]
	v_pk_fma_f32 v[150:151], v[30:31], s[2:3], v[150:151] op_sel_hi:[1,0,1]
	v_readlane_b32 s2, v241, 28
	v_readlane_b32 s3, v241, 29
	v_readlane_b32 s100, v241, 30
	v_readlane_b32 s101, v241, 31
	s_nop 1
	buffer_load_dwordx4 v[98:101], v129, s[44:47], s2 offen sc1
	buffer_load_dwordx2 v[102:103], v210, s[44:47], s2 offen sc1
	buffer_load_dwordx4 v[92:95], v129, s[44:47], s3 offen sc1
	buffer_load_dwordx2 v[96:97], v210, s[44:47], s3 offen sc1
	buffer_load_dwordx4 v[86:89], v129, s[44:47], s100 offen sc1
	buffer_load_dwordx2 v[90:91], v210, s[44:47], s100 offen sc1
	buffer_load_dwordx4 v[80:83], v129, s[44:47], s101 offen sc1
	buffer_load_dwordx2 v[84:85], v210, s[44:47], s101 offen sc1
	v_readlane_b32 s2, v131, 20
	s_waitcnt vmcnt(22)
	v_cvt_scalef32_pk32_f32_fp6 v[0:31], v[74:79], 1.0
	v_pk_fma_f32 v[74:75], v[0:1], s[2:3], v[180:181] op_sel_hi:[1,0,1]
	v_pk_fma_f32 v[76:77], v[2:3], s[2:3], v[178:179] op_sel_hi:[1,0,1]
	v_pk_fma_f32 v[78:79], v[4:5], s[2:3], v[176:177] op_sel_hi:[1,0,1]
	v_pk_fma_f32 v[174:175], v[6:7], s[2:3], v[174:175] op_sel_hi:[1,0,1]
	v_pk_fma_f32 v[172:173], v[8:9], s[2:3], v[172:173] op_sel_hi:[1,0,1]
	v_pk_fma_f32 v[170:171], v[10:11], s[2:3], v[170:171] op_sel_hi:[1,0,1]
	v_pk_fma_f32 v[168:169], v[12:13], s[2:3], v[168:169] op_sel_hi:[1,0,1]
	v_pk_fma_f32 v[166:167], v[14:15], s[2:3], v[166:167] op_sel_hi:[1,0,1]
	v_pk_fma_f32 v[164:165], v[16:17], s[2:3], v[164:165] op_sel_hi:[1,0,1]
	v_pk_fma_f32 v[162:163], v[18:19], s[2:3], v[162:163] op_sel_hi:[1,0,1]
	v_pk_fma_f32 v[160:161], v[20:21], s[2:3], v[160:161] op_sel_hi:[1,0,1]
	v_pk_fma_f32 v[158:159], v[22:23], s[2:3], v[158:159] op_sel_hi:[1,0,1]
	v_pk_fma_f32 v[156:157], v[24:25], s[2:3], v[156:157] op_sel_hi:[1,0,1]
	v_pk_fma_f32 v[154:155], v[26:27], s[2:3], v[154:155] op_sel_hi:[1,0,1]
	v_pk_fma_f32 v[152:153], v[28:29], s[2:3], v[152:153] op_sel_hi:[1,0,1]
	v_pk_fma_f32 v[150:151], v[30:31], s[2:3], v[150:151] op_sel_hi:[1,0,1]
	v_readlane_b32 s2, v131, 21
	s_waitcnt vmcnt(20)
	v_cvt_scalef32_pk32_f32_fp6 v[0:31], v[68:73], 1.0
	v_pk_fma_f32 v[68:69], v[0:1], s[2:3], v[74:75] op_sel_hi:[1,0,1]
	v_pk_fma_f32 v[70:71], v[2:3], s[2:3], v[76:77] op_sel_hi:[1,0,1]
	v_pk_fma_f32 v[72:73], v[4:5], s[2:3], v[78:79] op_sel_hi:[1,0,1]
	v_pk_fma_f32 v[74:75], v[6:7], s[2:3], v[174:175] op_sel_hi:[1,0,1]
	v_pk_fma_f32 v[76:77], v[8:9], s[2:3], v[172:173] op_sel_hi:[1,0,1]
	v_pk_fma_f32 v[78:79], v[10:11], s[2:3], v[170:171] op_sel_hi:[1,0,1]
	v_pk_fma_f32 v[168:169], v[12:13], s[2:3], v[168:169] op_sel_hi:[1,0,1]
	v_pk_fma_f32 v[166:167], v[14:15], s[2:3], v[166:167] op_sel_hi:[1,0,1]
	v_pk_fma_f32 v[164:165], v[16:17], s[2:3], v[164:165] op_sel_hi:[1,0,1]
	v_pk_fma_f32 v[162:163], v[18:19], s[2:3], v[162:163] op_sel_hi:[1,0,1]
	v_pk_fma_f32 v[160:161], v[20:21], s[2:3], v[160:161] op_sel_hi:[1,0,1]
	v_pk_fma_f32 v[158:159], v[22:23], s[2:3], v[158:159] op_sel_hi:[1,0,1]
	v_pk_fma_f32 v[156:157], v[24:25], s[2:3], v[156:157] op_sel_hi:[1,0,1]
	v_pk_fma_f32 v[154:155], v[26:27], s[2:3], v[154:155] op_sel_hi:[1,0,1]
	v_pk_fma_f32 v[152:153], v[28:29], s[2:3], v[152:153] op_sel_hi:[1,0,1]
	v_pk_fma_f32 v[150:151], v[30:31], s[2:3], v[150:151] op_sel_hi:[1,0,1]
	v_readlane_b32 s2, v131, 22
	s_waitcnt vmcnt(18)
	v_cvt_scalef32_pk32_f32_fp6 v[0:31], v[56:61], 1.0
	v_pk_fma_f32 v[56:57], v[0:1], s[2:3], v[68:69] op_sel_hi:[1,0,1]
	v_pk_fma_f32 v[58:59], v[2:3], s[2:3], v[70:71] op_sel_hi:[1,0,1]
	v_pk_fma_f32 v[60:61], v[4:5], s[2:3], v[72:73] op_sel_hi:[1,0,1]
	v_pk_fma_f32 v[68:69], v[6:7], s[2:3], v[74:75] op_sel_hi:[1,0,1]
	v_pk_fma_f32 v[70:71], v[8:9], s[2:3], v[76:77] op_sel_hi:[1,0,1]
	v_pk_fma_f32 v[72:73], v[10:11], s[2:3], v[78:79] op_sel_hi:[1,0,1]
	v_pk_fma_f32 v[74:75], v[12:13], s[2:3], v[168:169] op_sel_hi:[1,0,1]
	v_pk_fma_f32 v[76:77], v[14:15], s[2:3], v[166:167] op_sel_hi:[1,0,1]
	v_pk_fma_f32 v[78:79], v[16:17], s[2:3], v[164:165] op_sel_hi:[1,0,1]
	v_pk_fma_f32 v[162:163], v[18:19], s[2:3], v[162:163] op_sel_hi:[1,0,1]
	v_pk_fma_f32 v[160:161], v[20:21], s[2:3], v[160:161] op_sel_hi:[1,0,1]
	v_pk_fma_f32 v[158:159], v[22:23], s[2:3], v[158:159] op_sel_hi:[1,0,1]
	v_pk_fma_f32 v[156:157], v[24:25], s[2:3], v[156:157] op_sel_hi:[1,0,1]
	v_pk_fma_f32 v[154:155], v[26:27], s[2:3], v[154:155] op_sel_hi:[1,0,1]
	v_pk_fma_f32 v[152:153], v[28:29], s[2:3], v[152:153] op_sel_hi:[1,0,1]
	v_pk_fma_f32 v[150:151], v[30:31], s[2:3], v[150:151] op_sel_hi:[1,0,1]
	v_readlane_b32 s2, v131, 23
	s_waitcnt vmcnt(16)
	v_cvt_scalef32_pk32_f32_fp6 v[0:31], v[44:49], 1.0
	v_pk_fma_f32 v[164:165], v[0:1], s[2:3], v[56:57] op_sel_hi:[1,0,1]
	v_pk_fma_f32 v[166:167], v[2:3], s[2:3], v[58:59] op_sel_hi:[1,0,1]
	v_pk_fma_f32 v[168:169], v[4:5], s[2:3], v[60:61] op_sel_hi:[1,0,1]
	v_pk_fma_f32 v[170:171], v[6:7], s[2:3], v[68:69] op_sel_hi:[1,0,1]
	v_pk_fma_f32 v[172:173], v[8:9], s[2:3], v[70:71] op_sel_hi:[1,0,1]
	v_pk_fma_f32 v[174:175], v[10:11], s[2:3], v[72:73] op_sel_hi:[1,0,1]
	v_pk_fma_f32 v[176:177], v[12:13], s[2:3], v[74:75] op_sel_hi:[1,0,1]
	v_pk_fma_f32 v[178:179], v[14:15], s[2:3], v[76:77] op_sel_hi:[1,0,1]
	v_pk_fma_f32 v[180:181], v[16:17], s[2:3], v[78:79] op_sel_hi:[1,0,1]
	v_pk_fma_f32 v[162:163], v[18:19], s[2:3], v[162:163] op_sel_hi:[1,0,1]
	v_pk_fma_f32 v[160:161], v[20:21], s[2:3], v[160:161] op_sel_hi:[1,0,1]
	v_pk_fma_f32 v[158:159], v[22:23], s[2:3], v[158:159] op_sel_hi:[1,0,1]
	v_pk_fma_f32 v[156:157], v[24:25], s[2:3], v[156:157] op_sel_hi:[1,0,1]
	v_pk_fma_f32 v[154:155], v[26:27], s[2:3], v[154:155] op_sel_hi:[1,0,1]
	v_pk_fma_f32 v[152:153], v[28:29], s[2:3], v[152:153] op_sel_hi:[1,0,1]
	v_pk_fma_f32 v[150:151], v[30:31], s[2:3], v[150:151] op_sel_hi:[1,0,1]
	v_readlane_b32 s2, v241, 32
	v_readlane_b32 s3, v241, 33
	v_readlane_b32 s100, v241, 34
	v_readlane_b32 s101, v241, 35
	s_nop 1
	buffer_load_dwordx4 v[74:77], v129, s[44:47], s2 offen sc1
	buffer_load_dwordx2 v[78:79], v210, s[44:47], s2 offen sc1
	buffer_load_dwordx4 v[68:71], v129, s[44:47], s3 offen sc1
	buffer_load_dwordx2 v[72:73], v210, s[44:47], s3 offen sc1
	buffer_load_dwordx4 v[56:59], v129, s[44:47], s100 offen sc1
	buffer_load_dwordx2 v[60:61], v210, s[44:47], s100 offen sc1
	buffer_load_dwordx4 v[44:47], v129, s[44:47], s101 offen sc1
	buffer_load_dwordx2 v[48:49], v210, s[44:47], s101 offen sc1
	v_readlane_b32 s2, v131, 24
	s_waitcnt vmcnt(22)
	v_cvt_scalef32_pk32_f32_fp6 v[0:31], v[62:67], 1.0
	v_pk_fma_f32 v[62:63], v[0:1], s[2:3], v[164:165] op_sel_hi:[1,0,1]
	v_pk_fma_f32 v[64:65], v[2:3], s[2:3], v[166:167] op_sel_hi:[1,0,1]
	v_pk_fma_f32 v[66:67], v[4:5], s[2:3], v[168:169] op_sel_hi:[1,0,1]
	v_pk_fma_f32 v[164:165], v[6:7], s[2:3], v[170:171] op_sel_hi:[1,0,1]
	v_pk_fma_f32 v[166:167], v[8:9], s[2:3], v[172:173] op_sel_hi:[1,0,1]
	v_pk_fma_f32 v[168:169], v[10:11], s[2:3], v[174:175] op_sel_hi:[1,0,1]
	v_pk_fma_f32 v[170:171], v[12:13], s[2:3], v[176:177] op_sel_hi:[1,0,1]
	v_pk_fma_f32 v[172:173], v[14:15], s[2:3], v[178:179] op_sel_hi:[1,0,1]
	v_pk_fma_f32 v[174:175], v[16:17], s[2:3], v[180:181] op_sel_hi:[1,0,1]
	v_pk_fma_f32 v[162:163], v[18:19], s[2:3], v[162:163] op_sel_hi:[1,0,1]
	v_pk_fma_f32 v[160:161], v[20:21], s[2:3], v[160:161] op_sel_hi:[1,0,1]
	v_pk_fma_f32 v[158:159], v[22:23], s[2:3], v[158:159] op_sel_hi:[1,0,1]
	v_pk_fma_f32 v[156:157], v[24:25], s[2:3], v[156:157] op_sel_hi:[1,0,1]
	v_pk_fma_f32 v[154:155], v[26:27], s[2:3], v[154:155] op_sel_hi:[1,0,1]
	v_pk_fma_f32 v[152:153], v[28:29], s[2:3], v[152:153] op_sel_hi:[1,0,1]
	v_pk_fma_f32 v[150:151], v[30:31], s[2:3], v[150:151] op_sel_hi:[1,0,1]
	v_readlane_b32 s2, v131, 25
	s_waitcnt vmcnt(20)
	v_cvt_scalef32_pk32_f32_fp6 v[0:31], v[50:55], 1.0
	v_pk_fma_f32 v[50:51], v[0:1], s[2:3], v[62:63] op_sel_hi:[1,0,1]
	v_pk_fma_f32 v[52:53], v[2:3], s[2:3], v[64:65] op_sel_hi:[1,0,1]
	v_pk_fma_f32 v[54:55], v[4:5], s[2:3], v[66:67] op_sel_hi:[1,0,1]
	v_pk_fma_f32 v[62:63], v[6:7], s[2:3], v[164:165] op_sel_hi:[1,0,1]
	v_pk_fma_f32 v[64:65], v[8:9], s[2:3], v[166:167] op_sel_hi:[1,0,1]
	v_pk_fma_f32 v[66:67], v[10:11], s[2:3], v[168:169] op_sel_hi:[1,0,1]
	v_pk_fma_f32 v[164:165], v[12:13], s[2:3], v[170:171] op_sel_hi:[1,0,1]
	v_pk_fma_f32 v[166:167], v[14:15], s[2:3], v[172:173] op_sel_hi:[1,0,1]
	v_pk_fma_f32 v[168:169], v[16:17], s[2:3], v[174:175] op_sel_hi:[1,0,1]
	v_pk_fma_f32 v[162:163], v[18:19], s[2:3], v[162:163] op_sel_hi:[1,0,1]
	v_pk_fma_f32 v[160:161], v[20:21], s[2:3], v[160:161] op_sel_hi:[1,0,1]
	v_pk_fma_f32 v[158:159], v[22:23], s[2:3], v[158:159] op_sel_hi:[1,0,1]
	v_pk_fma_f32 v[156:157], v[24:25], s[2:3], v[156:157] op_sel_hi:[1,0,1]
	v_pk_fma_f32 v[154:155], v[26:27], s[2:3], v[154:155] op_sel_hi:[1,0,1]
	v_pk_fma_f32 v[152:153], v[28:29], s[2:3], v[152:153] op_sel_hi:[1,0,1]
	v_pk_fma_f32 v[150:151], v[30:31], s[2:3], v[150:151] op_sel_hi:[1,0,1]
	v_readlane_b32 s2, v131, 26
	s_waitcnt vmcnt(18)
	v_cvt_scalef32_pk32_f32_fp6 v[0:31], v[38:43], 1.0
	v_pk_fma_f32 v[38:39], v[0:1], s[2:3], v[50:51] op_sel_hi:[1,0,1]
	v_pk_fma_f32 v[40:41], v[2:3], s[2:3], v[52:53] op_sel_hi:[1,0,1]
	v_pk_fma_f32 v[42:43], v[4:5], s[2:3], v[54:55] op_sel_hi:[1,0,1]
	v_pk_fma_f32 v[50:51], v[6:7], s[2:3], v[62:63] op_sel_hi:[1,0,1]
	v_pk_fma_f32 v[52:53], v[8:9], s[2:3], v[64:65] op_sel_hi:[1,0,1]
	v_pk_fma_f32 v[54:55], v[10:11], s[2:3], v[66:67] op_sel_hi:[1,0,1]
	v_pk_fma_f32 v[62:63], v[12:13], s[2:3], v[164:165] op_sel_hi:[1,0,1]
	v_pk_fma_f32 v[64:65], v[14:15], s[2:3], v[166:167] op_sel_hi:[1,0,1]
	v_pk_fma_f32 v[66:67], v[16:17], s[2:3], v[168:169] op_sel_hi:[1,0,1]
	v_pk_fma_f32 v[162:163], v[18:19], s[2:3], v[162:163] op_sel_hi:[1,0,1]
	v_pk_fma_f32 v[160:161], v[20:21], s[2:3], v[160:161] op_sel_hi:[1,0,1]
	v_pk_fma_f32 v[158:159], v[22:23], s[2:3], v[158:159] op_sel_hi:[1,0,1]
	v_pk_fma_f32 v[156:157], v[24:25], s[2:3], v[156:157] op_sel_hi:[1,0,1]
	v_pk_fma_f32 v[154:155], v[26:27], s[2:3], v[154:155] op_sel_hi:[1,0,1]
	v_pk_fma_f32 v[152:153], v[28:29], s[2:3], v[152:153] op_sel_hi:[1,0,1]
	v_pk_fma_f32 v[150:151], v[30:31], s[2:3], v[150:151] op_sel_hi:[1,0,1]
	v_readlane_b32 s2, v131, 27
	s_waitcnt vmcnt(16)
	v_cvt_scalef32_pk32_f32_fp6 v[0:31], v[32:37], 1.0
	v_pk_fma_f32 v[164:165], v[0:1], s[2:3], v[38:39] op_sel_hi:[1,0,1]
	v_pk_fma_f32 v[166:167], v[2:3], s[2:3], v[40:41] op_sel_hi:[1,0,1]
	v_pk_fma_f32 v[168:169], v[4:5], s[2:3], v[42:43] op_sel_hi:[1,0,1]
	v_pk_fma_f32 v[170:171], v[6:7], s[2:3], v[50:51] op_sel_hi:[1,0,1]
	v_pk_fma_f32 v[172:173], v[8:9], s[2:3], v[52:53] op_sel_hi:[1,0,1]
	v_pk_fma_f32 v[174:175], v[10:11], s[2:3], v[54:55] op_sel_hi:[1,0,1]
	v_pk_fma_f32 v[176:177], v[12:13], s[2:3], v[62:63] op_sel_hi:[1,0,1]
	v_pk_fma_f32 v[178:179], v[14:15], s[2:3], v[64:65] op_sel_hi:[1,0,1]
	v_pk_fma_f32 v[180:181], v[16:17], s[2:3], v[66:67] op_sel_hi:[1,0,1]
	v_pk_fma_f32 v[162:163], v[18:19], s[2:3], v[162:163] op_sel_hi:[1,0,1]
	v_pk_fma_f32 v[160:161], v[20:21], s[2:3], v[160:161] op_sel_hi:[1,0,1]
	v_pk_fma_f32 v[158:159], v[22:23], s[2:3], v[158:159] op_sel_hi:[1,0,1]
	v_pk_fma_f32 v[156:157], v[24:25], s[2:3], v[156:157] op_sel_hi:[1,0,1]
	v_pk_fma_f32 v[154:155], v[26:27], s[2:3], v[154:155] op_sel_hi:[1,0,1]
	v_pk_fma_f32 v[152:153], v[28:29], s[2:3], v[152:153] op_sel_hi:[1,0,1]
	v_pk_fma_f32 v[150:151], v[30:31], s[2:3], v[150:151] op_sel_hi:[1,0,1]
	v_readlane_b32 s2, v241, 36
	v_readlane_b32 s3, v241, 37
	v_readlane_b32 s100, v241, 38
	v_readlane_b32 s101, v241, 39
	s_nop 1
	buffer_load_dwordx4 v[62:65], v129, s[44:47], s2 offen sc1
	buffer_load_dwordx2 v[66:67], v210, s[44:47], s2 offen sc1
	buffer_load_dwordx4 v[50:53], v129, s[44:47], s3 offen sc1
	buffer_load_dwordx2 v[54:55], v210, s[44:47], s3 offen sc1
	buffer_load_dwordx4 v[38:41], v129, s[44:47], s100 offen sc1
	buffer_load_dwordx2 v[42:43], v210, s[44:47], s100 offen sc1
	buffer_load_dwordx4 v[32:35], v129, s[44:47], s101 offen sc1
	buffer_load_dwordx2 v[36:37], v210, s[44:47], s101 offen sc1
	v_readlane_b32 s2, v131, 28
	s_waitcnt vmcnt(22)
	v_cvt_scalef32_pk32_f32_fp6 v[0:31], v[98:103], 1.0
	v_pk_fma_f32 v[98:99], v[0:1], s[2:3], v[164:165] op_sel_hi:[1,0,1]
	v_pk_fma_f32 v[100:101], v[2:3], s[2:3], v[166:167] op_sel_hi:[1,0,1]
	v_pk_fma_f32 v[102:103], v[4:5], s[2:3], v[168:169] op_sel_hi:[1,0,1]
	v_pk_fma_f32 v[164:165], v[6:7], s[2:3], v[170:171] op_sel_hi:[1,0,1]
	v_pk_fma_f32 v[166:167], v[8:9], s[2:3], v[172:173] op_sel_hi:[1,0,1]
	v_pk_fma_f32 v[168:169], v[10:11], s[2:3], v[174:175] op_sel_hi:[1,0,1]
	v_pk_fma_f32 v[170:171], v[12:13], s[2:3], v[176:177] op_sel_hi:[1,0,1]
	v_pk_fma_f32 v[172:173], v[14:15], s[2:3], v[178:179] op_sel_hi:[1,0,1]
	v_pk_fma_f32 v[174:175], v[16:17], s[2:3], v[180:181] op_sel_hi:[1,0,1]
	v_pk_fma_f32 v[162:163], v[18:19], s[2:3], v[162:163] op_sel_hi:[1,0,1]
	v_pk_fma_f32 v[160:161], v[20:21], s[2:3], v[160:161] op_sel_hi:[1,0,1]
	v_pk_fma_f32 v[158:159], v[22:23], s[2:3], v[158:159] op_sel_hi:[1,0,1]
	v_pk_fma_f32 v[156:157], v[24:25], s[2:3], v[156:157] op_sel_hi:[1,0,1]
	v_pk_fma_f32 v[154:155], v[26:27], s[2:3], v[154:155] op_sel_hi:[1,0,1]
	v_pk_fma_f32 v[152:153], v[28:29], s[2:3], v[152:153] op_sel_hi:[1,0,1]
	v_pk_fma_f32 v[150:151], v[30:31], s[2:3], v[150:151] op_sel_hi:[1,0,1]
	v_readlane_b32 s2, v131, 29
	s_waitcnt vmcnt(20)
	v_cvt_scalef32_pk32_f32_fp6 v[0:31], v[92:97], 1.0
	v_pk_fma_f32 v[92:93], v[0:1], s[2:3], v[98:99] op_sel_hi:[1,0,1]
	v_pk_fma_f32 v[94:95], v[2:3], s[2:3], v[100:101] op_sel_hi:[1,0,1]
	v_pk_fma_f32 v[96:97], v[4:5], s[2:3], v[102:103] op_sel_hi:[1,0,1]
	v_pk_fma_f32 v[98:99], v[6:7], s[2:3], v[164:165] op_sel_hi:[1,0,1]
	v_pk_fma_f32 v[100:101], v[8:9], s[2:3], v[166:167] op_sel_hi:[1,0,1]
	v_pk_fma_f32 v[102:103], v[10:11], s[2:3], v[168:169] op_sel_hi:[1,0,1]
	v_pk_fma_f32 v[164:165], v[12:13], s[2:3], v[170:171] op_sel_hi:[1,0,1]
	v_pk_fma_f32 v[166:167], v[14:15], s[2:3], v[172:173] op_sel_hi:[1,0,1]
	v_pk_fma_f32 v[168:169], v[16:17], s[2:3], v[174:175] op_sel_hi:[1,0,1]
	v_pk_fma_f32 v[162:163], v[18:19], s[2:3], v[162:163] op_sel_hi:[1,0,1]
	v_pk_fma_f32 v[160:161], v[20:21], s[2:3], v[160:161] op_sel_hi:[1,0,1]
	v_pk_fma_f32 v[158:159], v[22:23], s[2:3], v[158:159] op_sel_hi:[1,0,1]
	v_pk_fma_f32 v[156:157], v[24:25], s[2:3], v[156:157] op_sel_hi:[1,0,1]
	v_pk_fma_f32 v[154:155], v[26:27], s[2:3], v[154:155] op_sel_hi:[1,0,1]
	v_pk_fma_f32 v[152:153], v[28:29], s[2:3], v[152:153] op_sel_hi:[1,0,1]
	v_pk_fma_f32 v[150:151], v[30:31], s[2:3], v[150:151] op_sel_hi:[1,0,1]
	v_readlane_b32 s2, v131, 30
	s_waitcnt vmcnt(18)
	v_cvt_scalef32_pk32_f32_fp6 v[0:31], v[86:91], 1.0
	v_pk_fma_f32 v[86:87], v[0:1], s[2:3], v[92:93] op_sel_hi:[1,0,1]
	v_pk_fma_f32 v[88:89], v[2:3], s[2:3], v[94:95] op_sel_hi:[1,0,1]
	v_pk_fma_f32 v[90:91], v[4:5], s[2:3], v[96:97] op_sel_hi:[1,0,1]
	v_pk_fma_f32 v[92:93], v[6:7], s[2:3], v[98:99] op_sel_hi:[1,0,1]
	v_pk_fma_f32 v[94:95], v[8:9], s[2:3], v[100:101] op_sel_hi:[1,0,1]
	v_pk_fma_f32 v[96:97], v[10:11], s[2:3], v[102:103] op_sel_hi:[1,0,1]
	v_pk_fma_f32 v[98:99], v[12:13], s[2:3], v[164:165] op_sel_hi:[1,0,1]
	v_pk_fma_f32 v[100:101], v[14:15], s[2:3], v[166:167] op_sel_hi:[1,0,1]
	v_pk_fma_f32 v[102:103], v[16:17], s[2:3], v[168:169] op_sel_hi:[1,0,1]
	v_pk_fma_f32 v[162:163], v[18:19], s[2:3], v[162:163] op_sel_hi:[1,0,1]
	v_pk_fma_f32 v[160:161], v[20:21], s[2:3], v[160:161] op_sel_hi:[1,0,1]
	v_pk_fma_f32 v[158:159], v[22:23], s[2:3], v[158:159] op_sel_hi:[1,0,1]
	v_pk_fma_f32 v[156:157], v[24:25], s[2:3], v[156:157] op_sel_hi:[1,0,1]
	v_pk_fma_f32 v[154:155], v[26:27], s[2:3], v[154:155] op_sel_hi:[1,0,1]
	v_pk_fma_f32 v[152:153], v[28:29], s[2:3], v[152:153] op_sel_hi:[1,0,1]
	v_pk_fma_f32 v[150:151], v[30:31], s[2:3], v[150:151] op_sel_hi:[1,0,1]
	v_readlane_b32 s2, v131, 31
	s_waitcnt vmcnt(16)
	v_cvt_scalef32_pk32_f32_fp6 v[0:31], v[80:85], 1.0
	v_pk_fma_f32 v[180:181], v[0:1], s[2:3], v[86:87] op_sel_hi:[1,0,1]
	v_pk_fma_f32 v[178:179], v[2:3], s[2:3], v[88:89] op_sel_hi:[1,0,1]
	v_pk_fma_f32 v[176:177], v[4:5], s[2:3], v[90:91] op_sel_hi:[1,0,1]
	v_pk_fma_f32 v[174:175], v[6:7], s[2:3], v[92:93] op_sel_hi:[1,0,1]
	v_pk_fma_f32 v[172:173], v[8:9], s[2:3], v[94:95] op_sel_hi:[1,0,1]
	v_pk_fma_f32 v[170:171], v[10:11], s[2:3], v[96:97] op_sel_hi:[1,0,1]
	v_pk_fma_f32 v[168:169], v[12:13], s[2:3], v[98:99] op_sel_hi:[1,0,1]
	v_pk_fma_f32 v[166:167], v[14:15], s[2:3], v[100:101] op_sel_hi:[1,0,1]
	v_pk_fma_f32 v[164:165], v[16:17], s[2:3], v[102:103] op_sel_hi:[1,0,1]
	v_pk_fma_f32 v[162:163], v[18:19], s[2:3], v[162:163] op_sel_hi:[1,0,1]
	v_pk_fma_f32 v[160:161], v[20:21], s[2:3], v[160:161] op_sel_hi:[1,0,1]
	v_pk_fma_f32 v[158:159], v[22:23], s[2:3], v[158:159] op_sel_hi:[1,0,1]
	v_pk_fma_f32 v[156:157], v[24:25], s[2:3], v[156:157] op_sel_hi:[1,0,1]
	v_pk_fma_f32 v[154:155], v[26:27], s[2:3], v[154:155] op_sel_hi:[1,0,1]
	v_pk_fma_f32 v[152:153], v[28:29], s[2:3], v[152:153] op_sel_hi:[1,0,1]
	v_pk_fma_f32 v[150:151], v[30:31], s[2:3], v[150:151] op_sel_hi:[1,0,1]
	v_readlane_b32 s2, v241, 40
	v_readlane_b32 s3, v241, 41
	v_readlane_b32 s100, v241, 42
	v_readlane_b32 s101, v241, 43
	s_nop 1
	buffer_load_dwordx4 v[98:101], v129, s[44:47], s2 offen sc1
	buffer_load_dwordx2 v[102:103], v210, s[44:47], s2 offen sc1
	buffer_load_dwordx4 v[92:95], v129, s[44:47], s3 offen sc1
	buffer_load_dwordx2 v[96:97], v210, s[44:47], s3 offen sc1
	buffer_load_dwordx4 v[86:89], v129, s[44:47], s100 offen sc1
	buffer_load_dwordx2 v[90:91], v210, s[44:47], s100 offen sc1
	buffer_load_dwordx4 v[80:83], v129, s[44:47], s101 offen sc1
	buffer_load_dwordx2 v[84:85], v210, s[44:47], s101 offen sc1
	v_readlane_b32 s2, v131, 32
	s_waitcnt vmcnt(22)
	v_cvt_scalef32_pk32_f32_fp6 v[0:31], v[74:79], 1.0
	v_pk_fma_f32 v[74:75], v[0:1], s[2:3], v[180:181] op_sel_hi:[1,0,1]
	v_pk_fma_f32 v[76:77], v[2:3], s[2:3], v[178:179] op_sel_hi:[1,0,1]
	v_pk_fma_f32 v[78:79], v[4:5], s[2:3], v[176:177] op_sel_hi:[1,0,1]
	v_pk_fma_f32 v[174:175], v[6:7], s[2:3], v[174:175] op_sel_hi:[1,0,1]
	v_pk_fma_f32 v[172:173], v[8:9], s[2:3], v[172:173] op_sel_hi:[1,0,1]
	v_pk_fma_f32 v[170:171], v[10:11], s[2:3], v[170:171] op_sel_hi:[1,0,1]
	v_pk_fma_f32 v[168:169], v[12:13], s[2:3], v[168:169] op_sel_hi:[1,0,1]
	v_pk_fma_f32 v[166:167], v[14:15], s[2:3], v[166:167] op_sel_hi:[1,0,1]
	v_pk_fma_f32 v[164:165], v[16:17], s[2:3], v[164:165] op_sel_hi:[1,0,1]
	v_pk_fma_f32 v[162:163], v[18:19], s[2:3], v[162:163] op_sel_hi:[1,0,1]
	v_pk_fma_f32 v[160:161], v[20:21], s[2:3], v[160:161] op_sel_hi:[1,0,1]
	v_pk_fma_f32 v[158:159], v[22:23], s[2:3], v[158:159] op_sel_hi:[1,0,1]
	v_pk_fma_f32 v[156:157], v[24:25], s[2:3], v[156:157] op_sel_hi:[1,0,1]
	v_pk_fma_f32 v[154:155], v[26:27], s[2:3], v[154:155] op_sel_hi:[1,0,1]
	v_pk_fma_f32 v[152:153], v[28:29], s[2:3], v[152:153] op_sel_hi:[1,0,1]
	v_pk_fma_f32 v[150:151], v[30:31], s[2:3], v[150:151] op_sel_hi:[1,0,1]
	v_readlane_b32 s2, v131, 33
	s_waitcnt vmcnt(20)
	v_cvt_scalef32_pk32_f32_fp6 v[0:31], v[68:73], 1.0
	v_pk_fma_f32 v[68:69], v[0:1], s[2:3], v[74:75] op_sel_hi:[1,0,1]
	v_pk_fma_f32 v[70:71], v[2:3], s[2:3], v[76:77] op_sel_hi:[1,0,1]
	v_pk_fma_f32 v[72:73], v[4:5], s[2:3], v[78:79] op_sel_hi:[1,0,1]
	v_pk_fma_f32 v[74:75], v[6:7], s[2:3], v[174:175] op_sel_hi:[1,0,1]
	v_pk_fma_f32 v[76:77], v[8:9], s[2:3], v[172:173] op_sel_hi:[1,0,1]
	v_pk_fma_f32 v[78:79], v[10:11], s[2:3], v[170:171] op_sel_hi:[1,0,1]
	v_pk_fma_f32 v[168:169], v[12:13], s[2:3], v[168:169] op_sel_hi:[1,0,1]
	v_pk_fma_f32 v[166:167], v[14:15], s[2:3], v[166:167] op_sel_hi:[1,0,1]
	v_pk_fma_f32 v[164:165], v[16:17], s[2:3], v[164:165] op_sel_hi:[1,0,1]
	v_pk_fma_f32 v[162:163], v[18:19], s[2:3], v[162:163] op_sel_hi:[1,0,1]
	v_pk_fma_f32 v[160:161], v[20:21], s[2:3], v[160:161] op_sel_hi:[1,0,1]
	v_pk_fma_f32 v[158:159], v[22:23], s[2:3], v[158:159] op_sel_hi:[1,0,1]
	v_pk_fma_f32 v[156:157], v[24:25], s[2:3], v[156:157] op_sel_hi:[1,0,1]
	v_pk_fma_f32 v[154:155], v[26:27], s[2:3], v[154:155] op_sel_hi:[1,0,1]
	v_pk_fma_f32 v[152:153], v[28:29], s[2:3], v[152:153] op_sel_hi:[1,0,1]
	v_pk_fma_f32 v[150:151], v[30:31], s[2:3], v[150:151] op_sel_hi:[1,0,1]
	v_readlane_b32 s2, v131, 34
	s_waitcnt vmcnt(18)
	v_cvt_scalef32_pk32_f32_fp6 v[0:31], v[56:61], 1.0
	v_pk_fma_f32 v[56:57], v[0:1], s[2:3], v[68:69] op_sel_hi:[1,0,1]
	v_pk_fma_f32 v[58:59], v[2:3], s[2:3], v[70:71] op_sel_hi:[1,0,1]
	v_pk_fma_f32 v[60:61], v[4:5], s[2:3], v[72:73] op_sel_hi:[1,0,1]
	v_pk_fma_f32 v[68:69], v[6:7], s[2:3], v[74:75] op_sel_hi:[1,0,1]
	v_pk_fma_f32 v[70:71], v[8:9], s[2:3], v[76:77] op_sel_hi:[1,0,1]
	v_pk_fma_f32 v[72:73], v[10:11], s[2:3], v[78:79] op_sel_hi:[1,0,1]
	v_pk_fma_f32 v[74:75], v[12:13], s[2:3], v[168:169] op_sel_hi:[1,0,1]
	v_pk_fma_f32 v[76:77], v[14:15], s[2:3], v[166:167] op_sel_hi:[1,0,1]
	v_pk_fma_f32 v[78:79], v[16:17], s[2:3], v[164:165] op_sel_hi:[1,0,1]
	v_pk_fma_f32 v[162:163], v[18:19], s[2:3], v[162:163] op_sel_hi:[1,0,1]
	v_pk_fma_f32 v[160:161], v[20:21], s[2:3], v[160:161] op_sel_hi:[1,0,1]
	v_pk_fma_f32 v[158:159], v[22:23], s[2:3], v[158:159] op_sel_hi:[1,0,1]
	v_pk_fma_f32 v[156:157], v[24:25], s[2:3], v[156:157] op_sel_hi:[1,0,1]
	v_pk_fma_f32 v[154:155], v[26:27], s[2:3], v[154:155] op_sel_hi:[1,0,1]
	v_pk_fma_f32 v[152:153], v[28:29], s[2:3], v[152:153] op_sel_hi:[1,0,1]
	v_pk_fma_f32 v[150:151], v[30:31], s[2:3], v[150:151] op_sel_hi:[1,0,1]
	v_readlane_b32 s2, v131, 35
	s_waitcnt vmcnt(16)
	v_cvt_scalef32_pk32_f32_fp6 v[0:31], v[44:49], 1.0
	v_pk_fma_f32 v[164:165], v[0:1], s[2:3], v[56:57] op_sel_hi:[1,0,1]
	v_pk_fma_f32 v[166:167], v[2:3], s[2:3], v[58:59] op_sel_hi:[1,0,1]
	v_pk_fma_f32 v[168:169], v[4:5], s[2:3], v[60:61] op_sel_hi:[1,0,1]
	v_pk_fma_f32 v[170:171], v[6:7], s[2:3], v[68:69] op_sel_hi:[1,0,1]
	v_pk_fma_f32 v[172:173], v[8:9], s[2:3], v[70:71] op_sel_hi:[1,0,1]
	v_pk_fma_f32 v[174:175], v[10:11], s[2:3], v[72:73] op_sel_hi:[1,0,1]
	v_pk_fma_f32 v[176:177], v[12:13], s[2:3], v[74:75] op_sel_hi:[1,0,1]
	v_pk_fma_f32 v[178:179], v[14:15], s[2:3], v[76:77] op_sel_hi:[1,0,1]
	v_pk_fma_f32 v[180:181], v[16:17], s[2:3], v[78:79] op_sel_hi:[1,0,1]
	v_pk_fma_f32 v[162:163], v[18:19], s[2:3], v[162:163] op_sel_hi:[1,0,1]
	v_pk_fma_f32 v[160:161], v[20:21], s[2:3], v[160:161] op_sel_hi:[1,0,1]
	v_pk_fma_f32 v[158:159], v[22:23], s[2:3], v[158:159] op_sel_hi:[1,0,1]
	v_pk_fma_f32 v[156:157], v[24:25], s[2:3], v[156:157] op_sel_hi:[1,0,1]
	v_pk_fma_f32 v[154:155], v[26:27], s[2:3], v[154:155] op_sel_hi:[1,0,1]
	v_pk_fma_f32 v[152:153], v[28:29], s[2:3], v[152:153] op_sel_hi:[1,0,1]
	v_pk_fma_f32 v[150:151], v[30:31], s[2:3], v[150:151] op_sel_hi:[1,0,1]
	v_readlane_b32 s2, v241, 44
	v_readlane_b32 s3, v241, 45
	v_readlane_b32 s100, v241, 46
	v_readlane_b32 s101, v241, 47
	s_nop 1
	buffer_load_dwordx4 v[74:77], v129, s[44:47], s2 offen sc1
	buffer_load_dwordx2 v[78:79], v210, s[44:47], s2 offen sc1
	buffer_load_dwordx4 v[68:71], v129, s[44:47], s3 offen sc1
	buffer_load_dwordx2 v[72:73], v210, s[44:47], s3 offen sc1
	buffer_load_dwordx4 v[56:59], v129, s[44:47], s100 offen sc1
	buffer_load_dwordx2 v[60:61], v210, s[44:47], s100 offen sc1
	buffer_load_dwordx4 v[44:47], v129, s[44:47], s101 offen sc1
	buffer_load_dwordx2 v[48:49], v210, s[44:47], s101 offen sc1
	v_readlane_b32 s2, v131, 36
	s_waitcnt vmcnt(22)
	v_cvt_scalef32_pk32_f32_fp6 v[0:31], v[62:67], 1.0
	v_pk_fma_f32 v[62:63], v[0:1], s[2:3], v[164:165] op_sel_hi:[1,0,1]
	v_pk_fma_f32 v[64:65], v[2:3], s[2:3], v[166:167] op_sel_hi:[1,0,1]
	v_pk_fma_f32 v[66:67], v[4:5], s[2:3], v[168:169] op_sel_hi:[1,0,1]
	v_pk_fma_f32 v[164:165], v[6:7], s[2:3], v[170:171] op_sel_hi:[1,0,1]
	v_pk_fma_f32 v[166:167], v[8:9], s[2:3], v[172:173] op_sel_hi:[1,0,1]
	v_pk_fma_f32 v[168:169], v[10:11], s[2:3], v[174:175] op_sel_hi:[1,0,1]
	v_pk_fma_f32 v[170:171], v[12:13], s[2:3], v[176:177] op_sel_hi:[1,0,1]
	v_pk_fma_f32 v[172:173], v[14:15], s[2:3], v[178:179] op_sel_hi:[1,0,1]
	v_pk_fma_f32 v[174:175], v[16:17], s[2:3], v[180:181] op_sel_hi:[1,0,1]
	v_pk_fma_f32 v[162:163], v[18:19], s[2:3], v[162:163] op_sel_hi:[1,0,1]
	v_pk_fma_f32 v[160:161], v[20:21], s[2:3], v[160:161] op_sel_hi:[1,0,1]
	v_pk_fma_f32 v[158:159], v[22:23], s[2:3], v[158:159] op_sel_hi:[1,0,1]
	v_pk_fma_f32 v[156:157], v[24:25], s[2:3], v[156:157] op_sel_hi:[1,0,1]
	v_pk_fma_f32 v[154:155], v[26:27], s[2:3], v[154:155] op_sel_hi:[1,0,1]
	v_pk_fma_f32 v[152:153], v[28:29], s[2:3], v[152:153] op_sel_hi:[1,0,1]
	v_pk_fma_f32 v[150:151], v[30:31], s[2:3], v[150:151] op_sel_hi:[1,0,1]
	v_readlane_b32 s2, v131, 37
	s_waitcnt vmcnt(20)
	v_cvt_scalef32_pk32_f32_fp6 v[0:31], v[50:55], 1.0
	v_pk_fma_f32 v[50:51], v[0:1], s[2:3], v[62:63] op_sel_hi:[1,0,1]
	v_pk_fma_f32 v[52:53], v[2:3], s[2:3], v[64:65] op_sel_hi:[1,0,1]
	v_pk_fma_f32 v[54:55], v[4:5], s[2:3], v[66:67] op_sel_hi:[1,0,1]
	v_pk_fma_f32 v[62:63], v[6:7], s[2:3], v[164:165] op_sel_hi:[1,0,1]
	v_pk_fma_f32 v[64:65], v[8:9], s[2:3], v[166:167] op_sel_hi:[1,0,1]
	v_pk_fma_f32 v[66:67], v[10:11], s[2:3], v[168:169] op_sel_hi:[1,0,1]
	v_pk_fma_f32 v[164:165], v[12:13], s[2:3], v[170:171] op_sel_hi:[1,0,1]
	v_pk_fma_f32 v[166:167], v[14:15], s[2:3], v[172:173] op_sel_hi:[1,0,1]
	v_pk_fma_f32 v[168:169], v[16:17], s[2:3], v[174:175] op_sel_hi:[1,0,1]
	v_pk_fma_f32 v[162:163], v[18:19], s[2:3], v[162:163] op_sel_hi:[1,0,1]
	v_pk_fma_f32 v[160:161], v[20:21], s[2:3], v[160:161] op_sel_hi:[1,0,1]
	v_pk_fma_f32 v[158:159], v[22:23], s[2:3], v[158:159] op_sel_hi:[1,0,1]
	v_pk_fma_f32 v[156:157], v[24:25], s[2:3], v[156:157] op_sel_hi:[1,0,1]
	v_pk_fma_f32 v[154:155], v[26:27], s[2:3], v[154:155] op_sel_hi:[1,0,1]
	v_pk_fma_f32 v[152:153], v[28:29], s[2:3], v[152:153] op_sel_hi:[1,0,1]
	v_pk_fma_f32 v[150:151], v[30:31], s[2:3], v[150:151] op_sel_hi:[1,0,1]
	v_readlane_b32 s2, v131, 38
	s_waitcnt vmcnt(18)
	v_cvt_scalef32_pk32_f32_fp6 v[0:31], v[38:43], 1.0
	v_pk_fma_f32 v[38:39], v[0:1], s[2:3], v[50:51] op_sel_hi:[1,0,1]
	v_pk_fma_f32 v[40:41], v[2:3], s[2:3], v[52:53] op_sel_hi:[1,0,1]
	v_pk_fma_f32 v[42:43], v[4:5], s[2:3], v[54:55] op_sel_hi:[1,0,1]
	v_pk_fma_f32 v[50:51], v[6:7], s[2:3], v[62:63] op_sel_hi:[1,0,1]
	v_pk_fma_f32 v[52:53], v[8:9], s[2:3], v[64:65] op_sel_hi:[1,0,1]
	v_pk_fma_f32 v[54:55], v[10:11], s[2:3], v[66:67] op_sel_hi:[1,0,1]
	v_pk_fma_f32 v[62:63], v[12:13], s[2:3], v[164:165] op_sel_hi:[1,0,1]
	v_pk_fma_f32 v[64:65], v[14:15], s[2:3], v[166:167] op_sel_hi:[1,0,1]
	v_pk_fma_f32 v[66:67], v[16:17], s[2:3], v[168:169] op_sel_hi:[1,0,1]
	v_pk_fma_f32 v[162:163], v[18:19], s[2:3], v[162:163] op_sel_hi:[1,0,1]
	v_pk_fma_f32 v[160:161], v[20:21], s[2:3], v[160:161] op_sel_hi:[1,0,1]
	v_pk_fma_f32 v[158:159], v[22:23], s[2:3], v[158:159] op_sel_hi:[1,0,1]
	v_pk_fma_f32 v[156:157], v[24:25], s[2:3], v[156:157] op_sel_hi:[1,0,1]
	v_pk_fma_f32 v[154:155], v[26:27], s[2:3], v[154:155] op_sel_hi:[1,0,1]
	v_pk_fma_f32 v[152:153], v[28:29], s[2:3], v[152:153] op_sel_hi:[1,0,1]
	v_pk_fma_f32 v[150:151], v[30:31], s[2:3], v[150:151] op_sel_hi:[1,0,1]
	v_readlane_b32 s2, v131, 39
	s_waitcnt vmcnt(16)
	v_cvt_scalef32_pk32_f32_fp6 v[0:31], v[32:37], 1.0
	v_pk_fma_f32 v[164:165], v[0:1], s[2:3], v[38:39] op_sel_hi:[1,0,1]
	v_pk_fma_f32 v[166:167], v[2:3], s[2:3], v[40:41] op_sel_hi:[1,0,1]
	v_pk_fma_f32 v[168:169], v[4:5], s[2:3], v[42:43] op_sel_hi:[1,0,1]
	v_pk_fma_f32 v[170:171], v[6:7], s[2:3], v[50:51] op_sel_hi:[1,0,1]
	v_pk_fma_f32 v[172:173], v[8:9], s[2:3], v[52:53] op_sel_hi:[1,0,1]
	v_pk_fma_f32 v[174:175], v[10:11], s[2:3], v[54:55] op_sel_hi:[1,0,1]
	v_pk_fma_f32 v[176:177], v[12:13], s[2:3], v[62:63] op_sel_hi:[1,0,1]
	v_pk_fma_f32 v[178:179], v[14:15], s[2:3], v[64:65] op_sel_hi:[1,0,1]
	v_pk_fma_f32 v[180:181], v[16:17], s[2:3], v[66:67] op_sel_hi:[1,0,1]
	v_pk_fma_f32 v[162:163], v[18:19], s[2:3], v[162:163] op_sel_hi:[1,0,1]
	v_pk_fma_f32 v[160:161], v[20:21], s[2:3], v[160:161] op_sel_hi:[1,0,1]
	v_pk_fma_f32 v[158:159], v[22:23], s[2:3], v[158:159] op_sel_hi:[1,0,1]
	v_pk_fma_f32 v[156:157], v[24:25], s[2:3], v[156:157] op_sel_hi:[1,0,1]
	v_pk_fma_f32 v[154:155], v[26:27], s[2:3], v[154:155] op_sel_hi:[1,0,1]
	v_pk_fma_f32 v[152:153], v[28:29], s[2:3], v[152:153] op_sel_hi:[1,0,1]
	v_pk_fma_f32 v[150:151], v[30:31], s[2:3], v[150:151] op_sel_hi:[1,0,1]
	v_readlane_b32 s2, v241, 48
	v_readlane_b32 s3, v241, 49
	v_readlane_b32 s100, v241, 50
	v_readlane_b32 s101, v241, 51
	s_nop 1
	buffer_load_dwordx4 v[62:65], v129, s[44:47], s2 offen sc1
	buffer_load_dwordx2 v[66:67], v210, s[44:47], s2 offen sc1
	buffer_load_dwordx4 v[50:53], v129, s[44:47], s3 offen sc1
	buffer_load_dwordx2 v[54:55], v210, s[44:47], s3 offen sc1
	buffer_load_dwordx4 v[38:41], v129, s[44:47], s100 offen sc1
	buffer_load_dwordx2 v[42:43], v210, s[44:47], s100 offen sc1
	buffer_load_dwordx4 v[32:35], v129, s[44:47], s101 offen sc1
	buffer_load_dwordx2 v[36:37], v210, s[44:47], s101 offen sc1
	v_readlane_b32 s2, v131, 40
	s_waitcnt vmcnt(22)
	v_cvt_scalef32_pk32_f32_fp6 v[0:31], v[98:103], 1.0
	v_pk_fma_f32 v[98:99], v[0:1], s[2:3], v[164:165] op_sel_hi:[1,0,1]
	v_pk_fma_f32 v[100:101], v[2:3], s[2:3], v[166:167] op_sel_hi:[1,0,1]
	v_pk_fma_f32 v[102:103], v[4:5], s[2:3], v[168:169] op_sel_hi:[1,0,1]
	v_pk_fma_f32 v[164:165], v[6:7], s[2:3], v[170:171] op_sel_hi:[1,0,1]
	v_pk_fma_f32 v[166:167], v[8:9], s[2:3], v[172:173] op_sel_hi:[1,0,1]
	v_pk_fma_f32 v[168:169], v[10:11], s[2:3], v[174:175] op_sel_hi:[1,0,1]
	v_pk_fma_f32 v[170:171], v[12:13], s[2:3], v[176:177] op_sel_hi:[1,0,1]
	v_pk_fma_f32 v[172:173], v[14:15], s[2:3], v[178:179] op_sel_hi:[1,0,1]
	v_pk_fma_f32 v[174:175], v[16:17], s[2:3], v[180:181] op_sel_hi:[1,0,1]
	v_pk_fma_f32 v[162:163], v[18:19], s[2:3], v[162:163] op_sel_hi:[1,0,1]
	v_pk_fma_f32 v[160:161], v[20:21], s[2:3], v[160:161] op_sel_hi:[1,0,1]
	v_pk_fma_f32 v[158:159], v[22:23], s[2:3], v[158:159] op_sel_hi:[1,0,1]
	v_pk_fma_f32 v[156:157], v[24:25], s[2:3], v[156:157] op_sel_hi:[1,0,1]
	v_pk_fma_f32 v[154:155], v[26:27], s[2:3], v[154:155] op_sel_hi:[1,0,1]
	v_pk_fma_f32 v[152:153], v[28:29], s[2:3], v[152:153] op_sel_hi:[1,0,1]
	v_pk_fma_f32 v[150:151], v[30:31], s[2:3], v[150:151] op_sel_hi:[1,0,1]
	v_readlane_b32 s2, v131, 41
	s_waitcnt vmcnt(20)
	v_cvt_scalef32_pk32_f32_fp6 v[0:31], v[92:97], 1.0
	v_pk_fma_f32 v[92:93], v[0:1], s[2:3], v[98:99] op_sel_hi:[1,0,1]
	v_pk_fma_f32 v[94:95], v[2:3], s[2:3], v[100:101] op_sel_hi:[1,0,1]
	v_pk_fma_f32 v[96:97], v[4:5], s[2:3], v[102:103] op_sel_hi:[1,0,1]
	v_pk_fma_f32 v[98:99], v[6:7], s[2:3], v[164:165] op_sel_hi:[1,0,1]
	v_pk_fma_f32 v[100:101], v[8:9], s[2:3], v[166:167] op_sel_hi:[1,0,1]
	v_pk_fma_f32 v[102:103], v[10:11], s[2:3], v[168:169] op_sel_hi:[1,0,1]
	v_pk_fma_f32 v[164:165], v[12:13], s[2:3], v[170:171] op_sel_hi:[1,0,1]
	v_pk_fma_f32 v[166:167], v[14:15], s[2:3], v[172:173] op_sel_hi:[1,0,1]
	v_pk_fma_f32 v[168:169], v[16:17], s[2:3], v[174:175] op_sel_hi:[1,0,1]
	v_pk_fma_f32 v[162:163], v[18:19], s[2:3], v[162:163] op_sel_hi:[1,0,1]
	v_pk_fma_f32 v[160:161], v[20:21], s[2:3], v[160:161] op_sel_hi:[1,0,1]
	v_pk_fma_f32 v[158:159], v[22:23], s[2:3], v[158:159] op_sel_hi:[1,0,1]
	v_pk_fma_f32 v[156:157], v[24:25], s[2:3], v[156:157] op_sel_hi:[1,0,1]
	v_pk_fma_f32 v[154:155], v[26:27], s[2:3], v[154:155] op_sel_hi:[1,0,1]
	v_pk_fma_f32 v[152:153], v[28:29], s[2:3], v[152:153] op_sel_hi:[1,0,1]
	v_pk_fma_f32 v[150:151], v[30:31], s[2:3], v[150:151] op_sel_hi:[1,0,1]
	v_readlane_b32 s2, v131, 42
	s_waitcnt vmcnt(18)
	v_cvt_scalef32_pk32_f32_fp6 v[0:31], v[86:91], 1.0
	v_pk_fma_f32 v[86:87], v[0:1], s[2:3], v[92:93] op_sel_hi:[1,0,1]
	v_pk_fma_f32 v[88:89], v[2:3], s[2:3], v[94:95] op_sel_hi:[1,0,1]
	v_pk_fma_f32 v[90:91], v[4:5], s[2:3], v[96:97] op_sel_hi:[1,0,1]
	v_pk_fma_f32 v[92:93], v[6:7], s[2:3], v[98:99] op_sel_hi:[1,0,1]
	v_pk_fma_f32 v[94:95], v[8:9], s[2:3], v[100:101] op_sel_hi:[1,0,1]
	v_pk_fma_f32 v[96:97], v[10:11], s[2:3], v[102:103] op_sel_hi:[1,0,1]
	v_pk_fma_f32 v[98:99], v[12:13], s[2:3], v[164:165] op_sel_hi:[1,0,1]
	v_pk_fma_f32 v[100:101], v[14:15], s[2:3], v[166:167] op_sel_hi:[1,0,1]
	v_pk_fma_f32 v[102:103], v[16:17], s[2:3], v[168:169] op_sel_hi:[1,0,1]
	v_pk_fma_f32 v[162:163], v[18:19], s[2:3], v[162:163] op_sel_hi:[1,0,1]
	v_pk_fma_f32 v[160:161], v[20:21], s[2:3], v[160:161] op_sel_hi:[1,0,1]
	v_pk_fma_f32 v[158:159], v[22:23], s[2:3], v[158:159] op_sel_hi:[1,0,1]
	v_pk_fma_f32 v[156:157], v[24:25], s[2:3], v[156:157] op_sel_hi:[1,0,1]
	v_pk_fma_f32 v[154:155], v[26:27], s[2:3], v[154:155] op_sel_hi:[1,0,1]
	v_pk_fma_f32 v[152:153], v[28:29], s[2:3], v[152:153] op_sel_hi:[1,0,1]
	v_pk_fma_f32 v[150:151], v[30:31], s[2:3], v[150:151] op_sel_hi:[1,0,1]
	v_readlane_b32 s2, v131, 43
	s_waitcnt vmcnt(16)
	v_cvt_scalef32_pk32_f32_fp6 v[0:31], v[80:85], 1.0
	v_pk_fma_f32 v[180:181], v[0:1], s[2:3], v[86:87] op_sel_hi:[1,0,1]
	v_pk_fma_f32 v[178:179], v[2:3], s[2:3], v[88:89] op_sel_hi:[1,0,1]
	v_pk_fma_f32 v[176:177], v[4:5], s[2:3], v[90:91] op_sel_hi:[1,0,1]
	v_pk_fma_f32 v[174:175], v[6:7], s[2:3], v[92:93] op_sel_hi:[1,0,1]
	v_pk_fma_f32 v[172:173], v[8:9], s[2:3], v[94:95] op_sel_hi:[1,0,1]
	v_pk_fma_f32 v[170:171], v[10:11], s[2:3], v[96:97] op_sel_hi:[1,0,1]
	v_pk_fma_f32 v[168:169], v[12:13], s[2:3], v[98:99] op_sel_hi:[1,0,1]
	v_pk_fma_f32 v[166:167], v[14:15], s[2:3], v[100:101] op_sel_hi:[1,0,1]
	v_pk_fma_f32 v[164:165], v[16:17], s[2:3], v[102:103] op_sel_hi:[1,0,1]
	v_pk_fma_f32 v[162:163], v[18:19], s[2:3], v[162:163] op_sel_hi:[1,0,1]
	v_pk_fma_f32 v[160:161], v[20:21], s[2:3], v[160:161] op_sel_hi:[1,0,1]
	v_pk_fma_f32 v[158:159], v[22:23], s[2:3], v[158:159] op_sel_hi:[1,0,1]
	v_pk_fma_f32 v[156:157], v[24:25], s[2:3], v[156:157] op_sel_hi:[1,0,1]
	v_pk_fma_f32 v[154:155], v[26:27], s[2:3], v[154:155] op_sel_hi:[1,0,1]
	v_pk_fma_f32 v[152:153], v[28:29], s[2:3], v[152:153] op_sel_hi:[1,0,1]
	v_pk_fma_f32 v[150:151], v[30:31], s[2:3], v[150:151] op_sel_hi:[1,0,1]
	v_readlane_b32 s2, v241, 52
	v_readlane_b32 s3, v241, 53
	v_readlane_b32 s100, v241, 54
	v_readlane_b32 s101, v241, 55
	s_nop 1
	buffer_load_dwordx4 v[98:101], v129, s[44:47], s2 offen sc1
	buffer_load_dwordx2 v[102:103], v210, s[44:47], s2 offen sc1
	buffer_load_dwordx4 v[92:95], v129, s[44:47], s3 offen sc1
	buffer_load_dwordx2 v[96:97], v210, s[44:47], s3 offen sc1
	buffer_load_dwordx4 v[86:89], v129, s[44:47], s100 offen sc1
	buffer_load_dwordx2 v[90:91], v210, s[44:47], s100 offen sc1
	buffer_load_dwordx4 v[80:83], v129, s[44:47], s101 offen sc1
	buffer_load_dwordx2 v[84:85], v210, s[44:47], s101 offen sc1
	v_readlane_b32 s2, v131, 44
	s_waitcnt vmcnt(22)
	v_cvt_scalef32_pk32_f32_fp6 v[0:31], v[74:79], 1.0
	v_pk_fma_f32 v[74:75], v[0:1], s[2:3], v[180:181] op_sel_hi:[1,0,1]
	v_pk_fma_f32 v[76:77], v[2:3], s[2:3], v[178:179] op_sel_hi:[1,0,1]
	v_pk_fma_f32 v[78:79], v[4:5], s[2:3], v[176:177] op_sel_hi:[1,0,1]
	v_pk_fma_f32 v[174:175], v[6:7], s[2:3], v[174:175] op_sel_hi:[1,0,1]
	v_pk_fma_f32 v[172:173], v[8:9], s[2:3], v[172:173] op_sel_hi:[1,0,1]
	v_pk_fma_f32 v[170:171], v[10:11], s[2:3], v[170:171] op_sel_hi:[1,0,1]
	v_pk_fma_f32 v[168:169], v[12:13], s[2:3], v[168:169] op_sel_hi:[1,0,1]
	v_pk_fma_f32 v[166:167], v[14:15], s[2:3], v[166:167] op_sel_hi:[1,0,1]
	v_pk_fma_f32 v[164:165], v[16:17], s[2:3], v[164:165] op_sel_hi:[1,0,1]
	v_pk_fma_f32 v[162:163], v[18:19], s[2:3], v[162:163] op_sel_hi:[1,0,1]
	v_pk_fma_f32 v[160:161], v[20:21], s[2:3], v[160:161] op_sel_hi:[1,0,1]
	v_pk_fma_f32 v[158:159], v[22:23], s[2:3], v[158:159] op_sel_hi:[1,0,1]
	v_pk_fma_f32 v[156:157], v[24:25], s[2:3], v[156:157] op_sel_hi:[1,0,1]
	v_pk_fma_f32 v[154:155], v[26:27], s[2:3], v[154:155] op_sel_hi:[1,0,1]
	v_pk_fma_f32 v[152:153], v[28:29], s[2:3], v[152:153] op_sel_hi:[1,0,1]
	v_pk_fma_f32 v[150:151], v[30:31], s[2:3], v[150:151] op_sel_hi:[1,0,1]
	v_readlane_b32 s2, v131, 45
	s_waitcnt vmcnt(20)
	v_cvt_scalef32_pk32_f32_fp6 v[0:31], v[68:73], 1.0
	v_pk_fma_f32 v[68:69], v[0:1], s[2:3], v[74:75] op_sel_hi:[1,0,1]
	v_pk_fma_f32 v[70:71], v[2:3], s[2:3], v[76:77] op_sel_hi:[1,0,1]
	v_pk_fma_f32 v[72:73], v[4:5], s[2:3], v[78:79] op_sel_hi:[1,0,1]
	v_pk_fma_f32 v[74:75], v[6:7], s[2:3], v[174:175] op_sel_hi:[1,0,1]
	v_pk_fma_f32 v[76:77], v[8:9], s[2:3], v[172:173] op_sel_hi:[1,0,1]
	v_pk_fma_f32 v[78:79], v[10:11], s[2:3], v[170:171] op_sel_hi:[1,0,1]
	v_pk_fma_f32 v[168:169], v[12:13], s[2:3], v[168:169] op_sel_hi:[1,0,1]
	v_pk_fma_f32 v[166:167], v[14:15], s[2:3], v[166:167] op_sel_hi:[1,0,1]
	v_pk_fma_f32 v[164:165], v[16:17], s[2:3], v[164:165] op_sel_hi:[1,0,1]
	v_pk_fma_f32 v[162:163], v[18:19], s[2:3], v[162:163] op_sel_hi:[1,0,1]
	v_pk_fma_f32 v[160:161], v[20:21], s[2:3], v[160:161] op_sel_hi:[1,0,1]
	v_pk_fma_f32 v[158:159], v[22:23], s[2:3], v[158:159] op_sel_hi:[1,0,1]
	v_pk_fma_f32 v[156:157], v[24:25], s[2:3], v[156:157] op_sel_hi:[1,0,1]
	v_pk_fma_f32 v[154:155], v[26:27], s[2:3], v[154:155] op_sel_hi:[1,0,1]
	v_pk_fma_f32 v[152:153], v[28:29], s[2:3], v[152:153] op_sel_hi:[1,0,1]
	v_pk_fma_f32 v[150:151], v[30:31], s[2:3], v[150:151] op_sel_hi:[1,0,1]
	v_readlane_b32 s2, v131, 46
	s_waitcnt vmcnt(18)
	v_cvt_scalef32_pk32_f32_fp6 v[0:31], v[56:61], 1.0
	v_pk_fma_f32 v[56:57], v[0:1], s[2:3], v[68:69] op_sel_hi:[1,0,1]
	v_pk_fma_f32 v[58:59], v[2:3], s[2:3], v[70:71] op_sel_hi:[1,0,1]
	v_pk_fma_f32 v[60:61], v[4:5], s[2:3], v[72:73] op_sel_hi:[1,0,1]
	v_pk_fma_f32 v[68:69], v[6:7], s[2:3], v[74:75] op_sel_hi:[1,0,1]
	v_pk_fma_f32 v[70:71], v[8:9], s[2:3], v[76:77] op_sel_hi:[1,0,1]
	v_pk_fma_f32 v[72:73], v[10:11], s[2:3], v[78:79] op_sel_hi:[1,0,1]
	v_pk_fma_f32 v[74:75], v[12:13], s[2:3], v[168:169] op_sel_hi:[1,0,1]
	v_pk_fma_f32 v[76:77], v[14:15], s[2:3], v[166:167] op_sel_hi:[1,0,1]
	v_pk_fma_f32 v[78:79], v[16:17], s[2:3], v[164:165] op_sel_hi:[1,0,1]
	v_pk_fma_f32 v[162:163], v[18:19], s[2:3], v[162:163] op_sel_hi:[1,0,1]
	v_pk_fma_f32 v[160:161], v[20:21], s[2:3], v[160:161] op_sel_hi:[1,0,1]
	v_pk_fma_f32 v[158:159], v[22:23], s[2:3], v[158:159] op_sel_hi:[1,0,1]
	v_pk_fma_f32 v[156:157], v[24:25], s[2:3], v[156:157] op_sel_hi:[1,0,1]
	v_pk_fma_f32 v[154:155], v[26:27], s[2:3], v[154:155] op_sel_hi:[1,0,1]
	v_pk_fma_f32 v[152:153], v[28:29], s[2:3], v[152:153] op_sel_hi:[1,0,1]
	v_pk_fma_f32 v[150:151], v[30:31], s[2:3], v[150:151] op_sel_hi:[1,0,1]
	v_readlane_b32 s2, v131, 47
	s_waitcnt vmcnt(16)
	v_cvt_scalef32_pk32_f32_fp6 v[0:31], v[44:49], 1.0
	v_pk_fma_f32 v[164:165], v[0:1], s[2:3], v[56:57] op_sel_hi:[1,0,1]
	v_pk_fma_f32 v[166:167], v[2:3], s[2:3], v[58:59] op_sel_hi:[1,0,1]
	v_pk_fma_f32 v[168:169], v[4:5], s[2:3], v[60:61] op_sel_hi:[1,0,1]
	v_pk_fma_f32 v[170:171], v[6:7], s[2:3], v[68:69] op_sel_hi:[1,0,1]
	v_pk_fma_f32 v[172:173], v[8:9], s[2:3], v[70:71] op_sel_hi:[1,0,1]
	v_pk_fma_f32 v[174:175], v[10:11], s[2:3], v[72:73] op_sel_hi:[1,0,1]
	v_pk_fma_f32 v[176:177], v[12:13], s[2:3], v[74:75] op_sel_hi:[1,0,1]
	v_pk_fma_f32 v[178:179], v[14:15], s[2:3], v[76:77] op_sel_hi:[1,0,1]
	v_pk_fma_f32 v[180:181], v[16:17], s[2:3], v[78:79] op_sel_hi:[1,0,1]
	v_pk_fma_f32 v[162:163], v[18:19], s[2:3], v[162:163] op_sel_hi:[1,0,1]
	v_pk_fma_f32 v[160:161], v[20:21], s[2:3], v[160:161] op_sel_hi:[1,0,1]
	v_pk_fma_f32 v[158:159], v[22:23], s[2:3], v[158:159] op_sel_hi:[1,0,1]
	v_pk_fma_f32 v[156:157], v[24:25], s[2:3], v[156:157] op_sel_hi:[1,0,1]
	v_pk_fma_f32 v[154:155], v[26:27], s[2:3], v[154:155] op_sel_hi:[1,0,1]
	v_pk_fma_f32 v[152:153], v[28:29], s[2:3], v[152:153] op_sel_hi:[1,0,1]
	v_pk_fma_f32 v[150:151], v[30:31], s[2:3], v[150:151] op_sel_hi:[1,0,1]
	v_readlane_b32 s2, v241, 56
	v_readlane_b32 s3, v241, 57
	v_readlane_b32 s100, v241, 58
	v_readlane_b32 s101, v241, 59
	s_nop 1
	buffer_load_dwordx4 v[74:77], v129, s[44:47], s2 offen sc1
	buffer_load_dwordx2 v[78:79], v210, s[44:47], s2 offen sc1
	buffer_load_dwordx4 v[68:71], v129, s[44:47], s3 offen sc1
	buffer_load_dwordx2 v[72:73], v210, s[44:47], s3 offen sc1
	buffer_load_dwordx4 v[56:59], v129, s[44:47], s100 offen sc1
	buffer_load_dwordx2 v[60:61], v210, s[44:47], s100 offen sc1
	buffer_load_dwordx4 v[44:47], v129, s[44:47], s101 offen sc1
	buffer_load_dwordx2 v[48:49], v210, s[44:47], s101 offen sc1
	v_readlane_b32 s2, v131, 48
	s_waitcnt vmcnt(22)
	v_cvt_scalef32_pk32_f32_fp6 v[0:31], v[62:67], 1.0
	v_pk_fma_f32 v[62:63], v[0:1], s[2:3], v[164:165] op_sel_hi:[1,0,1]
	v_pk_fma_f32 v[64:65], v[2:3], s[2:3], v[166:167] op_sel_hi:[1,0,1]
	v_pk_fma_f32 v[66:67], v[4:5], s[2:3], v[168:169] op_sel_hi:[1,0,1]
	v_pk_fma_f32 v[164:165], v[6:7], s[2:3], v[170:171] op_sel_hi:[1,0,1]
	v_pk_fma_f32 v[166:167], v[8:9], s[2:3], v[172:173] op_sel_hi:[1,0,1]
	v_pk_fma_f32 v[168:169], v[10:11], s[2:3], v[174:175] op_sel_hi:[1,0,1]
	v_pk_fma_f32 v[170:171], v[12:13], s[2:3], v[176:177] op_sel_hi:[1,0,1]
	v_pk_fma_f32 v[172:173], v[14:15], s[2:3], v[178:179] op_sel_hi:[1,0,1]
	v_pk_fma_f32 v[174:175], v[16:17], s[2:3], v[180:181] op_sel_hi:[1,0,1]
	v_pk_fma_f32 v[162:163], v[18:19], s[2:3], v[162:163] op_sel_hi:[1,0,1]
	v_pk_fma_f32 v[160:161], v[20:21], s[2:3], v[160:161] op_sel_hi:[1,0,1]
	v_pk_fma_f32 v[158:159], v[22:23], s[2:3], v[158:159] op_sel_hi:[1,0,1]
	v_pk_fma_f32 v[156:157], v[24:25], s[2:3], v[156:157] op_sel_hi:[1,0,1]
	v_pk_fma_f32 v[154:155], v[26:27], s[2:3], v[154:155] op_sel_hi:[1,0,1]
	v_pk_fma_f32 v[152:153], v[28:29], s[2:3], v[152:153] op_sel_hi:[1,0,1]
	v_pk_fma_f32 v[150:151], v[30:31], s[2:3], v[150:151] op_sel_hi:[1,0,1]
	v_readlane_b32 s2, v131, 49
	s_waitcnt vmcnt(20)
	v_cvt_scalef32_pk32_f32_fp6 v[0:31], v[50:55], 1.0
	v_pk_fma_f32 v[50:51], v[0:1], s[2:3], v[62:63] op_sel_hi:[1,0,1]
	v_pk_fma_f32 v[52:53], v[2:3], s[2:3], v[64:65] op_sel_hi:[1,0,1]
	v_pk_fma_f32 v[54:55], v[4:5], s[2:3], v[66:67] op_sel_hi:[1,0,1]
	v_pk_fma_f32 v[62:63], v[6:7], s[2:3], v[164:165] op_sel_hi:[1,0,1]
	v_pk_fma_f32 v[64:65], v[8:9], s[2:3], v[166:167] op_sel_hi:[1,0,1]
	v_pk_fma_f32 v[66:67], v[10:11], s[2:3], v[168:169] op_sel_hi:[1,0,1]
	v_pk_fma_f32 v[164:165], v[12:13], s[2:3], v[170:171] op_sel_hi:[1,0,1]
	v_pk_fma_f32 v[166:167], v[14:15], s[2:3], v[172:173] op_sel_hi:[1,0,1]
	v_pk_fma_f32 v[168:169], v[16:17], s[2:3], v[174:175] op_sel_hi:[1,0,1]
	v_pk_fma_f32 v[162:163], v[18:19], s[2:3], v[162:163] op_sel_hi:[1,0,1]
	v_pk_fma_f32 v[160:161], v[20:21], s[2:3], v[160:161] op_sel_hi:[1,0,1]
	v_pk_fma_f32 v[158:159], v[22:23], s[2:3], v[158:159] op_sel_hi:[1,0,1]
	v_pk_fma_f32 v[156:157], v[24:25], s[2:3], v[156:157] op_sel_hi:[1,0,1]
	v_pk_fma_f32 v[154:155], v[26:27], s[2:3], v[154:155] op_sel_hi:[1,0,1]
	v_pk_fma_f32 v[152:153], v[28:29], s[2:3], v[152:153] op_sel_hi:[1,0,1]
	v_pk_fma_f32 v[150:151], v[30:31], s[2:3], v[150:151] op_sel_hi:[1,0,1]
	v_readlane_b32 s2, v131, 50
	s_waitcnt vmcnt(18)
	v_cvt_scalef32_pk32_f32_fp6 v[0:31], v[38:43], 1.0
	v_pk_fma_f32 v[38:39], v[0:1], s[2:3], v[50:51] op_sel_hi:[1,0,1]
	v_pk_fma_f32 v[40:41], v[2:3], s[2:3], v[52:53] op_sel_hi:[1,0,1]
	v_pk_fma_f32 v[42:43], v[4:5], s[2:3], v[54:55] op_sel_hi:[1,0,1]
	v_pk_fma_f32 v[50:51], v[6:7], s[2:3], v[62:63] op_sel_hi:[1,0,1]
	v_pk_fma_f32 v[52:53], v[8:9], s[2:3], v[64:65] op_sel_hi:[1,0,1]
	v_pk_fma_f32 v[54:55], v[10:11], s[2:3], v[66:67] op_sel_hi:[1,0,1]
	v_pk_fma_f32 v[62:63], v[12:13], s[2:3], v[164:165] op_sel_hi:[1,0,1]
	v_pk_fma_f32 v[64:65], v[14:15], s[2:3], v[166:167] op_sel_hi:[1,0,1]
	v_pk_fma_f32 v[66:67], v[16:17], s[2:3], v[168:169] op_sel_hi:[1,0,1]
	v_pk_fma_f32 v[162:163], v[18:19], s[2:3], v[162:163] op_sel_hi:[1,0,1]
	v_pk_fma_f32 v[160:161], v[20:21], s[2:3], v[160:161] op_sel_hi:[1,0,1]
	v_pk_fma_f32 v[158:159], v[22:23], s[2:3], v[158:159] op_sel_hi:[1,0,1]
	v_pk_fma_f32 v[156:157], v[24:25], s[2:3], v[156:157] op_sel_hi:[1,0,1]
	v_pk_fma_f32 v[154:155], v[26:27], s[2:3], v[154:155] op_sel_hi:[1,0,1]
	v_pk_fma_f32 v[152:153], v[28:29], s[2:3], v[152:153] op_sel_hi:[1,0,1]
	v_pk_fma_f32 v[150:151], v[30:31], s[2:3], v[150:151] op_sel_hi:[1,0,1]
	v_readlane_b32 s2, v131, 51
	s_waitcnt vmcnt(16)
	v_cvt_scalef32_pk32_f32_fp6 v[0:31], v[32:37], 1.0
	v_pk_fma_f32 v[164:165], v[0:1], s[2:3], v[38:39] op_sel_hi:[1,0,1]
	v_pk_fma_f32 v[166:167], v[2:3], s[2:3], v[40:41] op_sel_hi:[1,0,1]
	v_pk_fma_f32 v[168:169], v[4:5], s[2:3], v[42:43] op_sel_hi:[1,0,1]
	v_pk_fma_f32 v[170:171], v[6:7], s[2:3], v[50:51] op_sel_hi:[1,0,1]
	v_pk_fma_f32 v[172:173], v[8:9], s[2:3], v[52:53] op_sel_hi:[1,0,1]
	v_pk_fma_f32 v[174:175], v[10:11], s[2:3], v[54:55] op_sel_hi:[1,0,1]
	v_pk_fma_f32 v[176:177], v[12:13], s[2:3], v[62:63] op_sel_hi:[1,0,1]
	v_pk_fma_f32 v[178:179], v[14:15], s[2:3], v[64:65] op_sel_hi:[1,0,1]
	v_pk_fma_f32 v[180:181], v[16:17], s[2:3], v[66:67] op_sel_hi:[1,0,1]
	v_pk_fma_f32 v[162:163], v[18:19], s[2:3], v[162:163] op_sel_hi:[1,0,1]
	v_pk_fma_f32 v[160:161], v[20:21], s[2:3], v[160:161] op_sel_hi:[1,0,1]
	v_pk_fma_f32 v[158:159], v[22:23], s[2:3], v[158:159] op_sel_hi:[1,0,1]
	v_pk_fma_f32 v[156:157], v[24:25], s[2:3], v[156:157] op_sel_hi:[1,0,1]
	v_pk_fma_f32 v[154:155], v[26:27], s[2:3], v[154:155] op_sel_hi:[1,0,1]
	v_pk_fma_f32 v[152:153], v[28:29], s[2:3], v[152:153] op_sel_hi:[1,0,1]
	v_pk_fma_f32 v[150:151], v[30:31], s[2:3], v[150:151] op_sel_hi:[1,0,1]
	v_readlane_b32 s2, v241, 60
	v_readlane_b32 s3, v241, 61
	v_readlane_b32 s100, v241, 62
	v_readlane_b32 s101, v241, 63
	s_nop 1
	buffer_load_dwordx4 v[62:65], v129, s[44:47], s2 offen sc1
	buffer_load_dwordx2 v[66:67], v210, s[44:47], s2 offen sc1
	buffer_load_dwordx4 v[50:53], v129, s[44:47], s3 offen sc1
	buffer_load_dwordx2 v[54:55], v210, s[44:47], s3 offen sc1
	buffer_load_dwordx4 v[38:41], v129, s[44:47], s100 offen sc1
	buffer_load_dwordx2 v[42:43], v210, s[44:47], s100 offen sc1
	buffer_load_dwordx4 v[32:35], v129, s[44:47], s101 offen sc1
	buffer_load_dwordx2 v[36:37], v210, s[44:47], s101 offen sc1
	v_readlane_b32 s2, v131, 52
	s_waitcnt vmcnt(22)
	v_cvt_scalef32_pk32_f32_fp6 v[0:31], v[98:103], 1.0
	v_pk_fma_f32 v[98:99], v[0:1], s[2:3], v[164:165] op_sel_hi:[1,0,1]
	v_pk_fma_f32 v[100:101], v[2:3], s[2:3], v[166:167] op_sel_hi:[1,0,1]
	v_pk_fma_f32 v[102:103], v[4:5], s[2:3], v[168:169] op_sel_hi:[1,0,1]
	v_pk_fma_f32 v[164:165], v[6:7], s[2:3], v[170:171] op_sel_hi:[1,0,1]
	v_pk_fma_f32 v[166:167], v[8:9], s[2:3], v[172:173] op_sel_hi:[1,0,1]
	v_pk_fma_f32 v[168:169], v[10:11], s[2:3], v[174:175] op_sel_hi:[1,0,1]
	v_pk_fma_f32 v[170:171], v[12:13], s[2:3], v[176:177] op_sel_hi:[1,0,1]
	v_pk_fma_f32 v[172:173], v[14:15], s[2:3], v[178:179] op_sel_hi:[1,0,1]
	v_pk_fma_f32 v[174:175], v[16:17], s[2:3], v[180:181] op_sel_hi:[1,0,1]
	v_pk_fma_f32 v[162:163], v[18:19], s[2:3], v[162:163] op_sel_hi:[1,0,1]
	v_pk_fma_f32 v[160:161], v[20:21], s[2:3], v[160:161] op_sel_hi:[1,0,1]
	v_pk_fma_f32 v[158:159], v[22:23], s[2:3], v[158:159] op_sel_hi:[1,0,1]
	v_pk_fma_f32 v[156:157], v[24:25], s[2:3], v[156:157] op_sel_hi:[1,0,1]
	v_pk_fma_f32 v[154:155], v[26:27], s[2:3], v[154:155] op_sel_hi:[1,0,1]
	v_pk_fma_f32 v[152:153], v[28:29], s[2:3], v[152:153] op_sel_hi:[1,0,1]
	v_pk_fma_f32 v[150:151], v[30:31], s[2:3], v[150:151] op_sel_hi:[1,0,1]
	v_readlane_b32 s2, v131, 53
	s_waitcnt vmcnt(20)
	v_cvt_scalef32_pk32_f32_fp6 v[0:31], v[92:97], 1.0
	v_pk_fma_f32 v[92:93], v[0:1], s[2:3], v[98:99] op_sel_hi:[1,0,1]
	v_pk_fma_f32 v[94:95], v[2:3], s[2:3], v[100:101] op_sel_hi:[1,0,1]
	v_pk_fma_f32 v[96:97], v[4:5], s[2:3], v[102:103] op_sel_hi:[1,0,1]
	v_pk_fma_f32 v[98:99], v[6:7], s[2:3], v[164:165] op_sel_hi:[1,0,1]
	v_pk_fma_f32 v[100:101], v[8:9], s[2:3], v[166:167] op_sel_hi:[1,0,1]
	v_pk_fma_f32 v[102:103], v[10:11], s[2:3], v[168:169] op_sel_hi:[1,0,1]
	v_pk_fma_f32 v[164:165], v[12:13], s[2:3], v[170:171] op_sel_hi:[1,0,1]
	v_pk_fma_f32 v[166:167], v[14:15], s[2:3], v[172:173] op_sel_hi:[1,0,1]
	v_pk_fma_f32 v[168:169], v[16:17], s[2:3], v[174:175] op_sel_hi:[1,0,1]
	v_pk_fma_f32 v[162:163], v[18:19], s[2:3], v[162:163] op_sel_hi:[1,0,1]
	v_pk_fma_f32 v[160:161], v[20:21], s[2:3], v[160:161] op_sel_hi:[1,0,1]
	v_pk_fma_f32 v[158:159], v[22:23], s[2:3], v[158:159] op_sel_hi:[1,0,1]
	v_pk_fma_f32 v[156:157], v[24:25], s[2:3], v[156:157] op_sel_hi:[1,0,1]
	v_pk_fma_f32 v[154:155], v[26:27], s[2:3], v[154:155] op_sel_hi:[1,0,1]
	v_pk_fma_f32 v[152:153], v[28:29], s[2:3], v[152:153] op_sel_hi:[1,0,1]
	v_pk_fma_f32 v[150:151], v[30:31], s[2:3], v[150:151] op_sel_hi:[1,0,1]
	v_readlane_b32 s2, v131, 54
	s_waitcnt vmcnt(18)
	v_cvt_scalef32_pk32_f32_fp6 v[0:31], v[86:91], 1.0
	v_pk_fma_f32 v[86:87], v[0:1], s[2:3], v[92:93] op_sel_hi:[1,0,1]
	v_pk_fma_f32 v[88:89], v[2:3], s[2:3], v[94:95] op_sel_hi:[1,0,1]
	v_pk_fma_f32 v[90:91], v[4:5], s[2:3], v[96:97] op_sel_hi:[1,0,1]
	v_pk_fma_f32 v[92:93], v[6:7], s[2:3], v[98:99] op_sel_hi:[1,0,1]
	v_pk_fma_f32 v[94:95], v[8:9], s[2:3], v[100:101] op_sel_hi:[1,0,1]
	v_pk_fma_f32 v[96:97], v[10:11], s[2:3], v[102:103] op_sel_hi:[1,0,1]
	v_pk_fma_f32 v[98:99], v[12:13], s[2:3], v[164:165] op_sel_hi:[1,0,1]
	v_pk_fma_f32 v[100:101], v[14:15], s[2:3], v[166:167] op_sel_hi:[1,0,1]
	v_pk_fma_f32 v[102:103], v[16:17], s[2:3], v[168:169] op_sel_hi:[1,0,1]
	v_pk_fma_f32 v[162:163], v[18:19], s[2:3], v[162:163] op_sel_hi:[1,0,1]
	v_pk_fma_f32 v[160:161], v[20:21], s[2:3], v[160:161] op_sel_hi:[1,0,1]
	v_pk_fma_f32 v[158:159], v[22:23], s[2:3], v[158:159] op_sel_hi:[1,0,1]
	v_pk_fma_f32 v[156:157], v[24:25], s[2:3], v[156:157] op_sel_hi:[1,0,1]
	v_pk_fma_f32 v[154:155], v[26:27], s[2:3], v[154:155] op_sel_hi:[1,0,1]
	v_pk_fma_f32 v[152:153], v[28:29], s[2:3], v[152:153] op_sel_hi:[1,0,1]
	v_pk_fma_f32 v[150:151], v[30:31], s[2:3], v[150:151] op_sel_hi:[1,0,1]
	v_readlane_b32 s2, v131, 55
	s_waitcnt vmcnt(16)
	v_cvt_scalef32_pk32_f32_fp6 v[0:31], v[80:85], 1.0
	v_pk_fma_f32 v[180:181], v[0:1], s[2:3], v[86:87] op_sel_hi:[1,0,1]
	v_pk_fma_f32 v[178:179], v[2:3], s[2:3], v[88:89] op_sel_hi:[1,0,1]
	v_pk_fma_f32 v[176:177], v[4:5], s[2:3], v[90:91] op_sel_hi:[1,0,1]
	v_pk_fma_f32 v[174:175], v[6:7], s[2:3], v[92:93] op_sel_hi:[1,0,1]
	v_pk_fma_f32 v[172:173], v[8:9], s[2:3], v[94:95] op_sel_hi:[1,0,1]
	v_pk_fma_f32 v[170:171], v[10:11], s[2:3], v[96:97] op_sel_hi:[1,0,1]
	v_pk_fma_f32 v[168:169], v[12:13], s[2:3], v[98:99] op_sel_hi:[1,0,1]
	v_pk_fma_f32 v[166:167], v[14:15], s[2:3], v[100:101] op_sel_hi:[1,0,1]
	v_pk_fma_f32 v[164:165], v[16:17], s[2:3], v[102:103] op_sel_hi:[1,0,1]
	v_pk_fma_f32 v[162:163], v[18:19], s[2:3], v[162:163] op_sel_hi:[1,0,1]
	v_pk_fma_f32 v[160:161], v[20:21], s[2:3], v[160:161] op_sel_hi:[1,0,1]
	v_pk_fma_f32 v[158:159], v[22:23], s[2:3], v[158:159] op_sel_hi:[1,0,1]
	v_pk_fma_f32 v[156:157], v[24:25], s[2:3], v[156:157] op_sel_hi:[1,0,1]
	v_pk_fma_f32 v[154:155], v[26:27], s[2:3], v[154:155] op_sel_hi:[1,0,1]
	v_pk_fma_f32 v[152:153], v[28:29], s[2:3], v[152:153] op_sel_hi:[1,0,1]
	v_pk_fma_f32 v[150:151], v[30:31], s[2:3], v[150:151] op_sel_hi:[1,0,1]
	v_readlane_b32 s0, v131, 56
	s_waitcnt vmcnt(14)
	v_cvt_scalef32_pk32_f32_fp6 v[0:31], v[74:79], 1.0
	v_pk_fma_f32 v[74:75], v[0:1], s[0:1], v[180:181] op_sel_hi:[1,0,1]
	v_pk_fma_f32 v[76:77], v[2:3], s[0:1], v[178:179] op_sel_hi:[1,0,1]
	v_pk_fma_f32 v[78:79], v[4:5], s[0:1], v[176:177] op_sel_hi:[1,0,1]
	v_pk_fma_f32 v[80:81], v[6:7], s[0:1], v[174:175] op_sel_hi:[1,0,1]
	v_pk_fma_f32 v[82:83], v[8:9], s[0:1], v[172:173] op_sel_hi:[1,0,1]
	v_pk_fma_f32 v[84:85], v[10:11], s[0:1], v[170:171] op_sel_hi:[1,0,1]
	v_pk_fma_f32 v[86:87], v[12:13], s[0:1], v[168:169] op_sel_hi:[1,0,1]
	v_pk_fma_f32 v[88:89], v[14:15], s[0:1], v[166:167] op_sel_hi:[1,0,1]
	v_pk_fma_f32 v[90:91], v[16:17], s[0:1], v[164:165] op_sel_hi:[1,0,1]
	v_pk_fma_f32 v[92:93], v[18:19], s[0:1], v[162:163] op_sel_hi:[1,0,1]
	v_pk_fma_f32 v[94:95], v[20:21], s[0:1], v[160:161] op_sel_hi:[1,0,1]
	v_pk_fma_f32 v[96:97], v[22:23], s[0:1], v[158:159] op_sel_hi:[1,0,1]
	v_pk_fma_f32 v[98:99], v[24:25], s[0:1], v[156:157] op_sel_hi:[1,0,1]
	v_pk_fma_f32 v[100:101], v[26:27], s[0:1], v[154:155] op_sel_hi:[1,0,1]
	v_pk_fma_f32 v[102:103], v[28:29], s[0:1], v[152:153] op_sel_hi:[1,0,1]
	v_pk_fma_f32 v[150:151], v[30:31], s[0:1], v[150:151] op_sel_hi:[1,0,1]
	v_readlane_b32 s0, v131, 57
	s_waitcnt vmcnt(12)
	v_cvt_scalef32_pk32_f32_fp6 v[0:31], v[68:73], 1.0
	v_pk_fma_f32 v[68:69], v[0:1], s[0:1], v[74:75] op_sel_hi:[1,0,1]
	v_pk_fma_f32 v[70:71], v[2:3], s[0:1], v[76:77] op_sel_hi:[1,0,1]
	v_pk_fma_f32 v[72:73], v[4:5], s[0:1], v[78:79] op_sel_hi:[1,0,1]
	v_pk_fma_f32 v[74:75], v[6:7], s[0:1], v[80:81] op_sel_hi:[1,0,1]
	v_pk_fma_f32 v[76:77], v[8:9], s[0:1], v[82:83] op_sel_hi:[1,0,1]
	v_pk_fma_f32 v[78:79], v[10:11], s[0:1], v[84:85] op_sel_hi:[1,0,1]
	v_pk_fma_f32 v[80:81], v[12:13], s[0:1], v[86:87] op_sel_hi:[1,0,1]
	v_pk_fma_f32 v[82:83], v[14:15], s[0:1], v[88:89] op_sel_hi:[1,0,1]
	v_pk_fma_f32 v[84:85], v[16:17], s[0:1], v[90:91] op_sel_hi:[1,0,1]
	v_pk_fma_f32 v[86:87], v[18:19], s[0:1], v[92:93] op_sel_hi:[1,0,1]
	v_pk_fma_f32 v[88:89], v[20:21], s[0:1], v[94:95] op_sel_hi:[1,0,1]
	v_pk_fma_f32 v[90:91], v[22:23], s[0:1], v[96:97] op_sel_hi:[1,0,1]
	v_pk_fma_f32 v[92:93], v[24:25], s[0:1], v[98:99] op_sel_hi:[1,0,1]
	v_pk_fma_f32 v[94:95], v[26:27], s[0:1], v[100:101] op_sel_hi:[1,0,1]
	v_pk_fma_f32 v[96:97], v[28:29], s[0:1], v[102:103] op_sel_hi:[1,0,1]
	v_pk_fma_f32 v[98:99], v[30:31], s[0:1], v[150:151] op_sel_hi:[1,0,1]
	v_readlane_b32 s0, v131, 58
	s_waitcnt vmcnt(10)
	v_cvt_scalef32_pk32_f32_fp6 v[0:31], v[56:61], 1.0
	v_pk_fma_f32 v[56:57], v[0:1], s[0:1], v[68:69] op_sel_hi:[1,0,1]
	v_pk_fma_f32 v[58:59], v[2:3], s[0:1], v[70:71] op_sel_hi:[1,0,1]
	v_pk_fma_f32 v[60:61], v[4:5], s[0:1], v[72:73] op_sel_hi:[1,0,1]
	v_pk_fma_f32 v[68:69], v[6:7], s[0:1], v[74:75] op_sel_hi:[1,0,1]
	v_pk_fma_f32 v[70:71], v[8:9], s[0:1], v[76:77] op_sel_hi:[1,0,1]
	v_pk_fma_f32 v[72:73], v[10:11], s[0:1], v[78:79] op_sel_hi:[1,0,1]
	v_pk_fma_f32 v[74:75], v[12:13], s[0:1], v[80:81] op_sel_hi:[1,0,1]
	v_pk_fma_f32 v[76:77], v[14:15], s[0:1], v[82:83] op_sel_hi:[1,0,1]
	v_pk_fma_f32 v[78:79], v[16:17], s[0:1], v[84:85] op_sel_hi:[1,0,1]
	v_pk_fma_f32 v[80:81], v[18:19], s[0:1], v[86:87] op_sel_hi:[1,0,1]
	v_pk_fma_f32 v[82:83], v[20:21], s[0:1], v[88:89] op_sel_hi:[1,0,1]
	v_pk_fma_f32 v[84:85], v[22:23], s[0:1], v[90:91] op_sel_hi:[1,0,1]
	v_pk_fma_f32 v[86:87], v[24:25], s[0:1], v[92:93] op_sel_hi:[1,0,1]
	v_pk_fma_f32 v[88:89], v[26:27], s[0:1], v[94:95] op_sel_hi:[1,0,1]
	v_pk_fma_f32 v[90:91], v[28:29], s[0:1], v[96:97] op_sel_hi:[1,0,1]
	v_pk_fma_f32 v[92:93], v[30:31], s[0:1], v[98:99] op_sel_hi:[1,0,1]
	v_readlane_b32 s0, v131, 59
	s_waitcnt vmcnt(8)
	v_cvt_scalef32_pk32_f32_fp6 v[0:31], v[44:49], 1.0
	v_pk_fma_f32 v[46:47], v[2:3], s[0:1], v[58:59] op_sel_hi:[1,0,1]
	v_pk_fma_f32 v[44:45], v[0:1], s[0:1], v[56:57] op_sel_hi:[1,0,1]
	v_pk_fma_f32 v[48:49], v[4:5], s[0:1], v[60:61] op_sel_hi:[1,0,1]
	v_pk_fma_f32 v[56:57], v[6:7], s[0:1], v[68:69] op_sel_hi:[1,0,1]
	v_pk_fma_f32 v[58:59], v[8:9], s[0:1], v[70:71] op_sel_hi:[1,0,1]
	v_pk_fma_f32 v[60:61], v[10:11], s[0:1], v[72:73] op_sel_hi:[1,0,1]
	v_pk_fma_f32 v[68:69], v[12:13], s[0:1], v[74:75] op_sel_hi:[1,0,1]
	v_pk_fma_f32 v[70:71], v[14:15], s[0:1], v[76:77] op_sel_hi:[1,0,1]
	v_pk_fma_f32 v[72:73], v[16:17], s[0:1], v[78:79] op_sel_hi:[1,0,1]
	v_pk_fma_f32 v[74:75], v[18:19], s[0:1], v[80:81] op_sel_hi:[1,0,1]
	v_pk_fma_f32 v[76:77], v[20:21], s[0:1], v[82:83] op_sel_hi:[1,0,1]
	v_pk_fma_f32 v[78:79], v[22:23], s[0:1], v[84:85] op_sel_hi:[1,0,1]
	v_pk_fma_f32 v[80:81], v[24:25], s[0:1], v[86:87] op_sel_hi:[1,0,1]
	v_pk_fma_f32 v[82:83], v[26:27], s[0:1], v[88:89] op_sel_hi:[1,0,1]
	v_pk_fma_f32 v[84:85], v[28:29], s[0:1], v[90:91] op_sel_hi:[1,0,1]
	v_pk_fma_f32 v[86:87], v[30:31], s[0:1], v[92:93] op_sel_hi:[1,0,1]
	v_readlane_b32 s0, v131, 60
	s_waitcnt vmcnt(6)
	v_cvt_scalef32_pk32_f32_fp6 v[0:31], v[62:67], 1.0
	v_pk_fma_f32 v[44:45], v[0:1], s[0:1], v[44:45] op_sel_hi:[1,0,1]
	v_pk_fma_f32 v[46:47], v[2:3], s[0:1], v[46:47] op_sel_hi:[1,0,1]
	v_pk_fma_f32 v[48:49], v[4:5], s[0:1], v[48:49] op_sel_hi:[1,0,1]
	v_pk_fma_f32 v[56:57], v[6:7], s[0:1], v[56:57] op_sel_hi:[1,0,1]
	v_pk_fma_f32 v[58:59], v[8:9], s[0:1], v[58:59] op_sel_hi:[1,0,1]
	v_pk_fma_f32 v[60:61], v[10:11], s[0:1], v[60:61] op_sel_hi:[1,0,1]
	v_pk_fma_f32 v[62:63], v[12:13], s[0:1], v[68:69] op_sel_hi:[1,0,1]
	v_pk_fma_f32 v[64:65], v[14:15], s[0:1], v[70:71] op_sel_hi:[1,0,1]
	v_pk_fma_f32 v[66:67], v[16:17], s[0:1], v[72:73] op_sel_hi:[1,0,1]
	v_pk_fma_f32 v[68:69], v[18:19], s[0:1], v[74:75] op_sel_hi:[1,0,1]
	v_pk_fma_f32 v[70:71], v[20:21], s[0:1], v[76:77] op_sel_hi:[1,0,1]
	v_pk_fma_f32 v[72:73], v[22:23], s[0:1], v[78:79] op_sel_hi:[1,0,1]
	v_pk_fma_f32 v[74:75], v[24:25], s[0:1], v[80:81] op_sel_hi:[1,0,1]
	v_pk_fma_f32 v[76:77], v[26:27], s[0:1], v[82:83] op_sel_hi:[1,0,1]
	v_pk_fma_f32 v[78:79], v[28:29], s[0:1], v[84:85] op_sel_hi:[1,0,1]
	v_pk_fma_f32 v[80:81], v[30:31], s[0:1], v[86:87] op_sel_hi:[1,0,1]
	v_readlane_b32 s0, v131, 61
	s_waitcnt vmcnt(4)
	v_cvt_scalef32_pk32_f32_fp6 v[0:31], v[50:55], 1.0
	v_pk_fma_f32 v[44:45], v[0:1], s[0:1], v[44:45] op_sel_hi:[1,0,1]
	v_pk_fma_f32 v[46:47], v[2:3], s[0:1], v[46:47] op_sel_hi:[1,0,1]
	v_pk_fma_f32 v[48:49], v[4:5], s[0:1], v[48:49] op_sel_hi:[1,0,1]
	v_pk_fma_f32 v[50:51], v[6:7], s[0:1], v[56:57] op_sel_hi:[1,0,1]
	v_pk_fma_f32 v[52:53], v[8:9], s[0:1], v[58:59] op_sel_hi:[1,0,1]
	v_pk_fma_f32 v[54:55], v[10:11], s[0:1], v[60:61] op_sel_hi:[1,0,1]
	v_pk_fma_f32 v[56:57], v[12:13], s[0:1], v[62:63] op_sel_hi:[1,0,1]
	v_pk_fma_f32 v[58:59], v[14:15], s[0:1], v[64:65] op_sel_hi:[1,0,1]
	v_pk_fma_f32 v[60:61], v[16:17], s[0:1], v[66:67] op_sel_hi:[1,0,1]
	v_pk_fma_f32 v[62:63], v[18:19], s[0:1], v[68:69] op_sel_hi:[1,0,1]
	v_pk_fma_f32 v[64:65], v[20:21], s[0:1], v[70:71] op_sel_hi:[1,0,1]
	v_pk_fma_f32 v[66:67], v[22:23], s[0:1], v[72:73] op_sel_hi:[1,0,1]
	v_pk_fma_f32 v[68:69], v[24:25], s[0:1], v[74:75] op_sel_hi:[1,0,1]
	v_pk_fma_f32 v[70:71], v[26:27], s[0:1], v[76:77] op_sel_hi:[1,0,1]
	v_pk_fma_f32 v[72:73], v[28:29], s[0:1], v[78:79] op_sel_hi:[1,0,1]
	v_pk_fma_f32 v[74:75], v[30:31], s[0:1], v[80:81] op_sel_hi:[1,0,1]
	v_readlane_b32 s0, v131, 62
	s_waitcnt vmcnt(2)
	v_cvt_scalef32_pk32_f32_fp6 v[0:31], v[38:43], 1.0
	v_pk_fma_f32 v[38:39], v[0:1], s[0:1], v[44:45] op_sel_hi:[1,0,1]
	v_pk_fma_f32 v[40:41], v[2:3], s[0:1], v[46:47] op_sel_hi:[1,0,1]
	v_pk_fma_f32 v[42:43], v[4:5], s[0:1], v[48:49] op_sel_hi:[1,0,1]
	v_pk_fma_f32 v[44:45], v[6:7], s[0:1], v[50:51] op_sel_hi:[1,0,1]
	v_pk_fma_f32 v[46:47], v[8:9], s[0:1], v[52:53] op_sel_hi:[1,0,1]
	v_pk_fma_f32 v[48:49], v[10:11], s[0:1], v[54:55] op_sel_hi:[1,0,1]
	v_pk_fma_f32 v[50:51], v[12:13], s[0:1], v[56:57] op_sel_hi:[1,0,1]
	v_pk_fma_f32 v[52:53], v[14:15], s[0:1], v[58:59] op_sel_hi:[1,0,1]
	v_pk_fma_f32 v[54:55], v[16:17], s[0:1], v[60:61] op_sel_hi:[1,0,1]
	v_pk_fma_f32 v[56:57], v[18:19], s[0:1], v[62:63] op_sel_hi:[1,0,1]
	v_pk_fma_f32 v[58:59], v[20:21], s[0:1], v[64:65] op_sel_hi:[1,0,1]
	v_pk_fma_f32 v[62:63], v[22:23], s[0:1], v[66:67] op_sel_hi:[1,0,1]
	v_pk_fma_f32 v[64:65], v[24:25], s[0:1], v[68:69] op_sel_hi:[1,0,1]
	v_pk_fma_f32 v[66:67], v[26:27], s[0:1], v[70:71] op_sel_hi:[1,0,1]
	v_pk_fma_f32 v[68:69], v[28:29], s[0:1], v[72:73] op_sel_hi:[1,0,1]
	v_pk_fma_f32 v[70:71], v[30:31], s[0:1], v[74:75] op_sel_hi:[1,0,1]
	v_readlane_b32 s0, v131, 63
	s_waitcnt vmcnt(0)
	v_cvt_scalef32_pk32_f32_fp6 v[0:31], v[32:37], 1.0
	v_pk_fma_f32 v[34:35], v[0:1], s[0:1], v[38:39] op_sel_hi:[1,0,1]
	v_pk_fma_f32 v[32:33], v[2:3], s[0:1], v[40:41] op_sel_hi:[1,0,1]
	v_pk_fma_f32 v[38:39], v[4:5], s[0:1], v[42:43] op_sel_hi:[1,0,1]
	v_pk_fma_f32 v[36:37], v[6:7], s[0:1], v[44:45] op_sel_hi:[1,0,1]
	v_pk_fma_f32 v[42:43], v[8:9], s[0:1], v[46:47] op_sel_hi:[1,0,1]
	v_pk_fma_f32 v[40:41], v[10:11], s[0:1], v[48:49] op_sel_hi:[1,0,1]
	v_pk_fma_f32 v[48:49], v[12:13], s[0:1], v[50:51] op_sel_hi:[1,0,1]
	v_pk_fma_f32 v[46:47], v[14:15], s[0:1], v[52:53] op_sel_hi:[1,0,1]
	v_pk_fma_f32 v[50:51], v[18:19], s[0:1], v[56:57] op_sel_hi:[1,0,1]
	v_pk_fma_f32 v[54:55], v[16:17], s[0:1], v[54:55] op_sel_hi:[1,0,1]
	v_pk_fma_f32 v[60:61], v[20:21], s[0:1], v[58:59] op_sel_hi:[1,0,1]
	v_pk_fma_f32 v[56:57], v[22:23], s[0:1], v[62:63] op_sel_hi:[1,0,1]
	v_pk_fma_f32 v[44:45], v[24:25], s[0:1], v[64:65] op_sel_hi:[1,0,1]
	v_pk_fma_f32 v[64:65], v[26:27], s[0:1], v[66:67] op_sel_hi:[1,0,1]
	v_pk_fma_f32 v[18:19], v[28:29], s[0:1], v[68:69] op_sel_hi:[1,0,1]
	v_pk_fma_f32 v[24:25], v[30:31], s[0:1], v[70:71] op_sel_hi:[1,0,1]
	s_lshr_b32 s0, s58, 12
	s_ashr_i32 s59, s58, 31
	s_mul_i32 s4, s0, 0x3000
	s_lshl_b64 s[0:1], s[58:59], 12
	s_add_u32 s2, s71, s0
	v_lshlrev_b32_e32 v12, 2, v148
	s_addc_u32 s3, s74, s1
	v_ashrrev_i32_e32 v13, 31, v12
	v_lshlrev_b32_e32 v63, 3, v148
	v_lshl_add_u64 v[14:15], v[12:13], 1, s[2:3]
	v_add3_u32 v62, v201, s4, v63
	global_load_dwordx2 v[16:17], v[14:15], off
	ds_read2st64_b64 v[0:3], v62 offset1:1
	global_load_dwordx2 v[20:21], v[14:15], off offset:512
	global_load_dwordx2 v[22:23], v[14:15], off offset:1024
	ds_read2st64_b64 v[4:7], v62 offset0:2 offset1:3
	global_load_dwordx2 v[52:53], v[14:15], off offset:1536
	global_load_dwordx2 v[58:59], v[14:15], off offset:2048
	ds_read2st64_b64 v[8:11], v62 offset0:4 offset1:5
	global_load_dwordx2 v[66:67], v[14:15], off offset:2560
	global_load_dwordx2 v[68:69], v[14:15], off offset:3072
	global_load_dwordx2 v[26:27], v[14:15], off offset:3584
	ds_read2st64_b64 v[28:31], v62 offset0:6 offset1:7
	s_lshl_b64 s[2:3], s[58:59], 13
	s_add_u32 s4, s16, s2
	s_addc_u32 s5, s17, s3
	s_and_b64 vcc, exec, s[54:55]
	s_waitcnt lgkmcnt(0)
	v_lshlrev_b32_e32 v72, 16, v30
	v_and_b32_e32 v73, 0xffff0000, v30
	v_lshlrev_b32_e32 v30, 16, v31
	v_and_b32_e32 v31, 0xffff0000, v31
	v_pk_mul_f32 v[24:25], v[24:25], v[30:31]
	v_lshlrev_b32_e32 v30, 16, v28
	v_and_b32_e32 v31, 0xffff0000, v28
	v_pk_mul_f32 v[30:31], v[44:45], v[30:31]
	v_lshlrev_b32_e32 v28, 16, v29
	v_and_b32_e32 v29, 0xffff0000, v29
	v_pk_mul_f32 v[28:29], v[64:65], v[28:29]
	v_pk_mul_f32 v[18:19], v[18:19], v[72:73]
	s_waitcnt vmcnt(0)
	v_lshlrev_b32_e32 v70, 16, v26
	v_and_b32_e32 v71, 0xffff0000, v26
	v_lshlrev_b32_e32 v26, 16, v27
	v_and_b32_e32 v27, 0xffff0000, v27
	v_pk_fma_f32 v[24:25], v[26:27], s[38:39], v[24:25] op_sel_hi:[1,0,1]
	v_lshlrev_b32_e32 v26, 16, v68
	v_and_b32_e32 v27, 0xffff0000, v68
	v_pk_fma_f32 v[26:27], v[26:27], s[38:39], v[30:31] op_sel_hi:[1,0,1]
	v_lshlrev_b32_e32 v30, 16, v69
	v_and_b32_e32 v31, 0xffff0000, v69
	v_pk_fma_f32 v[44:45], v[30:31], s[38:39], v[28:29] op_sel_hi:[1,0,1]
	v_lshlrev_b32_e32 v30, 16, v10
	v_and_b32_e32 v31, 0xffff0000, v10
	v_lshlrev_b32_e32 v28, 16, v66
	v_and_b32_e32 v29, 0xffff0000, v66
	v_pk_mul_f32 v[30:31], v[60:61], v[30:31]
	v_lshlrev_b32_e32 v10, 16, v11
	v_and_b32_e32 v11, 0xffff0000, v11
	v_pk_fma_f32 v[28:29], v[28:29], s[38:39], v[30:31] op_sel_hi:[1,0,1]
	v_lshlrev_b32_e32 v30, 16, v67
	v_and_b32_e32 v31, 0xffff0000, v67
	v_pk_mul_f32 v[10:11], v[56:57], v[10:11]
	v_lshlrev_b32_e32 v56, 16, v8
	v_and_b32_e32 v57, 0xffff0000, v8
	v_pk_fma_f32 v[10:11], v[30:31], s[38:39], v[10:11] op_sel_hi:[1,0,1]
	v_lshlrev_b32_e32 v30, 16, v58
	v_and_b32_e32 v31, 0xffff0000, v58
	v_pk_mul_f32 v[54:55], v[54:55], v[56:57]
	v_lshlrev_b32_e32 v8, 16, v9
	v_and_b32_e32 v9, 0xffff0000, v9
	v_pk_fma_f32 v[30:31], v[30:31], s[38:39], v[54:55] op_sel_hi:[1,0,1]
	v_lshlrev_b32_e32 v54, 16, v59
	v_and_b32_e32 v55, 0xffff0000, v59
	v_pk_mul_f32 v[8:9], v[50:51], v[8:9]
	v_lshlrev_b32_e32 v50, 16, v52
	v_pk_fma_f32 v[8:9], v[54:55], s[38:39], v[8:9] op_sel_hi:[1,0,1]
	v_lshlrev_b32_e32 v54, 16, v6
	v_and_b32_e32 v55, 0xffff0000, v6
	v_and_b32_e32 v51, 0xffff0000, v52
	v_pk_mul_f32 v[48:49], v[48:49], v[54:55]
	v_lshlrev_b32_e32 v6, 16, v7
	v_and_b32_e32 v7, 0xffff0000, v7
	v_pk_fma_f32 v[48:49], v[50:51], s[38:39], v[48:49] op_sel_hi:[1,0,1]
	v_lshlrev_b32_e32 v50, 16, v53
	v_and_b32_e32 v51, 0xffff0000, v53
	v_pk_mul_f32 v[6:7], v[46:47], v[6:7]
	v_lshlrev_b32_e32 v46, 16, v22
	v_pk_fma_f32 v[6:7], v[50:51], s[38:39], v[6:7] op_sel_hi:[1,0,1]
	v_lshlrev_b32_e32 v50, 16, v4
	v_and_b32_e32 v51, 0xffff0000, v4
	v_lshlrev_b32_e32 v4, 16, v5
	v_and_b32_e32 v5, 0xffff0000, v5
	v_and_b32_e32 v47, 0xffff0000, v22
	v_lshlrev_b32_e32 v22, 16, v23
	v_and_b32_e32 v23, 0xffff0000, v23
	v_pk_mul_f32 v[4:5], v[40:41], v[4:5]
	v_lshlrev_b32_e32 v40, 16, v2
	v_and_b32_e32 v41, 0xffff0000, v2
	v_pk_fma_f32 v[4:5], v[22:23], s[38:39], v[4:5] op_sel_hi:[1,0,1]
	v_lshlrev_b32_e32 v22, 16, v20
	v_and_b32_e32 v23, 0xffff0000, v20
	v_pk_mul_f32 v[38:39], v[38:39], v[40:41]
	v_lshlrev_b32_e32 v40, 16, v0
	v_and_b32_e32 v41, 0xffff0000, v0
	v_pk_fma_f32 v[22:23], v[22:23], s[38:39], v[38:39] op_sel_hi:[1,0,1]
	v_lshlrev_b32_e32 v38, 16, v16
	v_and_b32_e32 v39, 0xffff0000, v16
	v_pk_mul_f32 v[34:35], v[34:35], v[40:41]
	v_lshlrev_b32_e32 v16, 16, v17
	v_pk_fma_f32 v[34:35], v[38:39], s[38:39], v[34:35] op_sel_hi:[1,0,1]
	v_and_b32_e32 v17, 0xffff0000, v17
	v_add_f32_e32 v0, 0, v34
	v_add_f32_e32 v38, v35, v0
	v_lshlrev_b32_e32 v0, 16, v1
	v_and_b32_e32 v1, 0xffff0000, v1
	v_pk_mul_f32 v[0:1], v[32:33], v[0:1]
	v_lshlrev_b32_e32 v2, 16, v3
	v_pk_fma_f32 v[0:1], v[16:17], s[38:39], v[0:1] op_sel_hi:[1,0,1]
	v_and_b32_e32 v3, 0xffff0000, v3
	v_add_f32_e32 v16, v0, v38
	v_add_f32_e32 v16, v1, v16
	v_lshlrev_b32_e32 v20, 16, v21
	v_and_b32_e32 v21, 0xffff0000, v21
	v_pk_mul_f32 v[2:3], v[36:37], v[2:3]
	v_add_f32_e32 v16, v22, v16
	v_pk_fma_f32 v[2:3], v[20:21], s[38:39], v[2:3] op_sel_hi:[1,0,1]
	v_add_f32_e32 v16, v23, v16
	v_pk_mul_f32 v[42:43], v[42:43], v[50:51]
	v_add_f32_e32 v16, v2, v16
	v_pk_fma_f32 v[52:53], v[46:47], s[38:39], v[42:43] op_sel_hi:[1,0,1]
	v_add_f32_e32 v16, v3, v16
	v_add_f32_e32 v16, v52, v16
	v_add_f32_e32 v16, v53, v16
	v_add_f32_e32 v16, v4, v16
	v_add_f32_e32 v16, v5, v16
	v_add_f32_e32 v16, v48, v16
	v_add_f32_e32 v16, v49, v16
	v_add_f32_e32 v16, v6, v16
	v_add_f32_e32 v16, v7, v16
	v_add_f32_e32 v16, v30, v16
	v_add_f32_e32 v16, v31, v16
	v_add_f32_e32 v16, v8, v16
	v_add_f32_e32 v16, v9, v16
	v_add_f32_e32 v16, v28, v16
	v_add_f32_e32 v16, v29, v16
	v_add_f32_e32 v16, v10, v16
	v_add_f32_e32 v16, v11, v16
	v_add_f32_e32 v16, v26, v16
	v_add_f32_e32 v16, v27, v16
	v_add_f32_e32 v16, v44, v16
	v_pk_fma_f32 v[18:19], v[70:71], s[38:39], v[18:19] op_sel_hi:[1,0,1]
	v_add_f32_e32 v16, v45, v16
	v_add_f32_e32 v16, v18, v16
	v_add_f32_e32 v16, v19, v16
	v_add_f32_e32 v16, v24, v16
	v_add_f32_e32 v16, v25, v16
	v_mov_b32_e32 v17, v105
	v_add_u32_e32 v50, v202, v63
	v_add_f32_dpp v16, v16, v16 quad_perm:[1,0,3,2] row_mask:0xf bank_mask:0xf bound_ctrl:1
	v_add_u32_e32 v51, v203, v63
	ds_read_b64 v[20:21], v50
	ds_read_b64 v[36:37], v51
	v_add_f32_dpp v16, v16, v16 quad_perm:[2,3,0,1] row_mask:0xf bank_mask:0xf bound_ctrl:1
	s_waitcnt lgkmcnt(1)
	v_lshlrev_b32_e32 v54, 16, v20
	v_add_f32_dpp v16, v16, v16 row_half_mirror row_mask:0xf bank_mask:0xf bound_ctrl:1
	s_waitcnt lgkmcnt(0)
	v_lshlrev_b32_e32 v56, 16, v36
	v_and_b32_e32 v57, 0xffff0000, v36
	v_add_f32_dpp v16, v16, v16 row_mirror row_mask:0xf bank_mask:0xf bound_ctrl:1
	v_lshlrev_b32_e32 v60, 16, v37
	v_and_b32_e32 v61, 0xffff0000, v37
	v_mov_b32_dpp v17, v16 row_bcast:15 row_mask:0xa bank_mask:0xf
	v_add_f32_e32 v16, v16, v17
	v_mov_b32_e32 v17, v105
	v_and_b32_e32 v55, 0xffff0000, v20
	v_lshlrev_b32_e32 v58, 16, v21
	v_mov_b32_dpp v17, v16 row_bcast:31 row_mask:0xc bank_mask:0xf
	v_add_f32_e32 v16, v16, v17
	v_and_b32_e32 v59, 0xffff0000, v21
	v_readlane_b32 s2, v16, 63
	s_nop 1
	v_mul_f32_e32 v64, s2, v187
	v_pk_add_f32 v[66:67], v[34:35], v[64:65] op_sel_hi:[1,0] neg_lo:[0,1] neg_hi:[0,1]
	v_pk_add_f32 v[70:71], v[0:1], v[64:65] op_sel_hi:[1,0] neg_lo:[0,1] neg_hi:[0,1]
	v_pk_mul_f32 v[68:69], v[66:67], v[66:67]
	v_pk_mul_f32 v[0:1], v[70:71], v[70:71]
	v_add_f32_e32 v63, v68, v69
	v_pk_add_f32 v[46:47], v[22:23], v[64:65] op_sel_hi:[1,0] neg_lo:[0,1] neg_hi:[0,1]
	v_add_f32_e32 v0, v0, v63
	v_pk_mul_f32 v[72:73], v[46:47], v[46:47]
	v_add_f32_e32 v0, v1, v0
	v_pk_add_f32 v[42:43], v[2:3], v[64:65] op_sel_hi:[1,0] neg_lo:[0,1] neg_hi:[0,1]
	v_add_f32_e32 v0, v72, v0
	v_pk_mul_f32 v[2:3], v[42:43], v[42:43]
	v_add_f32_e32 v0, v73, v0
	v_pk_add_f32 v[40:41], v[52:53], v[64:65] op_sel_hi:[1,0] neg_lo:[0,1] neg_hi:[0,1]
	v_add_f32_e32 v0, v2, v0
	v_pk_mul_f32 v[52:53], v[40:41], v[40:41]
	v_add_f32_e32 v0, v3, v0
	v_pk_add_f32 v[22:23], v[4:5], v[64:65] op_sel_hi:[1,0] neg_lo:[0,1] neg_hi:[0,1]
	v_add_f32_e32 v0, v52, v0
	v_pk_mul_f32 v[4:5], v[22:23], v[22:23]
	v_add_f32_e32 v0, v53, v0
	v_pk_add_f32 v[38:39], v[48:49], v[64:65] op_sel_hi:[1,0] neg_lo:[0,1] neg_hi:[0,1]
	v_add_f32_e32 v0, v4, v0
	v_pk_mul_f32 v[48:49], v[38:39], v[38:39]
	v_add_f32_e32 v0, v5, v0
	v_pk_add_f32 v[36:37], v[6:7], v[64:65] op_sel_hi:[1,0] neg_lo:[0,1] neg_hi:[0,1]
	v_add_f32_e32 v0, v48, v0
	v_pk_mul_f32 v[74:75], v[36:37], v[36:37]
	v_add_f32_e32 v0, v49, v0
	v_pk_add_f32 v[34:35], v[30:31], v[64:65] op_sel_hi:[1,0] neg_lo:[0,1] neg_hi:[0,1]
	v_add_f32_e32 v0, v74, v0
	v_pk_mul_f32 v[76:77], v[34:35], v[34:35]
	v_add_f32_e32 v0, v75, v0
	v_pk_add_f32 v[32:33], v[8:9], v[64:65] op_sel_hi:[1,0] neg_lo:[0,1] neg_hi:[0,1]
	v_add_f32_e32 v0, v76, v0
	v_pk_mul_f32 v[78:79], v[32:33], v[32:33]
	v_add_f32_e32 v0, v77, v0
	v_pk_add_f32 v[30:31], v[28:29], v[64:65] op_sel_hi:[1,0] neg_lo:[0,1] neg_hi:[0,1]
	v_add_f32_e32 v0, v78, v0
	v_pk_mul_f32 v[80:81], v[30:31], v[30:31]
	v_add_f32_e32 v0, v79, v0
	v_pk_add_f32 v[28:29], v[10:11], v[64:65] op_sel_hi:[1,0] neg_lo:[0,1] neg_hi:[0,1]
	v_add_f32_e32 v0, v80, v0
	v_pk_mul_f32 v[10:11], v[28:29], v[28:29]
	v_add_f32_e32 v0, v81, v0
	v_pk_add_f32 v[20:21], v[26:27], v[64:65] op_sel_hi:[1,0] neg_lo:[0,1] neg_hi:[0,1]
	v_add_f32_e32 v0, v10, v0
	v_pk_mul_f32 v[26:27], v[20:21], v[20:21]
	v_add_f32_e32 v0, v11, v0
	v_pk_add_f32 v[16:17], v[44:45], v[64:65] op_sel_hi:[1,0] neg_lo:[0,1] neg_hi:[0,1]
	v_add_f32_e32 v0, v26, v0
	v_pk_mul_f32 v[44:45], v[16:17], v[16:17]
	v_add_f32_e32 v0, v27, v0
	v_pk_add_f32 v[8:9], v[18:19], v[64:65] op_sel_hi:[1,0] neg_lo:[0,1] neg_hi:[0,1]
	v_add_f32_e32 v0, v44, v0
	v_pk_mul_f32 v[18:19], v[8:9], v[8:9]
	v_add_f32_e32 v0, v45, v0
	v_pk_add_f32 v[6:7], v[24:25], v[64:65] op_sel_hi:[1,0] neg_lo:[0,1] neg_hi:[0,1]
	v_add_f32_e32 v0, v18, v0
	v_pk_mul_f32 v[24:25], v[6:7], v[6:7]
	v_add_f32_e32 v0, v19, v0
	v_add_f32_e32 v0, v24, v0
	v_add_f32_e32 v0, v25, v0
	v_mov_b32_e32 v1, v105
	s_nop 0
	v_add_f32_dpp v0, v0, v0 quad_perm:[1,0,3,2] row_mask:0xf bank_mask:0xf bound_ctrl:1
	s_nop 1
	v_add_f32_dpp v0, v0, v0 quad_perm:[2,3,0,1] row_mask:0xf bank_mask:0xf bound_ctrl:1
	s_nop 1
	v_add_f32_dpp v0, v0, v0 row_half_mirror row_mask:0xf bank_mask:0xf bound_ctrl:1
	s_nop 1
	v_add_f32_dpp v0, v0, v0 row_mirror row_mask:0xf bank_mask:0xf bound_ctrl:1
	s_nop 1
	v_mov_b32_dpp v1, v0 row_bcast:15 row_mask:0xa bank_mask:0xf
	v_add_f32_e32 v0, v0, v1
	v_mov_b32_e32 v1, v105
	s_nop 1
	v_mov_b32_dpp v1, v0 row_bcast:31 row_mask:0xc bank_mask:0xf
	v_add_f32_e32 v0, v0, v1
	s_nop 0
	v_readlane_b32 s2, v0, 63
	s_nop 1
	v_fma_f32 v0, s2, v187, v183
	v_rsq_f32_e32 v10, v0
	s_mov_b64 s[2:3], -1
	v_pk_mul_f32 v[0:1], v[66:67], v[10:11] op_sel_hi:[1,0]
	v_pk_mul_f32 v[2:3], v[70:71], v[10:11] op_sel_hi:[1,0]
	v_pk_fma_f32 v[0:1], v[0:1], v[54:55], v[56:57]
	v_pk_fma_f32 v[2:3], v[2:3], v[58:59], v[60:61]
	s_cbranch_vccz .LBB0_1142
	ds_read2st64_b64 v[24:27], v62 offset0:8 offset1:16
	v_cvt_pk_bf16_f32 v4, v0, v1
	v_cvt_pk_bf16_f32 v5, v2, v3
	global_store_dwordx2 v[14:15], v[4:5], off
	s_mov_b64 s[2:3], 0
	s_waitcnt lgkmcnt(0)
	v_lshlrev_b32_e32 v18, 16, v26
	v_and_b32_e32 v19, 0xffff0000, v26
	v_lshlrev_b32_e32 v4, 16, v24
	v_and_b32_e32 v5, 0xffff0000, v24
	v_pk_add_f32 v[18:19], v[18:19], 1.0 op_sel_hi:[1,0]
	v_lshlrev_b32_e32 v24, 16, v27
	v_pk_fma_f32 v[4:5], v[0:1], v[18:19], v[4:5]
	v_lshlrev_b32_e32 v18, 16, v25
	v_and_b32_e32 v19, 0xffff0000, v25
	v_and_b32_e32 v25, 0xffff0000, v27
	v_pk_add_f32 v[24:25], v[24:25], 1.0 op_sel_hi:[1,0]
	v_cvt_pk_bf16_f32 v4, v4, v5
	v_pk_fma_f32 v[18:19], v[2:3], v[24:25], v[18:19]
	s_nop 0
	v_cvt_pk_bf16_f32 v5, v18, v19

.LBB0_1180:
	s_add_i32 s0, s36, 0x2000
	s_ashr_i32 s1, s0, 31
	s_lshl_b64 s[4:5], s[0:1], 9
	s_add_u32 s6, s18, s4
	v_mov_b32_e32 v80, v110
	s_addc_u32 s7, s19, s5
	s_add_u32 s4, s28, s4
	v_ashrrev_i32_e32 v81, 31, v80
	s_addc_u32 s5, s50, s5
	v_lshlrev_b64 v[0:1], 2, v[80:81]
	s_lshl_b64 s[34:35], s[0:1], 12
	v_lshl_add_u64 v[2:3], s[6:7], 0, v[0:1]
	s_add_u32 s6, s51, s34
	s_waitcnt vmcnt(1)
	v_lshlrev_b32_e32 v114, 2, v80
	s_addc_u32 s7, s70, s35
	v_ashrrev_i32_e32 v115, 31, v114
	s_waitcnt vmcnt(0)
	v_lshl_add_u64 v[112:113], v[114:115], 1, s[6:7]
	global_load_dword v116, v[2:3], off
	global_load_dword v118, v[2:3], off offset:256
	s_nop 0
	global_load_dwordx2 v[2:3], v[112:113], off offset:3584
	global_load_dwordx2 v[4:5], v[112:113], off offset:3072
	global_load_dwordx2 v[6:7], v[112:113], off offset:2560
	global_load_dwordx2 v[8:9], v[112:113], off offset:2048
	global_load_dwordx2 v[10:11], v[112:113], off offset:1536
	global_load_dwordx2 v[12:13], v[112:113], off offset:1024
	global_load_dwordx2 v[14:15], v[112:113], off offset:512
	global_load_dwordx2 v[16:17], v[112:113], off
	v_lshl_add_u64 v[0:1], s[4:5], 0, v[0:1]
	global_load_dword v83, v[0:1], off
	global_load_dword v81, v[0:1], off offset:256
	v_ashrrev_i32_e32 v70, 4, v80
	v_and_b32_e32 v78, 3, v80
	v_and_b32_e32 v71, 15, v80
	v_lshlrev_b32_e32 v152, 4, v80
	v_bfe_u32 v79, v80, 2, 2
	s_waitcnt vmcnt(9)
	v_lshlrev_b32_e32 v32, 16, v3
	v_and_b32_e32 v33, 0xffff0000, v3
	v_lshlrev_b32_e32 v34, 16, v2
	v_and_b32_e32 v35, 0xffff0000, v2
	s_waitcnt vmcnt(8)
	v_lshlrev_b32_e32 v38, 16, v4
	v_and_b32_e32 v39, 0xffff0000, v4
	s_waitcnt vmcnt(6)
	v_lshlrev_b32_e32 v50, 16, v9
	v_and_b32_e32 v51, 0xffff0000, v9
	v_lshlrev_b32_e32 v40, 16, v7
	v_and_b32_e32 v41, 0xffff0000, v7
	v_lshlrev_b32_e32 v42, 16, v6
	v_and_b32_e32 v43, 0xffff0000, v6
	s_waitcnt vmcnt(4)
	v_lshlrev_b32_e32 v58, 16, v13
	v_and_b32_e32 v59, 0xffff0000, v13
	v_lshlrev_b32_e32 v60, 16, v12
	v_and_b32_e32 v61, 0xffff0000, v12
	v_max_f32_e64 v0, |v33|, |v33|
	v_max_f32_e64 v1, |v32|, |v32|
	v_max_f32_e64 v2, |v35|, |v35|
	v_max_f32_e64 v3, |v34|, |v34|
	v_max_f32_e64 v6, |v39|, |v39|
	v_max_f32_e64 v7, |v38|, |v38|
	v_max_f32_e64 v12, |v51|, |v51|
	v_max_f32_e64 v13, |v50|, |v50|
	s_waitcnt vmcnt(3)
	v_lshlrev_b32_e32 v62, 16, v15
	v_and_b32_e32 v63, 0xffff0000, v15
	v_max_f32_e32 v0, v1, v0
	v_max_f32_e32 v1, v3, v2
	v_max_f32_e32 v3, v7, v6
	v_max_f32_e32 v6, v13, v12
	v_max_f32_e64 v12, |v63|, |v63|
	v_max_f32_e64 v13, |v62|, |v62|
	v_lshlrev_b32_e32 v64, 16, v14
	v_and_b32_e32 v65, 0xffff0000, v14
	v_max_f32_e32 v12, v13, v12
	v_max_f32_e64 v13, |v65|, |v65|
	v_max_f32_e64 v14, |v64|, |v64|
	s_waitcnt vmcnt(2)
	v_lshlrev_b32_e32 v66, 16, v17
	v_and_b32_e32 v67, 0xffff0000, v17
	v_max_f32_e32 v13, v14, v13
	v_max_f32_e64 v14, |v67|, |v67|
	v_max_f32_e64 v15, |v66|, |v66|
	v_lshlrev_b32_e32 v68, 16, v16
	v_and_b32_e32 v69, 0xffff0000, v16
	v_max_f32_e32 v14, v15, v14
	v_max_f32_e64 v15, |v69|, |v69|
	v_max_f32_e64 v16, |v68|, |v68|
	v_lshlrev_b32_e32 v36, 16, v5
	v_and_b32_e32 v37, 0xffff0000, v5
	v_max_f32_e32 v15, v16, v15
	v_lshlrev_b32_e32 v54, 16, v11
	v_and_b32_e32 v55, 0xffff0000, v11
	v_lshlrev_b32_e32 v56, 16, v10
	v_and_b32_e32 v57, 0xffff0000, v10
	v_max_f32_e64 v4, |v37|, |v37|
	v_max_f32_e64 v5, |v36|, |v36|
	v_max_f32_e64 v10, |v43|, |v43|
	v_max_f32_e64 v11, |v42|, |v42|
	v_max_f32_e64 v24, |v59|, |v59|
	v_max_f32_e64 v25, |v58|, |v58|
	v_max_f32_e64 v26, |v61|, |v61|
	v_max_f32_e64 v27, |v60|, |v60|
	v_max3_f32 v14, v15, 0, v14
	v_lshlrev_b32_e32 v52, 16, v8
	v_and_b32_e32 v53, 0xffff0000, v8
	v_max_f32_e64 v8, |v41|, |v41|
	v_max_f32_e64 v9, |v40|, |v40|
	v_max_f32_e64 v20, |v55|, |v55|
	v_max_f32_e64 v21, |v54|, |v54|
	v_max_f32_e64 v22, |v57|, |v57|
	v_max_f32_e64 v23, |v56|, |v56|
	v_max_f32_e32 v2, v5, v4
	v_max_f32_e32 v5, v11, v10
	v_max_f32_e32 v10, v25, v24
	v_max_f32_e32 v11, v27, v26
	v_max3_f32 v12, v14, v13, v12
	v_max_f32_e64 v18, |v53|, |v53|
	v_max_f32_e64 v19, |v52|, |v52|
	v_max_f32_e32 v4, v9, v8
	v_max_f32_e32 v8, v21, v20
	v_max_f32_e32 v9, v23, v22
	v_max3_f32 v10, v12, v11, v10
	v_max_f32_e32 v7, v19, v18
	v_max3_f32 v8, v10, v9, v8
	v_max3_f32 v6, v8, v7, v6
	v_max3_f32 v4, v6, v5, v4
	v_max3_f32 v2, v4, v3, v2
	v_max3_f32 v0, v2, v1, v0
	v_ashrrev_i32_e32 v117, 31, v116
	v_ashrrev_i32_e32 v119, 31, v118
	v_mov_b32_dpp v1, v0 quad_perm:[1,0,3,2] row_mask:0xf bank_mask:0xf bound_ctrl:1
	v_max_f32_e32 v1, v1, v1
	v_max_f32_e32 v0, v0, v1
	s_nop 1
	v_mov_b32_dpp v1, v0 quad_perm:[2,3,0,1] row_mask:0xf bank_mask:0xf bound_ctrl:1
	v_max_f32_e32 v1, v1, v1
	v_max_f32_e32 v0, v0, v1
	s_nop 1
	v_mov_b32_dpp v1, v0 row_half_mirror row_mask:0xf bank_mask:0xf bound_ctrl:1
	v_max_f32_e32 v1, v1, v1
	v_max_f32_e32 v0, v0, v1
	s_nop 1
	v_mov_b32_dpp v1, v0 row_mirror row_mask:0xf bank_mask:0xf bound_ctrl:1
	v_max_f32_e32 v1, v1, v1
	v_max_f32_e32 v0, v0, v1
	s_nop 0
	v_readlane_b32 s5, v0, 32
	v_readlane_b32 s6, v0, 48
	v_readlane_b32 s1, v0, 0
	v_readlane_b32 s4, v0, 16
	v_max_f32_e64 v0, s6, s6
	v_max_f32_e64 v1, s5, s5
	v_max_f32_e32 v0, v1, v0
	v_mov_b32_e32 v1, s4
	v_max3_f32 v0, s1, v1, v0
	s_mov_b32 s1, 0x40f00000
	v_div_scale_f32 v1, s[4:5], v0, v0, s1
	v_rcp_f32_e32 v2, v1
	s_nop 0
	v_fma_f32 v3, -v1, v2, 1.0
	v_fmac_f32_e32 v2, v3, v2
	v_div_scale_f32 v3, vcc, s1, v0, s1
	v_mul_f32_e32 v4, v3, v2
	v_fma_f32 v5, -v1, v4, v3
	v_fmac_f32_e32 v4, v5, v2
	v_fma_f32 v1, -v1, v4, v3
	v_div_fmas_f32 v1, v1, v2, v4
	v_div_fixup_f32 v1, v1, v0, s1
	v_cmp_lt_f32_e32 vcc, 0, v0
	s_nop 1
	v_cndmask_b32_e32 v82, 1.0, v1, vcc
	s_waitcnt vmcnt(1)
	v_pk_mul_f32 v[0:1], v[82:83], v[68:69] op_sel_hi:[0,1]
	v_pk_mul_f32 v[2:3], v[82:83], v[66:67] op_sel_hi:[0,1]
	v_cvt_pk_bf16_f32 v0, v0, v1
	v_cvt_pk_bf16_f32 v1, v2, v3
	v_pk_mul_f32 v[2:3], v[82:83], v[64:65] op_sel_hi:[0,1]
	v_pk_mul_f32 v[4:5], v[82:83], v[62:63] op_sel_hi:[0,1]
	v_cvt_pk_bf16_f32 v2, v2, v3
	v_cvt_pk_bf16_f32 v3, v4, v5
	v_pk_mul_f32 v[4:5], v[82:83], v[60:61] op_sel_hi:[0,1]
	v_pk_mul_f32 v[6:7], v[82:83], v[58:59] op_sel_hi:[0,1]
	v_cvt_pk_bf16_f32 v4, v4, v5
	v_cvt_pk_bf16_f32 v5, v6, v7
	v_pk_mul_f32 v[6:7], v[82:83], v[56:57] op_sel_hi:[0,1]
	v_pk_mul_f32 v[8:9], v[82:83], v[54:55] op_sel_hi:[0,1]
	v_cvt_pk_bf16_f32 v6, v6, v7
	v_cvt_pk_bf16_f32 v7, v8, v9
	v_pk_mul_f32 v[8:9], v[82:83], v[52:53] op_sel_hi:[0,1]
	v_pk_mul_f32 v[10:11], v[82:83], v[50:51] op_sel_hi:[0,1]
	v_cvt_pk_bf16_f32 v8, v8, v9
	v_cvt_pk_bf16_f32 v9, v10, v11
	v_pk_mul_f32 v[10:11], v[82:83], v[42:43] op_sel_hi:[0,1]
	v_pk_mul_f32 v[12:13], v[82:83], v[40:41] op_sel_hi:[0,1]
	v_cvt_pk_bf16_f32 v10, v10, v11
	v_cvt_pk_bf16_f32 v11, v12, v13
	v_pk_mul_f32 v[12:13], v[82:83], v[38:39] op_sel_hi:[0,1]
	v_pk_mul_f32 v[14:15], v[82:83], v[36:37] op_sel_hi:[0,1]
	v_cvt_pk_bf16_f32 v12, v12, v13
	v_cvt_pk_bf16_f32 v13, v14, v15
	v_pk_mul_f32 v[14:15], v[82:83], v[34:35] op_sel_hi:[0,1]
	v_pk_mul_f32 v[16:17], v[82:83], v[32:33] op_sel_hi:[0,1]
	v_cvt_pk_bf16_f32 v14, v14, v15
	v_cvt_pk_bf16_f32 v15, v16, v17
	v_cvt_scalef32_pk32_fp6_bf16 v[44:49], v[0:15], 1.0
	v_cvt_scalef32_pk32_f32_fp6 v[0:31], v[44:49], 1.0
	v_pk_fma_f32 v[0:1], v[82:83], v[68:69], v[0:1] op_sel_hi:[0,1,1] neg_lo:[0,0,1] neg_hi:[0,0,1]
	v_pk_fma_f32 v[2:3], v[82:83], v[66:67], v[2:3] op_sel_hi:[0,1,1] neg_lo:[0,0,1] neg_hi:[0,0,1]
	v_pk_mul_f32 v[0:1], v[0:1], s[48:49] op_sel_hi:[1,0]
	v_pk_mul_f32 v[2:3], v[2:3], s[48:49] op_sel_hi:[1,0]
	v_cvt_pk_bf16_f32 v0, v0, v1
	v_cvt_pk_bf16_f32 v1, v2, v3
	v_pk_fma_f32 v[2:3], v[82:83], v[64:65], v[4:5] op_sel_hi:[0,1,1] neg_lo:[0,0,1] neg_hi:[0,0,1]
	v_pk_fma_f32 v[4:5], v[82:83], v[62:63], v[6:7] op_sel_hi:[0,1,1] neg_lo:[0,0,1] neg_hi:[0,0,1]
	v_pk_mul_f32 v[2:3], v[2:3], s[48:49] op_sel_hi:[1,0]
	v_pk_mul_f32 v[4:5], v[4:5], s[48:49] op_sel_hi:[1,0]
	v_cvt_pk_bf16_f32 v2, v2, v3
	v_cvt_pk_bf16_f32 v3, v4, v5
	v_pk_fma_f32 v[4:5], v[82:83], v[60:61], v[8:9] op_sel_hi:[0,1,1] neg_lo:[0,0,1] neg_hi:[0,0,1]
	v_pk_fma_f32 v[6:7], v[82:83], v[58:59], v[10:11] op_sel_hi:[0,1,1] neg_lo:[0,0,1] neg_hi:[0,0,1]
	v_pk_mul_f32 v[4:5], v[4:5], s[48:49] op_sel_hi:[1,0]
	v_pk_mul_f32 v[6:7], v[6:7], s[48:49] op_sel_hi:[1,0]
	v_cvt_pk_bf16_f32 v4, v4, v5
	v_cvt_pk_bf16_f32 v5, v6, v7
	v_pk_fma_f32 v[6:7], v[82:83], v[56:57], v[12:13] op_sel_hi:[0,1,1] neg_lo:[0,0,1] neg_hi:[0,0,1]
	v_pk_fma_f32 v[8:9], v[82:83], v[54:55], v[14:15] op_sel_hi:[0,1,1] neg_lo:[0,0,1] neg_hi:[0,0,1]
	v_pk_mul_f32 v[6:7], v[6:7], s[48:49] op_sel_hi:[1,0]
	v_pk_mul_f32 v[8:9], v[8:9], s[48:49] op_sel_hi:[1,0]
	v_cvt_pk_bf16_f32 v6, v6, v7
	v_cvt_pk_bf16_f32 v7, v8, v9
	v_pk_fma_f32 v[8:9], v[82:83], v[52:53], v[16:17] op_sel_hi:[0,1,1] neg_lo:[0,0,1] neg_hi:[0,0,1]
	v_pk_fma_f32 v[10:11], v[82:83], v[50:51], v[18:19] op_sel_hi:[0,1,1] neg_lo:[0,0,1] neg_hi:[0,0,1]
	v_pk_mul_f32 v[8:9], v[8:9], s[48:49] op_sel_hi:[1,0]
	v_pk_mul_f32 v[10:11], v[10:11], s[48:49] op_sel_hi:[1,0]
	v_cvt_pk_bf16_f32 v8, v8, v9
	v_cvt_pk_bf16_f32 v9, v10, v11
	v_pk_fma_f32 v[10:11], v[82:83], v[42:43], v[20:21] op_sel_hi:[0,1,1] neg_lo:[0,0,1] neg_hi:[0,0,1]
	v_pk_fma_f32 v[12:13], v[82:83], v[40:41], v[22:23] op_sel_hi:[0,1,1] neg_lo:[0,0,1] neg_hi:[0,0,1]
	v_pk_mul_f32 v[10:11], v[10:11], s[48:49] op_sel_hi:[1,0]
	v_pk_mul_f32 v[12:13], v[12:13], s[48:49] op_sel_hi:[1,0]
	v_cvt_pk_bf16_f32 v10, v10, v11
	v_cvt_pk_bf16_f32 v11, v12, v13
	v_pk_fma_f32 v[12:13], v[82:83], v[38:39], v[24:25] op_sel_hi:[0,1,1] neg_lo:[0,0,1] neg_hi:[0,0,1]
	v_pk_fma_f32 v[14:15], v[82:83], v[36:37], v[26:27] op_sel_hi:[0,1,1] neg_lo:[0,0,1] neg_hi:[0,0,1]
	v_pk_mul_f32 v[12:13], v[12:13], s[48:49] op_sel_hi:[1,0]
	v_pk_mul_f32 v[14:15], v[14:15], s[48:49] op_sel_hi:[1,0]
	v_cvt_pk_bf16_f32 v12, v12, v13
	v_cvt_pk_bf16_f32 v13, v14, v15
	v_pk_fma_f32 v[14:15], v[82:83], v[34:35], v[28:29] op_sel_hi:[0,1,1] neg_lo:[0,0,1] neg_hi:[0,0,1]
	v_pk_fma_f32 v[16:17], v[82:83], v[32:33], v[30:31] op_sel_hi:[0,1,1] neg_lo:[0,0,1] neg_hi:[0,0,1]
	v_pk_mul_f32 v[14:15], v[14:15], s[48:49] op_sel_hi:[1,0]
	v_pk_mul_f32 v[16:17], v[16:17], s[48:49] op_sel_hi:[1,0]
	v_cvt_pk_bf16_f32 v14, v14, v15
	v_cvt_pk_bf16_f32 v15, v16, v17
	v_cvt_scalef32_pk32_fp6_bf16 v[16:21], v[0:15], 1.0
	v_mad_u64_u32 v[0:1], s[4:5], v80, 24, v[104:105]
	v_add_u32_e32 v1, 0xe000, v0
	v_add_u32_e32 v2, 0xe600, v0
	v_add_u32_e32 v0, 16, v0
	ds_write2_b64 v1, v[44:45], v[46:47] offset1:1
	ds_write2_b64 v2, v[16:17], v[18:19] offset1:1
	ds_write2st64_b64 v0, v[48:49], v[20:21] offset0:112 offset1:115
	v_bfe_i32 v0, v80, 2, 1
	v_lshl_or_b32 v1, v70, 2, v78
	v_and_b32_e32 v0, 0x600, v0
	v_mul_lo_u32 v1, v1, 24
	v_add3_u32 v0, v104, v0, v1
	v_add_u32_e32 v1, 0xe000, v0
	v_add_u32_e32 v2, 0xe180, v0
	ds_read2_b64 v[154:157], v1 offset0:2 offset1:50
	ds_read2_b64 v[18:21], v1 offset1:1
	ds_read2_b64 v[12:15], v2 offset1:1
	v_add_u32_e32 v2, 0xe300, v0
	v_add_u32_e32 v0, 0xe480, v0
	ds_read2_b64 v[158:161], v1 offset0:98 offset1:146
	ds_read2_b64 v[6:9], v2 offset1:1
	ds_read2_b64 v[0:3], v0 offset1:1
	v_lshlrev_b32_e32 v4, 4, v78
	v_lshl_or_b32 v102, v70, 6, v4
	v_lshlrev_b32_e32 v4, 5, v70
	v_lshl_or_b32 v5, v78, 3, v4
	v_cmp_gt_u32_e32 vcc, 8, v71
	v_add_u32_e32 v103, 0x400, v5
	v_cmp_eq_u32_e64 s[4:5], 0, v71
	v_cndmask_b32_e32 v5, 0, v252, vcc
	v_cmp_lt_u32_e32 vcc, 3, v71
	s_nop 1
	v_cndmask_b32_e32 v29, 1.0, v5, vcc
	v_add_u32_e32 v5, 0x80, v80
	v_cmp_eq_u32_e32 vcc, 2, v78
	v_cndmask_b32_e64 v22, v5, v4, s[4:5]
	s_waitcnt vmcnt(0) lgkmcnt(0)
	v_lshlrev_b64 v[4:5], 2, v[116:117]
	v_lshl_add_u64 v[10:11], s[12:13], 0, v[4:5]
	v_lshl_add_u64 v[4:5], s[14:15], 0, v[4:5]
	global_load_dword v26, v[10:11], off
	global_load_dword v27, v[4:5], off
	v_lshlrev_b64 v[10:11], 2, v[118:119]
	v_lshl_add_u64 v[16:17], s[12:13], 0, v[10:11]
	v_lshl_add_u64 v[4:5], s[14:15], 0, v[10:11]
	global_load_dword v25, v[16:17], off
	global_load_dword v24, v[4:5], off
	v_or_b32_e32 v4, s53, v79
	v_lshlrev_b32_e32 v4, 2, v4
	v_cndmask_b32_e64 v28, v118, v116, s[2:3]
	ds_bpermute_b32 v4, v4, v28
	v_cmp_eq_u32_e64 s[4:5], 1, v78
	s_waitcnt lgkmcnt(0)
	v_mul_lo_u32 v4, v4, s43
	v_add_u32_e32 v5, v4, v102
	v_add_u32_e32 v4, v4, v103
	buffer_load_dwordx4 v[30:33], v5, s[44:47], 0 offen sc1
	buffer_load_dwordx4 v[36:39], v5, s[44:47], s20 offen sc1
	buffer_load_dwordx4 v[42:45], v5, s[44:47], s21 offen sc1
	buffer_load_dwordx4 v[48:51], v5, s[44:47], s23 offen sc1
	buffer_load_dwordx2 v[34:35], v4, s[44:47], 0 offen sc1
	buffer_load_dwordx2 v[46:47], v4, s[44:47], s33 offen sc1
	buffer_load_dwordx2 v[40:41], v4, s[44:47], s21 offen sc1
	buffer_load_dwordx2 v[52:53], v4, s[44:47], s94 offen sc1
	v_or_b32_e32 v4, s57, v79
	v_lshlrev_b32_e32 v4, 2, v4
	ds_bpermute_b32 v4, v4, v28
	v_cmp_eq_u32_e64 s[6:7], 3, v78
	s_waitcnt lgkmcnt(0)
	v_mul_lo_u32 v4, v4, s43
	v_add_u32_e32 v5, v4, v102
	v_add_u32_e32 v4, v4, v103
	buffer_load_dwordx4 v[54:57], v5, s[44:47], 0 offen sc1
	buffer_load_dwordx4 v[60:63], v5, s[44:47], s20 offen sc1
	buffer_load_dwordx4 v[66:69], v5, s[44:47], s21 offen sc1
	buffer_load_dwordx4 v[72:75], v5, s[44:47], s23 offen sc1
	buffer_load_dwordx2 v[58:59], v4, s[44:47], 0 offen sc1
	buffer_load_dwordx2 v[70:71], v4, s[44:47], s33 offen sc1
	buffer_load_dwordx2 v[64:65], v4, s[44:47], s21 offen sc1
	buffer_load_dwordx2 v[76:77], v4, s[44:47], s94 offen sc1
	v_or_b32_e32 v4, s58, v79
	v_lshlrev_b32_e32 v4, 2, v4
	ds_bpermute_b32 v4, v4, v28
	s_waitcnt lgkmcnt(0)
	v_mul_lo_u32 v4, v4, s43
	v_add_u32_e32 v5, v4, v102
	v_add_u32_e32 v4, v4, v103
	buffer_load_dwordx4 v[84:87], v5, s[44:47], 0 offen sc1
	buffer_load_dwordx4 v[90:93], v5, s[44:47], s20 offen sc1
	buffer_load_dwordx4 v[96:99], v5, s[44:47], s21 offen sc1
	buffer_load_dwordx4 v[120:123], v5, s[44:47], s23 offen sc1
	buffer_load_dwordx2 v[88:89], v4, s[44:47], 0 offen sc1
	buffer_load_dwordx2 v[100:101], v4, s[44:47], s33 offen sc1
	buffer_load_dwordx2 v[94:95], v4, s[44:47], s21 offen sc1
	buffer_load_dwordx2 v[124:125], v4, s[44:47], s94 offen sc1
	v_or_b32_e32 v4, s62, v79
	v_lshlrev_b32_e32 v4, 2, v4
	ds_bpermute_b32 v4, v4, v28
	v_lshl_add_u32 v78, v22, 2, v176
	s_waitcnt lgkmcnt(0)
	v_mul_lo_u32 v4, v4, s43
	v_add_u32_e32 v5, v4, v102
	v_add_u32_e32 v4, v4, v103
	buffer_load_dwordx4 v[126:129], v5, s[44:47], 0 offen sc1
	buffer_load_dwordx4 v[132:135], v5, s[44:47], s20 offen sc1
	buffer_load_dwordx4 v[138:141], v5, s[44:47], s21 offen sc1
	buffer_load_dwordx4 v[144:147], v5, s[44:47], s23 offen sc1
	buffer_load_dwordx2 v[130:131], v4, s[44:47], 0 offen sc1
	buffer_load_dwordx2 v[142:143], v4, s[44:47], s33 offen sc1
	buffer_load_dwordx2 v[136:137], v4, s[44:47], s21 offen sc1
	buffer_load_dwordx2 v[148:149], v4, s[44:47], s94 offen sc1
	v_or_b32_e32 v4, s59, v79
	v_lshlrev_b32_e32 v117, 2, v4
	v_or_b32_e32 v4, s61, v79
	v_lshlrev_b32_e32 v119, 2, v4
	v_mov_b32_e32 v22, v154
	v_mov_b32_e32 v23, v155
	v_mov_b32_e32 v16, v156
	v_mov_b32_e32 v17, v157
	s_waitcnt vmcnt(27)
	v_mfma_f32_16x16x128_f8f6f4 v[30:33], v[30:35], v[18:23], 0 cbsz:2 blgp:2
	v_mov_b32_e32 v10, v158
	v_mov_b32_e32 v11, v159
	v_mov_b32_e32 v4, v160
	s_waitcnt vmcnt(26)
	v_mfma_f32_16x16x128_f8f6f4 v[30:33], v[42:47], v[12:17], v[30:33] cbsz:2 blgp:2
	v_mov_b32_e32 v5, v161
	s_waitcnt vmcnt(25)
	v_mfma_f32_16x16x128_f8f6f4 v[30:33], v[36:41], v[6:11], v[30:33] cbsz:2 blgp:2
	s_waitcnt vmcnt(24)
	v_mfma_f32_16x16x128_f8f6f4 v[30:33], v[48:53], v[0:5], v[30:33] cbsz:2 blgp:2
	s_nop 7
	v_cndmask_b32_e64 v30, v30, v31, s[4:5]
	v_cndmask_b32_e32 v30, v30, v32, vcc
	v_cndmask_b32_e64 v30, v30, v33, s[6:7]
	v_mul_f32_e32 v31, v29, v30
	s_nop 1
	v_mov_b32_dpp v31, v31 quad_perm:[1,0,3,2] row_mask:0xf bank_mask:0xf bound_ctrl:1
	v_fmac_f32_e32 v31, v29, v30
	s_nop 1
	v_add_f32_dpp v30, v31, v31 quad_perm:[2,3,0,1] row_mask:0xf bank_mask:0xf bound_ctrl:1
	s_nop 1
	v_add_f32_dpp v30, v30, v30 row_half_mirror row_mask:0xf bank_mask:0xf bound_ctrl:1
	ds_write_b32 v78, v30 offset:49152
	v_or_b32_e32 v30, s63, v79
	v_lshlrev_b32_e32 v30, 2, v30
	ds_bpermute_b32 v30, v30, v28
	s_waitcnt lgkmcnt(0)
	v_mul_lo_u32 v30, v30, s43
	v_add_u32_e32 v34, v30, v102
	v_add_u32_e32 v52, v30, v103
	buffer_load_dwordx4 v[30:33], v34, s[44:47], 0 offen sc1
	buffer_load_dwordx4 v[36:39], v34, s[44:47], s20 offen sc1
	buffer_load_dwordx4 v[42:45], v34, s[44:47], s21 offen sc1
	buffer_load_dwordx4 v[48:51], v34, s[44:47], s23 offen sc1
	s_nop 0
	buffer_load_dwordx2 v[34:35], v52, s[44:47], 0 offen sc1
	buffer_load_dwordx2 v[46:47], v52, s[44:47], s33 offen sc1
	buffer_load_dwordx2 v[40:41], v52, s[44:47], s21 offen sc1
	s_nop 0
	buffer_load_dwordx2 v[52:53], v52, s[44:47], s94 offen sc1
	s_waitcnt vmcnt(27)
	v_mfma_f32_16x16x128_f8f6f4 v[54:57], v[54:59], v[18:23], 0 cbsz:2 blgp:2
	s_waitcnt vmcnt(26)
	v_mfma_f32_16x16x128_f8f6f4 v[54:57], v[66:71], v[12:17], v[54:57] cbsz:2 blgp:2
	s_waitcnt vmcnt(25)
	v_mfma_f32_16x16x128_f8f6f4 v[54:57], v[60:65], v[6:11], v[54:57] cbsz:2 blgp:2
	s_waitcnt vmcnt(24)
	v_mfma_f32_16x16x128_f8f6f4 v[54:57], v[72:77], v[0:5], v[54:57] cbsz:2 blgp:2
	s_nop 7
	v_cndmask_b32_e64 v54, v54, v55, s[4:5]
	v_cndmask_b32_e32 v54, v54, v56, vcc
	v_cndmask_b32_e64 v54, v54, v57, s[6:7]
	v_mul_f32_e32 v55, v29, v54
	s_nop 1
	v_mov_b32_dpp v55, v55 quad_perm:[1,0,3,2] row_mask:0xf bank_mask:0xf bound_ctrl:1
	v_fmac_f32_e32 v55, v29, v54
	s_nop 1
	v_add_f32_dpp v54, v55, v55 quad_perm:[2,3,0,1] row_mask:0xf bank_mask:0xf bound_ctrl:1
	s_nop 1
	v_add_f32_dpp v54, v54, v54 row_half_mirror row_mask:0xf bank_mask:0xf bound_ctrl:1
	ds_write_b32 v78, v54 offset:49156
	ds_bpermute_b32 v54, v117, v28
	s_waitcnt lgkmcnt(0)
	v_mul_lo_u32 v54, v54, s43
	v_add_u32_e32 v58, v54, v102
	v_add_u32_e32 v76, v54, v103
	buffer_load_dwordx4 v[54:57], v58, s[44:47], 0 offen sc1
	buffer_load_dwordx4 v[60:63], v58, s[44:47], s20 offen sc1
	buffer_load_dwordx4 v[66:69], v58, s[44:47], s21 offen sc1
	buffer_load_dwordx4 v[72:75], v58, s[44:47], s23 offen sc1
	s_nop 0
	buffer_load_dwordx2 v[58:59], v76, s[44:47], 0 offen sc1
	buffer_load_dwordx2 v[70:71], v76, s[44:47], s33 offen sc1
	buffer_load_dwordx2 v[64:65], v76, s[44:47], s21 offen sc1
	s_nop 0
	buffer_load_dwordx2 v[76:77], v76, s[44:47], s94 offen sc1
	s_waitcnt vmcnt(27)
	v_mfma_f32_16x16x128_f8f6f4 v[84:87], v[84:89], v[18:23], 0 cbsz:2 blgp:2
	s_waitcnt vmcnt(26)
	v_mfma_f32_16x16x128_f8f6f4 v[84:87], v[96:101], v[12:17], v[84:87] cbsz:2 blgp:2
	s_waitcnt vmcnt(25)
	v_mfma_f32_16x16x128_f8f6f4 v[84:87], v[90:95], v[6:11], v[84:87] cbsz:2 blgp:2
	s_waitcnt vmcnt(24)
	v_mfma_f32_16x16x128_f8f6f4 v[84:87], v[120:125], v[0:5], v[84:87] cbsz:2 blgp:2
	s_nop 7
	v_cndmask_b32_e64 v84, v84, v85, s[4:5]
	v_cndmask_b32_e32 v84, v84, v86, vcc
	v_cndmask_b32_e64 v84, v84, v87, s[6:7]
	v_mul_f32_e32 v85, v29, v84
	s_nop 1
	v_mov_b32_dpp v85, v85 quad_perm:[1,0,3,2] row_mask:0xf bank_mask:0xf bound_ctrl:1
	v_fmac_f32_e32 v85, v29, v84
	s_nop 1
	v_add_f32_dpp v84, v85, v85 quad_perm:[2,3,0,1] row_mask:0xf bank_mask:0xf bound_ctrl:1
	s_nop 1
	v_add_f32_dpp v84, v84, v84 row_half_mirror row_mask:0xf bank_mask:0xf bound_ctrl:1
	ds_write_b32 v78, v84 offset:49160
	ds_bpermute_b32 v84, v119, v28
	s_waitcnt lgkmcnt(0)
	v_mul_lo_u32 v84, v84, s43
	v_add_u32_e32 v88, v84, v102
	v_add_u32_e32 v117, v84, v103
	buffer_load_dwordx4 v[84:87], v88, s[44:47], 0 offen sc1
	buffer_load_dwordx4 v[90:93], v88, s[44:47], s20 offen sc1
	buffer_load_dwordx4 v[96:99], v88, s[44:47], s21 offen sc1
	buffer_load_dwordx4 v[120:123], v88, s[44:47], s23 offen sc1
	s_nop 0
	buffer_load_dwordx2 v[88:89], v117, s[44:47], 0 offen sc1
	buffer_load_dwordx2 v[100:101], v117, s[44:47], s33 offen sc1
	buffer_load_dwordx2 v[94:95], v117, s[44:47], s21 offen sc1
	buffer_load_dwordx2 v[124:125], v117, s[44:47], s94 offen sc1
	s_waitcnt vmcnt(27)
	v_mfma_f32_16x16x128_f8f6f4 v[126:129], v[126:131], v[18:23], 0 cbsz:2 blgp:2
	s_waitcnt vmcnt(26)
	v_mfma_f32_16x16x128_f8f6f4 v[126:129], v[138:143], v[12:17], v[126:129] cbsz:2 blgp:2
	s_waitcnt vmcnt(25)
	v_mfma_f32_16x16x128_f8f6f4 v[126:129], v[132:137], v[6:11], v[126:129] cbsz:2 blgp:2
	s_waitcnt vmcnt(24)
	v_mfma_f32_16x16x128_f8f6f4 v[126:129], v[144:149], v[0:5], v[126:129] cbsz:2 blgp:2
	s_nop 7
	v_cndmask_b32_e64 v117, v126, v127, s[4:5]
	v_cndmask_b32_e32 v117, v117, v128, vcc
	v_cndmask_b32_e64 v117, v117, v129, s[6:7]
	v_mul_f32_e32 v119, v29, v117
	s_nop 1
	v_mov_b32_dpp v119, v119 quad_perm:[1,0,3,2] row_mask:0xf bank_mask:0xf bound_ctrl:1
	v_fmac_f32_e32 v119, v29, v117
	s_nop 1
	v_add_f32_dpp v117, v119, v119 quad_perm:[2,3,0,1] row_mask:0xf bank_mask:0xf bound_ctrl:1
	s_nop 1
	v_add_f32_dpp v117, v117, v117 row_half_mirror row_mask:0xf bank_mask:0xf bound_ctrl:1
	ds_write_b32 v78, v117 offset:49164
	v_or_b32_e32 v79, s65, v79
	v_lshlrev_b32_e32 v79, 2, v79
	ds_bpermute_b32 v79, v79, v28
	s_waitcnt lgkmcnt(0)
	v_mul_lo_u32 v79, v79, s43
	v_add_u32_e32 v102, v79, v102
	v_add_u32_e32 v79, v79, v103
	buffer_load_dwordx4 v[126:129], v102, s[44:47], 0 offen sc1
	buffer_load_dwordx4 v[132:135], v102, s[44:47], s20 offen sc1
	buffer_load_dwordx4 v[138:141], v102, s[44:47], s21 offen sc1
	buffer_load_dwordx4 v[144:147], v102, s[44:47], s23 offen sc1
	buffer_load_dwordx2 v[130:131], v79, s[44:47], 0 offen sc1
	buffer_load_dwordx2 v[142:143], v79, s[44:47], s33 offen sc1
	buffer_load_dwordx2 v[136:137], v79, s[44:47], s21 offen sc1
	buffer_load_dwordx2 v[148:149], v79, s[44:47], s94 offen sc1
	s_waitcnt vmcnt(27)
	v_mfma_f32_16x16x128_f8f6f4 v[30:33], v[30:35], v[18:23], 0 cbsz:2 blgp:2
	s_waitcnt vmcnt(26)
	v_mfma_f32_16x16x128_f8f6f4 v[30:33], v[42:47], v[12:17], v[30:33] cbsz:2 blgp:2
	s_waitcnt vmcnt(25)
	v_mfma_f32_16x16x128_f8f6f4 v[30:33], v[36:41], v[6:11], v[30:33] cbsz:2 blgp:2
	s_waitcnt vmcnt(24)
	v_mfma_f32_16x16x128_f8f6f4 v[30:33], v[48:53], v[0:5], v[30:33] cbsz:2 blgp:2
	s_nop 7
	v_cndmask_b32_e64 v30, v30, v31, s[4:5]
	v_cndmask_b32_e32 v30, v30, v32, vcc
	v_cndmask_b32_e64 v30, v30, v33, s[6:7]
	v_mul_f32_e32 v31, v29, v30
	s_nop 1
	v_mov_b32_dpp v31, v31 quad_perm:[1,0,3,2] row_mask:0xf bank_mask:0xf bound_ctrl:1
	v_fmac_f32_e32 v31, v29, v30
	s_nop 1
	v_add_f32_dpp v30, v31, v31 quad_perm:[2,3,0,1] row_mask:0xf bank_mask:0xf bound_ctrl:1
	s_nop 1
	v_add_f32_dpp v30, v30, v30 row_half_mirror row_mask:0xf bank_mask:0xf bound_ctrl:1
	ds_write_b32 v78, v30 offset:49168
	s_waitcnt vmcnt(19)
	v_mfma_f32_16x16x128_f8f6f4 v[30:33], v[54:59], v[18:23], 0 cbsz:2 blgp:2
	s_waitcnt vmcnt(18)
	v_mfma_f32_16x16x128_f8f6f4 v[30:33], v[66:71], v[12:17], v[30:33] cbsz:2 blgp:2
	s_waitcnt vmcnt(17)
	v_mfma_f32_16x16x128_f8f6f4 v[30:33], v[60:65], v[6:11], v[30:33] cbsz:2 blgp:2
	s_waitcnt vmcnt(16)
	v_mfma_f32_16x16x128_f8f6f4 v[30:33], v[72:77], v[0:5], v[30:33] cbsz:2 blgp:2
	s_nop 7
	v_cndmask_b32_e64 v30, v30, v31, s[4:5]
	v_cndmask_b32_e32 v30, v30, v32, vcc
	v_cndmask_b32_e64 v30, v30, v33, s[6:7]
	v_mul_f32_e32 v31, v29, v30
	s_nop 1
	v_mov_b32_dpp v31, v31 quad_perm:[1,0,3,2] row_mask:0xf bank_mask:0xf bound_ctrl:1
	v_fmac_f32_e32 v31, v29, v30
	s_nop 1
	v_add_f32_dpp v30, v31, v31 quad_perm:[2,3,0,1] row_mask:0xf bank_mask:0xf bound_ctrl:1
	s_nop 1
	v_add_f32_dpp v30, v30, v30 row_half_mirror row_mask:0xf bank_mask:0xf bound_ctrl:1
	ds_write_b32 v78, v30 offset:49172
	s_waitcnt vmcnt(11)
	v_mfma_f32_16x16x128_f8f6f4 v[30:33], v[84:89], v[18:23], 0 cbsz:2 blgp:2
	s_waitcnt vmcnt(10)
	v_mfma_f32_16x16x128_f8f6f4 v[30:33], v[96:101], v[12:17], v[30:33] cbsz:2 blgp:2
	s_waitcnt vmcnt(9)
	v_mfma_f32_16x16x128_f8f6f4 v[30:33], v[90:95], v[6:11], v[30:33] cbsz:2 blgp:2
	s_waitcnt vmcnt(8)
	v_mfma_f32_16x16x128_f8f6f4 v[30:33], v[120:125], v[0:5], v[30:33] cbsz:2 blgp:2
	s_nop 7
	v_cndmask_b32_e64 v30, v30, v31, s[4:5]
	v_cndmask_b32_e32 v30, v30, v32, vcc
	v_cndmask_b32_e64 v30, v30, v33, s[6:7]
	v_mul_f32_e32 v31, v29, v30
	s_nop 1
	v_mov_b32_dpp v31, v31 quad_perm:[1,0,3,2] row_mask:0xf bank_mask:0xf bound_ctrl:1
	v_fmac_f32_e32 v31, v29, v30
	s_nop 1
	v_add_f32_dpp v30, v31, v31 quad_perm:[2,3,0,1] row_mask:0xf bank_mask:0xf bound_ctrl:1
	s_nop 1
	v_add_f32_dpp v30, v30, v30 row_half_mirror row_mask:0xf bank_mask:0xf bound_ctrl:1
	ds_write_b32 v78, v30 offset:49176
	s_waitcnt vmcnt(3)
	v_mfma_f32_16x16x128_f8f6f4 v[18:21], v[126:131], v[18:23], 0 cbsz:2 blgp:2
	s_waitcnt vmcnt(2)
	v_mfma_f32_16x16x128_f8f6f4 v[12:15], v[138:143], v[12:17], v[18:21] cbsz:2 blgp:2
	s_waitcnt vmcnt(1)
	v_mfma_f32_16x16x128_f8f6f4 v[6:9], v[132:137], v[6:11], v[12:15] cbsz:2 blgp:2
	s_waitcnt vmcnt(0)
	v_mfma_f32_16x16x128_f8f6f4 v[0:3], v[144:149], v[0:5], v[6:9] cbsz:2 blgp:2
	s_nop 7
	v_cndmask_b32_e64 v0, v0, v1, s[4:5]
	v_cndmask_b32_e32 v0, v0, v2, vcc
	v_cndmask_b32_e64 v0, v0, v3, s[6:7]
	v_mul_f32_e32 v1, v29, v0
	s_nop 1
	v_mov_b32_dpp v1, v1 quad_perm:[1,0,3,2] row_mask:0xf bank_mask:0xf bound_ctrl:1
	v_fmac_f32_e32 v1, v29, v0
	s_nop 1
	v_add_f32_dpp v0, v1, v1 quad_perm:[2,3,0,1] row_mask:0xf bank_mask:0xf bound_ctrl:1
	s_nop 1
	v_add_f32_dpp v0, v0, v0 row_half_mirror row_mask:0xf bank_mask:0xf bound_ctrl:1
	ds_write_b32 v78, v0 offset:49180
	v_readlane_b32 s1, v28, s42
	s_mulk_i32 s1, 0x600
	s_add_i32 s1, s1, 0x8000000
	v_lshrrev_b32_e32 v0, 1, v152
	s_nop 1
	buffer_load_dwordx4 v[74:77], v152, s[44:47], s1 offen sc1
	buffer_load_dwordx2 v[78:79], v0, s[44:47], s1 offen offset:1024 sc1
	v_readlane_b32 s1, v28, s66
	s_mulk_i32 s1, 0x600
	s_add_i32 s1, s1, 0x8000000
	s_nop 2
	buffer_load_dwordx4 v[68:71], v152, s[44:47], s1 offen sc1
	buffer_load_dwordx2 v[72:73], v0, s[44:47], s1 offen offset:1024 sc1
	v_readlane_b32 s1, v28, s67
	s_mulk_i32 s1, 0x600
	s_add_i32 s1, s1, 0x8000000
	s_nop 2
	buffer_load_dwordx4 v[56:59], v152, s[44:47], s1 offen sc1
	buffer_load_dwordx2 v[60:61], v0, s[44:47], s1 offen offset:1024 sc1
	v_readlane_b32 s1, v28, s68
	s_mulk_i32 s1, 0x600
	s_add_i32 s1, s1, 0x8000000
	s_nop 2
	buffer_load_dwordx4 v[44:47], v152, s[44:47], s1 offen sc1
	buffer_load_dwordx2 v[48:49], v0, s[44:47], s1 offen offset:1024 sc1
	v_add_u32_e32 v117, 0x400, v0
	v_readlane_b32 s1, v28, s56
	s_mulk_i32 s1, 0x600
	s_add_i32 s1, s1, 0x8000000
	s_nop 2
	buffer_load_dwordx4 v[62:65], v152, s[44:47], s1 offen sc1
	buffer_load_dwordx2 v[66:67], v0, s[44:47], s1 offen offset:1024 sc1
	v_readlane_b32 s1, v28, s69
	s_mulk_i32 s1, 0x600
	s_add_i32 s1, s1, 0x8000000
	s_nop 2
	buffer_load_dwordx4 v[50:53], v152, s[44:47], s1 offen sc1
	buffer_load_dwordx2 v[54:55], v0, s[44:47], s1 offen offset:1024 sc1
	v_readlane_b32 s1, v28, s72
	s_mulk_i32 s1, 0x600
	s_add_i32 s1, s1, 0x8000000
	s_nop 2
	buffer_load_dwordx4 v[38:41], v152, s[44:47], s1 offen sc1
	buffer_load_dwordx2 v[42:43], v0, s[44:47], s1 offen offset:1024 sc1
	v_readlane_b32 s1, v28, s73
	s_mulk_i32 s1, 0x600
	s_add_i32 s1, s1, 0x8000000
	s_nop 2
	buffer_load_dwordx4 v[32:35], v152, s[44:47], s1 offen sc1
	buffer_load_dwordx2 v[36:37], v0, s[44:47], s1 offen offset:1024 sc1
	v_div_scale_f32 v2, s[4:5], v82, v82, 1.0
	v_rcp_f32_e32 v3, v2
	v_div_scale_f32 v4, vcc, 1.0, v82, 1.0
	v_and_b32_e32 v1, -4, v80
	v_fma_f32 v0, -v2, v3, 1.0
	v_fmac_f32_e32 v3, v0, v3
	v_mul_f32_e32 v5, v4, v3
	v_fma_f32 v0, -v2, v5, v4
	v_fmac_f32_e32 v5, v0, v3
	v_lshlrev_b32_e32 v0, 7, v80
	v_and_b32_e32 v0, 0x180, v0
	v_add3_u32 v0, v111, v0, v1
	v_add_u32_e32 v0, 0xc000, v0
	ds_read2_b32 v[0:1], v0 offset1:16
	v_fma_f32 v2, -v2, v5, v4
	v_div_fmas_f32 v2, v2, v3, v5
	v_div_fixup_f32 v2, v2, v82, 1.0
	s_mov_b32 s1, 0x3e6d3388
	s_waitcnt lgkmcnt(0)
	v_mul_f32_e32 v0, v2, v0
	v_mul_f32_e32 v0, v26, v0
	v_fma_f32 v3, |v0|, s1, 1.0
	v_rcp_f32_e32 v3, v3
	v_mul_f32_e32 v5, v0, v0
	v_mul_f32_e32 v5, 0xbf38aa3b, v5
	v_exp_f32_e32 v5, v5
	v_fmamk_f32 v4, v3, 0x3f07dc22, v184
	v_fmaak_f32 v4, v3, v4, 0x3f35f0e3
	v_fmaak_f32 v4, v3, v4, 0xbe11a98e
	v_mul_f32_e32 v1, v2, v1
	v_fmaak_f32 v4, v3, v4, 0x3e027906
	v_mul_f32_e32 v3, v3, v4
	v_mul_f32_e32 v1, v25, v1
	v_mul_f32_e32 v3, v5, v3
	v_fma_f32 v5, |v1|, s1, 1.0
	v_rcp_f32_e32 v5, v5
	v_mul_f32_e32 v4, v0, v3
	v_fma_f32 v3, -v0, v3, v0
	v_cmp_gt_f32_e32 vcc, 0, v0
	v_mul_f32_e32 v2, v83, v27
	v_mov_b32_e32 v150, 0
	v_cndmask_b32_e32 v0, v3, v4, vcc
	v_mul_f32_e32 v119, v2, v0
	v_mul_f32_e32 v2, v1, v1
	v_fmamk_f32 v0, v5, 0x3f07dc22, v184
	v_mul_f32_e32 v2, 0xbf38aa3b, v2
	v_fmaak_f32 v0, v5, v0, 0x3f35f0e3
	v_exp_f32_e32 v2, v2
	v_fmaak_f32 v0, v5, v0, 0xbe11a98e
	v_fmaak_f32 v0, v5, v0, 0x3e027906
	v_mul_f32_e32 v0, v5, v0
	v_mul_f32_e32 v0, v2, v0
	v_mul_f32_e32 v2, v1, v0
	v_fma_f32 v0, -v1, v0, v1
	v_cmp_gt_f32_e32 vcc, 0, v1
	v_mul_f32_e32 v1, v81, v24
	s_mov_b32 s1, s82
	v_cndmask_b32_e32 v0, v0, v2, vcc
	v_mul_f32_e32 v153, v1, v0
	v_mov_b32_e32 v151, v150
	v_mov_b32_e32 v148, v150
	v_mov_b32_e32 v149, v150
	v_mov_b32_e32 v146, v150
	v_mov_b32_e32 v147, v150
	v_mov_b32_e32 v144, v150
	v_mov_b32_e32 v145, v150
	v_mov_b32_e32 v142, v150
	v_mov_b32_e32 v143, v150
	v_mov_b32_e32 v140, v150
	v_mov_b32_e32 v141, v150
	v_mov_b32_e32 v138, v150
	v_mov_b32_e32 v139, v150
	v_mov_b32_e32 v136, v150
	v_mov_b32_e32 v137, v150
	v_mov_b32_e32 v134, v150
	v_mov_b32_e32 v135, v150
	v_mov_b32_e32 v132, v150
	v_mov_b32_e32 v133, v150
	v_mov_b32_e32 v130, v150
	v_mov_b32_e32 v131, v150
	v_mov_b32_e32 v128, v150
	v_mov_b32_e32 v129, v150
	v_mov_b32_e32 v126, v150
	v_mov_b32_e32 v127, v150
	v_mov_b32_e32 v124, v150
	v_mov_b32_e32 v125, v150
	v_mov_b32_e32 v122, v150
	v_mov_b32_e32 v123, v150
	v_mov_b32_e32 v120, v150
	v_mov_b32_e32 v121, v150
.LBB0_1181:
	s_add_i32 s40, s1, -3
	s_sub_i32 s41, s1, 19
	s_add_i32 s26, s1, -11
	s_cmp_lt_u32 s41, 56
	s_cselect_b64 vcc, -1, 0
	v_cndmask_b32_e32 v0, v118, v116, vcc
	s_add_i32 s24, s1, -10
	v_readlane_b32 s4, v0, s26
	s_mulk_i32 s4, 0x600
	s_add_i32 s4, s4, 0x8000000
	s_nop 2
	buffer_load_dwordx4 v[98:101], v152, s[44:47], s4 offen sc1
	buffer_load_dwordx2 v[102:103], v117, s[44:47], s4 offen sc1
	v_readlane_b32 s4, v0, s24
	s_mulk_i32 s4, 0x600
	s_add_i32 s4, s4, 0x8000000
	s_add_i32 s7, s1, -9
	s_nop 1
	buffer_load_dwordx4 v[92:95], v152, s[44:47], s4 offen sc1
	buffer_load_dwordx2 v[96:97], v117, s[44:47], s4 offen sc1
	v_readlane_b32 s4, v0, s7
	s_mulk_i32 s4, 0x600
	s_add_i32 s4, s4, 0x8000000
	s_add_i32 s6, s1, -8
	s_nop 1
	buffer_load_dwordx4 v[86:89], v152, s[44:47], s4 offen sc1
	buffer_load_dwordx2 v[90:91], v117, s[44:47], s4 offen sc1
	v_readlane_b32 s4, v0, s6
	s_mulk_i32 s4, 0x600
	s_add_i32 s4, s4, 0x8000000
	s_nop 2
	buffer_load_dwordx4 v[80:83], v152, s[44:47], s4 offen sc1
	buffer_load_dwordx2 v[84:85], v117, s[44:47], s4 offen sc1
	s_cmp_lt_u32 s41, 64
	s_cselect_b64 s[4:5], -1, 0
	v_cndmask_b32_e64 v154, v153, v119, s[4:5]
	s_waitcnt vmcnt(22)
	v_cvt_scalef32_pk32_f32_fp6 v[0:31], v[74:79], 1.0
	v_readlane_b32 s4, v154, s41
	s_nop 1
	v_pk_fma_f32 v[74:75], v[0:1], s[4:5], v[150:151] op_sel_hi:[1,0,1]
	v_pk_fma_f32 v[76:77], v[2:3], s[4:5], v[148:149] op_sel_hi:[1,0,1]
	v_pk_fma_f32 v[78:79], v[4:5], s[4:5], v[146:147] op_sel_hi:[1,0,1]
	v_pk_fma_f32 v[144:145], v[6:7], s[4:5], v[144:145] op_sel_hi:[1,0,1]
	v_pk_fma_f32 v[142:143], v[8:9], s[4:5], v[142:143] op_sel_hi:[1,0,1]
	v_pk_fma_f32 v[140:141], v[10:11], s[4:5], v[140:141] op_sel_hi:[1,0,1]
	v_pk_fma_f32 v[138:139], v[12:13], s[4:5], v[138:139] op_sel_hi:[1,0,1]
	v_pk_fma_f32 v[136:137], v[14:15], s[4:5], v[136:137] op_sel_hi:[1,0,1]
	v_pk_fma_f32 v[134:135], v[16:17], s[4:5], v[134:135] op_sel_hi:[1,0,1]
	v_pk_fma_f32 v[132:133], v[18:19], s[4:5], v[132:133] op_sel_hi:[1,0,1]
	v_pk_fma_f32 v[130:131], v[20:21], s[4:5], v[130:131] op_sel_hi:[1,0,1]
	v_pk_fma_f32 v[128:129], v[22:23], s[4:5], v[128:129] op_sel_hi:[1,0,1]
	v_pk_fma_f32 v[126:127], v[24:25], s[4:5], v[126:127] op_sel_hi:[1,0,1]
	v_pk_fma_f32 v[124:125], v[26:27], s[4:5], v[124:125] op_sel_hi:[1,0,1]
	v_pk_fma_f32 v[122:123], v[28:29], s[4:5], v[122:123] op_sel_hi:[1,0,1]
	v_pk_fma_f32 v[120:121], v[30:31], s[4:5], v[120:121] op_sel_hi:[1,0,1]
	s_sub_i32 s4, s1, 18
	v_readlane_b32 s4, v154, s4
	s_waitcnt vmcnt(20)
	v_cvt_scalef32_pk32_f32_fp6 v[0:31], v[68:73], 1.0
	v_pk_fma_f32 v[68:69], v[0:1], s[4:5], v[74:75] op_sel_hi:[1,0,1]
	v_pk_fma_f32 v[70:71], v[2:3], s[4:5], v[76:77] op_sel_hi:[1,0,1]
	v_pk_fma_f32 v[72:73], v[4:5], s[4:5], v[78:79] op_sel_hi:[1,0,1]
	v_pk_fma_f32 v[74:75], v[6:7], s[4:5], v[144:145] op_sel_hi:[1,0,1]
	v_pk_fma_f32 v[76:77], v[8:9], s[4:5], v[142:143] op_sel_hi:[1,0,1]
	v_pk_fma_f32 v[78:79], v[10:11], s[4:5], v[140:141] op_sel_hi:[1,0,1]
	v_pk_fma_f32 v[138:139], v[12:13], s[4:5], v[138:139] op_sel_hi:[1,0,1]
	v_pk_fma_f32 v[136:137], v[14:15], s[4:5], v[136:137] op_sel_hi:[1,0,1]
	v_pk_fma_f32 v[134:135], v[16:17], s[4:5], v[134:135] op_sel_hi:[1,0,1]
	v_pk_fma_f32 v[132:133], v[18:19], s[4:5], v[132:133] op_sel_hi:[1,0,1]
	v_pk_fma_f32 v[130:131], v[20:21], s[4:5], v[130:131] op_sel_hi:[1,0,1]
	v_pk_fma_f32 v[128:129], v[22:23], s[4:5], v[128:129] op_sel_hi:[1,0,1]
	v_pk_fma_f32 v[126:127], v[24:25], s[4:5], v[126:127] op_sel_hi:[1,0,1]
	v_pk_fma_f32 v[124:125], v[26:27], s[4:5], v[124:125] op_sel_hi:[1,0,1]
	v_pk_fma_f32 v[122:123], v[28:29], s[4:5], v[122:123] op_sel_hi:[1,0,1]
	v_pk_fma_f32 v[120:121], v[30:31], s[4:5], v[120:121] op_sel_hi:[1,0,1]
	s_sub_i32 s4, s1, 17
	v_readlane_b32 s4, v154, s4
	s_waitcnt vmcnt(18)
	v_cvt_scalef32_pk32_f32_fp6 v[0:31], v[56:61], 1.0
	v_pk_fma_f32 v[56:57], v[0:1], s[4:5], v[68:69] op_sel_hi:[1,0,1]
	v_pk_fma_f32 v[58:59], v[2:3], s[4:5], v[70:71] op_sel_hi:[1,0,1]
	v_pk_fma_f32 v[60:61], v[4:5], s[4:5], v[72:73] op_sel_hi:[1,0,1]
	v_pk_fma_f32 v[68:69], v[6:7], s[4:5], v[74:75] op_sel_hi:[1,0,1]
	v_pk_fma_f32 v[70:71], v[8:9], s[4:5], v[76:77] op_sel_hi:[1,0,1]
	v_pk_fma_f32 v[72:73], v[10:11], s[4:5], v[78:79] op_sel_hi:[1,0,1]
	v_pk_fma_f32 v[74:75], v[12:13], s[4:5], v[138:139] op_sel_hi:[1,0,1]
	v_pk_fma_f32 v[76:77], v[14:15], s[4:5], v[136:137] op_sel_hi:[1,0,1]
	v_pk_fma_f32 v[78:79], v[16:17], s[4:5], v[134:135] op_sel_hi:[1,0,1]
	v_pk_fma_f32 v[132:133], v[18:19], s[4:5], v[132:133] op_sel_hi:[1,0,1]
	v_pk_fma_f32 v[130:131], v[20:21], s[4:5], v[130:131] op_sel_hi:[1,0,1]
	v_pk_fma_f32 v[128:129], v[22:23], s[4:5], v[128:129] op_sel_hi:[1,0,1]
	v_pk_fma_f32 v[126:127], v[24:25], s[4:5], v[126:127] op_sel_hi:[1,0,1]
	v_pk_fma_f32 v[124:125], v[26:27], s[4:5], v[124:125] op_sel_hi:[1,0,1]
	v_pk_fma_f32 v[122:123], v[28:29], s[4:5], v[122:123] op_sel_hi:[1,0,1]
	v_pk_fma_f32 v[120:121], v[30:31], s[4:5], v[120:121] op_sel_hi:[1,0,1]
	s_add_i32 s4, s1, -16
	v_readlane_b32 s4, v154, s4
	s_waitcnt vmcnt(16)
	v_cvt_scalef32_pk32_f32_fp6 v[0:31], v[44:49], 1.0
	v_pk_fma_f32 v[134:135], v[0:1], s[4:5], v[56:57] op_sel_hi:[1,0,1]
	v_pk_fma_f32 v[136:137], v[2:3], s[4:5], v[58:59] op_sel_hi:[1,0,1]
	v_pk_fma_f32 v[138:139], v[4:5], s[4:5], v[60:61] op_sel_hi:[1,0,1]
	v_pk_fma_f32 v[140:141], v[6:7], s[4:5], v[68:69] op_sel_hi:[1,0,1]
	v_pk_fma_f32 v[142:143], v[8:9], s[4:5], v[70:71] op_sel_hi:[1,0,1]
	v_pk_fma_f32 v[144:145], v[10:11], s[4:5], v[72:73] op_sel_hi:[1,0,1]
	v_pk_fma_f32 v[146:147], v[12:13], s[4:5], v[74:75] op_sel_hi:[1,0,1]
	v_pk_fma_f32 v[148:149], v[14:15], s[4:5], v[76:77] op_sel_hi:[1,0,1]
	v_pk_fma_f32 v[150:151], v[16:17], s[4:5], v[78:79] op_sel_hi:[1,0,1]
	v_pk_fma_f32 v[132:133], v[18:19], s[4:5], v[132:133] op_sel_hi:[1,0,1]
	v_pk_fma_f32 v[130:131], v[20:21], s[4:5], v[130:131] op_sel_hi:[1,0,1]
	v_pk_fma_f32 v[128:129], v[22:23], s[4:5], v[128:129] op_sel_hi:[1,0,1]
	v_pk_fma_f32 v[126:127], v[24:25], s[4:5], v[126:127] op_sel_hi:[1,0,1]
	v_pk_fma_f32 v[124:125], v[26:27], s[4:5], v[124:125] op_sel_hi:[1,0,1]
	v_pk_fma_f32 v[122:123], v[28:29], s[4:5], v[122:123] op_sel_hi:[1,0,1]
	v_pk_fma_f32 v[120:121], v[30:31], s[4:5], v[120:121] op_sel_hi:[1,0,1]
	s_add_i32 s83, s1, -7
	s_cmp_lt_u32 s41, 52
	s_cselect_b64 s[4:5], -1, 0
	v_cndmask_b32_e64 v0, v118, v116, s[4:5]
	s_nop 0
	v_readlane_b32 s4, v0, s83
	s_mulk_i32 s4, 0x600
	s_add_i32 s4, s4, 0x8000000
	s_nop 2
	buffer_load_dwordx4 v[74:77], v152, s[44:47], s4 offen sc1
	buffer_load_dwordx2 v[78:79], v117, s[44:47], s4 offen sc1
	s_add_i32 s4, s1, -6
	v_readlane_b32 s4, v0, s4
	s_mulk_i32 s4, 0x600
	s_add_i32 s4, s4, 0x8000000
	s_nop 2
	buffer_load_dwordx4 v[68:71], v152, s[44:47], s4 offen sc1
	buffer_load_dwordx2 v[72:73], v117, s[44:47], s4 offen sc1
	s_add_i32 s4, s1, -5
	v_readlane_b32 s4, v0, s4
	s_mulk_i32 s4, 0x600
	s_add_i32 s4, s4, 0x8000000
	s_nop 2
	buffer_load_dwordx4 v[56:59], v152, s[44:47], s4 offen sc1
	buffer_load_dwordx2 v[60:61], v117, s[44:47], s4 offen sc1
	s_add_i32 s4, s1, -4
	v_readlane_b32 s4, v0, s4
	s_mulk_i32 s4, 0x600
	s_add_i32 s4, s4, 0x8000000
	s_nop 2
	buffer_load_dwordx4 v[44:47], v152, s[44:47], s4 offen sc1
	buffer_load_dwordx2 v[48:49], v117, s[44:47], s4 offen sc1
	s_add_i32 s83, s1, -15
	s_cmp_lt_u32 s41, 60
	s_cselect_b64 s[4:5], -1, 0
	v_cndmask_b32_e64 v154, v153, v119, s[4:5]
	s_waitcnt vmcnt(22)
	v_cvt_scalef32_pk32_f32_fp6 v[0:31], v[62:67], 1.0
	v_readlane_b32 s4, v154, s83
	s_nop 1
	v_pk_fma_f32 v[62:63], v[0:1], s[4:5], v[134:135] op_sel_hi:[1,0,1]
	v_pk_fma_f32 v[64:65], v[2:3], s[4:5], v[136:137] op_sel_hi:[1,0,1]
	v_pk_fma_f32 v[66:67], v[4:5], s[4:5], v[138:139] op_sel_hi:[1,0,1]
	v_pk_fma_f32 v[134:135], v[6:7], s[4:5], v[140:141] op_sel_hi:[1,0,1]
	v_pk_fma_f32 v[136:137], v[8:9], s[4:5], v[142:143] op_sel_hi:[1,0,1]
	v_pk_fma_f32 v[138:139], v[10:11], s[4:5], v[144:145] op_sel_hi:[1,0,1]
	v_pk_fma_f32 v[140:141], v[12:13], s[4:5], v[146:147] op_sel_hi:[1,0,1]
	v_pk_fma_f32 v[142:143], v[14:15], s[4:5], v[148:149] op_sel_hi:[1,0,1]
	v_pk_fma_f32 v[144:145], v[16:17], s[4:5], v[150:151] op_sel_hi:[1,0,1]
	v_pk_fma_f32 v[132:133], v[18:19], s[4:5], v[132:133] op_sel_hi:[1,0,1]
	v_pk_fma_f32 v[130:131], v[20:21], s[4:5], v[130:131] op_sel_hi:[1,0,1]
	v_pk_fma_f32 v[128:129], v[22:23], s[4:5], v[128:129] op_sel_hi:[1,0,1]
	v_pk_fma_f32 v[126:127], v[24:25], s[4:5], v[126:127] op_sel_hi:[1,0,1]
	v_pk_fma_f32 v[124:125], v[26:27], s[4:5], v[124:125] op_sel_hi:[1,0,1]
	v_pk_fma_f32 v[122:123], v[28:29], s[4:5], v[122:123] op_sel_hi:[1,0,1]
	v_pk_fma_f32 v[120:121], v[30:31], s[4:5], v[120:121] op_sel_hi:[1,0,1]
	s_add_i32 s4, s1, -14
	v_readlane_b32 s4, v154, s4
	s_waitcnt vmcnt(20)
	v_cvt_scalef32_pk32_f32_fp6 v[0:31], v[50:55], 1.0
	v_pk_fma_f32 v[50:51], v[0:1], s[4:5], v[62:63] op_sel_hi:[1,0,1]
	v_pk_fma_f32 v[52:53], v[2:3], s[4:5], v[64:65] op_sel_hi:[1,0,1]
	v_pk_fma_f32 v[54:55], v[4:5], s[4:5], v[66:67] op_sel_hi:[1,0,1]
	v_pk_fma_f32 v[62:63], v[6:7], s[4:5], v[134:135] op_sel_hi:[1,0,1]
	v_pk_fma_f32 v[64:65], v[8:9], s[4:5], v[136:137] op_sel_hi:[1,0,1]
	v_pk_fma_f32 v[66:67], v[10:11], s[4:5], v[138:139] op_sel_hi:[1,0,1]
	v_pk_fma_f32 v[134:135], v[12:13], s[4:5], v[140:141] op_sel_hi:[1,0,1]
	v_pk_fma_f32 v[136:137], v[14:15], s[4:5], v[142:143] op_sel_hi:[1,0,1]
	v_pk_fma_f32 v[138:139], v[16:17], s[4:5], v[144:145] op_sel_hi:[1,0,1]
	v_pk_fma_f32 v[132:133], v[18:19], s[4:5], v[132:133] op_sel_hi:[1,0,1]
	v_pk_fma_f32 v[130:131], v[20:21], s[4:5], v[130:131] op_sel_hi:[1,0,1]
	v_pk_fma_f32 v[128:129], v[22:23], s[4:5], v[128:129] op_sel_hi:[1,0,1]
	v_pk_fma_f32 v[126:127], v[24:25], s[4:5], v[126:127] op_sel_hi:[1,0,1]
	v_pk_fma_f32 v[124:125], v[26:27], s[4:5], v[124:125] op_sel_hi:[1,0,1]
	v_pk_fma_f32 v[122:123], v[28:29], s[4:5], v[122:123] op_sel_hi:[1,0,1]
	v_pk_fma_f32 v[120:121], v[30:31], s[4:5], v[120:121] op_sel_hi:[1,0,1]
	s_add_i32 s4, s1, -13
	v_readlane_b32 s4, v154, s4
	s_waitcnt vmcnt(18)
	v_cvt_scalef32_pk32_f32_fp6 v[0:31], v[38:43], 1.0
	v_pk_fma_f32 v[38:39], v[0:1], s[4:5], v[50:51] op_sel_hi:[1,0,1]
	v_pk_fma_f32 v[40:41], v[2:3], s[4:5], v[52:53] op_sel_hi:[1,0,1]
	v_pk_fma_f32 v[42:43], v[4:5], s[4:5], v[54:55] op_sel_hi:[1,0,1]
	v_pk_fma_f32 v[50:51], v[6:7], s[4:5], v[62:63] op_sel_hi:[1,0,1]
	v_pk_fma_f32 v[52:53], v[8:9], s[4:5], v[64:65] op_sel_hi:[1,0,1]
	v_pk_fma_f32 v[54:55], v[10:11], s[4:5], v[66:67] op_sel_hi:[1,0,1]
	v_pk_fma_f32 v[62:63], v[12:13], s[4:5], v[134:135] op_sel_hi:[1,0,1]
	v_pk_fma_f32 v[64:65], v[14:15], s[4:5], v[136:137] op_sel_hi:[1,0,1]
	v_pk_fma_f32 v[66:67], v[16:17], s[4:5], v[138:139] op_sel_hi:[1,0,1]
	v_pk_fma_f32 v[132:133], v[18:19], s[4:5], v[132:133] op_sel_hi:[1,0,1]
	v_pk_fma_f32 v[130:131], v[20:21], s[4:5], v[130:131] op_sel_hi:[1,0,1]
	v_pk_fma_f32 v[128:129], v[22:23], s[4:5], v[128:129] op_sel_hi:[1,0,1]
	v_pk_fma_f32 v[126:127], v[24:25], s[4:5], v[126:127] op_sel_hi:[1,0,1]
	v_pk_fma_f32 v[124:125], v[26:27], s[4:5], v[124:125] op_sel_hi:[1,0,1]
	v_pk_fma_f32 v[122:123], v[28:29], s[4:5], v[122:123] op_sel_hi:[1,0,1]
	v_pk_fma_f32 v[120:121], v[30:31], s[4:5], v[120:121] op_sel_hi:[1,0,1]
	s_add_i32 s4, s1, -12
	v_readlane_b32 s4, v154, s4
	s_waitcnt vmcnt(16)
	v_cvt_scalef32_pk32_f32_fp6 v[0:31], v[32:37], 1.0
	v_pk_fma_f32 v[134:135], v[0:1], s[4:5], v[38:39] op_sel_hi:[1,0,1]
	v_pk_fma_f32 v[136:137], v[2:3], s[4:5], v[40:41] op_sel_hi:[1,0,1]
	v_pk_fma_f32 v[138:139], v[4:5], s[4:5], v[42:43] op_sel_hi:[1,0,1]
	v_pk_fma_f32 v[140:141], v[6:7], s[4:5], v[50:51] op_sel_hi:[1,0,1]
	v_pk_fma_f32 v[142:143], v[8:9], s[4:5], v[52:53] op_sel_hi:[1,0,1]
	v_pk_fma_f32 v[144:145], v[10:11], s[4:5], v[54:55] op_sel_hi:[1,0,1]
	v_pk_fma_f32 v[146:147], v[12:13], s[4:5], v[62:63] op_sel_hi:[1,0,1]
	v_pk_fma_f32 v[148:149], v[14:15], s[4:5], v[64:65] op_sel_hi:[1,0,1]
	v_pk_fma_f32 v[150:151], v[16:17], s[4:5], v[66:67] op_sel_hi:[1,0,1]
	v_pk_fma_f32 v[132:133], v[18:19], s[4:5], v[132:133] op_sel_hi:[1,0,1]
	v_pk_fma_f32 v[130:131], v[20:21], s[4:5], v[130:131] op_sel_hi:[1,0,1]
	v_pk_fma_f32 v[128:129], v[22:23], s[4:5], v[128:129] op_sel_hi:[1,0,1]
	v_pk_fma_f32 v[126:127], v[24:25], s[4:5], v[126:127] op_sel_hi:[1,0,1]
	v_pk_fma_f32 v[124:125], v[26:27], s[4:5], v[124:125] op_sel_hi:[1,0,1]
	v_pk_fma_f32 v[122:123], v[28:29], s[4:5], v[122:123] op_sel_hi:[1,0,1]
	v_pk_fma_f32 v[120:121], v[30:31], s[4:5], v[120:121] op_sel_hi:[1,0,1]
	s_cmp_lt_u32 s41, 48
	s_cselect_b64 s[4:5], -1, 0
	v_cndmask_b32_e64 v0, v118, v116, s[4:5]
	s_nop 0
	v_readlane_b32 s4, v0, s40
	s_mulk_i32 s4, 0x600
	s_add_i32 s4, s4, 0x8000000
	s_nop 2
	buffer_load_dwordx4 v[62:65], v152, s[44:47], s4 offen sc1
	buffer_load_dwordx2 v[66:67], v117, s[44:47], s4 offen sc1
	s_add_i32 s4, s1, -2
	v_readlane_b32 s4, v0, s4
	s_mulk_i32 s4, 0x600
	s_add_i32 s4, s4, 0x8000000
	s_nop 2
	buffer_load_dwordx4 v[50:53], v152, s[44:47], s4 offen sc1
	buffer_load_dwordx2 v[54:55], v117, s[44:47], s4 offen sc1
	s_add_i32 s4, s1, -1
	v_readlane_b32 s4, v0, s4
	s_mulk_i32 s4, 0x600
	s_add_i32 s4, s4, 0x8000000
	s_nop 2
	buffer_load_dwordx4 v[38:41], v152, s[44:47], s4 offen sc1
	buffer_load_dwordx2 v[42:43], v117, s[44:47], s4 offen sc1
	v_readlane_b32 s4, v0, s1
	s_mulk_i32 s4, 0x600
	s_add_i32 s4, s4, 0x8000000
	s_nop 2
	buffer_load_dwordx4 v[32:35], v152, s[44:47], s4 offen sc1
	buffer_load_dwordx2 v[36:37], v117, s[44:47], s4 offen sc1
	v_cndmask_b32_e32 v154, v153, v119, vcc
	s_waitcnt vmcnt(22)
	v_cvt_scalef32_pk32_f32_fp6 v[0:31], v[98:103], 1.0
	v_readlane_b32 s4, v154, s26
	s_nop 1
	v_pk_fma_f32 v[98:99], v[0:1], s[4:5], v[134:135] op_sel_hi:[1,0,1]
	v_pk_fma_f32 v[100:101], v[2:3], s[4:5], v[136:137] op_sel_hi:[1,0,1]
	v_pk_fma_f32 v[102:103], v[4:5], s[4:5], v[138:139] op_sel_hi:[1,0,1]
	v_pk_fma_f32 v[134:135], v[6:7], s[4:5], v[140:141] op_sel_hi:[1,0,1]
	v_pk_fma_f32 v[136:137], v[8:9], s[4:5], v[142:143] op_sel_hi:[1,0,1]
	v_pk_fma_f32 v[138:139], v[10:11], s[4:5], v[144:145] op_sel_hi:[1,0,1]
	v_pk_fma_f32 v[140:141], v[12:13], s[4:5], v[146:147] op_sel_hi:[1,0,1]
	v_pk_fma_f32 v[142:143], v[14:15], s[4:5], v[148:149] op_sel_hi:[1,0,1]
	v_pk_fma_f32 v[144:145], v[16:17], s[4:5], v[150:151] op_sel_hi:[1,0,1]
	v_pk_fma_f32 v[132:133], v[18:19], s[4:5], v[132:133] op_sel_hi:[1,0,1]
	v_pk_fma_f32 v[130:131], v[20:21], s[4:5], v[130:131] op_sel_hi:[1,0,1]
	v_pk_fma_f32 v[128:129], v[22:23], s[4:5], v[128:129] op_sel_hi:[1,0,1]
	v_pk_fma_f32 v[126:127], v[24:25], s[4:5], v[126:127] op_sel_hi:[1,0,1]
	v_pk_fma_f32 v[124:125], v[26:27], s[4:5], v[124:125] op_sel_hi:[1,0,1]
	v_pk_fma_f32 v[122:123], v[28:29], s[4:5], v[122:123] op_sel_hi:[1,0,1]
	v_pk_fma_f32 v[120:121], v[30:31], s[4:5], v[120:121] op_sel_hi:[1,0,1]
	v_readlane_b32 s4, v154, s24
	s_waitcnt vmcnt(20)
	v_cvt_scalef32_pk32_f32_fp6 v[0:31], v[92:97], 1.0
	v_pk_fma_f32 v[92:93], v[0:1], s[4:5], v[98:99] op_sel_hi:[1,0,1]
	v_pk_fma_f32 v[94:95], v[2:3], s[4:5], v[100:101] op_sel_hi:[1,0,1]
	v_pk_fma_f32 v[96:97], v[4:5], s[4:5], v[102:103] op_sel_hi:[1,0,1]
	v_pk_fma_f32 v[98:99], v[6:7], s[4:5], v[134:135] op_sel_hi:[1,0,1]
	v_pk_fma_f32 v[100:101], v[8:9], s[4:5], v[136:137] op_sel_hi:[1,0,1]
	v_pk_fma_f32 v[102:103], v[10:11], s[4:5], v[138:139] op_sel_hi:[1,0,1]
	v_pk_fma_f32 v[134:135], v[12:13], s[4:5], v[140:141] op_sel_hi:[1,0,1]
	v_pk_fma_f32 v[136:137], v[14:15], s[4:5], v[142:143] op_sel_hi:[1,0,1]
	v_pk_fma_f32 v[138:139], v[16:17], s[4:5], v[144:145] op_sel_hi:[1,0,1]
	v_pk_fma_f32 v[132:133], v[18:19], s[4:5], v[132:133] op_sel_hi:[1,0,1]
	v_pk_fma_f32 v[130:131], v[20:21], s[4:5], v[130:131] op_sel_hi:[1,0,1]
	v_pk_fma_f32 v[128:129], v[22:23], s[4:5], v[128:129] op_sel_hi:[1,0,1]
	v_pk_fma_f32 v[126:127], v[24:25], s[4:5], v[126:127] op_sel_hi:[1,0,1]
	v_pk_fma_f32 v[124:125], v[26:27], s[4:5], v[124:125] op_sel_hi:[1,0,1]
	v_pk_fma_f32 v[122:123], v[28:29], s[4:5], v[122:123] op_sel_hi:[1,0,1]
	v_pk_fma_f32 v[120:121], v[30:31], s[4:5], v[120:121] op_sel_hi:[1,0,1]
	v_readlane_b32 s4, v154, s7
	s_waitcnt vmcnt(18)
	v_cvt_scalef32_pk32_f32_fp6 v[0:31], v[86:91], 1.0
	v_pk_fma_f32 v[86:87], v[0:1], s[4:5], v[92:93] op_sel_hi:[1,0,1]
	v_pk_fma_f32 v[88:89], v[2:3], s[4:5], v[94:95] op_sel_hi:[1,0,1]
	v_pk_fma_f32 v[90:91], v[4:5], s[4:5], v[96:97] op_sel_hi:[1,0,1]
	v_pk_fma_f32 v[92:93], v[6:7], s[4:5], v[98:99] op_sel_hi:[1,0,1]
	v_pk_fma_f32 v[94:95], v[8:9], s[4:5], v[100:101] op_sel_hi:[1,0,1]
	v_pk_fma_f32 v[96:97], v[10:11], s[4:5], v[102:103] op_sel_hi:[1,0,1]
	v_pk_fma_f32 v[98:99], v[12:13], s[4:5], v[134:135] op_sel_hi:[1,0,1]
	v_pk_fma_f32 v[100:101], v[14:15], s[4:5], v[136:137] op_sel_hi:[1,0,1]
	v_pk_fma_f32 v[102:103], v[16:17], s[4:5], v[138:139] op_sel_hi:[1,0,1]
	v_pk_fma_f32 v[132:133], v[18:19], s[4:5], v[132:133] op_sel_hi:[1,0,1]
	v_pk_fma_f32 v[130:131], v[20:21], s[4:5], v[130:131] op_sel_hi:[1,0,1]
	v_pk_fma_f32 v[128:129], v[22:23], s[4:5], v[128:129] op_sel_hi:[1,0,1]
	v_pk_fma_f32 v[126:127], v[24:25], s[4:5], v[126:127] op_sel_hi:[1,0,1]
	v_pk_fma_f32 v[124:125], v[26:27], s[4:5], v[124:125] op_sel_hi:[1,0,1]
	v_pk_fma_f32 v[122:123], v[28:29], s[4:5], v[122:123] op_sel_hi:[1,0,1]
	v_pk_fma_f32 v[120:121], v[30:31], s[4:5], v[120:121] op_sel_hi:[1,0,1]
	v_readlane_b32 s4, v154, s6
	s_waitcnt vmcnt(16)
	v_cvt_scalef32_pk32_f32_fp6 v[0:31], v[80:85], 1.0
	v_pk_fma_f32 v[150:151], v[0:1], s[4:5], v[86:87] op_sel_hi:[1,0,1]
	v_pk_fma_f32 v[148:149], v[2:3], s[4:5], v[88:89] op_sel_hi:[1,0,1]
	v_pk_fma_f32 v[146:147], v[4:5], s[4:5], v[90:91] op_sel_hi:[1,0,1]
	v_pk_fma_f32 v[144:145], v[6:7], s[4:5], v[92:93] op_sel_hi:[1,0,1]
	v_pk_fma_f32 v[142:143], v[8:9], s[4:5], v[94:95] op_sel_hi:[1,0,1]
	v_pk_fma_f32 v[140:141], v[10:11], s[4:5], v[96:97] op_sel_hi:[1,0,1]
	v_pk_fma_f32 v[138:139], v[12:13], s[4:5], v[98:99] op_sel_hi:[1,0,1]
	v_pk_fma_f32 v[136:137], v[14:15], s[4:5], v[100:101] op_sel_hi:[1,0,1]
	v_pk_fma_f32 v[134:135], v[16:17], s[4:5], v[102:103] op_sel_hi:[1,0,1]
	v_pk_fma_f32 v[132:133], v[18:19], s[4:5], v[132:133] op_sel_hi:[1,0,1]
	v_pk_fma_f32 v[130:131], v[20:21], s[4:5], v[130:131] op_sel_hi:[1,0,1]
	v_pk_fma_f32 v[128:129], v[22:23], s[4:5], v[128:129] op_sel_hi:[1,0,1]
	v_pk_fma_f32 v[126:127], v[24:25], s[4:5], v[126:127] op_sel_hi:[1,0,1]
	v_pk_fma_f32 v[124:125], v[26:27], s[4:5], v[124:125] op_sel_hi:[1,0,1]
	v_pk_fma_f32 v[122:123], v[28:29], s[4:5], v[122:123] op_sel_hi:[1,0,1]
	v_pk_fma_f32 v[120:121], v[30:31], s[4:5], v[120:121] op_sel_hi:[1,0,1]
	s_add_i32 s4, s1, 12
	s_add_i32 s1, s1, 9
	s_cmp_lt_u32 s1, s52
	s_mov_b32 s1, s4
	s_cbranch_scc1 .LBB0_1181
	v_cndmask_b32_e64 v118, v153, v119, s[2:3]
	s_waitcnt vmcnt(14)
	v_cvt_scalef32_pk32_f32_fp6 v[0:31], v[74:79], 1.0
	v_readlane_b32 s4, v118, s60
	s_nop 1
	v_pk_fma_f32 v[74:75], v[0:1], s[4:5], v[150:151] op_sel_hi:[1,0,1]
	v_pk_fma_f32 v[76:77], v[2:3], s[4:5], v[148:149] op_sel_hi:[1,0,1]
	v_pk_fma_f32 v[78:79], v[4:5], s[4:5], v[146:147] op_sel_hi:[1,0,1]
	v_pk_fma_f32 v[80:81], v[6:7], s[4:5], v[144:145] op_sel_hi:[1,0,1]
	v_pk_fma_f32 v[82:83], v[8:9], s[4:5], v[142:143] op_sel_hi:[1,0,1]
	v_pk_fma_f32 v[84:85], v[10:11], s[4:5], v[140:141] op_sel_hi:[1,0,1]
	v_pk_fma_f32 v[86:87], v[12:13], s[4:5], v[138:139] op_sel_hi:[1,0,1]
	v_pk_fma_f32 v[88:89], v[14:15], s[4:5], v[136:137] op_sel_hi:[1,0,1]
	v_pk_fma_f32 v[90:91], v[16:17], s[4:5], v[134:135] op_sel_hi:[1,0,1]
	v_pk_fma_f32 v[92:93], v[18:19], s[4:5], v[132:133] op_sel_hi:[1,0,1]
	v_pk_fma_f32 v[94:95], v[20:21], s[4:5], v[130:131] op_sel_hi:[1,0,1]
	v_pk_fma_f32 v[96:97], v[22:23], s[4:5], v[128:129] op_sel_hi:[1,0,1]
	v_pk_fma_f32 v[98:99], v[24:25], s[4:5], v[126:127] op_sel_hi:[1,0,1]
	v_pk_fma_f32 v[100:101], v[26:27], s[4:5], v[124:125] op_sel_hi:[1,0,1]
	v_pk_fma_f32 v[102:103], v[28:29], s[4:5], v[122:123] op_sel_hi:[1,0,1]
	v_pk_fma_f32 v[116:117], v[30:31], s[4:5], v[120:121] op_sel_hi:[1,0,1]
	v_readlane_b32 s4, v118, s75
	s_waitcnt vmcnt(12)
	v_cvt_scalef32_pk32_f32_fp6 v[0:31], v[68:73], 1.0
	v_pk_fma_f32 v[68:69], v[0:1], s[4:5], v[74:75] op_sel_hi:[1,0,1]
	v_pk_fma_f32 v[70:71], v[2:3], s[4:5], v[76:77] op_sel_hi:[1,0,1]
	v_pk_fma_f32 v[72:73], v[4:5], s[4:5], v[78:79] op_sel_hi:[1,0,1]
	v_pk_fma_f32 v[74:75], v[6:7], s[4:5], v[80:81] op_sel_hi:[1,0,1]
	v_pk_fma_f32 v[76:77], v[8:9], s[4:5], v[82:83] op_sel_hi:[1,0,1]
	v_pk_fma_f32 v[78:79], v[10:11], s[4:5], v[84:85] op_sel_hi:[1,0,1]
	v_pk_fma_f32 v[80:81], v[12:13], s[4:5], v[86:87] op_sel_hi:[1,0,1]
	v_pk_fma_f32 v[82:83], v[14:15], s[4:5], v[88:89] op_sel_hi:[1,0,1]
	v_pk_fma_f32 v[84:85], v[16:17], s[4:5], v[90:91] op_sel_hi:[1,0,1]
	v_pk_fma_f32 v[86:87], v[18:19], s[4:5], v[92:93] op_sel_hi:[1,0,1]
	v_pk_fma_f32 v[88:89], v[20:21], s[4:5], v[94:95] op_sel_hi:[1,0,1]
	v_pk_fma_f32 v[90:91], v[22:23], s[4:5], v[96:97] op_sel_hi:[1,0,1]
	v_pk_fma_f32 v[92:93], v[24:25], s[4:5], v[98:99] op_sel_hi:[1,0,1]
	v_pk_fma_f32 v[94:95], v[26:27], s[4:5], v[100:101] op_sel_hi:[1,0,1]
	v_pk_fma_f32 v[96:97], v[28:29], s[4:5], v[102:103] op_sel_hi:[1,0,1]
	v_pk_fma_f32 v[98:99], v[30:31], s[4:5], v[116:117] op_sel_hi:[1,0,1]
	v_readlane_b32 s4, v118, s76
	s_waitcnt vmcnt(10)
	v_cvt_scalef32_pk32_f32_fp6 v[0:31], v[56:61], 1.0
	v_pk_fma_f32 v[56:57], v[0:1], s[4:5], v[68:69] op_sel_hi:[1,0,1]
	v_pk_fma_f32 v[58:59], v[2:3], s[4:5], v[70:71] op_sel_hi:[1,0,1]
	v_pk_fma_f32 v[60:61], v[4:5], s[4:5], v[72:73] op_sel_hi:[1,0,1]
	v_pk_fma_f32 v[68:69], v[6:7], s[4:5], v[74:75] op_sel_hi:[1,0,1]
	v_pk_fma_f32 v[70:71], v[8:9], s[4:5], v[76:77] op_sel_hi:[1,0,1]
	v_pk_fma_f32 v[72:73], v[10:11], s[4:5], v[78:79] op_sel_hi:[1,0,1]
	v_pk_fma_f32 v[74:75], v[12:13], s[4:5], v[80:81] op_sel_hi:[1,0,1]
	v_pk_fma_f32 v[76:77], v[14:15], s[4:5], v[82:83] op_sel_hi:[1,0,1]
	v_pk_fma_f32 v[78:79], v[16:17], s[4:5], v[84:85] op_sel_hi:[1,0,1]
	v_pk_fma_f32 v[80:81], v[18:19], s[4:5], v[86:87] op_sel_hi:[1,0,1]
	v_pk_fma_f32 v[82:83], v[20:21], s[4:5], v[88:89] op_sel_hi:[1,0,1]
	v_pk_fma_f32 v[84:85], v[22:23], s[4:5], v[90:91] op_sel_hi:[1,0,1]
	v_pk_fma_f32 v[86:87], v[24:25], s[4:5], v[92:93] op_sel_hi:[1,0,1]
	v_pk_fma_f32 v[88:89], v[26:27], s[4:5], v[94:95] op_sel_hi:[1,0,1]
	v_pk_fma_f32 v[90:91], v[28:29], s[4:5], v[96:97] op_sel_hi:[1,0,1]
	v_pk_fma_f32 v[92:93], v[30:31], s[4:5], v[98:99] op_sel_hi:[1,0,1]
	v_readlane_b32 s4, v118, s77
	s_waitcnt vmcnt(8)
	v_cvt_scalef32_pk32_f32_fp6 v[0:31], v[44:49], 1.0
	v_pk_fma_f32 v[44:45], v[0:1], s[4:5], v[56:57] op_sel_hi:[1,0,1]
	v_pk_fma_f32 v[48:49], v[4:5], s[4:5], v[60:61] op_sel_hi:[1,0,1]
	v_pk_fma_f32 v[56:57], v[6:7], s[4:5], v[68:69] op_sel_hi:[1,0,1]
	v_pk_fma_f32 v[60:61], v[10:11], s[4:5], v[72:73] op_sel_hi:[1,0,1]
	v_pk_fma_f32 v[68:69], v[12:13], s[4:5], v[74:75] op_sel_hi:[1,0,1]
	v_pk_fma_f32 v[72:73], v[16:17], s[4:5], v[78:79] op_sel_hi:[1,0,1]
	v_pk_fma_f32 v[74:75], v[18:19], s[4:5], v[80:81] op_sel_hi:[1,0,1]
	v_pk_fma_f32 v[78:79], v[22:23], s[4:5], v[84:85] op_sel_hi:[1,0,1]
	v_pk_fma_f32 v[80:81], v[24:25], s[4:5], v[86:87] op_sel_hi:[1,0,1]
	v_pk_fma_f32 v[84:85], v[28:29], s[4:5], v[90:91] op_sel_hi:[1,0,1]
	v_pk_fma_f32 v[46:47], v[2:3], s[4:5], v[58:59] op_sel_hi:[1,0,1]
	v_pk_fma_f32 v[58:59], v[8:9], s[4:5], v[70:71] op_sel_hi:[1,0,1]
	v_pk_fma_f32 v[70:71], v[14:15], s[4:5], v[76:77] op_sel_hi:[1,0,1]
	v_pk_fma_f32 v[76:77], v[20:21], s[4:5], v[82:83] op_sel_hi:[1,0,1]
	v_pk_fma_f32 v[82:83], v[26:27], s[4:5], v[88:89] op_sel_hi:[1,0,1]
	v_pk_fma_f32 v[86:87], v[30:31], s[4:5], v[92:93] op_sel_hi:[1,0,1]
	v_readlane_b32 s4, v118, s64
	s_waitcnt vmcnt(6)
	v_cvt_scalef32_pk32_f32_fp6 v[0:31], v[62:67], 1.0
	v_pk_fma_f32 v[44:45], v[0:1], s[4:5], v[44:45] op_sel_hi:[1,0,1]
	v_pk_fma_f32 v[46:47], v[2:3], s[4:5], v[46:47] op_sel_hi:[1,0,1]
	v_pk_fma_f32 v[48:49], v[4:5], s[4:5], v[48:49] op_sel_hi:[1,0,1]
	v_pk_fma_f32 v[56:57], v[6:7], s[4:5], v[56:57] op_sel_hi:[1,0,1]
	v_pk_fma_f32 v[58:59], v[8:9], s[4:5], v[58:59] op_sel_hi:[1,0,1]
	v_pk_fma_f32 v[60:61], v[10:11], s[4:5], v[60:61] op_sel_hi:[1,0,1]
	v_pk_fma_f32 v[62:63], v[12:13], s[4:5], v[68:69] op_sel_hi:[1,0,1]
	v_pk_fma_f32 v[64:65], v[14:15], s[4:5], v[70:71] op_sel_hi:[1,0,1]
	v_pk_fma_f32 v[66:67], v[16:17], s[4:5], v[72:73] op_sel_hi:[1,0,1]
	v_pk_fma_f32 v[68:69], v[18:19], s[4:5], v[74:75] op_sel_hi:[1,0,1]
	v_pk_fma_f32 v[70:71], v[20:21], s[4:5], v[76:77] op_sel_hi:[1,0,1]
	v_pk_fma_f32 v[72:73], v[22:23], s[4:5], v[78:79] op_sel_hi:[1,0,1]
	v_pk_fma_f32 v[74:75], v[24:25], s[4:5], v[80:81] op_sel_hi:[1,0,1]
	v_pk_fma_f32 v[76:77], v[26:27], s[4:5], v[82:83] op_sel_hi:[1,0,1]
	v_pk_fma_f32 v[78:79], v[28:29], s[4:5], v[84:85] op_sel_hi:[1,0,1]
	v_pk_fma_f32 v[80:81], v[30:31], s[4:5], v[86:87] op_sel_hi:[1,0,1]
	v_readlane_b32 s4, v118, s78
	s_waitcnt vmcnt(4)
	v_cvt_scalef32_pk32_f32_fp6 v[0:31], v[50:55], 1.0
	v_pk_fma_f32 v[44:45], v[0:1], s[4:5], v[44:45] op_sel_hi:[1,0,1]
	v_pk_fma_f32 v[46:47], v[2:3], s[4:5], v[46:47] op_sel_hi:[1,0,1]
	v_pk_fma_f32 v[48:49], v[4:5], s[4:5], v[48:49] op_sel_hi:[1,0,1]
	v_pk_fma_f32 v[50:51], v[6:7], s[4:5], v[56:57] op_sel_hi:[1,0,1]
	v_pk_fma_f32 v[52:53], v[8:9], s[4:5], v[58:59] op_sel_hi:[1,0,1]
	v_pk_fma_f32 v[54:55], v[10:11], s[4:5], v[60:61] op_sel_hi:[1,0,1]
	v_pk_fma_f32 v[56:57], v[12:13], s[4:5], v[62:63] op_sel_hi:[1,0,1]
	v_pk_fma_f32 v[58:59], v[14:15], s[4:5], v[64:65] op_sel_hi:[1,0,1]
	v_pk_fma_f32 v[60:61], v[16:17], s[4:5], v[66:67] op_sel_hi:[1,0,1]
	v_pk_fma_f32 v[62:63], v[18:19], s[4:5], v[68:69] op_sel_hi:[1,0,1]
	v_pk_fma_f32 v[64:65], v[20:21], s[4:5], v[70:71] op_sel_hi:[1,0,1]
	v_pk_fma_f32 v[66:67], v[22:23], s[4:5], v[72:73] op_sel_hi:[1,0,1]
	v_pk_fma_f32 v[68:69], v[24:25], s[4:5], v[74:75] op_sel_hi:[1,0,1]
	v_pk_fma_f32 v[70:71], v[26:27], s[4:5], v[76:77] op_sel_hi:[1,0,1]
	v_pk_fma_f32 v[72:73], v[28:29], s[4:5], v[78:79] op_sel_hi:[1,0,1]
	v_pk_fma_f32 v[74:75], v[30:31], s[4:5], v[80:81] op_sel_hi:[1,0,1]
	v_readlane_b32 s4, v118, s79
	s_waitcnt vmcnt(2)
	v_cvt_scalef32_pk32_f32_fp6 v[0:31], v[38:43], 1.0
	v_pk_fma_f32 v[38:39], v[0:1], s[4:5], v[44:45] op_sel_hi:[1,0,1]
	v_pk_fma_f32 v[40:41], v[2:3], s[4:5], v[46:47] op_sel_hi:[1,0,1]
	v_pk_fma_f32 v[42:43], v[4:5], s[4:5], v[48:49] op_sel_hi:[1,0,1]
	v_pk_fma_f32 v[44:45], v[6:7], s[4:5], v[50:51] op_sel_hi:[1,0,1]
	v_pk_fma_f32 v[46:47], v[8:9], s[4:5], v[52:53] op_sel_hi:[1,0,1]
	v_pk_fma_f32 v[48:49], v[10:11], s[4:5], v[54:55] op_sel_hi:[1,0,1]
	v_pk_fma_f32 v[50:51], v[12:13], s[4:5], v[56:57] op_sel_hi:[1,0,1]
	v_pk_fma_f32 v[52:53], v[14:15], s[4:5], v[58:59] op_sel_hi:[1,0,1]
	v_pk_fma_f32 v[54:55], v[16:17], s[4:5], v[60:61] op_sel_hi:[1,0,1]
	v_pk_fma_f32 v[56:57], v[18:19], s[4:5], v[62:63] op_sel_hi:[1,0,1]
	v_pk_fma_f32 v[58:59], v[20:21], s[4:5], v[64:65] op_sel_hi:[1,0,1]
	v_pk_fma_f32 v[60:61], v[22:23], s[4:5], v[66:67] op_sel_hi:[1,0,1]
	v_pk_fma_f32 v[62:63], v[24:25], s[4:5], v[68:69] op_sel_hi:[1,0,1]
	v_pk_fma_f32 v[66:67], v[26:27], s[4:5], v[70:71] op_sel_hi:[1,0,1]
	v_pk_fma_f32 v[70:71], v[28:29], s[4:5], v[72:73] op_sel_hi:[1,0,1]
	v_pk_fma_f32 v[72:73], v[30:31], s[4:5], v[74:75] op_sel_hi:[1,0,1]
	v_readlane_b32 s4, v118, s80
	s_waitcnt vmcnt(0)
	v_cvt_scalef32_pk32_f32_fp6 v[0:31], v[32:37], 1.0
	v_pk_fma_f32 v[32:33], v[0:1], s[4:5], v[38:39] op_sel_hi:[1,0,1]
	v_pk_fma_f32 v[34:35], v[2:3], s[4:5], v[40:41] op_sel_hi:[1,0,1]
	v_pk_fma_f32 v[78:79], v[4:5], s[4:5], v[42:43] op_sel_hi:[1,0,1]
	v_pk_fma_f32 v[80:81], v[6:7], s[4:5], v[44:45] op_sel_hi:[1,0,1]
	v_pk_fma_f32 v[100:101], v[8:9], s[4:5], v[46:47] op_sel_hi:[1,0,1]
	v_pk_fma_f32 v[102:103], v[10:11], s[4:5], v[48:49] op_sel_hi:[1,0,1]
	v_pk_fma_f32 v[84:85], v[12:13], s[4:5], v[50:51] op_sel_hi:[1,0,1]
	v_pk_fma_f32 v[90:91], v[14:15], s[4:5], v[52:53] op_sel_hi:[1,0,1]
	v_pk_fma_f32 v[64:65], v[16:17], s[4:5], v[54:55] op_sel_hi:[1,0,1]
	v_pk_fma_f32 v[68:69], v[18:19], s[4:5], v[56:57] op_sel_hi:[1,0,1]
	v_pk_fma_f32 v[42:43], v[20:21], s[4:5], v[58:59] op_sel_hi:[1,0,1]
	v_pk_fma_f32 v[44:45], v[22:23], s[4:5], v[60:61] op_sel_hi:[1,0,1]
	v_pk_fma_f32 v[38:39], v[24:25], s[4:5], v[62:63] op_sel_hi:[1,0,1]
	v_pk_fma_f32 v[40:41], v[26:27], s[4:5], v[66:67] op_sel_hi:[1,0,1]
	v_pk_fma_f32 v[22:23], v[28:29], s[4:5], v[70:71] op_sel_hi:[1,0,1]
	v_pk_fma_f32 v[20:21], v[30:31], s[4:5], v[72:73] op_sel_hi:[1,0,1]
	s_andn2_b64 vcc, exec, s[54:55]
	s_cbranch_vccnz .LBB0_1178
	ds_write2st64_b32 v174, v32, v33 offset1:1
	ds_write2st64_b32 v174, v34, v35 offset0:2 offset1:3
	ds_write2st64_b32 v174, v78, v79 offset0:4 offset1:5
	ds_write2st64_b32 v174, v80, v81 offset0:6 offset1:7
	ds_write2st64_b32 v174, v100, v101 offset0:8 offset1:9
	ds_write2st64_b32 v174, v102, v103 offset0:10 offset1:11
	ds_write2st64_b32 v174, v84, v85 offset0:12 offset1:13
	ds_write2st64_b32 v174, v90, v91 offset0:14 offset1:15
	ds_write2st64_b32 v174, v64, v65 offset0:16 offset1:17
	ds_write2st64_b32 v174, v68, v69 offset0:18 offset1:19
	ds_write2st64_b32 v174, v42, v43 offset0:20 offset1:21
	ds_write2st64_b32 v174, v44, v45 offset0:22 offset1:23
	ds_write2st64_b32 v174, v38, v39 offset0:24 offset1:25
	ds_write2st64_b32 v174, v40, v41 offset0:26 offset1:27
	ds_write2st64_b32 v174, v22, v23 offset0:28 offset1:29
	ds_write2st64_b32 v174, v20, v21 offset0:30 offset1:31
	s_branch .LBB0_1178
